# routing group-max via DPP instead of ds_bpermute; stick-breaking tile loop: causal-mask flag folded into the per-lane key limit (no per-element scalar OR), key-index compares against inline constants
# baseline (speedup 1.0000x reference)
; #define LAS __attribute__((address_space(3)))
; __device__ __forceinline__ int crow(int r, int hi) { return (r & 3) + 8 * (r >> 2) + 4 * hi; }
; __device__ __forceinline__ void qkt(f32x16& p0, f32x16& p1, const LAS char* Ks, const bf16x8* qr, int r32, int hi) {
;     ...
;     for (int d0 = 0; d0 < 8; ++d0) { const int cb = (d0 * 16 + hi * 8) * 2;
;         const bf16x8 b0 = *(const LAS bf16x8*)(Ks + KSWZ(r32, cb));
;         const bf16x8 b1 = *(const LAS bf16x8*)(Ks + KSWZ(32 + r32, cb));
;         p0 = __builtin_amdgcn_mfma_f32_32x32x16_bf16(b0, qr[d0], p0, 0, 0, 0);
;         p1 = __builtin_amdgcn_mfma_f32_32x32x16_bf16(b1, qr[d0], p1, 0, 0, 0); }
; template <int MODE>
; __device__ __forceinline__ void attn_unit(const AttnArgs& A, int b, int qb, int qc, int kc, int vc, int oc, float slope2, int dmax, LAS char* lds) {
;     ...
;                 const bool need_mask = (k0 + 63 >= r0);
;                 float lsum = 0.f;
;                 float lk0[16], lk1[16];
; #pragma unroll
;                 for (int r = 0; r < 16; ++r) {
;                     { const float zl = p0[r] * QK_C, u = __builtin_amdgcn_exp2f(-fabsf(zl)), L = __builtin_amdgcn_logf(1.f + u), sp = fmaxf(zl, 0.f) + L;
;                       const bool ok = !need_mask || (k0 + crow(r, hi) < tq); lk0[r] = ok ? -sp : 0.f; p0[r] = ok ? (zl - sp) : -INFINITY; lsum += lk0[r]; }
;                     { const float zl = p1[r] * QK_C, u = __builtin_amdgcn_exp2f(-fabsf(zl)), L = __builtin_amdgcn_logf(1.f + u), sp = fmaxf(zl, 0.f) + L;
;                       const bool ok = !need_mask || (k0 + 32 + crow(r, hi) < tq); lk1[r] = ok ? -sp : 0.f; p1[r] = ok ? (zl - sp) : -INFINITY; lsum += lk1[r]; }
.LBB0_372:
	s_cmp_gt_i32 s38, s35
	s_cselect_b64 s[16:17], -1, 0
	s_or_b64 s[16:17], s[16:17], s[14:15]
	s_and_b64 vcc, exec, s[16:17]
	s_cbranch_vccnz .LBB0_374
	s_lshl_b32 s16, s41, 14
	v_add_u32_e32 v67, s16, v199
	v_add_u32_e32 v72, v67, v184
	ds_read_b128 v[68:71], v72 offset:32768
	ds_read_b128 v[72:75], v72 offset:40960
	v_add_u32_e32 v104, v67, v185
	ds_read_b128 v[100:103], v104 offset:32768
	ds_read_b128 v[104:107], v104 offset:40960
	s_add_i32 s14, s38, 63
	s_waitcnt lgkmcnt(0)
	v_mfma_f32_32x32x16_bf16 v[84:99], v[68:71], v[122:125], 0
	s_cmp_lt_i32 s14, s35
	s_cselect_b64 s[14:15], -1, 0
	v_mov_b32_e32 v254, 0x7fffffff
	v_cndmask_b32_e64 v253, v210, v254, s[14:15]
	s_mov_b32 s22, s20
	s_mov_b32 s23, s20
	s_mov_b32 s21, s20
	v_mfma_f32_32x32x16_bf16 v[68:83], v[72:75], v[122:125], 0
	v_mfma_f32_32x32x16_bf16 v[84:99], v[100:103], v[126:129], v[84:99]
	v_mfma_f32_32x32x16_bf16 v[68:83], v[104:107], v[126:129], v[68:83]
	v_add_u32_e32 v104, v67, v186
	ds_read_b128 v[100:103], v104 offset:32768
	ds_read_b128 v[104:107], v104 offset:40960
	s_waitcnt lgkmcnt(0)
	v_mfma_f32_32x32x16_bf16 v[84:99], v[100:103], v[130:133], v[84:99]
	v_mfma_f32_32x32x16_bf16 v[68:83], v[104:107], v[130:133], v[68:83]
	v_add_u32_e32 v104, v67, v187
	ds_read_b128 v[100:103], v104 offset:32768
	ds_read_b128 v[104:107], v104 offset:40960
	s_waitcnt lgkmcnt(0)
	v_mfma_f32_32x32x16_bf16 v[84:99], v[100:103], v[134:137], v[84:99]
	v_mfma_f32_32x32x16_bf16 v[68:83], v[104:107], v[134:137], v[68:83]
	v_add_u32_e32 v104, v67, v188
	ds_read_b128 v[100:103], v104 offset:32768
	ds_read_b128 v[104:107], v104 offset:40960
	s_waitcnt lgkmcnt(0)
	v_mfma_f32_32x32x16_bf16 v[84:99], v[100:103], v[138:141], v[84:99]
	v_mfma_f32_32x32x16_bf16 v[68:83], v[104:107], v[138:141], v[68:83]
	v_add_u32_e32 v104, v67, v189
	ds_read_b128 v[100:103], v104 offset:32768
	ds_read_b128 v[104:107], v104 offset:40960
	s_waitcnt lgkmcnt(0)
	v_mfma_f32_32x32x16_bf16 v[84:99], v[100:103], v[142:145], v[84:99]
	v_mfma_f32_32x32x16_bf16 v[68:83], v[104:107], v[142:145], v[68:83]
	v_add_u32_e32 v104, v67, v190
	ds_read_b128 v[100:103], v104 offset:32768
	ds_read_b128 v[104:107], v104 offset:40960
	v_add_u32_e32 v67, v67, v191
	s_waitcnt lgkmcnt(0)
	v_mfma_f32_32x32x16_bf16 v[84:99], v[100:103], v[146:149], v[84:99]
	v_mfma_f32_32x32x16_bf16 v[68:83], v[104:107], v[146:149], v[68:83]
	ds_read_b128 v[100:103], v67 offset:32768
	ds_read_b128 v[104:107], v67 offset:40960
	v_add_u32_e32 v67, s38, v192
	v_sub_u32_e32 v254, v253, v67
	v_cmp_lt_i32_e32 vcc, 0, v254
	s_waitcnt lgkmcnt(0)
	v_mfma_f32_32x32x16_bf16 v[84:99], v[100:103], v[150:153], v[84:99]
	v_mfma_f32_32x32x16_bf16 v[68:83], v[104:107], v[150:153], v[68:83]
	s_nop 9
	v_mul_f32_e32 v100, 0x3e0293ee, v84
	v_exp_f32_e64 v102, -|v100|
	v_max_f32_e32 v100, 0, v100
	v_add_f32_e32 v102, 1.0, v102
	v_log_f32_e32 v102, v102
	s_nop 0
	v_add_f32_e32 v102, v100, v102
	v_fma_f32 v84, v84, s26, -v102
	v_cndmask_b32_e32 v211, v208, v84, vcc
	v_mul_f32_e32 v84, 0x3e0293ee, v68
	v_exp_f32_e64 v103, -|v84|
	v_max_f32_e32 v84, 0, v84
	v_cndmask_b32_e64 v100, 0, -v102, vcc
	v_cmp_lt_i32_e32 vcc, 32, v254
	v_add_f32_e32 v103, 1.0, v103
	v_log_f32_e32 v103, v103
	v_add_f32_e32 v102, 0, v100
	v_add_f32_e32 v103, v84, v103
	v_fma_f32 v68, v68, s26, -v103
	v_cndmask_b32_e64 v84, 0, -v103, vcc
	v_cndmask_b32_e32 v212, v208, v68, vcc
	v_mul_f32_e32 v68, 0x3e0293ee, v85
	v_add_f32_e32 v101, v102, v84
	v_exp_f32_e64 v102, -|v68|
	v_max_f32_e32 v68, 0, v68
	v_add_f32_e32 v102, 1.0, v102
	v_log_f32_e32 v102, v102
	s_nop 0
	v_add_f32_e32 v102, v68, v102
	v_cmp_lt_i32_e32 vcc, 1, v254
	v_fma_f32 v85, v85, s26, -v102
	v_cndmask_b32_e32 v213, v208, v85, vcc
	v_mul_f32_e32 v85, 0x3e0293ee, v69
	v_cndmask_b32_e64 v68, 0, -v102, vcc
	v_exp_f32_e64 v102, -|v85|
	v_max_f32_e32 v85, 0, v85
	v_add_f32_e32 v101, v68, v101
	v_add_f32_e32 v102, 1.0, v102
	v_log_f32_e32 v102, v102
	s_nop 0
	v_add_f32_e32 v102, v85, v102
	v_cmp_lt_i32_e32 vcc, 33, v254
	v_fma_f32 v69, v69, s26, -v102
	v_cndmask_b32_e32 v214, v208, v69, vcc
	v_mul_f32_e32 v69, 0x3e0293ee, v86
	v_cndmask_b32_e64 v85, 0, -v102, vcc
	v_exp_f32_e64 v102, -|v69|
	v_max_f32_e32 v69, 0, v69
	v_add_f32_e32 v101, v85, v101
	v_cvt_pkrtz_f16_f32 v238, v84, v85
	v_add_f32_e32 v102, 1.0, v102
	v_log_f32_e32 v102, v102
	s_nop 0
	v_add_f32_e32 v102, v69, v102
	v_cmp_lt_i32_e32 vcc, 2, v254
	v_fma_f32 v86, v86, s26, -v102
	v_cndmask_b32_e32 v215, v208, v86, vcc
	v_mul_f32_e32 v86, 0x3e0293ee, v70
	v_cndmask_b32_e64 v69, 0, -v102, vcc
	v_exp_f32_e64 v102, -|v86|
	v_max_f32_e32 v86, 0, v86
	v_add_f32_e32 v101, v69, v101
	v_add_f32_e32 v102, 1.0, v102
	v_log_f32_e32 v102, v102
	s_nop 0
	v_add_f32_e32 v102, v86, v102
	v_cmp_lt_i32_e32 vcc, 34, v254
	v_fma_f32 v70, v70, s26, -v102
	v_cndmask_b32_e32 v216, v208, v70, vcc
	v_mul_f32_e32 v70, 0x3e0293ee, v87
	v_cndmask_b32_e64 v86, 0, -v102, vcc
	v_exp_f32_e64 v102, -|v70|
	v_max_f32_e32 v70, 0, v70
	v_add_f32_e32 v101, v86, v101
	v_add_f32_e32 v102, 1.0, v102
	v_log_f32_e32 v102, v102
	s_nop 0
	v_add_f32_e32 v102, v70, v102
	v_cmp_lt_i32_e32 vcc, 3, v254
	v_fma_f32 v87, v87, s26, -v102
	v_cndmask_b32_e32 v217, v208, v87, vcc
	v_mul_f32_e32 v87, 0x3e0293ee, v71
	v_cndmask_b32_e64 v70, 0, -v102, vcc
	v_exp_f32_e64 v102, -|v87|
	v_max_f32_e32 v87, 0, v87
	v_add_f32_e32 v101, v70, v101
	v_add_f32_e32 v102, 1.0, v102
	v_log_f32_e32 v102, v102
	s_nop 0
	v_add_f32_e32 v102, v87, v102
	v_cmp_lt_i32_e32 vcc, 35, v254
	v_fma_f32 v71, v71, s26, -v102
	v_cndmask_b32_e32 v218, v208, v71, vcc
	v_mul_f32_e32 v71, 0x3e0293ee, v88
	v_cndmask_b32_e64 v87, 0, -v102, vcc
	v_exp_f32_e64 v102, -|v71|
; __device__ __forceinline__ int crow(int r, int hi) { return (r & 3) + 8 * (r >> 2) + 4 * hi; }
; template <int MODE>
; __device__ __forceinline__ void attn_unit(const AttnArgs& A, int b, int qb, int qc, int kc, int vc, int oc, float slope2, int dmax, LAS char* lds) {
;     ...
;                 for (int r = 0; r < 16; ++r) {
;                     { const float zl = p0[r] * QK_C, u = __builtin_amdgcn_exp2f(-fabsf(zl)), L = __builtin_amdgcn_logf(1.f + u), sp = fmaxf(zl, 0.f) + L;
;                       const bool ok = !need_mask || (k0 + crow(r, hi) < tq); lk0[r] = ok ? -sp : 0.f; p0[r] = ok ? (zl - sp) : -INFINITY; lsum += lk0[r]; }
;                     { const float zl = p1[r] * QK_C, u = __builtin_amdgcn_exp2f(-fabsf(zl)), L = __builtin_amdgcn_logf(1.f + u), sp = fmaxf(zl, 0.f) + L;
;                       const bool ok = !need_mask || (k0 + 32 + crow(r, hi) < tq); lk1[r] = ok ? -sp : 0.f; p1[r] = ok ? (zl - sp) : -INFINITY; lsum += lk1[r]; }
;                 }
;                 f16x8 f0, f1, f2, f3; PK4H(lk0, 0, f0); PK4H(lk0, 8, f1); PK4H(lk1, 0, f2); PK4H(lk1, 8, f3);
	v_max_f32_e32 v71, 0, v71
	v_add_f32_e32 v101, v87, v101
	v_cvt_pkrtz_f16_f32 v239, v86, v87
	v_add_f32_e32 v102, 1.0, v102
	v_log_f32_e32 v102, v102
	s_nop 0
	v_add_f32_e32 v102, v71, v102
	v_cmp_lt_i32_e32 vcc, 8, v254
	v_fma_f32 v88, v88, s26, -v102
	v_cndmask_b32_e32 v219, v208, v88, vcc
	v_mul_f32_e32 v88, 0x3e0293ee, v72
	v_cndmask_b32_e64 v71, 0, -v102, vcc
	v_exp_f32_e64 v102, -|v88|
	v_max_f32_e32 v88, 0, v88
	v_add_f32_e32 v101, v71, v101
	v_add_f32_e32 v102, 1.0, v102
	v_log_f32_e32 v102, v102
	s_nop 0
	v_add_f32_e32 v102, v88, v102
	v_cmp_lt_i32_e32 vcc, 40, v254
	v_fma_f32 v72, v72, s26, -v102
	v_cndmask_b32_e32 v220, v208, v72, vcc
	v_mul_f32_e32 v72, 0x3e0293ee, v89
	v_cndmask_b32_e64 v88, 0, -v102, vcc
	v_exp_f32_e64 v102, -|v72|
	v_max_f32_e32 v72, 0, v72
	v_add_f32_e32 v101, v88, v101
	v_add_f32_e32 v102, 1.0, v102
	v_log_f32_e32 v102, v102
	s_nop 0
	v_add_f32_e32 v102, v72, v102
	v_cmp_lt_i32_e32 vcc, 9, v254
	v_fma_f32 v89, v89, s26, -v102
	v_cndmask_b32_e32 v221, v208, v89, vcc
	v_mul_f32_e32 v89, 0x3e0293ee, v73
	v_cndmask_b32_e64 v72, 0, -v102, vcc
	v_exp_f32_e64 v102, -|v89|
	v_max_f32_e32 v89, 0, v89
	v_add_f32_e32 v101, v72, v101
	v_add_f32_e32 v102, 1.0, v102
	v_log_f32_e32 v102, v102
	s_nop 0
	v_add_f32_e32 v102, v89, v102
	v_cmp_lt_i32_e32 vcc, 41, v254
	v_fma_f32 v73, v73, s26, -v102
	v_cndmask_b32_e32 v222, v208, v73, vcc
	v_mul_f32_e32 v73, 0x3e0293ee, v90
	v_cndmask_b32_e64 v89, 0, -v102, vcc
	v_exp_f32_e64 v102, -|v73|
	v_max_f32_e32 v73, 0, v73
	v_add_f32_e32 v101, v89, v101
	v_cvt_pkrtz_f16_f32 v240, v88, v89
	v_add_f32_e32 v102, 1.0, v102
	v_log_f32_e32 v102, v102
	v_permlane32_swap_b32_e32 v238, v240
	v_add_f32_e32 v102, v73, v102
	v_cmp_lt_i32_e32 vcc, 10, v254
	v_fma_f32 v90, v90, s26, -v102
	v_cndmask_b32_e32 v223, v208, v90, vcc
	v_mul_f32_e32 v90, 0x3e0293ee, v74
	v_cndmask_b32_e64 v73, 0, -v102, vcc
	v_exp_f32_e64 v102, -|v90|
	v_max_f32_e32 v90, 0, v90
	v_add_f32_e32 v101, v73, v101
	v_add_f32_e32 v102, 1.0, v102
	v_log_f32_e32 v102, v102
	s_nop 0
	v_add_f32_e32 v102, v90, v102
	v_cmp_lt_i32_e32 vcc, 42, v254
	v_fma_f32 v74, v74, s26, -v102
	v_cndmask_b32_e32 v224, v208, v74, vcc
	v_mul_f32_e32 v74, 0x3e0293ee, v91
	v_cndmask_b32_e64 v90, 0, -v102, vcc
	v_exp_f32_e64 v102, -|v74|
	v_max_f32_e32 v74, 0, v74
	v_add_f32_e32 v101, v90, v101
	v_add_f32_e32 v102, 1.0, v102
	v_log_f32_e32 v102, v102
	s_nop 0
	v_add_f32_e32 v102, v74, v102
	v_cmp_lt_i32_e32 vcc, 11, v254
	v_fma_f32 v91, v91, s26, -v102
	v_cndmask_b32_e32 v225, v208, v91, vcc
	v_mul_f32_e32 v91, 0x3e0293ee, v75
	v_cndmask_b32_e64 v74, 0, -v102, vcc
	v_exp_f32_e64 v102, -|v91|
	v_max_f32_e32 v91, 0, v91
	v_add_f32_e32 v101, v74, v101
	v_add_f32_e32 v102, 1.0, v102
	v_log_f32_e32 v102, v102
	s_nop 0
	v_add_f32_e32 v102, v91, v102
	v_cmp_lt_i32_e32 vcc, 43, v254
	v_fma_f32 v75, v75, s26, -v102
	v_cndmask_b32_e32 v226, v208, v75, vcc
	v_mul_f32_e32 v75, 0x3e0293ee, v92
	v_cndmask_b32_e64 v91, 0, -v102, vcc
	v_exp_f32_e64 v102, -|v75|
	v_max_f32_e32 v75, 0, v75
	v_add_f32_e32 v101, v91, v101
	v_cvt_pkrtz_f16_f32 v241, v90, v91
	v_add_f32_e32 v102, 1.0, v102
	v_log_f32_e32 v102, v102
	v_permlane32_swap_b32_e32 v239, v241
	v_add_f32_e32 v102, v75, v102
	v_cmp_lt_i32_e32 vcc, 16, v254
	v_fma_f32 v92, v92, s26, -v102
	v_cndmask_b32_e32 v227, v208, v92, vcc
	v_mul_f32_e32 v92, 0x3e0293ee, v76
	v_cndmask_b32_e64 v75, 0, -v102, vcc
	v_exp_f32_e64 v102, -|v92|
	v_max_f32_e32 v92, 0, v92
	v_add_f32_e32 v101, v75, v101
	v_add_f32_e32 v102, 1.0, v102
	v_log_f32_e32 v102, v102
	s_nop 0
	v_add_f32_e32 v102, v92, v102
	v_cmp_lt_i32_e32 vcc, 48, v254
	v_fma_f32 v76, v76, s26, -v102
	v_cndmask_b32_e32 v228, v208, v76, vcc
	v_mul_f32_e32 v76, 0x3e0293ee, v93
	v_cndmask_b32_e64 v92, 0, -v102, vcc
	v_exp_f32_e64 v102, -|v76|
	v_max_f32_e32 v76, 0, v76
	v_add_f32_e32 v101, v92, v101
	v_add_f32_e32 v102, 1.0, v102
	v_log_f32_e32 v102, v102
	s_nop 0
	v_add_f32_e32 v102, v76, v102
	v_cmp_lt_i32_e32 vcc, 17, v254
	v_fma_f32 v93, v93, s26, -v102
	v_cndmask_b32_e32 v229, v208, v93, vcc
	v_mul_f32_e32 v93, 0x3e0293ee, v77
	v_cndmask_b32_e64 v76, 0, -v102, vcc
	v_exp_f32_e64 v102, -|v93|
	v_max_f32_e32 v93, 0, v93
	v_add_f32_e32 v101, v76, v101
	v_add_f32_e32 v102, 1.0, v102
	v_log_f32_e32 v102, v102
	s_nop 0
	v_add_f32_e32 v102, v93, v102
	v_cmp_lt_i32_e32 vcc, 49, v254
	v_fma_f32 v77, v77, s26, -v102
	v_cndmask_b32_e32 v231, v208, v77, vcc
	v_mul_f32_e32 v77, 0x3e0293ee, v94
	v_cndmask_b32_e64 v93, 0, -v102, vcc
	v_exp_f32_e64 v102, -|v77|
	v_max_f32_e32 v77, 0, v77
	v_add_f32_e32 v101, v93, v101
	v_cvt_pkrtz_f16_f32 v242, v92, v93
	v_add_f32_e32 v102, 1.0, v102
	v_log_f32_e32 v102, v102
	s_nop 0
	v_add_f32_e32 v102, v77, v102
	v_cmp_lt_i32_e32 vcc, 18, v254
	v_fma_f32 v94, v94, s26, -v102
	v_cndmask_b32_e64 v77, 0, -v102, vcc
	v_cndmask_b32_e32 v232, v208, v94, vcc
	v_add_f32_e32 v94, v77, v101
	v_mul_f32_e32 v101, 0x3e0293ee, v78
	v_exp_f32_e64 v102, -|v101|
	v_max_f32_e32 v101, 0, v101
	v_add_f32_e32 v102, 1.0, v102
	v_log_f32_e32 v102, v102
	s_nop 0
	v_add_f32_e32 v101, v101, v102
	v_cmp_lt_i32_e32 vcc, 50, v254
	v_fma_f32 v78, v78, s26, -v101
	v_cndmask_b32_e64 v106, 0, -v101, vcc
	v_cndmask_b32_e32 v233, v208, v78, vcc
	v_add_f32_e32 v78, v106, v94
	v_mul_f32_e32 v94, 0x3e0293ee, v95
	v_exp_f32_e64 v101, -|v94|
	v_max_f32_e32 v94, 0, v94
	v_cvt_pkrtz_f16_f32 v102, v75, v76
	v_mov_b32_e32 v75, v66
	v_add_f32_e32 v101, 1.0, v101
	v_log_f32_e32 v101, v101
	v_mov_b32_e32 v76, v66
	v_add_f32_e32 v94, v94, v101
	v_cmp_lt_i32_e32 vcc, 19, v254
	v_cvt_pkrtz_f16_f32 v101, v73, v74
	v_cndmask_b32_e64 v103, 0, -v94, vcc
	v_fma_f32 v94, v95, s26, -v94
; __device__ __forceinline__ int crow(int r, int hi) { return (r & 3) + 8 * (r >> 2) + 4 * hi; }
; template <int MODE>
; __device__ __forceinline__ void attn_unit(const AttnArgs& A, int b, int qb, int qc, int kc, int vc, int oc, float slope2, int dmax, LAS char* lds) {
;     ...
;                 for (int r = 0; r < 16; ++r) {
;                     { const float zl = p0[r] * QK_C, u = __builtin_amdgcn_exp2f(-fabsf(zl)), L = __builtin_amdgcn_logf(1.f + u), sp = fmaxf(zl, 0.f) + L;
;                       const bool ok = !need_mask || (k0 + crow(r, hi) < tq); lk0[r] = ok ? -sp : 0.f; p0[r] = ok ? (zl - sp) : -INFINITY; lsum += lk0[r]; }
;                     { const float zl = p1[r] * QK_C, u = __builtin_amdgcn_exp2f(-fabsf(zl)), L = __builtin_amdgcn_logf(1.f + u), sp = fmaxf(zl, 0.f) + L;
;                       const bool ok = !need_mask || (k0 + 32 + crow(r, hi) < tq); lk1[r] = ok ? -sp : 0.f; p1[r] = ok ? (zl - sp) : -INFINITY; lsum += lk1[r]; }
;                 }
;                 f16x8 f0, f1, f2, f3; PK4H(lk0, 0, f0); PK4H(lk0, 8, f1); PK4H(lk1, 0, f2); PK4H(lk1, 8, f3);
;                 f32x16 w0, w1;
; #pragma unroll
;                 for (int r = 0; r < 16; ++r) { w0[r] = carry; w1[r] = carry; }
;                 w0 = __builtin_amdgcn_mfma_f32_32x32x16_f16(tri0, f0, w0, 0, 0, 0); w0 = __builtin_amdgcn_mfma_f32_32x32x16_f16(tri1, f1, w0, 0, 0, 0);
;                 w0 = __builtin_amdgcn_mfma_f32_32x32x16_f16(ones, f2, w0, 0, 0, 0); w0 = __builtin_amdgcn_mfma_f32_32x32x16_f16(ones, f3, w0, 0, 0, 0);
;                 w1 = __builtin_amdgcn_mfma_f32_32x32x16_f16(tri0, f2, w1, 0, 0, 0); w1 = __builtin_amdgcn_mfma_f32_32x32x16_f16(tri1, f3, w1, 0, 0, 0);
; #pragma unroll
;                 for (int r = 0; r < 16; ++r) { p0[r] = __builtin_amdgcn_exp2f(p0[r] + w0[r]); p1[r] = __builtin_amdgcn_exp2f(p1[r] + w1[r]); }
	v_cndmask_b32_e32 v234, v208, v94, vcc
	v_mul_f32_e32 v94, 0x3e0293ee, v79
	v_exp_f32_e64 v95, -|v94|
	v_max_f32_e32 v94, 0, v94
	v_add_f32_e32 v78, v103, v78
	v_cvt_pkrtz_f16_f32 v103, v77, v103
	v_add_f32_e32 v95, 1.0, v95
	v_log_f32_e32 v95, v95
	v_mov_b32_e32 v73, v66
	v_mov_b32_e32 v74, v66
	v_mov_b32_e32 v77, v66
	v_add_f32_e32 v94, v94, v95
	v_cmp_lt_i32_e32 vcc, 51, v254
	v_fma_f32 v79, v79, s26, -v94
	v_cndmask_b32_e32 v235, v208, v79, vcc
	v_mul_f32_e32 v79, 0x3e0293ee, v96
	v_cndmask_b32_e64 v95, 0, -v94, vcc
	v_exp_f32_e64 v94, -|v79|
	v_max_f32_e32 v79, 0, v79
	v_add_f32_e32 v78, v95, v78
	v_cvt_pkrtz_f16_f32 v243, v106, v95
	v_add_f32_e32 v94, 1.0, v94
	v_log_f32_e32 v94, v94
	s_nop 0
	v_add_f32_e32 v79, v79, v94
	v_cmp_lt_i32_e32 vcc, 24, v254
	s_nop 0
	v_cndmask_b32_e64 v94, 0, -v79, vcc
	v_fma_f32 v79, v96, s26, -v79
	v_cndmask_b32_e32 v236, v208, v79, vcc
	v_mul_f32_e32 v79, 0x3e0293ee, v80
	v_exp_f32_e64 v96, -|v79|
	v_max_f32_e32 v79, 0, v79
	v_add_f32_e32 v78, v94, v78
	v_add_f32_e32 v96, 1.0, v96
	v_log_f32_e32 v96, v96
	s_nop 0
	v_add_f32_e32 v79, v79, v96
	v_cmp_lt_i32_e32 vcc, 56, v254
	s_nop 0
	v_cndmask_b32_e64 v96, 0, -v79, vcc
	v_fma_f32 v79, v80, s26, -v79
	v_cndmask_b32_e32 v237, v208, v79, vcc
	v_mul_f32_e32 v79, 0x3e0293ee, v97
	v_exp_f32_e64 v80, -|v79|
	v_max_f32_e32 v79, 0, v79
	v_add_f32_e32 v78, v96, v78
	v_add_f32_e32 v80, 1.0, v80
	v_log_f32_e32 v80, v80
	s_nop 0
	v_add_f32_e32 v79, v79, v80
	v_cmp_lt_i32_e32 vcc, 25, v254
	s_nop 0
	v_cndmask_b32_e64 v80, 0, -v79, vcc
	v_fma_f32 v79, v97, s26, -v79
	v_cndmask_b32_e32 v246, v208, v79, vcc
	v_mul_f32_e32 v79, 0x3e0293ee, v81
	v_exp_f32_e64 v97, -|v79|
	v_max_f32_e32 v79, 0, v79
	v_add_f32_e32 v78, v80, v78
	v_cvt_pkrtz_f16_f32 v104, v94, v80
	v_add_f32_e32 v97, 1.0, v97
	v_log_f32_e32 v97, v97
	v_mov_b32_e32 v80, v66
	v_permlane32_swap_b32_e32 v102, v104
	v_add_f32_e32 v79, v79, v97
	v_cmp_lt_i32_e32 vcc, 57, v254
	s_nop 0
	v_cndmask_b32_e64 v97, 0, -v79, vcc
	v_fma_f32 v79, v81, s26, -v79
	v_cndmask_b32_e32 v247, v208, v79, vcc
	v_mul_f32_e32 v79, 0x3e0293ee, v98
	v_exp_f32_e64 v81, -|v79|
	v_max_f32_e32 v79, 0, v79
	v_add_f32_e32 v78, v97, v78
	v_cvt_pkrtz_f16_f32 v244, v96, v97
	v_add_f32_e32 v81, 1.0, v81
	v_log_f32_e32 v81, v81
	v_permlane32_swap_b32_e32 v242, v244
	v_add_f32_e32 v79, v79, v81
	v_cmp_lt_i32_e32 vcc, 26, v254
	s_nop 0
	v_cndmask_b32_e64 v81, 0, -v79, vcc
	v_fma_f32 v79, v98, s26, -v79
	v_cndmask_b32_e32 v248, v208, v79, vcc
	v_mul_f32_e32 v79, 0x3e0293ee, v82
	v_exp_f32_e64 v98, -|v79|
	v_max_f32_e32 v79, 0, v79
	v_add_f32_e32 v78, v81, v78
	v_add_f32_e32 v98, 1.0, v98
	v_log_f32_e32 v98, v98
	s_nop 0
	v_add_f32_e32 v79, v79, v98
	v_cmp_lt_i32_e32 vcc, 58, v254
	s_nop 0
	v_cndmask_b32_e64 v107, 0, -v79, vcc
	v_fma_f32 v79, v82, s26, -v79
	v_cndmask_b32_e32 v249, v208, v79, vcc
	v_mul_f32_e32 v79, 0x3e0293ee, v99
	v_exp_f32_e64 v82, -|v79|
	v_max_f32_e32 v79, 0, v79
	v_add_f32_e32 v78, v107, v78
	v_add_f32_e32 v82, 1.0, v82
	v_log_f32_e32 v82, v82
	s_nop 0
	v_add_f32_e32 v79, v79, v82
	v_cmp_lt_i32_e32 vcc, 27, v254
	v_cndmask_b32_e64 v82, 0, -v79, vcc
	v_fma_f32 v79, v99, s26, -v79
	v_cndmask_b32_e32 v250, v208, v79, vcc
	v_mul_f32_e32 v79, 0x3e0293ee, v83
	v_exp_f32_e64 v98, -|v79|
	v_max_f32_e32 v79, 0, v79
	v_cmp_lt_i32_e32 vcc, 59, v254
	v_add_f32_e32 v98, 1.0, v98
	v_log_f32_e32 v98, v98
	v_add_f32_e32 v78, v82, v78
	v_cvt_pkrtz_f16_f32 v99, v69, v70
	s_nop 1
	v_permlane32_swap_b32_e32 v99, v101
	v_add_f32_e32 v79, v79, v98
	v_cndmask_b32_e64 v67, 0, -v79, vcc
	v_fma_f32 v79, v83, s26, -v79
	v_cvt_pkrtz_f16_f32 v98, v100, v68
	v_cvt_pkrtz_f16_f32 v100, v71, v72
	v_cndmask_b32_e32 v251, v208, v79, vcc
	v_add_f32_e32 v252, v67, v78
	v_permlane32_swap_b32_e32 v98, v100
	v_cvt_pkrtz_f16_f32 v105, v81, v82
	v_cvt_pkrtz_f16_f32 v245, v107, v67
	v_mov_b32_e32 v67, v66
	v_mov_b32_e32 v68, v66
	v_mov_b32_e32 v69, v66
	v_mov_b32_e32 v70, v66
	v_mov_b32_e32 v71, v66
	v_mov_b32_e32 v72, v66
	v_mov_b32_e32 v78, v66
	v_mov_b32_e32 v79, v66
	v_mov_b32_e32 v81, v66
	v_permlane32_swap_b32_e32 v103, v105
	s_nop 0
	v_mfma_f32_32x32x16_f16 v[82:97], v[114:117], v[98:101], v[66:81]
	v_mov_b64_e32 v[100:101], s[22:23]
	v_mov_b64_e32 v[98:99], s[20:21]
	v_permlane32_swap_b32_e32 v243, v245
	v_mfma_f32_32x32x16_f16 v[82:97], v[118:121], v[102:105], v[82:97]
	v_mfma_f32_32x32x16_f16 v[82:97], v[98:101], v[238:241], v[82:97]
	v_mfma_f32_32x32x16_f16 v[82:97], v[98:101], v[242:245], v[82:97]
	v_mov_b64_e32 v[112:113], v[80:81]
	v_mov_b64_e32 v[110:111], v[78:79]
	v_mov_b64_e32 v[108:109], v[76:77]
	v_mov_b64_e32 v[106:107], v[74:75]
	v_mov_b64_e32 v[104:105], v[72:73]
	v_mov_b64_e32 v[102:103], v[70:71]
	v_mov_b64_e32 v[100:101], v[68:69]
	v_mov_b64_e32 v[98:99], v[66:67]
	s_nop 3
	v_add_f32_e32 v67, v211, v82
	v_add_f32_e32 v97, v250, v97
	v_mfma_f32_32x32x16_f16 v[98:113], v[114:117], v[238:241], v[98:113]
	v_exp_f32_e32 v67, v67
	v_exp_f32_e32 v97, v97
	v_mfma_f32_32x32x16_f16 v[98:113], v[118:121], v[242:245], v[98:113]
	s_nop 11
	v_add_f32_e32 v69, v214, v99
	v_mov_b32_e32 v99, v252
	s_nop 1
	v_permlane32_swap_b32_e32 v252, v99
	v_add_f32_e32 v99, v252, v99
	v_add_f32_e32 v68, v212, v98
	v_add_f32_e32 v70, v216, v100
	v_add_f32_e32 v71, v218, v101
; template <int MODE>
; __device__ __forceinline__ void attn_unit(const AttnArgs& A, int b, int qb, int qc, int kc, int vc, int oc, float slope2, int dmax, LAS char* lds) {
;     ...
;                 for (int r = 0; r < 16; ++r) { p0[r] = __builtin_amdgcn_exp2f(p0[r] + w0[r]); p1[r] = __builtin_amdgcn_exp2f(p1[r] + w1[r]); }
;                 carry += xhalf_sum(lsum);
;                 wdone = __all(carry < -150.f);
;             } else {
;                 const bool need_mask = (k0 + 63 > r0);
;                 const float fb = (float)(k0 - tq + 4 * hi);
;                 float mx = -1e30f;
; #pragma unroll
;                 for (int r = 0; r < 16; ++r) { const float t0 = fb + (float)((r & 3) + 8 * (r >> 2)), t1 = t0 + 32.f;
;                     float z0 = fmaf(slope2, t0, p0[r] * QK_C), z1 = fmaf(slope2, t1, p1[r] * QK_C);
;                     if (need_mask) { if (t0 > 0.f) z0 = -INFINITY; if (t1 > 0.f) z1 = -INFINITY; }
;                     p0[r] = z0; p1[r] = z1; mx = fmaxf(mx, fmaxf(z0, z1)); }
;                 mx = xhalf_max(mx);
;                 const float mn = fmaxf(m_run, mx), alpha = __builtin_amdgcn_exp2f(m_run - mn); m_run = mn;
;                 float ps = 0.f;
; #pragma unroll
;                 for (int r = 0; r < 16; ++r) { p0[r] = __builtin_amdgcn_exp2f(p0[r] - mn); p1[r] = __builtin_amdgcn_exp2f(p1[r] - mn); ps += p0[r] + p1[r]; }
;                 l_run = l_run * alpha + xhalf_sum(ps);
;                 if (__any(alpha < 1.f)) { if (hi == 0) ws[r32] = alpha; asm volatile("s_waitcnt lgkmcnt(0)" ::: "memory");
; #pragma unroll
;                     for (int r = 0; r < 16; ++r) { const float a_ = ws[crow(r, hi)];
; #pragma unroll
;                         for (int d = 0; d < 4; ++d) o[d][r] *= a_; } }
;             }
;             PK4BF(p0, 0, pa0); PK4BF(p0, 8, pa1); PK4BF(p1, 0, pa2); PK4BF(p1, 8, pa3);
;             SBAR();
;             {
;               s16x4 aL0, aH0, aL1, aH1, bL0, bH0, bL1, bH1;
;     ...
;               PVRD(a, 0, 0);
;               PVRD(b, 1, 0); PVMM(a, o[0], pa0, pa1, 4); PVRD(a, 2, 0); PVMM(b, o[1], pa0, pa1, 4);
;               PVRD(b, 3, 0); PVMM(a, o[2], pa0, pa1, 4); PVRD(a, 0, 2); PVMM(b, o[3], pa0, pa1, 4);
;               PVRD(b, 1, 2); PVMM(a, o[0], pa2, pa3, 4); PVRD(a, 2, 2); PVMM(b, o[1], pa2, pa3, 4);
;               PVRD(b, 3, 2); PVMM(a, o[2], pa2, pa3, 4);                PVMM(b, o[3], pa2, pa3, 0);
	v_add_f32_e32 v72, v220, v102
	v_add_f32_e32 v73, v222, v103
	v_add_f32_e32 v74, v224, v104
	v_add_f32_e32 v75, v226, v105
	v_add_f32_e32 v66, v66, v99
	v_exp_f32_e32 v76, v68
	v_add_f32_e32 v68, v213, v83
	v_exp_f32_e32 v77, v69
	v_add_f32_e32 v69, v215, v84
	v_exp_f32_e32 v78, v70
	v_add_f32_e32 v70, v217, v85
	v_exp_f32_e32 v79, v71
	v_add_f32_e32 v71, v219, v86
	v_exp_f32_e32 v80, v72
	v_add_f32_e32 v72, v221, v87
	v_exp_f32_e32 v81, v73
	v_add_f32_e32 v73, v223, v88
	v_exp_f32_e32 v82, v74
	v_add_f32_e32 v74, v225, v89
	v_exp_f32_e32 v83, v75
	v_add_f32_e32 v75, v227, v90
	v_cmp_gt_f32_e32 vcc, s27, v66
	v_exp_f32_e32 v68, v68
	v_exp_f32_e32 v69, v69
	v_exp_f32_e32 v70, v70
	v_exp_f32_e32 v71, v71
	v_exp_f32_e32 v72, v72
	v_exp_f32_e32 v73, v73
	v_exp_f32_e32 v74, v74
	v_exp_f32_e32 v75, v75
	v_add_f32_e32 v84, v228, v106
	v_add_f32_e32 v85, v229, v91
	v_add_f32_e32 v86, v231, v107
	v_add_f32_e32 v87, v232, v92
	v_add_f32_e32 v88, v233, v108
	v_add_f32_e32 v89, v234, v93
	v_add_f32_e32 v90, v235, v109
	v_add_f32_e32 v91, v236, v94
	v_add_f32_e32 v92, v237, v110
	v_add_f32_e32 v93, v246, v95
	v_add_f32_e32 v94, v247, v111
	v_add_f32_e32 v95, v248, v96
	v_add_f32_e32 v96, v249, v112
	v_add_f32_e32 v98, v251, v113
	s_cmp_eq_u64 vcc, exec
	v_exp_f32_e32 v84, v84
	v_exp_f32_e32 v85, v85
	v_exp_f32_e32 v86, v86
	v_exp_f32_e32 v87, v87
	v_exp_f32_e32 v88, v88
	v_exp_f32_e32 v89, v89
	v_exp_f32_e32 v90, v90
	v_exp_f32_e32 v91, v91
	v_exp_f32_e32 v92, v92
	v_exp_f32_e32 v93, v93
	v_exp_f32_e32 v94, v94
	v_exp_f32_e32 v95, v95
	v_exp_f32_e32 v96, v96
	v_exp_f32_e32 v98, v98
	s_cselect_b64 s[14:15], -1, 0
	v_cvt_pk_bf16_f32 v68, v67, v68
	v_cvt_pk_bf16_f32 v69, v69, v70
	v_cvt_pk_bf16_f32 v70, v71, v72
	v_cvt_pk_bf16_f32 v71, v73, v74
	v_cvt_pk_bf16_f32 v72, v75, v85
	v_cvt_pk_bf16_f32 v73, v87, v89
	v_cvt_pk_bf16_f32 v74, v91, v93
	v_cvt_pk_bf16_f32 v75, v95, v97
	v_cvt_pk_bf16_f32 v76, v76, v77
	v_cvt_pk_bf16_f32 v77, v78, v79
	v_cvt_pk_bf16_f32 v78, v80, v81
	v_cvt_pk_bf16_f32 v79, v82, v83
	v_cvt_pk_bf16_f32 v80, v84, v86
	v_cvt_pk_bf16_f32 v81, v88, v90
	v_cvt_pk_bf16_f32 v82, v92, v94
	v_cvt_pk_bf16_f32 v83, v96, v98
	v_add_u32_e32 v100, s16, v200
	v_permlane32_swap_b32_e32 v68, v70
	v_permlane32_swap_b32_e32 v69, v71
	v_permlane32_swap_b32_e32 v72, v74
	v_permlane32_swap_b32_e32 v73, v75
	v_permlane32_swap_b32_e32 v76, v78
	v_permlane32_swap_b32_e32 v77, v79
	v_permlane32_swap_b32_e32 v80, v82
	v_permlane32_swap_b32_e32 v81, v83
	ds_read_b64_tr_b16 v[84:85], v100 offset:0
	ds_read_b64_tr_b16 v[86:87], v100 offset:0x800
	ds_read_b64_tr_b16 v[88:89], v100 offset:0x1000
	ds_read_b64_tr_b16 v[90:91], v100 offset:0x1800
	ds_read_b64_tr_b16 v[92:93], v100 offset:0x200
	ds_read_b64_tr_b16 v[94:95], v100 offset:0xa00
	ds_read_b64_tr_b16 v[96:97], v100 offset:0x1200
	ds_read_b64_tr_b16 v[98:99], v100 offset:0x1a00
	s_waitcnt lgkmcnt(4)
	s_nop 0
	v_mfma_f32_32x32x16_bf16 v[2:17], v[68:71], v[84:87], v[2:17]
	v_mfma_f32_32x32x16_bf16 v[2:17], v[72:75], v[88:91], v[2:17]
	ds_read_b64_tr_b16 v[84:85], v100 offset:0x400
	ds_read_b64_tr_b16 v[86:87], v100 offset:0xc00
	ds_read_b64_tr_b16 v[88:89], v100 offset:0x1400
	ds_read_b64_tr_b16 v[90:91], v100 offset:0x1c00
	s_waitcnt lgkmcnt(4)
	v_mfma_f32_32x32x16_bf16 v[18:33], v[68:71], v[92:95], v[18:33]
	v_mfma_f32_32x32x16_bf16 v[18:33], v[72:75], v[96:99], v[18:33]
	ds_read_b64_tr_b16 v[92:93], v100 offset:0x600
	ds_read_b64_tr_b16 v[94:95], v100 offset:0xe00
	ds_read_b64_tr_b16 v[96:97], v100 offset:0x1600
	ds_read_b64_tr_b16 v[98:99], v100 offset:0x1e00
	s_waitcnt lgkmcnt(4)
	v_mfma_f32_32x32x16_bf16 v[34:49], v[68:71], v[84:87], v[34:49]
	v_mfma_f32_32x32x16_bf16 v[34:49], v[72:75], v[88:91], v[34:49]
	ds_read_b64_tr_b16 v[84:85], v100 offset:0x2000
	ds_read_b64_tr_b16 v[86:87], v100 offset:0x2800
	ds_read_b64_tr_b16 v[88:89], v100 offset:0x3000
	ds_read_b64_tr_b16 v[90:91], v100 offset:0x3800
	s_waitcnt lgkmcnt(4)
	v_mfma_f32_32x32x16_bf16 v[50:65], v[68:71], v[92:95], v[50:65]
	v_mfma_f32_32x32x16_bf16 v[50:65], v[72:75], v[96:99], v[50:65]
	ds_read_b64_tr_b16 v[68:69], v100 offset:0x2200
	ds_read_b64_tr_b16 v[70:71], v100 offset:0x2a00
	ds_read_b64_tr_b16 v[72:73], v100 offset:0x3200
	ds_read_b64_tr_b16 v[74:75], v100 offset:0x3a00
	s_waitcnt lgkmcnt(4)
	v_mfma_f32_32x32x16_bf16 v[2:17], v[76:79], v[84:87], v[2:17]
	v_mfma_f32_32x32x16_bf16 v[2:17], v[80:83], v[88:91], v[2:17]
	ds_read_b64_tr_b16 v[84:85], v100 offset:0x2400
	ds_read_b64_tr_b16 v[86:87], v100 offset:0x2c00
	ds_read_b64_tr_b16 v[88:89], v100 offset:0x3400
	ds_read_b64_tr_b16 v[90:91], v100 offset:0x3c00
	s_waitcnt lgkmcnt(4)
	v_mfma_f32_32x32x16_bf16 v[18:33], v[76:79], v[68:71], v[18:33]
	v_mfma_f32_32x32x16_bf16 v[18:33], v[80:83], v[72:75], v[18:33]
	ds_read_b64_tr_b16 v[68:69], v100 offset:0x2600
	ds_read_b64_tr_b16 v[70:71], v100 offset:0x2e00
	ds_read_b64_tr_b16 v[72:73], v100 offset:0x3600
	ds_read_b64_tr_b16 v[74:75], v100 offset:0x3e00
	s_waitcnt lgkmcnt(4)
	v_mfma_f32_32x32x16_bf16 v[34:49], v[76:79], v[84:87], v[34:49]
	v_mfma_f32_32x32x16_bf16 v[34:49], v[80:83], v[88:91], v[34:49]
	s_waitcnt lgkmcnt(0)
	v_mfma_f32_32x32x16_bf16 v[50:65], v[76:79], v[68:71], v[50:65]
	v_mfma_f32_32x32x16_bf16 v[50:65], v[80:83], v[72:75], v[50:65]

; #define LAS __attribute__((address_space(3)))
; __device__ __forceinline__ void phase_nrr(const Frame& F, const Args& a, int l, const bf16_t* XA, const float* g, const float* modl, unsigned char* XN8) {
;     ...
;         __syncthreads();
; #pragma unroll
;         for (int rb = 0; rb < 4; ++rb) *(LAS f32x4*)(Pl + (size_t)((kq * 64 + 16 * rb + fr) * NE + 16 * eb + 4 * fq)) = acc[rb];
;         __syncthreads();
;         const float bias = rbias[lane];
; #pragma unroll
;         for (int i = 0; i < 8; ++i) { const int t = tb + i;
;             const float lg = Pl[(w * 8 + i) * NE + lane] + Pl[(64 + w * 8 + i) * NE + lane]; const float sc = 1.f / (1.f + __expf(-lg)); const float bb = sc + bias;
;             float m1 = bb; m1 = fmaxf(m1, __shfl_xor(m1, 1)); m1 = fmaxf(m1, __shfl_xor(m1, 2)); m1 = fmaxf(m1, __shfl_xor(m1, 4));
;             const unsigned long long eq = __ballot(bb == m1); const int gbase = lane & ~7; const unsigned grpmask = (unsigned)((eq >> gbase) & 0xffull);
;             const int first = gbase + __builtin_ctz(grpmask);
;             float m2 = (lane == first) ? -INFINITY : bb; m2 = fmaxf(m2, __shfl_xor(m2, 1)); m2 = fmaxf(m2, __shfl_xor(m2, 2)); m2 = fmaxf(m2, __shfl_xor(m2, 4));
;             const float gsum = m1 + m2; const int gq = lane >> 3;
;             int grank = 0;
; #pragma unroll
;             for (int g2 = 0; g2 < 8; ++g2) { const float v = __int_as_float(__builtin_amdgcn_readlane(__float_as_int(gsum), g2 * 8)); grank += (v > gsum || (v == gsum && g2 < gq)) ? 1 : 0; }
;             const bool keep = grank < 4; const float val = keep ? bb : -INFINITY;
;             int rank = 0;
; #pragma unroll 8
;             for (int e2 = 0; e2 < 64; ++e2) { const float v = __int_as_float(__builtin_amdgcn_readlane(__float_as_int(val), e2)); rank += (v > val || (v == val && e2 < lane)) ? 1 : 0; }
.LBB0_535:
	s_barrier
	ds_write_b128 v242, v[110:113]
	ds_write_b128 v242, v[118:121] offset:4096
	s_nop 0
	ds_write_b128 v242, v[126:129] offset:8192
	s_nop 1
	ds_write_b128 v242, v[130:133] offset:12288
	s_waitcnt lgkmcnt(0)
	s_barrier
	global_load_dword v3, v[198:199], off
	s_waitcnt vmcnt(15)
	v_add_u32_e32 v4, s76, v226
	ds_read2st64_b32 v[6:7], v4 offset1:64
	s_mov_b32 s3, 0
	s_waitcnt lgkmcnt(0)
	v_add_f32_e32 v2, v6, v7
	v_mul_f32_e32 v2, 0xbfb8aa3b, v2
	v_exp_f32_e32 v2, v2
	s_nop 0
	v_add_f32_e32 v2, 1.0, v2
	v_div_scale_f32 v5, s[22:23], v2, v2, 1.0
	v_rcp_f32_e32 v6, v5
	s_nop 0
	v_fma_f32 v7, -v5, v6, 1.0
	v_fmac_f32_e32 v6, v7, v6
	v_div_scale_f32 v7, vcc, 1.0, v2, 1.0
	v_mul_f32_e32 v8, v7, v6
	v_fma_f32 v9, -v5, v8, v7
	v_fmac_f32_e32 v8, v9, v6
	v_fma_f32 v5, -v5, v8, v7
	v_div_fmas_f32 v5, v5, v6, v8
	v_div_fixup_f32 v2, v5, v2, 1.0
	s_waitcnt vmcnt(0)
	v_add_f32_e32 v5, v3, v2
	s_nop 1
	s_waitcnt lgkmcnt(0)
	v_max_f32_dpp v6, v5, v5 quad_perm:[1,0,3,2] row_mask:0xf bank_mask:0xf
	s_nop 1
	s_waitcnt lgkmcnt(0)
	v_max_f32_dpp v6, v6, v6 quad_perm:[2,3,0,1] row_mask:0xf bank_mask:0xf
	s_nop 1
	s_waitcnt lgkmcnt(0)
	v_max_f32_dpp v8, v6, v6 row_half_mirror row_mask:0xf bank_mask:0xf
	v_cmp_eq_f32_e32 vcc, v5, v8
	s_nop 1
	v_lshrrev_b64 v[6:7], v200, vcc
	v_ffbl_b32_sdwa v6, v6 dst_sel:DWORD dst_unused:UNUSED_PAD src0_sel:BYTE_0
	v_add_u32_e32 v6, v6, v200
	v_cmp_ne_u32_e32 vcc, v230, v6
	s_nop 1
	v_cndmask_b32_e32 v6, v245, v5, vcc
	s_nop 1
	s_waitcnt lgkmcnt(0)
	v_max_f32_dpp v6, v6, v6 quad_perm:[1,0,3,2] row_mask:0xf bank_mask:0xf
	s_nop 1
	s_waitcnt lgkmcnt(0)
	v_max_f32_dpp v6, v6, v6 quad_perm:[2,3,0,1] row_mask:0xf bank_mask:0xf
	s_nop 1
	s_waitcnt lgkmcnt(0)
	v_max_f32_dpp v6, v6, v6 row_half_mirror row_mask:0xf bank_mask:0xf
	v_add_f32_e32 v6, v8, v6
	s_nop 0
	v_readlane_b32 s5, v6, 0
	s_nop 1
	v_cmp_eq_f32_e64 s[22:23], s5, v6
	v_cmp_gt_f32_e32 vcc, s5, v6
	s_and_b64 s[22:23], s[6:7], s[22:23]
	s_or_b64 s[22:23], vcc, s[22:23]
	v_readlane_b32 s5, v6, 8
	v_cndmask_b32_e64 v7, 0, 1, s[22:23]
	s_nop 0
	v_cmp_eq_f32_e64 s[22:23], s5, v6
	v_cmp_gt_f32_e32 vcc, s5, v6
	s_and_b64 s[22:23], s[8:9], s[22:23]
	s_or_b64 s[22:23], vcc, s[22:23]
	v_readlane_b32 s5, v6, 16
	v_cndmask_b32_e64 v8, 0, 1, s[22:23]
	s_nop 0
	v_cmp_eq_f32_e64 s[22:23], s5, v6
	v_cmp_gt_f32_e32 vcc, s5, v6
	s_and_b64 s[22:23], s[10:11], s[22:23]
	s_or_b64 s[22:23], vcc, s[22:23]
	v_readlane_b32 s5, v6, 24
	v_cndmask_b32_e64 v9, 0, 1, s[22:23]
	s_nop 0
	v_cmp_eq_f32_e64 s[22:23], s5, v6
	v_cmp_gt_f32_e32 vcc, s5, v6
	s_and_b64 s[22:23], s[12:13], s[22:23]
	s_or_b64 s[22:23], vcc, s[22:23]
	v_readlane_b32 s5, v6, 32
	v_cndmask_b32_e64 v10, 0, 1, s[22:23]
	s_nop 0
	v_cmp_eq_f32_e64 s[22:23], s5, v6
	v_cmp_gt_f32_e32 vcc, s5, v6
	s_and_b64 s[22:23], s[14:15], s[22:23]
	s_or_b64 s[22:23], vcc, s[22:23]
	v_readlane_b32 s5, v6, 40
	v_cndmask_b32_e64 v11, 0, 1, s[22:23]
	s_nop 0
	v_cmp_eq_f32_e64 s[22:23], s5, v6
	v_cmp_gt_f32_e32 vcc, s5, v6
	s_and_b64 s[22:23], s[16:17], s[22:23]
	s_or_b64 s[22:23], vcc, s[22:23]
	v_readlane_b32 s5, v6, 48
	v_cndmask_b32_e64 v12, 0, 1, s[22:23]
	s_nop 0
	v_cmp_eq_f32_e64 s[22:23], s5, v6
	v_cmp_gt_f32_e32 vcc, s5, v6
	s_and_b64 s[22:23], s[18:19], s[22:23]
	v_readlane_b32 s5, v6, 56
	s_or_b64 s[22:23], vcc, s[22:23]
	v_cndmask_b32_e64 v13, 0, 1, s[22:23]
	v_cmp_gt_f32_e32 vcc, s5, v6
	s_nop 1
	v_cndmask_b32_e64 v6, 0, 1, vcc
	v_add_u32_e32 v6, v8, v6
	v_add3_u32 v6, v6, v7, v9
	v_add3_u32 v6, v6, v10, v11
	v_add3_u32 v6, v6, v12, v13
	v_cmp_gt_u32_e32 vcc, 4, v6
	v_mov_b32_e32 v6, 0
	s_nop 0
	v_cndmask_b32_e32 v5, v245, v5, vcc
	v_ashrrev_i32_e32 v9, 31, v5
	v_sub_u32_e32 v8, 63, v230
	v_and_b32_e32 v9, 0x7fffffff, v9
	v_xor_b32_e32 v9, v5, v9
	s_nop 0
	v_readlane_b32 s25, v9, 0
	s_movk_i32 s24, 63
	v_readlane_b32 s23, v9, 1
	s_movk_i32 s22, 62
	v_cmp_gt_i64_e32 vcc, s[24:25], v[8:9]
	v_readlane_b32 s25, v9, 2
	s_movk_i32 s24, 61
	v_addc_co_u32_e32 v6, vcc, 0, v6, vcc
	v_cmp_gt_i64_e32 vcc, s[22:23], v[8:9]
	v_readlane_b32 s23, v9, 3
	s_movk_i32 s22, 60
	v_addc_co_u32_e32 v6, vcc, 0, v6, vcc
	v_cmp_gt_i64_e32 vcc, s[24:25], v[8:9]
	v_readlane_b32 s25, v9, 4
	s_movk_i32 s24, 59
	v_addc_co_u32_e32 v6, vcc, 0, v6, vcc
	v_cmp_gt_i64_e32 vcc, s[22:23], v[8:9]
	v_readlane_b32 s23, v9, 5
	s_movk_i32 s22, 58
	v_addc_co_u32_e32 v6, vcc, 0, v6, vcc
	v_cmp_gt_i64_e32 vcc, s[24:25], v[8:9]
	v_readlane_b32 s25, v9, 6
	s_movk_i32 s24, 57
	v_addc_co_u32_e32 v6, vcc, 0, v6, vcc
	v_cmp_gt_i64_e32 vcc, s[22:23], v[8:9]
	v_readlane_b32 s23, v9, 7
	s_movk_i32 s22, 56
	v_addc_co_u32_e32 v6, vcc, 0, v6, vcc
	v_cmp_gt_i64_e32 vcc, s[24:25], v[8:9]
	v_readlane_b32 s25, v9, 8
	s_movk_i32 s24, 55
	v_addc_co_u32_e32 v6, vcc, 0, v6, vcc
	v_cmp_gt_i64_e32 vcc, s[22:23], v[8:9]
	v_readlane_b32 s23, v9, 9
	s_movk_i32 s22, 54
	v_addc_co_u32_e32 v6, vcc, 0, v6, vcc
	v_cmp_gt_i64_e32 vcc, s[24:25], v[8:9]
	v_readlane_b32 s25, v9, 10
	s_movk_i32 s24, 53
	v_addc_co_u32_e32 v6, vcc, 0, v6, vcc
	v_cmp_gt_i64_e32 vcc, s[22:23], v[8:9]
	v_readlane_b32 s23, v9, 11
	s_movk_i32 s22, 52
	v_addc_co_u32_e32 v6, vcc, 0, v6, vcc
	v_cmp_gt_i64_e32 vcc, s[24:25], v[8:9]
	v_readlane_b32 s25, v9, 12
	s_movk_i32 s24, 51
	v_addc_co_u32_e32 v6, vcc, 0, v6, vcc
	v_cmp_gt_i64_e32 vcc, s[22:23], v[8:9]
	v_readlane_b32 s23, v9, 13
	s_movk_i32 s22, 50
	v_addc_co_u32_e32 v6, vcc, 0, v6, vcc
	v_cmp_gt_i64_e32 vcc, s[24:25], v[8:9]
	v_readlane_b32 s25, v9, 14
	s_movk_i32 s24, 49
	v_addc_co_u32_e32 v6, vcc, 0, v6, vcc
	v_cmp_gt_i64_e32 vcc, s[22:23], v[8:9]
	v_readlane_b32 s23, v9, 15
	s_movk_i32 s22, 48
	v_addc_co_u32_e32 v6, vcc, 0, v6, vcc
	v_cmp_gt_i64_e32 vcc, s[24:25], v[8:9]
; __device__ __forceinline__ void phase_nrr(const Frame& F, const Args& a, int l, const bf16_t* XA, const float* g, const float* modl, unsigned char* XN8) {
;     ...
;             int rank = 0;
; #pragma unroll 8
;             for (int e2 = 0; e2 < 64; ++e2) { const float v = __int_as_float(__builtin_amdgcn_readlane(__float_as_int(val), e2)); rank += (v > val || (v == val && e2 < lane)) ? 1 : 0; }
;             const bool sel = rank < TOPK;
;             const float ssum = wave_sum(sel ? sc : 0.f);
	v_readlane_b32 s25, v9, 16
	s_movk_i32 s24, 47
	v_addc_co_u32_e32 v6, vcc, 0, v6, vcc
	v_cmp_gt_i64_e32 vcc, s[22:23], v[8:9]
	v_readlane_b32 s23, v9, 17
	s_movk_i32 s22, 46
	v_addc_co_u32_e32 v6, vcc, 0, v6, vcc
	v_cmp_gt_i64_e32 vcc, s[24:25], v[8:9]
	v_readlane_b32 s25, v9, 18
	s_movk_i32 s24, 45
	v_addc_co_u32_e32 v6, vcc, 0, v6, vcc
	v_cmp_gt_i64_e32 vcc, s[22:23], v[8:9]
	v_readlane_b32 s23, v9, 19
	s_movk_i32 s22, 44
	v_addc_co_u32_e32 v6, vcc, 0, v6, vcc
	v_cmp_gt_i64_e32 vcc, s[24:25], v[8:9]
	v_readlane_b32 s25, v9, 20
	s_movk_i32 s24, 43
	v_addc_co_u32_e32 v6, vcc, 0, v6, vcc
	v_cmp_gt_i64_e32 vcc, s[22:23], v[8:9]
	v_readlane_b32 s23, v9, 21
	s_movk_i32 s22, 42
	v_addc_co_u32_e32 v6, vcc, 0, v6, vcc
	v_cmp_gt_i64_e32 vcc, s[24:25], v[8:9]
	v_readlane_b32 s25, v9, 22
	s_movk_i32 s24, 41
	v_addc_co_u32_e32 v6, vcc, 0, v6, vcc
	v_cmp_gt_i64_e32 vcc, s[22:23], v[8:9]
	v_readlane_b32 s23, v9, 23
	s_movk_i32 s22, 40
	v_addc_co_u32_e32 v6, vcc, 0, v6, vcc
	v_cmp_gt_i64_e32 vcc, s[24:25], v[8:9]
	v_readlane_b32 s25, v9, 24
	s_movk_i32 s24, 39
	v_addc_co_u32_e32 v6, vcc, 0, v6, vcc
	v_cmp_gt_i64_e32 vcc, s[22:23], v[8:9]
	v_readlane_b32 s23, v9, 25
	s_movk_i32 s22, 38
	v_addc_co_u32_e32 v6, vcc, 0, v6, vcc
	v_cmp_gt_i64_e32 vcc, s[24:25], v[8:9]
	v_readlane_b32 s25, v9, 26
	s_movk_i32 s24, 37
	v_addc_co_u32_e32 v6, vcc, 0, v6, vcc
	v_cmp_gt_i64_e32 vcc, s[22:23], v[8:9]
	v_readlane_b32 s23, v9, 27
	s_movk_i32 s22, 36
	v_addc_co_u32_e32 v6, vcc, 0, v6, vcc
	v_cmp_gt_i64_e32 vcc, s[24:25], v[8:9]
	v_readlane_b32 s25, v9, 28
	s_movk_i32 s24, 35
	v_addc_co_u32_e32 v6, vcc, 0, v6, vcc
	v_cmp_gt_i64_e32 vcc, s[22:23], v[8:9]
	v_readlane_b32 s23, v9, 29
	s_movk_i32 s22, 34
	v_addc_co_u32_e32 v6, vcc, 0, v6, vcc
	v_cmp_gt_i64_e32 vcc, s[24:25], v[8:9]
	v_readlane_b32 s25, v9, 30
	s_movk_i32 s24, 33
	v_addc_co_u32_e32 v6, vcc, 0, v6, vcc
	v_cmp_gt_i64_e32 vcc, s[22:23], v[8:9]
	v_readlane_b32 s23, v9, 31
	s_movk_i32 s22, 32
	v_addc_co_u32_e32 v6, vcc, 0, v6, vcc
	v_cmp_gt_i64_e32 vcc, s[24:25], v[8:9]
	v_readlane_b32 s25, v9, 32
	s_movk_i32 s24, 31
	v_addc_co_u32_e32 v6, vcc, 0, v6, vcc
	v_cmp_gt_i64_e32 vcc, s[22:23], v[8:9]
	v_readlane_b32 s23, v9, 33
	s_movk_i32 s22, 30
	v_addc_co_u32_e32 v6, vcc, 0, v6, vcc
	v_cmp_gt_i64_e32 vcc, s[24:25], v[8:9]
	v_readlane_b32 s25, v9, 34
	s_movk_i32 s24, 29
	v_addc_co_u32_e32 v6, vcc, 0, v6, vcc
	v_cmp_gt_i64_e32 vcc, s[22:23], v[8:9]
	v_readlane_b32 s23, v9, 35
	s_movk_i32 s22, 28
	v_addc_co_u32_e32 v6, vcc, 0, v6, vcc
	v_cmp_gt_i64_e32 vcc, s[24:25], v[8:9]
	v_readlane_b32 s25, v9, 36
	s_movk_i32 s24, 27
	v_addc_co_u32_e32 v6, vcc, 0, v6, vcc
	v_cmp_gt_i64_e32 vcc, s[22:23], v[8:9]
	v_readlane_b32 s23, v9, 37
	s_movk_i32 s22, 26
	v_addc_co_u32_e32 v6, vcc, 0, v6, vcc
	v_cmp_gt_i64_e32 vcc, s[24:25], v[8:9]
	v_readlane_b32 s25, v9, 38
	s_movk_i32 s24, 25
	v_addc_co_u32_e32 v6, vcc, 0, v6, vcc
	v_cmp_gt_i64_e32 vcc, s[22:23], v[8:9]
	v_readlane_b32 s23, v9, 39
	s_movk_i32 s22, 24
	v_addc_co_u32_e32 v6, vcc, 0, v6, vcc
	v_cmp_gt_i64_e32 vcc, s[24:25], v[8:9]
	v_readlane_b32 s25, v9, 40
	s_movk_i32 s24, 23
	v_addc_co_u32_e32 v6, vcc, 0, v6, vcc
	v_cmp_gt_i64_e32 vcc, s[22:23], v[8:9]
	v_readlane_b32 s23, v9, 41
	s_movk_i32 s22, 22
	v_addc_co_u32_e32 v6, vcc, 0, v6, vcc
	v_cmp_gt_i64_e32 vcc, s[24:25], v[8:9]
	v_readlane_b32 s25, v9, 42
	s_movk_i32 s24, 21
	v_addc_co_u32_e32 v6, vcc, 0, v6, vcc
	v_cmp_gt_i64_e32 vcc, s[22:23], v[8:9]
	v_readlane_b32 s23, v9, 43
	s_movk_i32 s22, 20
	v_addc_co_u32_e32 v6, vcc, 0, v6, vcc
	v_cmp_gt_i64_e32 vcc, s[24:25], v[8:9]
	v_readlane_b32 s25, v9, 44
	s_movk_i32 s24, 19
	v_addc_co_u32_e32 v6, vcc, 0, v6, vcc
	v_cmp_gt_i64_e32 vcc, s[22:23], v[8:9]
	v_readlane_b32 s23, v9, 45
	s_movk_i32 s22, 18
	v_addc_co_u32_e32 v6, vcc, 0, v6, vcc
	v_cmp_gt_i64_e32 vcc, s[24:25], v[8:9]
	v_readlane_b32 s25, v9, 46
	s_movk_i32 s24, 17
	v_addc_co_u32_e32 v6, vcc, 0, v6, vcc
	v_cmp_gt_i64_e32 vcc, s[22:23], v[8:9]
	v_readlane_b32 s23, v9, 47
	s_movk_i32 s22, 16
	v_addc_co_u32_e32 v6, vcc, 0, v6, vcc
	v_cmp_gt_i64_e32 vcc, s[24:25], v[8:9]
	v_readlane_b32 s25, v9, 48
	s_movk_i32 s24, 15
	v_addc_co_u32_e32 v6, vcc, 0, v6, vcc
	v_cmp_gt_i64_e32 vcc, s[22:23], v[8:9]
	v_readlane_b32 s23, v9, 49
	s_movk_i32 s22, 14
	v_addc_co_u32_e32 v6, vcc, 0, v6, vcc
	v_cmp_gt_i64_e32 vcc, s[24:25], v[8:9]
	v_readlane_b32 s25, v9, 50
	s_movk_i32 s24, 13
	v_addc_co_u32_e32 v6, vcc, 0, v6, vcc
	v_cmp_gt_i64_e32 vcc, s[22:23], v[8:9]
	v_readlane_b32 s23, v9, 51
	s_movk_i32 s22, 12
	v_addc_co_u32_e32 v6, vcc, 0, v6, vcc
	v_cmp_gt_i64_e32 vcc, s[24:25], v[8:9]
	v_readlane_b32 s25, v9, 52
	s_movk_i32 s24, 11
	v_addc_co_u32_e32 v6, vcc, 0, v6, vcc
	v_cmp_gt_i64_e32 vcc, s[22:23], v[8:9]
	v_readlane_b32 s23, v9, 53
	s_movk_i32 s22, 10
	v_addc_co_u32_e32 v6, vcc, 0, v6, vcc
	v_cmp_gt_i64_e32 vcc, s[24:25], v[8:9]
	v_readlane_b32 s25, v9, 54
	s_movk_i32 s24, 9
	v_addc_co_u32_e32 v6, vcc, 0, v6, vcc
	v_cmp_gt_i64_e32 vcc, s[22:23], v[8:9]
	v_readlane_b32 s23, v9, 55
	s_movk_i32 s22, 8
	v_addc_co_u32_e32 v6, vcc, 0, v6, vcc
	v_cmp_gt_i64_e32 vcc, s[24:25], v[8:9]
	v_readlane_b32 s25, v9, 56
	s_movk_i32 s24, 7
	v_addc_co_u32_e32 v6, vcc, 0, v6, vcc
	v_cmp_gt_i64_e32 vcc, s[22:23], v[8:9]
	v_readlane_b32 s23, v9, 57
	s_movk_i32 s22, 6
	v_addc_co_u32_e32 v6, vcc, 0, v6, vcc
	v_cmp_gt_i64_e32 vcc, s[24:25], v[8:9]
	v_readlane_b32 s25, v9, 58
	s_movk_i32 s24, 5
	v_addc_co_u32_e32 v6, vcc, 0, v6, vcc
	v_cmp_gt_i64_e32 vcc, s[22:23], v[8:9]
	v_readlane_b32 s23, v9, 59
	s_movk_i32 s22, 4
	v_addc_co_u32_e32 v6, vcc, 0, v6, vcc
	v_cmp_gt_i64_e32 vcc, s[24:25], v[8:9]
	v_readlane_b32 s25, v9, 60
	s_movk_i32 s24, 3
	v_addc_co_u32_e32 v6, vcc, 0, v6, vcc
	v_cmp_gt_i64_e32 vcc, s[22:23], v[8:9]
	v_readlane_b32 s23, v9, 61
	s_movk_i32 s22, 2
	v_addc_co_u32_e32 v6, vcc, 0, v6, vcc
	v_cmp_gt_i64_e32 vcc, s[24:25], v[8:9]
	v_readlane_b32 s25, v9, 62
	s_movk_i32 s24, 1
	v_addc_co_u32_e32 v6, vcc, 0, v6, vcc
	v_cmp_gt_i64_e32 vcc, s[22:23], v[8:9]
	v_readlane_b32 s23, v9, 63
	s_movk_i32 s22, 0
	v_addc_co_u32_e32 v6, vcc, 0, v6, vcc
	v_cmp_gt_i64_e32 vcc, s[24:25], v[8:9]
	s_nop 1
	v_addc_co_u32_e32 v6, vcc, 0, v6, vcc
	v_cmp_gt_i64_e32 vcc, s[22:23], v[8:9]
	s_nop 1
	v_addc_co_u32_e32 v6, vcc, 0, v6, vcc
	v_cmp_gt_u32_e32 vcc, 6, v6
	s_mul_i32 s36, s44, 6
	s_nop 0
	v_cndmask_b32_e32 v5, 0, v2, vcc
	ds_bpermute_b32 v7, v1, v5
	s_waitcnt lgkmcnt(0)
	v_add_f32_e32 v5, v5, v7
	ds_bpermute_b32 v7, v201, v5
	s_waitcnt lgkmcnt(0)
	v_add_f32_e32 v5, v5, v7
	ds_bpermute_b32 v7, v220, v5
	s_waitcnt lgkmcnt(0)
	v_add_f32_e32 v5, v5, v7
	ds_bpermute_b32 v7, v221, v5
	s_waitcnt lgkmcnt(0)
	v_add_f32_e32 v5, v5, v7
	ds_bpermute_b32 v7, v222, v5
	s_waitcnt lgkmcnt(0)
	v_add_f32_e32 v5, v5, v7
	ds_bpermute_b32 v7, v223, v5
	s_and_saveexec_b64 s[22:23], vcc
	s_cbranch_execz .LBB0_539
; __device__ __forceinline__ void phase_nrr(const Frame& F, const Args& a, int l, const bf16_t* XA, const float* g, const float* modl, unsigned char* XN8) {
;     ...
;         for (int i = 0; i < 8; ++i) { const int t = tb + i;
;             const float lg = Pl[(w * 8 + i) * NE + lane] + Pl[(64 + w * 8 + i) * NE + lane]; const float sc = 1.f / (1.f + __expf(-lg)); const float bb = sc + bias;
;             float m1 = bb; m1 = fmaxf(m1, __shfl_xor(m1, 1)); m1 = fmaxf(m1, __shfl_xor(m1, 2)); m1 = fmaxf(m1, __shfl_xor(m1, 4));
;             const unsigned long long eq = __ballot(bb == m1); const int gbase = lane & ~7; const unsigned grpmask = (unsigned)((eq >> gbase) & 0xffull);
;             const int first = gbase + __builtin_ctz(grpmask);
;             float m2 = (lane == first) ? -INFINITY : bb; m2 = fmaxf(m2, __shfl_xor(m2, 1)); m2 = fmaxf(m2, __shfl_xor(m2, 2)); m2 = fmaxf(m2, __shfl_xor(m2, 4));
;             const float gsum = m1 + m2; const int gq = lane >> 3;
;             int grank = 0;
; #pragma unroll
;             for (int g2 = 0; g2 < 8; ++g2) { const float v = __int_as_float(__builtin_amdgcn_readlane(__float_as_int(gsum), g2 * 8)); grank += (v > gsum || (v == gsum && g2 < gq)) ? 1 : 0; }
;             const bool keep = grank < 4; const float val = keep ? bb : -INFINITY;
;             int rank = 0;
; #pragma unroll 8
;             for (int e2 = 0; e2 < 64; ++e2) { const float v = __int_as_float(__builtin_amdgcn_readlane(__float_as_int(val), e2)); rank += (v > val || (v == val && e2 < lane)) ? 1 : 0; }
;             const bool sel = rank < TOPK;
;             const float ssum = wave_sum(sel ? sc : 0.f);
;             if (sel) { const int p = atomicAdd((int*)(hist + lane), 1); top_e[t * TOPK + rank] = lane; gate[t * TOPK + rank] = sc / ssum * 2.5f; lpos[t * TOPK + rank] = p; }
	s_waitcnt lgkmcnt(0)
	v_add_f32_e32 v5, v5, v7
	v_div_scale_f32 v11, s[24:25], v5, v5, v2
	v_or_b32_e32 v6, s36, v6
	v_rcp_f32_e32 v12, v11
	v_ashrrev_i32_e32 v7, 31, v6
	v_lshlrev_b64 v[6:7], 2, v[6:7]
	v_lshl_add_u64 v[8:9], s[26:27], 0, v[6:7]
	ds_add_rtn_u32 v10, v227, v243
	global_store_dword v[8:9], v230, off
	v_fma_f32 v8, -v11, v12, 1.0
	v_fmac_f32_e32 v12, v8, v12
	v_div_scale_f32 v8, vcc, v2, v5, v2
	v_mul_f32_e32 v9, v8, v12
	v_fma_f32 v13, -v11, v9, v8
	v_fmac_f32_e32 v9, v13, v12
	v_fma_f32 v8, -v11, v9, v8
	v_div_fmas_f32 v8, v8, v12, v9
	v_div_fixup_f32 v2, v8, v5, v2
	v_mul_f32_e32 v2, 0x40200000, v2
	v_lshl_add_u64 v[8:9], s[28:29], 0, v[6:7]
	v_lshl_add_u64 v[6:7], s[30:31], 0, v[6:7]
	global_store_dword v[8:9], v2, off
	s_waitcnt lgkmcnt(0)
	global_store_dword v[6:7], v10, off
.LBB0_539:
	s_or_b64 exec, exec, s[22:23]
	v_add_u32_e32 v2, s77, v226
	ds_read_b32 v2, v2
	ds_read_b32 v5, v4 offset:16640
	s_mov_b32 s3, 0
	s_waitcnt lgkmcnt(0)
	v_add_f32_e32 v2, v2, v5
	v_mul_f32_e32 v2, 0xbfb8aa3b, v2
	v_exp_f32_e32 v2, v2
	s_nop 0
	v_add_f32_e32 v2, 1.0, v2
	v_div_scale_f32 v5, s[22:23], v2, v2, 1.0
	v_rcp_f32_e32 v6, v5
	s_nop 0
	v_fma_f32 v7, -v5, v6, 1.0
	v_fmac_f32_e32 v6, v7, v6
	v_div_scale_f32 v7, vcc, 1.0, v2, 1.0
	v_mul_f32_e32 v8, v7, v6
	v_fma_f32 v9, -v5, v8, v7
	v_fmac_f32_e32 v8, v9, v6
	v_fma_f32 v5, -v5, v8, v7
	v_div_fmas_f32 v5, v5, v6, v8
	v_div_fixup_f32 v5, v5, v2, 1.0
	v_add_f32_e32 v2, v3, v5
	s_nop 1
	s_waitcnt lgkmcnt(0)
	v_max_f32_dpp v6, v2, v2 quad_perm:[1,0,3,2] row_mask:0xf bank_mask:0xf
	s_nop 1
	s_waitcnt lgkmcnt(0)
	v_max_f32_dpp v6, v6, v6 quad_perm:[2,3,0,1] row_mask:0xf bank_mask:0xf
	s_nop 1
	s_waitcnt lgkmcnt(0)
	v_max_f32_dpp v8, v6, v6 row_half_mirror row_mask:0xf bank_mask:0xf
	v_cmp_eq_f32_e32 vcc, v2, v8
	s_nop 1
	v_lshrrev_b64 v[6:7], v200, vcc
	v_ffbl_b32_sdwa v6, v6 dst_sel:DWORD dst_unused:UNUSED_PAD src0_sel:BYTE_0
	v_add_u32_e32 v6, v6, v200
	v_cmp_ne_u32_e32 vcc, v230, v6
	s_nop 1
	v_cndmask_b32_e32 v6, v245, v2, vcc
	s_nop 1
	s_waitcnt lgkmcnt(0)
	v_max_f32_dpp v6, v6, v6 quad_perm:[1,0,3,2] row_mask:0xf bank_mask:0xf
	s_nop 1
	s_waitcnt lgkmcnt(0)
	v_max_f32_dpp v6, v6, v6 quad_perm:[2,3,0,1] row_mask:0xf bank_mask:0xf
	s_nop 1
	s_waitcnt lgkmcnt(0)
	v_max_f32_dpp v6, v6, v6 row_half_mirror row_mask:0xf bank_mask:0xf
	v_add_f32_e32 v6, v8, v6
	s_nop 0
	v_readlane_b32 s5, v6, 0
	s_nop 1
	v_cmp_eq_f32_e64 s[22:23], s5, v6
	v_cmp_gt_f32_e32 vcc, s5, v6
	s_and_b64 s[22:23], s[6:7], s[22:23]
	s_or_b64 s[22:23], vcc, s[22:23]
	v_readlane_b32 s5, v6, 8
	v_cndmask_b32_e64 v7, 0, 1, s[22:23]
	s_nop 0
	v_cmp_eq_f32_e64 s[22:23], s5, v6
	v_cmp_gt_f32_e32 vcc, s5, v6
	s_and_b64 s[22:23], s[8:9], s[22:23]
	s_or_b64 s[22:23], vcc, s[22:23]
	v_readlane_b32 s5, v6, 16
	v_cndmask_b32_e64 v8, 0, 1, s[22:23]
	s_nop 0
	v_cmp_eq_f32_e64 s[22:23], s5, v6
	v_cmp_gt_f32_e32 vcc, s5, v6
	s_and_b64 s[22:23], s[10:11], s[22:23]
	s_or_b64 s[22:23], vcc, s[22:23]
	v_readlane_b32 s5, v6, 24
	v_cndmask_b32_e64 v9, 0, 1, s[22:23]
	s_nop 0
	v_cmp_eq_f32_e64 s[22:23], s5, v6
	v_cmp_gt_f32_e32 vcc, s5, v6
	s_and_b64 s[22:23], s[12:13], s[22:23]
	s_or_b64 s[22:23], vcc, s[22:23]
	v_readlane_b32 s5, v6, 32
	v_cndmask_b32_e64 v10, 0, 1, s[22:23]
	s_nop 0
	v_cmp_eq_f32_e64 s[22:23], s5, v6
	v_cmp_gt_f32_e32 vcc, s5, v6
	s_and_b64 s[22:23], s[14:15], s[22:23]
	s_or_b64 s[22:23], vcc, s[22:23]
	v_readlane_b32 s5, v6, 40
	v_cndmask_b32_e64 v11, 0, 1, s[22:23]
	s_nop 0
	v_cmp_eq_f32_e64 s[22:23], s5, v6
	v_cmp_gt_f32_e32 vcc, s5, v6
	s_and_b64 s[22:23], s[16:17], s[22:23]
	s_or_b64 s[22:23], vcc, s[22:23]
	v_readlane_b32 s5, v6, 48
	v_cndmask_b32_e64 v12, 0, 1, s[22:23]
	s_nop 0
	v_cmp_eq_f32_e64 s[22:23], s5, v6
	v_cmp_gt_f32_e32 vcc, s5, v6
	s_and_b64 s[22:23], s[18:19], s[22:23]
	v_readlane_b32 s5, v6, 56
	s_or_b64 s[22:23], vcc, s[22:23]
	v_cndmask_b32_e64 v13, 0, 1, s[22:23]
	v_cmp_gt_f32_e32 vcc, s5, v6
	s_nop 1
	v_cndmask_b32_e64 v6, 0, 1, vcc
	v_add_u32_e32 v6, v8, v6
	v_add3_u32 v6, v6, v7, v9
	v_add3_u32 v6, v6, v10, v11
	v_add3_u32 v6, v6, v12, v13
	v_cmp_gt_u32_e32 vcc, 4, v6
	s_nop 1
	v_cndmask_b32_e32 v6, v245, v2, vcc
	v_mov_b32_e32 v2, 0
	v_ashrrev_i32_e32 v9, 31, v6
	v_sub_u32_e32 v8, 63, v230
	v_and_b32_e32 v9, 0x7fffffff, v9
	v_xor_b32_e32 v9, v6, v9
	s_nop 0
	v_readlane_b32 s25, v9, 0
	s_movk_i32 s24, 63
	v_readlane_b32 s23, v9, 1
	s_movk_i32 s22, 62
	v_cmp_gt_i64_e32 vcc, s[24:25], v[8:9]
	v_readlane_b32 s25, v9, 2
	s_movk_i32 s24, 61
	v_addc_co_u32_e32 v2, vcc, 0, v2, vcc
	v_cmp_gt_i64_e32 vcc, s[22:23], v[8:9]
	v_readlane_b32 s23, v9, 3
	s_movk_i32 s22, 60
	v_addc_co_u32_e32 v2, vcc, 0, v2, vcc
	v_cmp_gt_i64_e32 vcc, s[24:25], v[8:9]
	v_readlane_b32 s25, v9, 4
	s_movk_i32 s24, 59
	v_addc_co_u32_e32 v2, vcc, 0, v2, vcc
	v_cmp_gt_i64_e32 vcc, s[22:23], v[8:9]
	v_readlane_b32 s23, v9, 5
	s_movk_i32 s22, 58
	v_addc_co_u32_e32 v2, vcc, 0, v2, vcc
	v_cmp_gt_i64_e32 vcc, s[24:25], v[8:9]
	v_readlane_b32 s25, v9, 6
	s_movk_i32 s24, 57
	v_addc_co_u32_e32 v2, vcc, 0, v2, vcc
	v_cmp_gt_i64_e32 vcc, s[22:23], v[8:9]
	v_readlane_b32 s23, v9, 7
	s_movk_i32 s22, 56
	v_addc_co_u32_e32 v2, vcc, 0, v2, vcc
	v_cmp_gt_i64_e32 vcc, s[24:25], v[8:9]
	v_readlane_b32 s25, v9, 8
	s_movk_i32 s24, 55
	v_addc_co_u32_e32 v2, vcc, 0, v2, vcc
	v_cmp_gt_i64_e32 vcc, s[22:23], v[8:9]
	v_readlane_b32 s23, v9, 9
	s_movk_i32 s22, 54
	v_addc_co_u32_e32 v2, vcc, 0, v2, vcc
	v_cmp_gt_i64_e32 vcc, s[24:25], v[8:9]
	v_readlane_b32 s25, v9, 10
	s_movk_i32 s24, 53
	v_addc_co_u32_e32 v2, vcc, 0, v2, vcc
	v_cmp_gt_i64_e32 vcc, s[22:23], v[8:9]
	v_readlane_b32 s23, v9, 11
	s_movk_i32 s22, 52
	v_addc_co_u32_e32 v2, vcc, 0, v2, vcc
; __device__ __forceinline__ void phase_nrr(const Frame& F, const Args& a, int l, const bf16_t* XA, const float* g, const float* modl, unsigned char* XN8) {
;     ...
;             int rank = 0;
; #pragma unroll 8
;             for (int e2 = 0; e2 < 64; ++e2) { const float v = __int_as_float(__builtin_amdgcn_readlane(__float_as_int(val), e2)); rank += (v > val || (v == val && e2 < lane)) ? 1 : 0; }
;             const bool sel = rank < TOPK;
;             const float ssum = wave_sum(sel ? sc : 0.f);
	v_cmp_gt_i64_e32 vcc, s[24:25], v[8:9]
	v_readlane_b32 s25, v9, 12
	s_movk_i32 s24, 51
	v_addc_co_u32_e32 v2, vcc, 0, v2, vcc
	v_cmp_gt_i64_e32 vcc, s[22:23], v[8:9]
	v_readlane_b32 s23, v9, 13
	s_movk_i32 s22, 50
	v_addc_co_u32_e32 v2, vcc, 0, v2, vcc
	v_cmp_gt_i64_e32 vcc, s[24:25], v[8:9]
	v_readlane_b32 s25, v9, 14
	s_movk_i32 s24, 49
	v_addc_co_u32_e32 v2, vcc, 0, v2, vcc
	v_cmp_gt_i64_e32 vcc, s[22:23], v[8:9]
	v_readlane_b32 s23, v9, 15
	s_movk_i32 s22, 48
	v_addc_co_u32_e32 v2, vcc, 0, v2, vcc
	v_cmp_gt_i64_e32 vcc, s[24:25], v[8:9]
	v_readlane_b32 s25, v9, 16
	s_movk_i32 s24, 47
	v_addc_co_u32_e32 v2, vcc, 0, v2, vcc
	v_cmp_gt_i64_e32 vcc, s[22:23], v[8:9]
	v_readlane_b32 s23, v9, 17
	s_movk_i32 s22, 46
	v_addc_co_u32_e32 v2, vcc, 0, v2, vcc
	v_cmp_gt_i64_e32 vcc, s[24:25], v[8:9]
	v_readlane_b32 s25, v9, 18
	s_movk_i32 s24, 45
	v_addc_co_u32_e32 v2, vcc, 0, v2, vcc
	v_cmp_gt_i64_e32 vcc, s[22:23], v[8:9]
	v_readlane_b32 s23, v9, 19
	s_movk_i32 s22, 44
	v_addc_co_u32_e32 v2, vcc, 0, v2, vcc
	v_cmp_gt_i64_e32 vcc, s[24:25], v[8:9]
	v_readlane_b32 s25, v9, 20
	s_movk_i32 s24, 43
	v_addc_co_u32_e32 v2, vcc, 0, v2, vcc
	v_cmp_gt_i64_e32 vcc, s[22:23], v[8:9]
	v_readlane_b32 s23, v9, 21
	s_movk_i32 s22, 42
	v_addc_co_u32_e32 v2, vcc, 0, v2, vcc
	v_cmp_gt_i64_e32 vcc, s[24:25], v[8:9]
	v_readlane_b32 s25, v9, 22
	s_movk_i32 s24, 41
	v_addc_co_u32_e32 v2, vcc, 0, v2, vcc
	v_cmp_gt_i64_e32 vcc, s[22:23], v[8:9]
	v_readlane_b32 s23, v9, 23
	s_movk_i32 s22, 40
	v_addc_co_u32_e32 v2, vcc, 0, v2, vcc
	v_cmp_gt_i64_e32 vcc, s[24:25], v[8:9]
	v_readlane_b32 s25, v9, 24
	s_movk_i32 s24, 39
	v_addc_co_u32_e32 v2, vcc, 0, v2, vcc
	v_cmp_gt_i64_e32 vcc, s[22:23], v[8:9]
	v_readlane_b32 s23, v9, 25
	s_movk_i32 s22, 38
	v_addc_co_u32_e32 v2, vcc, 0, v2, vcc
	v_cmp_gt_i64_e32 vcc, s[24:25], v[8:9]
	v_readlane_b32 s25, v9, 26
	s_movk_i32 s24, 37
	v_addc_co_u32_e32 v2, vcc, 0, v2, vcc
	v_cmp_gt_i64_e32 vcc, s[22:23], v[8:9]
	v_readlane_b32 s23, v9, 27
	s_movk_i32 s22, 36
	v_addc_co_u32_e32 v2, vcc, 0, v2, vcc
	v_cmp_gt_i64_e32 vcc, s[24:25], v[8:9]
	v_readlane_b32 s25, v9, 28
	s_movk_i32 s24, 35
	v_addc_co_u32_e32 v2, vcc, 0, v2, vcc
	v_cmp_gt_i64_e32 vcc, s[22:23], v[8:9]
	v_readlane_b32 s23, v9, 29
	s_movk_i32 s22, 34
	v_addc_co_u32_e32 v2, vcc, 0, v2, vcc
	v_cmp_gt_i64_e32 vcc, s[24:25], v[8:9]
	v_readlane_b32 s25, v9, 30
	s_movk_i32 s24, 33
	v_addc_co_u32_e32 v2, vcc, 0, v2, vcc
	v_cmp_gt_i64_e32 vcc, s[22:23], v[8:9]
	v_readlane_b32 s23, v9, 31
	s_movk_i32 s22, 32
	v_addc_co_u32_e32 v2, vcc, 0, v2, vcc
	v_cmp_gt_i64_e32 vcc, s[24:25], v[8:9]
	v_readlane_b32 s25, v9, 32
	s_movk_i32 s24, 31
	v_addc_co_u32_e32 v2, vcc, 0, v2, vcc
	v_cmp_gt_i64_e32 vcc, s[22:23], v[8:9]
	v_readlane_b32 s23, v9, 33
	s_movk_i32 s22, 30
	v_addc_co_u32_e32 v2, vcc, 0, v2, vcc
	v_cmp_gt_i64_e32 vcc, s[24:25], v[8:9]
	v_readlane_b32 s25, v9, 34
	s_movk_i32 s24, 29
	v_addc_co_u32_e32 v2, vcc, 0, v2, vcc
	v_cmp_gt_i64_e32 vcc, s[22:23], v[8:9]
	v_readlane_b32 s23, v9, 35
	s_movk_i32 s22, 28
	v_addc_co_u32_e32 v2, vcc, 0, v2, vcc
	v_cmp_gt_i64_e32 vcc, s[24:25], v[8:9]
	v_readlane_b32 s25, v9, 36
	s_movk_i32 s24, 27
	v_addc_co_u32_e32 v2, vcc, 0, v2, vcc
	v_cmp_gt_i64_e32 vcc, s[22:23], v[8:9]
	v_readlane_b32 s23, v9, 37
	s_movk_i32 s22, 26
	v_addc_co_u32_e32 v2, vcc, 0, v2, vcc
	v_cmp_gt_i64_e32 vcc, s[24:25], v[8:9]
	v_readlane_b32 s25, v9, 38
	s_movk_i32 s24, 25
	v_addc_co_u32_e32 v2, vcc, 0, v2, vcc
	v_cmp_gt_i64_e32 vcc, s[22:23], v[8:9]
	v_readlane_b32 s23, v9, 39
	s_movk_i32 s22, 24
	v_addc_co_u32_e32 v2, vcc, 0, v2, vcc
	v_cmp_gt_i64_e32 vcc, s[24:25], v[8:9]
	v_readlane_b32 s25, v9, 40
	s_movk_i32 s24, 23
	v_addc_co_u32_e32 v2, vcc, 0, v2, vcc
	v_cmp_gt_i64_e32 vcc, s[22:23], v[8:9]
	v_readlane_b32 s23, v9, 41
	s_movk_i32 s22, 22
	v_addc_co_u32_e32 v2, vcc, 0, v2, vcc
	v_cmp_gt_i64_e32 vcc, s[24:25], v[8:9]
	v_readlane_b32 s25, v9, 42
	s_movk_i32 s24, 21
	v_addc_co_u32_e32 v2, vcc, 0, v2, vcc
	v_cmp_gt_i64_e32 vcc, s[22:23], v[8:9]
	v_readlane_b32 s23, v9, 43
	s_movk_i32 s22, 20
	v_addc_co_u32_e32 v2, vcc, 0, v2, vcc
	v_cmp_gt_i64_e32 vcc, s[24:25], v[8:9]
	v_readlane_b32 s25, v9, 44
	s_movk_i32 s24, 19
	v_addc_co_u32_e32 v2, vcc, 0, v2, vcc
	v_cmp_gt_i64_e32 vcc, s[22:23], v[8:9]
	v_readlane_b32 s23, v9, 45
	s_movk_i32 s22, 18
	v_addc_co_u32_e32 v2, vcc, 0, v2, vcc
	v_cmp_gt_i64_e32 vcc, s[24:25], v[8:9]
	v_readlane_b32 s25, v9, 46
	s_movk_i32 s24, 17
	v_addc_co_u32_e32 v2, vcc, 0, v2, vcc
	v_cmp_gt_i64_e32 vcc, s[22:23], v[8:9]
	v_readlane_b32 s23, v9, 47
	s_movk_i32 s22, 16
	v_addc_co_u32_e32 v2, vcc, 0, v2, vcc
	v_cmp_gt_i64_e32 vcc, s[24:25], v[8:9]
	v_readlane_b32 s25, v9, 48
	s_movk_i32 s24, 15
	v_addc_co_u32_e32 v2, vcc, 0, v2, vcc
	v_cmp_gt_i64_e32 vcc, s[22:23], v[8:9]
	v_readlane_b32 s23, v9, 49
	s_movk_i32 s22, 14
	v_addc_co_u32_e32 v2, vcc, 0, v2, vcc
	v_cmp_gt_i64_e32 vcc, s[24:25], v[8:9]
	v_readlane_b32 s25, v9, 50
	s_movk_i32 s24, 13
	v_addc_co_u32_e32 v2, vcc, 0, v2, vcc
	v_cmp_gt_i64_e32 vcc, s[22:23], v[8:9]
	v_readlane_b32 s23, v9, 51
	s_movk_i32 s22, 12
	v_addc_co_u32_e32 v2, vcc, 0, v2, vcc
	v_cmp_gt_i64_e32 vcc, s[24:25], v[8:9]
	v_readlane_b32 s25, v9, 52
	s_movk_i32 s24, 11
	v_addc_co_u32_e32 v2, vcc, 0, v2, vcc
	v_cmp_gt_i64_e32 vcc, s[22:23], v[8:9]
	v_readlane_b32 s23, v9, 53
	s_movk_i32 s22, 10
	v_addc_co_u32_e32 v2, vcc, 0, v2, vcc
	v_cmp_gt_i64_e32 vcc, s[24:25], v[8:9]
	v_readlane_b32 s25, v9, 54
	s_movk_i32 s24, 9
	v_addc_co_u32_e32 v2, vcc, 0, v2, vcc
	v_cmp_gt_i64_e32 vcc, s[22:23], v[8:9]
	v_readlane_b32 s23, v9, 55
	s_movk_i32 s22, 8
	v_addc_co_u32_e32 v2, vcc, 0, v2, vcc
	v_cmp_gt_i64_e32 vcc, s[24:25], v[8:9]
	v_readlane_b32 s25, v9, 56
	s_movk_i32 s24, 7
	v_addc_co_u32_e32 v2, vcc, 0, v2, vcc
	v_cmp_gt_i64_e32 vcc, s[22:23], v[8:9]
	v_readlane_b32 s23, v9, 57
	s_movk_i32 s22, 6
	v_addc_co_u32_e32 v2, vcc, 0, v2, vcc
	v_cmp_gt_i64_e32 vcc, s[24:25], v[8:9]
	v_readlane_b32 s25, v9, 58
	s_movk_i32 s24, 5
	v_addc_co_u32_e32 v2, vcc, 0, v2, vcc
	v_cmp_gt_i64_e32 vcc, s[22:23], v[8:9]
	v_readlane_b32 s23, v9, 59
	s_movk_i32 s22, 4
	v_addc_co_u32_e32 v2, vcc, 0, v2, vcc
	v_cmp_gt_i64_e32 vcc, s[24:25], v[8:9]
	v_readlane_b32 s25, v9, 60
	s_movk_i32 s24, 3
	v_addc_co_u32_e32 v2, vcc, 0, v2, vcc
	v_cmp_gt_i64_e32 vcc, s[22:23], v[8:9]
	v_readlane_b32 s23, v9, 61
	s_movk_i32 s22, 2
	v_addc_co_u32_e32 v2, vcc, 0, v2, vcc
	v_cmp_gt_i64_e32 vcc, s[24:25], v[8:9]
	v_readlane_b32 s25, v9, 62
	s_movk_i32 s24, 1
	v_addc_co_u32_e32 v2, vcc, 0, v2, vcc
	v_cmp_gt_i64_e32 vcc, s[22:23], v[8:9]
	v_readlane_b32 s23, v9, 63
	s_movk_i32 s22, 0
	v_addc_co_u32_e32 v2, vcc, 0, v2, vcc
	v_cmp_gt_i64_e32 vcc, s[24:25], v[8:9]
	s_nop 1
	v_addc_co_u32_e32 v2, vcc, 0, v2, vcc
	v_cmp_gt_i64_e32 vcc, s[22:23], v[8:9]
	s_nop 1
	v_addc_co_u32_e32 v2, vcc, 0, v2, vcc
	v_cmp_gt_u32_e32 vcc, 6, v2
	s_nop 1
	v_cndmask_b32_e32 v6, 0, v5, vcc
	ds_bpermute_b32 v7, v1, v6
	s_waitcnt lgkmcnt(0)
; __device__ __forceinline__ void phase_nrr(const Frame& F, const Args& a, int l, const bf16_t* XA, const float* g, const float* modl, unsigned char* XN8) {
;     ...
;         for (int i = 0; i < 8; ++i) { const int t = tb + i;
;             const float lg = Pl[(w * 8 + i) * NE + lane] + Pl[(64 + w * 8 + i) * NE + lane]; const float sc = 1.f / (1.f + __expf(-lg)); const float bb = sc + bias;
;             float m1 = bb; m1 = fmaxf(m1, __shfl_xor(m1, 1)); m1 = fmaxf(m1, __shfl_xor(m1, 2)); m1 = fmaxf(m1, __shfl_xor(m1, 4));
;             const unsigned long long eq = __ballot(bb == m1); const int gbase = lane & ~7; const unsigned grpmask = (unsigned)((eq >> gbase) & 0xffull);
;             const int first = gbase + __builtin_ctz(grpmask);
;             float m2 = (lane == first) ? -INFINITY : bb; m2 = fmaxf(m2, __shfl_xor(m2, 1)); m2 = fmaxf(m2, __shfl_xor(m2, 2)); m2 = fmaxf(m2, __shfl_xor(m2, 4));
;             const float gsum = m1 + m2; const int gq = lane >> 3;
;             int grank = 0;
; #pragma unroll
;             for (int g2 = 0; g2 < 8; ++g2) { const float v = __int_as_float(__builtin_amdgcn_readlane(__float_as_int(gsum), g2 * 8)); grank += (v > gsum || (v == gsum && g2 < gq)) ? 1 : 0; }
;             const bool keep = grank < 4; const float val = keep ? bb : -INFINITY;
;             int rank = 0;
; #pragma unroll 8
;             for (int e2 = 0; e2 < 64; ++e2) { const float v = __int_as_float(__builtin_amdgcn_readlane(__float_as_int(val), e2)); rank += (v > val || (v == val && e2 < lane)) ? 1 : 0; }
;             const bool sel = rank < TOPK;
;             const float ssum = wave_sum(sel ? sc : 0.f);
;             if (sel) { const int p = atomicAdd((int*)(hist + lane), 1); top_e[t * TOPK + rank] = lane; gate[t * TOPK + rank] = sc / ssum * 2.5f; lpos[t * TOPK + rank] = p; }
	v_add_f32_e32 v6, v6, v7
	ds_bpermute_b32 v7, v201, v6
	s_waitcnt lgkmcnt(0)
	v_add_f32_e32 v6, v6, v7
	ds_bpermute_b32 v7, v220, v6
	s_waitcnt lgkmcnt(0)
	v_add_f32_e32 v6, v6, v7
	ds_bpermute_b32 v7, v221, v6
	s_waitcnt lgkmcnt(0)
	v_add_f32_e32 v6, v6, v7
	ds_bpermute_b32 v7, v222, v6
	s_waitcnt lgkmcnt(0)
	v_add_f32_e32 v6, v6, v7
	ds_bpermute_b32 v7, v223, v6
	s_and_saveexec_b64 s[22:23], vcc
	s_cbranch_execz .LBB0_543
	s_waitcnt lgkmcnt(0)
	v_add_f32_e32 v10, v6, v7
	v_mad_u64_u32 v[6:7], s[24:25], s42, 6, v[2:3]
	v_div_scale_f32 v2, s[24:25], v10, v10, v5
	v_rcp_f32_e32 v12, v2
	v_ashrrev_i32_e32 v7, 31, v6
	v_lshlrev_b64 v[6:7], 2, v[6:7]
	v_lshl_add_u64 v[8:9], s[26:27], 0, v[6:7]
	ds_add_rtn_u32 v11, v227, v243
	global_store_dword v[8:9], v230, off
	v_fma_f32 v8, -v2, v12, 1.0
	v_fmac_f32_e32 v12, v8, v12
	v_div_scale_f32 v8, vcc, v5, v10, v5
	v_mul_f32_e32 v9, v8, v12
	v_fma_f32 v13, -v2, v9, v8
	v_fmac_f32_e32 v9, v13, v12
	v_fma_f32 v2, -v2, v9, v8
	v_div_fmas_f32 v2, v2, v12, v9
	v_div_fixup_f32 v2, v2, v10, v5
	v_mul_f32_e32 v2, 0x40200000, v2
	v_lshl_add_u64 v[8:9], s[28:29], 0, v[6:7]
	v_lshl_add_u64 v[6:7], s[30:31], 0, v[6:7]
	global_store_dword v[8:9], v2, off
	s_waitcnt lgkmcnt(0)
	global_store_dword v[6:7], v11, off
.LBB0_543:
	s_or_b64 exec, exec, s[22:23]
	v_add_u32_e32 v2, s78, v226
	ds_read_b32 v2, v2
	ds_read_b32 v5, v4 offset:16896
	s_mov_b32 s3, 0
	s_waitcnt lgkmcnt(0)
	v_add_f32_e32 v2, v2, v5
	v_mul_f32_e32 v2, 0xbfb8aa3b, v2
	v_exp_f32_e32 v2, v2
	s_nop 0
	v_add_f32_e32 v2, 1.0, v2
	v_div_scale_f32 v5, s[22:23], v2, v2, 1.0
	v_rcp_f32_e32 v6, v5
	s_nop 0
	v_fma_f32 v7, -v5, v6, 1.0
	v_fmac_f32_e32 v6, v7, v6
	v_div_scale_f32 v7, vcc, 1.0, v2, 1.0
	v_mul_f32_e32 v8, v7, v6
	v_fma_f32 v9, -v5, v8, v7
	v_fmac_f32_e32 v8, v9, v6
	v_fma_f32 v5, -v5, v8, v7
	v_div_fmas_f32 v5, v5, v6, v8
	v_div_fixup_f32 v5, v5, v2, 1.0
	v_add_f32_e32 v2, v3, v5
	s_nop 1
	s_waitcnt lgkmcnt(0)
	v_max_f32_dpp v6, v2, v2 quad_perm:[1,0,3,2] row_mask:0xf bank_mask:0xf
	s_nop 1
	s_waitcnt lgkmcnt(0)
	v_max_f32_dpp v6, v6, v6 quad_perm:[2,3,0,1] row_mask:0xf bank_mask:0xf
	s_nop 1
	s_waitcnt lgkmcnt(0)
	v_max_f32_dpp v8, v6, v6 row_half_mirror row_mask:0xf bank_mask:0xf
	v_cmp_eq_f32_e32 vcc, v2, v8
	s_nop 1
	v_lshrrev_b64 v[6:7], v200, vcc
	v_ffbl_b32_sdwa v6, v6 dst_sel:DWORD dst_unused:UNUSED_PAD src0_sel:BYTE_0
	v_add_u32_e32 v6, v6, v200
	v_cmp_ne_u32_e32 vcc, v230, v6
	s_nop 1
	v_cndmask_b32_e32 v6, v245, v2, vcc
	s_nop 1
	s_waitcnt lgkmcnt(0)
	v_max_f32_dpp v6, v6, v6 quad_perm:[1,0,3,2] row_mask:0xf bank_mask:0xf
	s_nop 1
	s_waitcnt lgkmcnt(0)
	v_max_f32_dpp v6, v6, v6 quad_perm:[2,3,0,1] row_mask:0xf bank_mask:0xf
	s_nop 1
	s_waitcnt lgkmcnt(0)
	v_max_f32_dpp v6, v6, v6 row_half_mirror row_mask:0xf bank_mask:0xf
	v_add_f32_e32 v6, v8, v6
	s_nop 0
	v_readlane_b32 s5, v6, 0
	s_nop 1
	v_cmp_eq_f32_e64 s[22:23], s5, v6
	v_cmp_gt_f32_e32 vcc, s5, v6
	s_and_b64 s[22:23], s[6:7], s[22:23]
	s_or_b64 s[22:23], vcc, s[22:23]
	v_readlane_b32 s5, v6, 8
	v_cndmask_b32_e64 v7, 0, 1, s[22:23]
	s_nop 0
	v_cmp_eq_f32_e64 s[22:23], s5, v6
	v_cmp_gt_f32_e32 vcc, s5, v6
	s_and_b64 s[22:23], s[8:9], s[22:23]
	s_or_b64 s[22:23], vcc, s[22:23]
	v_readlane_b32 s5, v6, 16
	v_cndmask_b32_e64 v8, 0, 1, s[22:23]
	s_nop 0
	v_cmp_eq_f32_e64 s[22:23], s5, v6
	v_cmp_gt_f32_e32 vcc, s5, v6
	s_and_b64 s[22:23], s[10:11], s[22:23]
	s_or_b64 s[22:23], vcc, s[22:23]
	v_readlane_b32 s5, v6, 24
	v_cndmask_b32_e64 v9, 0, 1, s[22:23]
	s_nop 0
	v_cmp_eq_f32_e64 s[22:23], s5, v6
	v_cmp_gt_f32_e32 vcc, s5, v6
	s_and_b64 s[22:23], s[12:13], s[22:23]
	s_or_b64 s[22:23], vcc, s[22:23]
	v_readlane_b32 s5, v6, 32
	v_cndmask_b32_e64 v10, 0, 1, s[22:23]
	s_nop 0
	v_cmp_eq_f32_e64 s[22:23], s5, v6
	v_cmp_gt_f32_e32 vcc, s5, v6
	s_and_b64 s[22:23], s[14:15], s[22:23]
	s_or_b64 s[22:23], vcc, s[22:23]
	v_readlane_b32 s5, v6, 40
	v_cndmask_b32_e64 v11, 0, 1, s[22:23]
	s_nop 0
	v_cmp_eq_f32_e64 s[22:23], s5, v6
	v_cmp_gt_f32_e32 vcc, s5, v6
	s_and_b64 s[22:23], s[16:17], s[22:23]
	s_or_b64 s[22:23], vcc, s[22:23]
	v_readlane_b32 s5, v6, 48
	v_cndmask_b32_e64 v12, 0, 1, s[22:23]
	s_nop 0
	v_cmp_eq_f32_e64 s[22:23], s5, v6
	v_cmp_gt_f32_e32 vcc, s5, v6
	s_and_b64 s[22:23], s[18:19], s[22:23]
	v_readlane_b32 s5, v6, 56
	s_or_b64 s[22:23], vcc, s[22:23]
	v_cndmask_b32_e64 v13, 0, 1, s[22:23]
	v_cmp_gt_f32_e32 vcc, s5, v6
	s_nop 1
	v_cndmask_b32_e64 v6, 0, 1, vcc
	v_add_u32_e32 v6, v8, v6
	v_add3_u32 v6, v6, v7, v9
	v_add3_u32 v6, v6, v10, v11
	v_add3_u32 v6, v6, v12, v13
	v_cmp_gt_u32_e32 vcc, 4, v6
	s_nop 1
	v_cndmask_b32_e32 v6, v245, v2, vcc
	v_mov_b32_e32 v2, 0
	v_ashrrev_i32_e32 v9, 31, v6
	v_sub_u32_e32 v8, 63, v230
	v_and_b32_e32 v9, 0x7fffffff, v9
	v_xor_b32_e32 v9, v6, v9
	s_nop 0
	v_readlane_b32 s25, v9, 0
	s_movk_i32 s24, 63
	v_readlane_b32 s23, v9, 1
	s_movk_i32 s22, 62
	v_cmp_gt_i64_e32 vcc, s[24:25], v[8:9]
	v_readlane_b32 s25, v9, 2
	s_movk_i32 s24, 61
	v_addc_co_u32_e32 v2, vcc, 0, v2, vcc
	v_cmp_gt_i64_e32 vcc, s[22:23], v[8:9]
	v_readlane_b32 s23, v9, 3
	s_movk_i32 s22, 60
	v_addc_co_u32_e32 v2, vcc, 0, v2, vcc
	v_cmp_gt_i64_e32 vcc, s[24:25], v[8:9]
	v_readlane_b32 s25, v9, 4
	s_movk_i32 s24, 59
	v_addc_co_u32_e32 v2, vcc, 0, v2, vcc
	v_cmp_gt_i64_e32 vcc, s[22:23], v[8:9]
	v_readlane_b32 s23, v9, 5
	s_movk_i32 s22, 58
	v_addc_co_u32_e32 v2, vcc, 0, v2, vcc
	v_cmp_gt_i64_e32 vcc, s[24:25], v[8:9]
	v_readlane_b32 s25, v9, 6
	s_movk_i32 s24, 57
	v_addc_co_u32_e32 v2, vcc, 0, v2, vcc
	v_cmp_gt_i64_e32 vcc, s[22:23], v[8:9]
	v_readlane_b32 s23, v9, 7
	s_movk_i32 s22, 56
	v_addc_co_u32_e32 v2, vcc, 0, v2, vcc
	v_cmp_gt_i64_e32 vcc, s[24:25], v[8:9]
	v_readlane_b32 s25, v9, 8
; __device__ __forceinline__ void phase_nrr(const Frame& F, const Args& a, int l, const bf16_t* XA, const float* g, const float* modl, unsigned char* XN8) {
;     ...
;             int rank = 0;
; #pragma unroll 8
;             for (int e2 = 0; e2 < 64; ++e2) { const float v = __int_as_float(__builtin_amdgcn_readlane(__float_as_int(val), e2)); rank += (v > val || (v == val && e2 < lane)) ? 1 : 0; }
	s_movk_i32 s24, 55
	v_addc_co_u32_e32 v2, vcc, 0, v2, vcc
	v_cmp_gt_i64_e32 vcc, s[22:23], v[8:9]
	v_readlane_b32 s23, v9, 9
	s_movk_i32 s22, 54
	v_addc_co_u32_e32 v2, vcc, 0, v2, vcc
	v_cmp_gt_i64_e32 vcc, s[24:25], v[8:9]
	v_readlane_b32 s25, v9, 10
	s_movk_i32 s24, 53
	v_addc_co_u32_e32 v2, vcc, 0, v2, vcc
	v_cmp_gt_i64_e32 vcc, s[22:23], v[8:9]
	v_readlane_b32 s23, v9, 11
	s_movk_i32 s22, 52
	v_addc_co_u32_e32 v2, vcc, 0, v2, vcc
	v_cmp_gt_i64_e32 vcc, s[24:25], v[8:9]
	v_readlane_b32 s25, v9, 12
	s_movk_i32 s24, 51
	v_addc_co_u32_e32 v2, vcc, 0, v2, vcc
	v_cmp_gt_i64_e32 vcc, s[22:23], v[8:9]
	v_readlane_b32 s23, v9, 13
	s_movk_i32 s22, 50
	v_addc_co_u32_e32 v2, vcc, 0, v2, vcc
	v_cmp_gt_i64_e32 vcc, s[24:25], v[8:9]
	v_readlane_b32 s25, v9, 14
	s_movk_i32 s24, 49
	v_addc_co_u32_e32 v2, vcc, 0, v2, vcc
	v_cmp_gt_i64_e32 vcc, s[22:23], v[8:9]
	v_readlane_b32 s23, v9, 15
	s_movk_i32 s22, 48
	v_addc_co_u32_e32 v2, vcc, 0, v2, vcc
	v_cmp_gt_i64_e32 vcc, s[24:25], v[8:9]
	v_readlane_b32 s25, v9, 16
	s_movk_i32 s24, 47
	v_addc_co_u32_e32 v2, vcc, 0, v2, vcc
	v_cmp_gt_i64_e32 vcc, s[22:23], v[8:9]
	v_readlane_b32 s23, v9, 17
	s_movk_i32 s22, 46
	v_addc_co_u32_e32 v2, vcc, 0, v2, vcc
	v_cmp_gt_i64_e32 vcc, s[24:25], v[8:9]
	v_readlane_b32 s25, v9, 18
	s_movk_i32 s24, 45
	v_addc_co_u32_e32 v2, vcc, 0, v2, vcc
	v_cmp_gt_i64_e32 vcc, s[22:23], v[8:9]
	v_readlane_b32 s23, v9, 19
	s_movk_i32 s22, 44
	v_addc_co_u32_e32 v2, vcc, 0, v2, vcc
	v_cmp_gt_i64_e32 vcc, s[24:25], v[8:9]
	v_readlane_b32 s25, v9, 20
	s_movk_i32 s24, 43
	v_addc_co_u32_e32 v2, vcc, 0, v2, vcc
	v_cmp_gt_i64_e32 vcc, s[22:23], v[8:9]
	v_readlane_b32 s23, v9, 21
	s_movk_i32 s22, 42
	v_addc_co_u32_e32 v2, vcc, 0, v2, vcc
	v_cmp_gt_i64_e32 vcc, s[24:25], v[8:9]
	v_readlane_b32 s25, v9, 22
	s_movk_i32 s24, 41
	v_addc_co_u32_e32 v2, vcc, 0, v2, vcc
	v_cmp_gt_i64_e32 vcc, s[22:23], v[8:9]
	v_readlane_b32 s23, v9, 23
	s_movk_i32 s22, 40
	v_addc_co_u32_e32 v2, vcc, 0, v2, vcc
	v_cmp_gt_i64_e32 vcc, s[24:25], v[8:9]
	v_readlane_b32 s25, v9, 24
	s_movk_i32 s24, 39
	v_addc_co_u32_e32 v2, vcc, 0, v2, vcc
	v_cmp_gt_i64_e32 vcc, s[22:23], v[8:9]
	v_readlane_b32 s23, v9, 25
	s_movk_i32 s22, 38
	v_addc_co_u32_e32 v2, vcc, 0, v2, vcc
	v_cmp_gt_i64_e32 vcc, s[24:25], v[8:9]
	v_readlane_b32 s25, v9, 26
	s_movk_i32 s24, 37
	v_addc_co_u32_e32 v2, vcc, 0, v2, vcc
	v_cmp_gt_i64_e32 vcc, s[22:23], v[8:9]
	v_readlane_b32 s23, v9, 27
	s_movk_i32 s22, 36
	v_addc_co_u32_e32 v2, vcc, 0, v2, vcc
	v_cmp_gt_i64_e32 vcc, s[24:25], v[8:9]
	v_readlane_b32 s25, v9, 28
	s_movk_i32 s24, 35
	v_addc_co_u32_e32 v2, vcc, 0, v2, vcc
	v_cmp_gt_i64_e32 vcc, s[22:23], v[8:9]
	v_readlane_b32 s23, v9, 29
	s_movk_i32 s22, 34
	v_addc_co_u32_e32 v2, vcc, 0, v2, vcc
	v_cmp_gt_i64_e32 vcc, s[24:25], v[8:9]
	v_readlane_b32 s25, v9, 30
	s_movk_i32 s24, 33
	v_addc_co_u32_e32 v2, vcc, 0, v2, vcc
	v_cmp_gt_i64_e32 vcc, s[22:23], v[8:9]
	v_readlane_b32 s23, v9, 31
	s_movk_i32 s22, 32
	v_addc_co_u32_e32 v2, vcc, 0, v2, vcc
	v_cmp_gt_i64_e32 vcc, s[24:25], v[8:9]
	v_readlane_b32 s25, v9, 32
	s_movk_i32 s24, 31
	v_addc_co_u32_e32 v2, vcc, 0, v2, vcc
	v_cmp_gt_i64_e32 vcc, s[22:23], v[8:9]
	v_readlane_b32 s23, v9, 33
	s_movk_i32 s22, 30
	v_addc_co_u32_e32 v2, vcc, 0, v2, vcc
	v_cmp_gt_i64_e32 vcc, s[24:25], v[8:9]
	v_readlane_b32 s25, v9, 34
	s_movk_i32 s24, 29
	v_addc_co_u32_e32 v2, vcc, 0, v2, vcc
	v_cmp_gt_i64_e32 vcc, s[22:23], v[8:9]
	v_readlane_b32 s23, v9, 35
	s_movk_i32 s22, 28
	v_addc_co_u32_e32 v2, vcc, 0, v2, vcc
	v_cmp_gt_i64_e32 vcc, s[24:25], v[8:9]
	v_readlane_b32 s25, v9, 36
	s_movk_i32 s24, 27
	v_addc_co_u32_e32 v2, vcc, 0, v2, vcc
	v_cmp_gt_i64_e32 vcc, s[22:23], v[8:9]
	v_readlane_b32 s23, v9, 37
	s_movk_i32 s22, 26
	v_addc_co_u32_e32 v2, vcc, 0, v2, vcc
	v_cmp_gt_i64_e32 vcc, s[24:25], v[8:9]
	v_readlane_b32 s25, v9, 38
	s_movk_i32 s24, 25
	v_addc_co_u32_e32 v2, vcc, 0, v2, vcc
	v_cmp_gt_i64_e32 vcc, s[22:23], v[8:9]
	v_readlane_b32 s23, v9, 39
	s_movk_i32 s22, 24
	v_addc_co_u32_e32 v2, vcc, 0, v2, vcc
	v_cmp_gt_i64_e32 vcc, s[24:25], v[8:9]
	v_readlane_b32 s25, v9, 40
	s_movk_i32 s24, 23
	v_addc_co_u32_e32 v2, vcc, 0, v2, vcc
	v_cmp_gt_i64_e32 vcc, s[22:23], v[8:9]
	v_readlane_b32 s23, v9, 41
	s_movk_i32 s22, 22
	v_addc_co_u32_e32 v2, vcc, 0, v2, vcc
	v_cmp_gt_i64_e32 vcc, s[24:25], v[8:9]
	v_readlane_b32 s25, v9, 42
	s_movk_i32 s24, 21
	v_addc_co_u32_e32 v2, vcc, 0, v2, vcc
	v_cmp_gt_i64_e32 vcc, s[22:23], v[8:9]
	v_readlane_b32 s23, v9, 43
	s_movk_i32 s22, 20
	v_addc_co_u32_e32 v2, vcc, 0, v2, vcc
	v_cmp_gt_i64_e32 vcc, s[24:25], v[8:9]
	v_readlane_b32 s25, v9, 44
	s_movk_i32 s24, 19
	v_addc_co_u32_e32 v2, vcc, 0, v2, vcc
	v_cmp_gt_i64_e32 vcc, s[22:23], v[8:9]
	v_readlane_b32 s23, v9, 45
	s_movk_i32 s22, 18
	v_addc_co_u32_e32 v2, vcc, 0, v2, vcc
	v_cmp_gt_i64_e32 vcc, s[24:25], v[8:9]
	v_readlane_b32 s25, v9, 46
	s_movk_i32 s24, 17
	v_addc_co_u32_e32 v2, vcc, 0, v2, vcc
	v_cmp_gt_i64_e32 vcc, s[22:23], v[8:9]
	v_readlane_b32 s23, v9, 47
	s_movk_i32 s22, 16
	v_addc_co_u32_e32 v2, vcc, 0, v2, vcc
	v_cmp_gt_i64_e32 vcc, s[24:25], v[8:9]
	v_readlane_b32 s25, v9, 48
	s_movk_i32 s24, 15
	v_addc_co_u32_e32 v2, vcc, 0, v2, vcc
	v_cmp_gt_i64_e32 vcc, s[22:23], v[8:9]
	v_readlane_b32 s23, v9, 49
	s_movk_i32 s22, 14
	v_addc_co_u32_e32 v2, vcc, 0, v2, vcc
	v_cmp_gt_i64_e32 vcc, s[24:25], v[8:9]
	v_readlane_b32 s25, v9, 50
	s_movk_i32 s24, 13
	v_addc_co_u32_e32 v2, vcc, 0, v2, vcc
	v_cmp_gt_i64_e32 vcc, s[22:23], v[8:9]
	v_readlane_b32 s23, v9, 51
	s_movk_i32 s22, 12
	v_addc_co_u32_e32 v2, vcc, 0, v2, vcc
	v_cmp_gt_i64_e32 vcc, s[24:25], v[8:9]
	v_readlane_b32 s25, v9, 52
	s_movk_i32 s24, 11
	v_addc_co_u32_e32 v2, vcc, 0, v2, vcc
; __device__ __forceinline__ void phase_nrr(const Frame& F, const Args& a, int l, const bf16_t* XA, const float* g, const float* modl, unsigned char* XN8) {
;     ...
;         for (int i = 0; i < 8; ++i) { const int t = tb + i;
;             const float lg = Pl[(w * 8 + i) * NE + lane] + Pl[(64 + w * 8 + i) * NE + lane]; const float sc = 1.f / (1.f + __expf(-lg)); const float bb = sc + bias;
;             float m1 = bb; m1 = fmaxf(m1, __shfl_xor(m1, 1)); m1 = fmaxf(m1, __shfl_xor(m1, 2)); m1 = fmaxf(m1, __shfl_xor(m1, 4));
;             const unsigned long long eq = __ballot(bb == m1); const int gbase = lane & ~7; const unsigned grpmask = (unsigned)((eq >> gbase) & 0xffull);
;             const int first = gbase + __builtin_ctz(grpmask);
;             float m2 = (lane == first) ? -INFINITY : bb; m2 = fmaxf(m2, __shfl_xor(m2, 1)); m2 = fmaxf(m2, __shfl_xor(m2, 2)); m2 = fmaxf(m2, __shfl_xor(m2, 4));
;             const float gsum = m1 + m2; const int gq = lane >> 3;
;             int grank = 0;
; #pragma unroll
;             for (int g2 = 0; g2 < 8; ++g2) { const float v = __int_as_float(__builtin_amdgcn_readlane(__float_as_int(gsum), g2 * 8)); grank += (v > gsum || (v == gsum && g2 < gq)) ? 1 : 0; }
;             const bool keep = grank < 4; const float val = keep ? bb : -INFINITY;
;             int rank = 0;
; #pragma unroll 8
;             for (int e2 = 0; e2 < 64; ++e2) { const float v = __int_as_float(__builtin_amdgcn_readlane(__float_as_int(val), e2)); rank += (v > val || (v == val && e2 < lane)) ? 1 : 0; }
;             const bool sel = rank < TOPK;
;             const float ssum = wave_sum(sel ? sc : 0.f);
;             if (sel) { const int p = atomicAdd((int*)(hist + lane), 1); top_e[t * TOPK + rank] = lane; gate[t * TOPK + rank] = sc / ssum * 2.5f; lpos[t * TOPK + rank] = p; }
	v_cmp_gt_i64_e32 vcc, s[22:23], v[8:9]
	v_readlane_b32 s23, v9, 53
	s_movk_i32 s22, 10
	v_addc_co_u32_e32 v2, vcc, 0, v2, vcc
	v_cmp_gt_i64_e32 vcc, s[24:25], v[8:9]
	v_readlane_b32 s25, v9, 54
	s_movk_i32 s24, 9
	v_addc_co_u32_e32 v2, vcc, 0, v2, vcc
	v_cmp_gt_i64_e32 vcc, s[22:23], v[8:9]
	v_readlane_b32 s23, v9, 55
	s_movk_i32 s22, 8
	v_addc_co_u32_e32 v2, vcc, 0, v2, vcc
	v_cmp_gt_i64_e32 vcc, s[24:25], v[8:9]
	v_readlane_b32 s25, v9, 56
	s_movk_i32 s24, 7
	v_addc_co_u32_e32 v2, vcc, 0, v2, vcc
	v_cmp_gt_i64_e32 vcc, s[22:23], v[8:9]
	v_readlane_b32 s23, v9, 57
	s_movk_i32 s22, 6
	v_addc_co_u32_e32 v2, vcc, 0, v2, vcc
	v_cmp_gt_i64_e32 vcc, s[24:25], v[8:9]
	v_readlane_b32 s25, v9, 58
	s_movk_i32 s24, 5
	v_addc_co_u32_e32 v2, vcc, 0, v2, vcc
	v_cmp_gt_i64_e32 vcc, s[22:23], v[8:9]
	v_readlane_b32 s23, v9, 59
	s_movk_i32 s22, 4
	v_addc_co_u32_e32 v2, vcc, 0, v2, vcc
	v_cmp_gt_i64_e32 vcc, s[24:25], v[8:9]
	v_readlane_b32 s25, v9, 60
	s_movk_i32 s24, 3
	v_addc_co_u32_e32 v2, vcc, 0, v2, vcc
	v_cmp_gt_i64_e32 vcc, s[22:23], v[8:9]
	v_readlane_b32 s23, v9, 61
	s_movk_i32 s22, 2
	v_addc_co_u32_e32 v2, vcc, 0, v2, vcc
	v_cmp_gt_i64_e32 vcc, s[24:25], v[8:9]
	v_readlane_b32 s25, v9, 62
	s_movk_i32 s24, 1
	v_addc_co_u32_e32 v2, vcc, 0, v2, vcc
	v_cmp_gt_i64_e32 vcc, s[22:23], v[8:9]
	v_readlane_b32 s23, v9, 63
	s_movk_i32 s22, 0
	v_addc_co_u32_e32 v2, vcc, 0, v2, vcc
	v_cmp_gt_i64_e32 vcc, s[24:25], v[8:9]
	s_nop 1
	v_addc_co_u32_e32 v2, vcc, 0, v2, vcc
	v_cmp_gt_i64_e32 vcc, s[22:23], v[8:9]
	s_nop 1
	v_addc_co_u32_e32 v2, vcc, 0, v2, vcc
	v_cmp_gt_u32_e32 vcc, 6, v2
	s_nop 1
	v_cndmask_b32_e32 v6, 0, v5, vcc
	ds_bpermute_b32 v7, v1, v6
	s_waitcnt lgkmcnt(0)
	v_add_f32_e32 v6, v6, v7
	ds_bpermute_b32 v7, v201, v6
	s_waitcnt lgkmcnt(0)
	v_add_f32_e32 v6, v6, v7
	ds_bpermute_b32 v7, v220, v6
	s_waitcnt lgkmcnt(0)
	v_add_f32_e32 v6, v6, v7
	ds_bpermute_b32 v7, v221, v6
	s_waitcnt lgkmcnt(0)
	v_add_f32_e32 v6, v6, v7
	ds_bpermute_b32 v7, v222, v6
	s_waitcnt lgkmcnt(0)
	v_add_f32_e32 v6, v6, v7
	ds_bpermute_b32 v7, v223, v6
	s_and_saveexec_b64 s[22:23], vcc
	s_cbranch_execz .LBB0_547
	s_waitcnt lgkmcnt(0)
	v_add_f32_e32 v10, v6, v7
	v_mad_u64_u32 v[6:7], s[24:25], s40, 6, v[2:3]
	v_div_scale_f32 v2, s[24:25], v10, v10, v5
	v_rcp_f32_e32 v12, v2
	v_ashrrev_i32_e32 v7, 31, v6
	v_lshlrev_b64 v[6:7], 2, v[6:7]
	v_lshl_add_u64 v[8:9], s[26:27], 0, v[6:7]
	ds_add_rtn_u32 v11, v227, v243
	global_store_dword v[8:9], v230, off
	v_fma_f32 v8, -v2, v12, 1.0
	v_fmac_f32_e32 v12, v8, v12
	v_div_scale_f32 v8, vcc, v5, v10, v5
	v_mul_f32_e32 v9, v8, v12
	v_fma_f32 v13, -v2, v9, v8
	v_fmac_f32_e32 v9, v13, v12
	v_fma_f32 v2, -v2, v9, v8
	v_div_fmas_f32 v2, v2, v12, v9
	v_div_fixup_f32 v2, v2, v10, v5
	v_mul_f32_e32 v2, 0x40200000, v2
	v_lshl_add_u64 v[8:9], s[28:29], 0, v[6:7]
	v_lshl_add_u64 v[6:7], s[30:31], 0, v[6:7]
	global_store_dword v[8:9], v2, off
	s_waitcnt lgkmcnt(0)
	global_store_dword v[6:7], v11, off
.LBB0_547:
	s_or_b64 exec, exec, s[22:23]
	v_add_u32_e32 v2, s79, v226
	ds_read_b32 v2, v2
	ds_read_b32 v5, v4 offset:17152
	s_mov_b32 s3, 0
	s_waitcnt lgkmcnt(0)
	v_add_f32_e32 v2, v2, v5
	v_mul_f32_e32 v2, 0xbfb8aa3b, v2
	v_exp_f32_e32 v2, v2
	s_nop 0
	v_add_f32_e32 v2, 1.0, v2
	v_div_scale_f32 v5, s[22:23], v2, v2, 1.0
	v_rcp_f32_e32 v6, v5
	s_nop 0
	v_fma_f32 v7, -v5, v6, 1.0
	v_fmac_f32_e32 v6, v7, v6
	v_div_scale_f32 v7, vcc, 1.0, v2, 1.0
	v_mul_f32_e32 v8, v7, v6
	v_fma_f32 v9, -v5, v8, v7
	v_fmac_f32_e32 v8, v9, v6
	v_fma_f32 v5, -v5, v8, v7
	v_div_fmas_f32 v5, v5, v6, v8
	v_div_fixup_f32 v5, v5, v2, 1.0
	v_add_f32_e32 v2, v3, v5
	s_nop 1
	s_waitcnt lgkmcnt(0)
	v_max_f32_dpp v6, v2, v2 quad_perm:[1,0,3,2] row_mask:0xf bank_mask:0xf
	s_nop 1
	s_waitcnt lgkmcnt(0)
	v_max_f32_dpp v6, v6, v6 quad_perm:[2,3,0,1] row_mask:0xf bank_mask:0xf
	s_nop 1
	s_waitcnt lgkmcnt(0)
	v_max_f32_dpp v8, v6, v6 row_half_mirror row_mask:0xf bank_mask:0xf
	v_cmp_eq_f32_e32 vcc, v2, v8
	s_nop 1
	v_lshrrev_b64 v[6:7], v200, vcc
	v_ffbl_b32_sdwa v6, v6 dst_sel:DWORD dst_unused:UNUSED_PAD src0_sel:BYTE_0
	v_add_u32_e32 v6, v6, v200
	v_cmp_ne_u32_e32 vcc, v230, v6
	s_nop 1
	v_cndmask_b32_e32 v6, v245, v2, vcc
	s_nop 1
	s_waitcnt lgkmcnt(0)
	v_max_f32_dpp v6, v6, v6 quad_perm:[1,0,3,2] row_mask:0xf bank_mask:0xf
	s_nop 1
	s_waitcnt lgkmcnt(0)
	v_max_f32_dpp v6, v6, v6 quad_perm:[2,3,0,1] row_mask:0xf bank_mask:0xf
	s_nop 1
	s_waitcnt lgkmcnt(0)
; __device__ __forceinline__ void phase_nrr(const Frame& F, const Args& a, int l, const bf16_t* XA, const float* g, const float* modl, unsigned char* XN8) {
;     ...
;             float m2 = (lane == first) ? -INFINITY : bb; m2 = fmaxf(m2, __shfl_xor(m2, 1)); m2 = fmaxf(m2, __shfl_xor(m2, 2)); m2 = fmaxf(m2, __shfl_xor(m2, 4));
;             const float gsum = m1 + m2; const int gq = lane >> 3;
;             int grank = 0;
; #pragma unroll
;             for (int g2 = 0; g2 < 8; ++g2) { const float v = __int_as_float(__builtin_amdgcn_readlane(__float_as_int(gsum), g2 * 8)); grank += (v > gsum || (v == gsum && g2 < gq)) ? 1 : 0; }
;             const bool keep = grank < 4; const float val = keep ? bb : -INFINITY;
;             int rank = 0;
; #pragma unroll 8
;             for (int e2 = 0; e2 < 64; ++e2) { const float v = __int_as_float(__builtin_amdgcn_readlane(__float_as_int(val), e2)); rank += (v > val || (v == val && e2 < lane)) ? 1 : 0; }
	v_max_f32_dpp v6, v6, v6 row_half_mirror row_mask:0xf bank_mask:0xf
	v_add_f32_e32 v6, v8, v6
	s_nop 0
	v_readlane_b32 s5, v6, 0
	s_nop 1
	v_cmp_eq_f32_e64 s[22:23], s5, v6
	v_cmp_gt_f32_e32 vcc, s5, v6
	s_and_b64 s[22:23], s[6:7], s[22:23]
	s_or_b64 s[22:23], vcc, s[22:23]
	v_readlane_b32 s5, v6, 8
	v_cndmask_b32_e64 v7, 0, 1, s[22:23]
	s_nop 0
	v_cmp_eq_f32_e64 s[22:23], s5, v6
	v_cmp_gt_f32_e32 vcc, s5, v6
	s_and_b64 s[22:23], s[8:9], s[22:23]
	s_or_b64 s[22:23], vcc, s[22:23]
	v_readlane_b32 s5, v6, 16
	v_cndmask_b32_e64 v8, 0, 1, s[22:23]
	s_nop 0
	v_cmp_eq_f32_e64 s[22:23], s5, v6
	v_cmp_gt_f32_e32 vcc, s5, v6
	s_and_b64 s[22:23], s[10:11], s[22:23]
	s_or_b64 s[22:23], vcc, s[22:23]
	v_readlane_b32 s5, v6, 24
	v_cndmask_b32_e64 v9, 0, 1, s[22:23]
	s_nop 0
	v_cmp_eq_f32_e64 s[22:23], s5, v6
	v_cmp_gt_f32_e32 vcc, s5, v6
	s_and_b64 s[22:23], s[12:13], s[22:23]
	s_or_b64 s[22:23], vcc, s[22:23]
	v_readlane_b32 s5, v6, 32
	v_cndmask_b32_e64 v10, 0, 1, s[22:23]
	s_nop 0
	v_cmp_eq_f32_e64 s[22:23], s5, v6
	v_cmp_gt_f32_e32 vcc, s5, v6
	s_and_b64 s[22:23], s[14:15], s[22:23]
	s_or_b64 s[22:23], vcc, s[22:23]
	v_readlane_b32 s5, v6, 40
	v_cndmask_b32_e64 v11, 0, 1, s[22:23]
	s_nop 0
	v_cmp_eq_f32_e64 s[22:23], s5, v6
	v_cmp_gt_f32_e32 vcc, s5, v6
	s_and_b64 s[22:23], s[16:17], s[22:23]
	s_or_b64 s[22:23], vcc, s[22:23]
	v_readlane_b32 s5, v6, 48
	v_cndmask_b32_e64 v12, 0, 1, s[22:23]
	s_nop 0
	v_cmp_eq_f32_e64 s[22:23], s5, v6
	v_cmp_gt_f32_e32 vcc, s5, v6
	s_and_b64 s[22:23], s[18:19], s[22:23]
	v_readlane_b32 s5, v6, 56
	s_or_b64 s[22:23], vcc, s[22:23]
	v_cndmask_b32_e64 v13, 0, 1, s[22:23]
	v_cmp_gt_f32_e32 vcc, s5, v6
	s_nop 1
	v_cndmask_b32_e64 v6, 0, 1, vcc
	v_add_u32_e32 v6, v8, v6
	v_add3_u32 v6, v6, v7, v9
	v_add3_u32 v6, v6, v10, v11
	v_add3_u32 v6, v6, v12, v13
	v_cmp_gt_u32_e32 vcc, 4, v6
	s_nop 1
	v_cndmask_b32_e32 v6, v245, v2, vcc
	v_mov_b32_e32 v2, 0
	v_ashrrev_i32_e32 v9, 31, v6
	v_sub_u32_e32 v8, 63, v230
	v_and_b32_e32 v9, 0x7fffffff, v9
	v_xor_b32_e32 v9, v6, v9
	s_nop 0
	v_readlane_b32 s25, v9, 0
	s_movk_i32 s24, 63
	v_readlane_b32 s23, v9, 1
	s_movk_i32 s22, 62
	v_cmp_gt_i64_e32 vcc, s[24:25], v[8:9]
	v_readlane_b32 s25, v9, 2
	s_movk_i32 s24, 61
	v_addc_co_u32_e32 v2, vcc, 0, v2, vcc
	v_cmp_gt_i64_e32 vcc, s[22:23], v[8:9]
	v_readlane_b32 s23, v9, 3
	s_movk_i32 s22, 60
	v_addc_co_u32_e32 v2, vcc, 0, v2, vcc
	v_cmp_gt_i64_e32 vcc, s[24:25], v[8:9]
	v_readlane_b32 s25, v9, 4
	s_movk_i32 s24, 59
	v_addc_co_u32_e32 v2, vcc, 0, v2, vcc
	v_cmp_gt_i64_e32 vcc, s[22:23], v[8:9]
	v_readlane_b32 s23, v9, 5
	s_movk_i32 s22, 58
	v_addc_co_u32_e32 v2, vcc, 0, v2, vcc
	v_cmp_gt_i64_e32 vcc, s[24:25], v[8:9]
	v_readlane_b32 s25, v9, 6
	s_movk_i32 s24, 57
	v_addc_co_u32_e32 v2, vcc, 0, v2, vcc
	v_cmp_gt_i64_e32 vcc, s[22:23], v[8:9]
	v_readlane_b32 s23, v9, 7
	s_movk_i32 s22, 56
	v_addc_co_u32_e32 v2, vcc, 0, v2, vcc
	v_cmp_gt_i64_e32 vcc, s[24:25], v[8:9]
	v_readlane_b32 s25, v9, 8
	s_movk_i32 s24, 55
	v_addc_co_u32_e32 v2, vcc, 0, v2, vcc
	v_cmp_gt_i64_e32 vcc, s[22:23], v[8:9]
	v_readlane_b32 s23, v9, 9
	s_movk_i32 s22, 54
	v_addc_co_u32_e32 v2, vcc, 0, v2, vcc
	v_cmp_gt_i64_e32 vcc, s[24:25], v[8:9]
	v_readlane_b32 s25, v9, 10
	s_movk_i32 s24, 53
	v_addc_co_u32_e32 v2, vcc, 0, v2, vcc
	v_cmp_gt_i64_e32 vcc, s[22:23], v[8:9]
	v_readlane_b32 s23, v9, 11
	s_movk_i32 s22, 52
	v_addc_co_u32_e32 v2, vcc, 0, v2, vcc
	v_cmp_gt_i64_e32 vcc, s[24:25], v[8:9]
	v_readlane_b32 s25, v9, 12
	s_movk_i32 s24, 51
	v_addc_co_u32_e32 v2, vcc, 0, v2, vcc
	v_cmp_gt_i64_e32 vcc, s[22:23], v[8:9]
	v_readlane_b32 s23, v9, 13
	s_movk_i32 s22, 50
	v_addc_co_u32_e32 v2, vcc, 0, v2, vcc
	v_cmp_gt_i64_e32 vcc, s[24:25], v[8:9]
	v_readlane_b32 s25, v9, 14
	s_movk_i32 s24, 49
	v_addc_co_u32_e32 v2, vcc, 0, v2, vcc
	v_cmp_gt_i64_e32 vcc, s[22:23], v[8:9]
	v_readlane_b32 s23, v9, 15
	s_movk_i32 s22, 48
	v_addc_co_u32_e32 v2, vcc, 0, v2, vcc
	v_cmp_gt_i64_e32 vcc, s[24:25], v[8:9]
	v_readlane_b32 s25, v9, 16
	s_movk_i32 s24, 47
	v_addc_co_u32_e32 v2, vcc, 0, v2, vcc
	v_cmp_gt_i64_e32 vcc, s[22:23], v[8:9]
	v_readlane_b32 s23, v9, 17
	s_movk_i32 s22, 46
	v_addc_co_u32_e32 v2, vcc, 0, v2, vcc
	v_cmp_gt_i64_e32 vcc, s[24:25], v[8:9]
	v_readlane_b32 s25, v9, 18
	s_movk_i32 s24, 45
	v_addc_co_u32_e32 v2, vcc, 0, v2, vcc
	v_cmp_gt_i64_e32 vcc, s[22:23], v[8:9]
	v_readlane_b32 s23, v9, 19
	s_movk_i32 s22, 44
	v_addc_co_u32_e32 v2, vcc, 0, v2, vcc
	v_cmp_gt_i64_e32 vcc, s[24:25], v[8:9]
	v_readlane_b32 s25, v9, 20
	s_movk_i32 s24, 43
	v_addc_co_u32_e32 v2, vcc, 0, v2, vcc
	v_cmp_gt_i64_e32 vcc, s[22:23], v[8:9]
	v_readlane_b32 s23, v9, 21
	s_movk_i32 s22, 42
	v_addc_co_u32_e32 v2, vcc, 0, v2, vcc
	v_cmp_gt_i64_e32 vcc, s[24:25], v[8:9]
	v_readlane_b32 s25, v9, 22
	s_movk_i32 s24, 41
	v_addc_co_u32_e32 v2, vcc, 0, v2, vcc
	v_cmp_gt_i64_e32 vcc, s[22:23], v[8:9]
	v_readlane_b32 s23, v9, 23
	s_movk_i32 s22, 40
	v_addc_co_u32_e32 v2, vcc, 0, v2, vcc
	v_cmp_gt_i64_e32 vcc, s[24:25], v[8:9]
	v_readlane_b32 s25, v9, 24
	s_movk_i32 s24, 39
	v_addc_co_u32_e32 v2, vcc, 0, v2, vcc
	v_cmp_gt_i64_e32 vcc, s[22:23], v[8:9]
	v_readlane_b32 s23, v9, 25
	s_movk_i32 s22, 38
	v_addc_co_u32_e32 v2, vcc, 0, v2, vcc
	v_cmp_gt_i64_e32 vcc, s[24:25], v[8:9]
	v_readlane_b32 s25, v9, 26
	s_movk_i32 s24, 37
	v_addc_co_u32_e32 v2, vcc, 0, v2, vcc
	v_cmp_gt_i64_e32 vcc, s[22:23], v[8:9]
	v_readlane_b32 s23, v9, 27
	s_movk_i32 s22, 36
	v_addc_co_u32_e32 v2, vcc, 0, v2, vcc
	v_cmp_gt_i64_e32 vcc, s[24:25], v[8:9]
	v_readlane_b32 s25, v9, 28
	s_movk_i32 s24, 35
	v_addc_co_u32_e32 v2, vcc, 0, v2, vcc
	v_cmp_gt_i64_e32 vcc, s[22:23], v[8:9]
	v_readlane_b32 s23, v9, 29
	s_movk_i32 s22, 34
; __device__ __forceinline__ void phase_nrr(const Frame& F, const Args& a, int l, const bf16_t* XA, const float* g, const float* modl, unsigned char* XN8) {
;     ...
;             int rank = 0;
; #pragma unroll 8
;             for (int e2 = 0; e2 < 64; ++e2) { const float v = __int_as_float(__builtin_amdgcn_readlane(__float_as_int(val), e2)); rank += (v > val || (v == val && e2 < lane)) ? 1 : 0; }
;             const bool sel = rank < TOPK;
;             const float ssum = wave_sum(sel ? sc : 0.f);
;             if (sel) { const int p = atomicAdd((int*)(hist + lane), 1); top_e[t * TOPK + rank] = lane; gate[t * TOPK + rank] = sc / ssum * 2.5f; lpos[t * TOPK + rank] = p; }
	v_addc_co_u32_e32 v2, vcc, 0, v2, vcc
	v_cmp_gt_i64_e32 vcc, s[24:25], v[8:9]
	v_readlane_b32 s25, v9, 30
	s_movk_i32 s24, 33
	v_addc_co_u32_e32 v2, vcc, 0, v2, vcc
	v_cmp_gt_i64_e32 vcc, s[22:23], v[8:9]
	v_readlane_b32 s23, v9, 31
	s_movk_i32 s22, 32
	v_addc_co_u32_e32 v2, vcc, 0, v2, vcc
	v_cmp_gt_i64_e32 vcc, s[24:25], v[8:9]
	v_readlane_b32 s25, v9, 32
	s_movk_i32 s24, 31
	v_addc_co_u32_e32 v2, vcc, 0, v2, vcc
	v_cmp_gt_i64_e32 vcc, s[22:23], v[8:9]
	v_readlane_b32 s23, v9, 33
	s_movk_i32 s22, 30
	v_addc_co_u32_e32 v2, vcc, 0, v2, vcc
	v_cmp_gt_i64_e32 vcc, s[24:25], v[8:9]
	v_readlane_b32 s25, v9, 34
	s_movk_i32 s24, 29
	v_addc_co_u32_e32 v2, vcc, 0, v2, vcc
	v_cmp_gt_i64_e32 vcc, s[22:23], v[8:9]
	v_readlane_b32 s23, v9, 35
	s_movk_i32 s22, 28
	v_addc_co_u32_e32 v2, vcc, 0, v2, vcc
	v_cmp_gt_i64_e32 vcc, s[24:25], v[8:9]
	v_readlane_b32 s25, v9, 36
	s_movk_i32 s24, 27
	v_addc_co_u32_e32 v2, vcc, 0, v2, vcc
	v_cmp_gt_i64_e32 vcc, s[22:23], v[8:9]
	v_readlane_b32 s23, v9, 37
	s_movk_i32 s22, 26
	v_addc_co_u32_e32 v2, vcc, 0, v2, vcc
	v_cmp_gt_i64_e32 vcc, s[24:25], v[8:9]
	v_readlane_b32 s25, v9, 38
	s_movk_i32 s24, 25
	v_addc_co_u32_e32 v2, vcc, 0, v2, vcc
	v_cmp_gt_i64_e32 vcc, s[22:23], v[8:9]
	v_readlane_b32 s23, v9, 39
	s_movk_i32 s22, 24
	v_addc_co_u32_e32 v2, vcc, 0, v2, vcc
	v_cmp_gt_i64_e32 vcc, s[24:25], v[8:9]
	v_readlane_b32 s25, v9, 40
	s_movk_i32 s24, 23
	v_addc_co_u32_e32 v2, vcc, 0, v2, vcc
	v_cmp_gt_i64_e32 vcc, s[22:23], v[8:9]
	v_readlane_b32 s23, v9, 41
	s_movk_i32 s22, 22
	v_addc_co_u32_e32 v2, vcc, 0, v2, vcc
	v_cmp_gt_i64_e32 vcc, s[24:25], v[8:9]
	v_readlane_b32 s25, v9, 42
	s_movk_i32 s24, 21
	v_addc_co_u32_e32 v2, vcc, 0, v2, vcc
	v_cmp_gt_i64_e32 vcc, s[22:23], v[8:9]
	v_readlane_b32 s23, v9, 43
	s_movk_i32 s22, 20
	v_addc_co_u32_e32 v2, vcc, 0, v2, vcc
	v_cmp_gt_i64_e32 vcc, s[24:25], v[8:9]
	v_readlane_b32 s25, v9, 44
	s_movk_i32 s24, 19
	v_addc_co_u32_e32 v2, vcc, 0, v2, vcc
	v_cmp_gt_i64_e32 vcc, s[22:23], v[8:9]
	v_readlane_b32 s23, v9, 45
	s_movk_i32 s22, 18
	v_addc_co_u32_e32 v2, vcc, 0, v2, vcc
	v_cmp_gt_i64_e32 vcc, s[24:25], v[8:9]
	v_readlane_b32 s25, v9, 46
	s_movk_i32 s24, 17
	v_addc_co_u32_e32 v2, vcc, 0, v2, vcc
	v_cmp_gt_i64_e32 vcc, s[22:23], v[8:9]
	v_readlane_b32 s23, v9, 47
	s_movk_i32 s22, 16
	v_addc_co_u32_e32 v2, vcc, 0, v2, vcc
	v_cmp_gt_i64_e32 vcc, s[24:25], v[8:9]
	v_readlane_b32 s25, v9, 48
	s_movk_i32 s24, 15
	v_addc_co_u32_e32 v2, vcc, 0, v2, vcc
	v_cmp_gt_i64_e32 vcc, s[22:23], v[8:9]
	v_readlane_b32 s23, v9, 49
	s_movk_i32 s22, 14
	v_addc_co_u32_e32 v2, vcc, 0, v2, vcc
	v_cmp_gt_i64_e32 vcc, s[24:25], v[8:9]
	v_readlane_b32 s25, v9, 50
	s_movk_i32 s24, 13
	v_addc_co_u32_e32 v2, vcc, 0, v2, vcc
	v_cmp_gt_i64_e32 vcc, s[22:23], v[8:9]
	v_readlane_b32 s23, v9, 51
	s_movk_i32 s22, 12
	v_addc_co_u32_e32 v2, vcc, 0, v2, vcc
	v_cmp_gt_i64_e32 vcc, s[24:25], v[8:9]
	v_readlane_b32 s25, v9, 52
	s_movk_i32 s24, 11
	v_addc_co_u32_e32 v2, vcc, 0, v2, vcc
	v_cmp_gt_i64_e32 vcc, s[22:23], v[8:9]
	v_readlane_b32 s23, v9, 53
	s_movk_i32 s22, 10
	v_addc_co_u32_e32 v2, vcc, 0, v2, vcc
	v_cmp_gt_i64_e32 vcc, s[24:25], v[8:9]
	v_readlane_b32 s25, v9, 54
	s_movk_i32 s24, 9
	v_addc_co_u32_e32 v2, vcc, 0, v2, vcc
	v_cmp_gt_i64_e32 vcc, s[22:23], v[8:9]
	v_readlane_b32 s23, v9, 55
	s_movk_i32 s22, 8
	v_addc_co_u32_e32 v2, vcc, 0, v2, vcc
	v_cmp_gt_i64_e32 vcc, s[24:25], v[8:9]
	v_readlane_b32 s25, v9, 56
	s_movk_i32 s24, 7
	v_addc_co_u32_e32 v2, vcc, 0, v2, vcc
	v_cmp_gt_i64_e32 vcc, s[22:23], v[8:9]
	v_readlane_b32 s23, v9, 57
	s_movk_i32 s22, 6
	v_addc_co_u32_e32 v2, vcc, 0, v2, vcc
	v_cmp_gt_i64_e32 vcc, s[24:25], v[8:9]
	v_readlane_b32 s25, v9, 58
	s_movk_i32 s24, 5
	v_addc_co_u32_e32 v2, vcc, 0, v2, vcc
	v_cmp_gt_i64_e32 vcc, s[22:23], v[8:9]
	v_readlane_b32 s23, v9, 59
	s_movk_i32 s22, 4
	v_addc_co_u32_e32 v2, vcc, 0, v2, vcc
	v_cmp_gt_i64_e32 vcc, s[24:25], v[8:9]
	v_readlane_b32 s25, v9, 60
	s_movk_i32 s24, 3
	v_addc_co_u32_e32 v2, vcc, 0, v2, vcc
	v_cmp_gt_i64_e32 vcc, s[22:23], v[8:9]
	v_readlane_b32 s23, v9, 61
	s_movk_i32 s22, 2
	v_addc_co_u32_e32 v2, vcc, 0, v2, vcc
	v_cmp_gt_i64_e32 vcc, s[24:25], v[8:9]
	v_readlane_b32 s25, v9, 62
	s_movk_i32 s24, 1
	v_addc_co_u32_e32 v2, vcc, 0, v2, vcc
	v_cmp_gt_i64_e32 vcc, s[22:23], v[8:9]
	v_readlane_b32 s23, v9, 63
	s_movk_i32 s22, 0
	v_addc_co_u32_e32 v2, vcc, 0, v2, vcc
	v_cmp_gt_i64_e32 vcc, s[24:25], v[8:9]
	s_nop 1
	v_addc_co_u32_e32 v2, vcc, 0, v2, vcc
	v_cmp_gt_i64_e32 vcc, s[22:23], v[8:9]
	s_nop 1
	v_addc_co_u32_e32 v2, vcc, 0, v2, vcc
	v_cmp_gt_u32_e32 vcc, 6, v2
	s_nop 1
	v_cndmask_b32_e32 v6, 0, v5, vcc
	ds_bpermute_b32 v7, v1, v6
	s_waitcnt lgkmcnt(0)
	v_add_f32_e32 v6, v6, v7
	ds_bpermute_b32 v7, v201, v6
	s_waitcnt lgkmcnt(0)
	v_add_f32_e32 v6, v6, v7
	ds_bpermute_b32 v7, v220, v6
	s_waitcnt lgkmcnt(0)
	v_add_f32_e32 v6, v6, v7
	ds_bpermute_b32 v7, v221, v6
	s_waitcnt lgkmcnt(0)
	v_add_f32_e32 v6, v6, v7
	ds_bpermute_b32 v7, v222, v6
	s_waitcnt lgkmcnt(0)
	v_add_f32_e32 v6, v6, v7
	ds_bpermute_b32 v7, v223, v6
	s_and_saveexec_b64 s[22:23], vcc
	s_cbranch_execz .LBB0_551
	s_waitcnt lgkmcnt(0)
	v_add_f32_e32 v10, v6, v7
	v_mad_u64_u32 v[6:7], s[4:5], s4, 6, v[2:3]
	v_div_scale_f32 v2, s[4:5], v10, v10, v5
	v_rcp_f32_e32 v12, v2
	v_ashrrev_i32_e32 v7, 31, v6
	v_lshlrev_b64 v[6:7], 2, v[6:7]
	v_lshl_add_u64 v[8:9], s[26:27], 0, v[6:7]
	ds_add_rtn_u32 v11, v227, v243
	global_store_dword v[8:9], v230, off
	v_fma_f32 v8, -v2, v12, 1.0
	v_fmac_f32_e32 v12, v8, v12
	v_div_scale_f32 v8, vcc, v5, v10, v5
	v_mul_f32_e32 v9, v8, v12
	v_fma_f32 v13, -v2, v9, v8
	v_fmac_f32_e32 v9, v13, v12
	v_fma_f32 v2, -v2, v9, v8
	v_div_fmas_f32 v2, v2, v12, v9
	v_div_fixup_f32 v2, v2, v10, v5
	v_mul_f32_e32 v2, 0x40200000, v2
	v_lshl_add_u64 v[8:9], s[28:29], 0, v[6:7]
	v_lshl_add_u64 v[6:7], s[30:31], 0, v[6:7]
	global_store_dword v[8:9], v2, off
	s_waitcnt lgkmcnt(0)
	global_store_dword v[6:7], v11, off
; __device__ __forceinline__ void phase_nrr(const Frame& F, const Args& a, int l, const bf16_t* XA, const float* g, const float* modl, unsigned char* XN8) {
;     ...
;         for (int i = 0; i < 8; ++i) { const int t = tb + i;
;             const float lg = Pl[(w * 8 + i) * NE + lane] + Pl[(64 + w * 8 + i) * NE + lane]; const float sc = 1.f / (1.f + __expf(-lg)); const float bb = sc + bias;
;             float m1 = bb; m1 = fmaxf(m1, __shfl_xor(m1, 1)); m1 = fmaxf(m1, __shfl_xor(m1, 2)); m1 = fmaxf(m1, __shfl_xor(m1, 4));
;             const unsigned long long eq = __ballot(bb == m1); const int gbase = lane & ~7; const unsigned grpmask = (unsigned)((eq >> gbase) & 0xffull);
;             const int first = gbase + __builtin_ctz(grpmask);
;             float m2 = (lane == first) ? -INFINITY : bb; m2 = fmaxf(m2, __shfl_xor(m2, 1)); m2 = fmaxf(m2, __shfl_xor(m2, 2)); m2 = fmaxf(m2, __shfl_xor(m2, 4));
;             const float gsum = m1 + m2; const int gq = lane >> 3;
;             int grank = 0;
; #pragma unroll
;             for (int g2 = 0; g2 < 8; ++g2) { const float v = __int_as_float(__builtin_amdgcn_readlane(__float_as_int(gsum), g2 * 8)); grank += (v > gsum || (v == gsum && g2 < gq)) ? 1 : 0; }
;             const bool keep = grank < 4; const float val = keep ? bb : -INFINITY;
;             int rank = 0;
; #pragma unroll 8
;             for (int e2 = 0; e2 < 64; ++e2) { const float v = __int_as_float(__builtin_amdgcn_readlane(__float_as_int(val), e2)); rank += (v > val || (v == val && e2 < lane)) ? 1 : 0; }
.LBB0_551:
	s_or_b64 exec, exec, s[22:23]
	v_add_u32_e32 v2, s84, v226
	ds_read_b32 v2, v2
	ds_read_b32 v5, v4 offset:17408
	s_mov_b32 s3, 0
	s_waitcnt lgkmcnt(0)
	v_add_f32_e32 v2, v2, v5
	v_mul_f32_e32 v2, 0xbfb8aa3b, v2
	v_exp_f32_e32 v2, v2
	s_nop 0
	v_add_f32_e32 v2, 1.0, v2
	v_div_scale_f32 v5, s[4:5], v2, v2, 1.0
	v_rcp_f32_e32 v6, v5
	s_nop 0
	v_fma_f32 v7, -v5, v6, 1.0
	v_fmac_f32_e32 v6, v7, v6
	v_div_scale_f32 v7, vcc, 1.0, v2, 1.0
	v_mul_f32_e32 v8, v7, v6
	v_fma_f32 v9, -v5, v8, v7
	v_fmac_f32_e32 v8, v9, v6
	v_fma_f32 v5, -v5, v8, v7
	v_div_fmas_f32 v5, v5, v6, v8
	v_div_fixup_f32 v2, v5, v2, 1.0
	v_add_f32_e32 v5, v3, v2
	s_nop 1
	s_waitcnt lgkmcnt(0)
	v_max_f32_dpp v6, v5, v5 quad_perm:[1,0,3,2] row_mask:0xf bank_mask:0xf
	s_nop 1
	s_waitcnt lgkmcnt(0)
	v_max_f32_dpp v6, v6, v6 quad_perm:[2,3,0,1] row_mask:0xf bank_mask:0xf
	s_nop 1
	s_waitcnt lgkmcnt(0)
	v_max_f32_dpp v8, v6, v6 row_half_mirror row_mask:0xf bank_mask:0xf
	v_cmp_eq_f32_e32 vcc, v5, v8
	s_nop 1
	v_lshrrev_b64 v[6:7], v200, vcc
	v_ffbl_b32_sdwa v6, v6 dst_sel:DWORD dst_unused:UNUSED_PAD src0_sel:BYTE_0
	v_add_u32_e32 v6, v6, v200
	v_cmp_ne_u32_e32 vcc, v230, v6
	s_nop 1
	v_cndmask_b32_e32 v6, v245, v5, vcc
	s_nop 1
	s_waitcnt lgkmcnt(0)
	v_max_f32_dpp v6, v6, v6 quad_perm:[1,0,3,2] row_mask:0xf bank_mask:0xf
	s_nop 1
	s_waitcnt lgkmcnt(0)
	v_max_f32_dpp v6, v6, v6 quad_perm:[2,3,0,1] row_mask:0xf bank_mask:0xf
	s_nop 1
	s_waitcnt lgkmcnt(0)
	v_max_f32_dpp v6, v6, v6 row_half_mirror row_mask:0xf bank_mask:0xf
	v_add_f32_e32 v6, v8, v6
	s_nop 0
	v_readlane_b32 s4, v6, 0
	s_nop 1
	v_cmp_eq_f32_e64 s[22:23], s4, v6
	v_cmp_gt_f32_e32 vcc, s4, v6
	s_and_b64 s[4:5], s[6:7], s[22:23]
	s_or_b64 s[4:5], vcc, s[4:5]
	v_cndmask_b32_e64 v7, 0, 1, s[4:5]
	v_readlane_b32 s4, v6, 8
	s_nop 1
	v_cmp_eq_f32_e64 s[22:23], s4, v6
	v_cmp_gt_f32_e32 vcc, s4, v6
	s_and_b64 s[4:5], s[8:9], s[22:23]
	s_or_b64 s[4:5], vcc, s[4:5]
	v_cndmask_b32_e64 v8, 0, 1, s[4:5]
	v_readlane_b32 s4, v6, 16
	s_nop 1
	v_cmp_eq_f32_e64 s[22:23], s4, v6
	v_cmp_gt_f32_e32 vcc, s4, v6
	s_and_b64 s[4:5], s[10:11], s[22:23]
	s_or_b64 s[4:5], vcc, s[4:5]
	v_cndmask_b32_e64 v9, 0, 1, s[4:5]
	v_readlane_b32 s4, v6, 24
	s_nop 1
	v_cmp_eq_f32_e64 s[22:23], s4, v6
	v_cmp_gt_f32_e32 vcc, s4, v6
	s_and_b64 s[4:5], s[12:13], s[22:23]
	s_or_b64 s[4:5], vcc, s[4:5]
	v_cndmask_b32_e64 v10, 0, 1, s[4:5]
	v_readlane_b32 s4, v6, 32
	s_nop 1
	v_cmp_eq_f32_e64 s[22:23], s4, v6
	v_cmp_gt_f32_e32 vcc, s4, v6
	s_and_b64 s[4:5], s[14:15], s[22:23]
	s_or_b64 s[4:5], vcc, s[4:5]
	v_cndmask_b32_e64 v11, 0, 1, s[4:5]
	v_readlane_b32 s4, v6, 40
	s_nop 1
	v_cmp_eq_f32_e64 s[22:23], s4, v6
	v_cmp_gt_f32_e32 vcc, s4, v6
	s_and_b64 s[4:5], s[16:17], s[22:23]
	s_or_b64 s[4:5], vcc, s[4:5]
	v_cndmask_b32_e64 v12, 0, 1, s[4:5]
	v_readlane_b32 s4, v6, 48
	s_nop 1
	v_cmp_eq_f32_e64 s[22:23], s4, v6
	v_cmp_gt_f32_e32 vcc, s4, v6
	s_and_b64 s[4:5], s[18:19], s[22:23]
	s_or_b64 s[4:5], vcc, s[4:5]
	v_cndmask_b32_e64 v13, 0, 1, s[4:5]
	v_readlane_b32 s4, v6, 56
	s_nop 1
	v_cmp_gt_f32_e32 vcc, s4, v6
	s_nop 1
	v_cndmask_b32_e64 v6, 0, 1, vcc
	v_add_u32_e32 v6, v8, v6
	v_add3_u32 v6, v6, v7, v9
	v_add3_u32 v6, v6, v10, v11
	v_add3_u32 v6, v6, v12, v13
	v_cmp_gt_u32_e32 vcc, 4, v6
	v_mov_b32_e32 v6, 0
	s_nop 0
	v_cndmask_b32_e32 v5, v245, v5, vcc
	v_ashrrev_i32_e32 v9, 31, v5
	v_sub_u32_e32 v8, 63, v230
	v_and_b32_e32 v9, 0x7fffffff, v9
	v_xor_b32_e32 v9, v5, v9
	s_nop 0
	v_readlane_b32 s25, v9, 0
	s_movk_i32 s24, 63
	v_readlane_b32 s23, v9, 1
	s_movk_i32 s22, 62
	v_cmp_gt_i64_e32 vcc, s[24:25], v[8:9]
	v_readlane_b32 s25, v9, 2
	s_movk_i32 s24, 61
	v_addc_co_u32_e32 v6, vcc, 0, v6, vcc
	v_cmp_gt_i64_e32 vcc, s[22:23], v[8:9]
	v_readlane_b32 s23, v9, 3
	s_movk_i32 s22, 60
	v_addc_co_u32_e32 v6, vcc, 0, v6, vcc
	v_cmp_gt_i64_e32 vcc, s[24:25], v[8:9]
	v_readlane_b32 s25, v9, 4
	s_movk_i32 s24, 59
	v_addc_co_u32_e32 v6, vcc, 0, v6, vcc
	v_cmp_gt_i64_e32 vcc, s[22:23], v[8:9]
	v_readlane_b32 s23, v9, 5
	s_movk_i32 s22, 58
	v_addc_co_u32_e32 v6, vcc, 0, v6, vcc
	v_cmp_gt_i64_e32 vcc, s[24:25], v[8:9]
	v_readlane_b32 s25, v9, 6
	s_movk_i32 s24, 57
	v_addc_co_u32_e32 v6, vcc, 0, v6, vcc
	v_cmp_gt_i64_e32 vcc, s[22:23], v[8:9]
	v_readlane_b32 s23, v9, 7
	s_movk_i32 s22, 56
	v_addc_co_u32_e32 v6, vcc, 0, v6, vcc
	v_cmp_gt_i64_e32 vcc, s[24:25], v[8:9]
	v_readlane_b32 s25, v9, 8
	s_movk_i32 s24, 55
	v_addc_co_u32_e32 v6, vcc, 0, v6, vcc
	v_cmp_gt_i64_e32 vcc, s[22:23], v[8:9]
	v_readlane_b32 s23, v9, 9
	s_movk_i32 s22, 54
	v_addc_co_u32_e32 v6, vcc, 0, v6, vcc
	v_cmp_gt_i64_e32 vcc, s[24:25], v[8:9]
	v_readlane_b32 s25, v9, 10
	s_movk_i32 s24, 53
	v_addc_co_u32_e32 v6, vcc, 0, v6, vcc
	v_cmp_gt_i64_e32 vcc, s[22:23], v[8:9]
	v_readlane_b32 s23, v9, 11
	s_movk_i32 s22, 52
	v_addc_co_u32_e32 v6, vcc, 0, v6, vcc
	v_cmp_gt_i64_e32 vcc, s[24:25], v[8:9]
	v_readlane_b32 s25, v9, 12
	s_movk_i32 s24, 51
	v_addc_co_u32_e32 v6, vcc, 0, v6, vcc
	v_cmp_gt_i64_e32 vcc, s[22:23], v[8:9]
	v_readlane_b32 s23, v9, 13
	s_movk_i32 s22, 50
	v_addc_co_u32_e32 v6, vcc, 0, v6, vcc
	v_cmp_gt_i64_e32 vcc, s[24:25], v[8:9]
	v_readlane_b32 s25, v9, 14
	s_movk_i32 s24, 49
	v_addc_co_u32_e32 v6, vcc, 0, v6, vcc
	v_cmp_gt_i64_e32 vcc, s[22:23], v[8:9]
	v_readlane_b32 s23, v9, 15
	s_movk_i32 s22, 48
	v_addc_co_u32_e32 v6, vcc, 0, v6, vcc
	v_cmp_gt_i64_e32 vcc, s[24:25], v[8:9]
	v_readlane_b32 s25, v9, 16
	s_movk_i32 s24, 47
	v_addc_co_u32_e32 v6, vcc, 0, v6, vcc
	v_cmp_gt_i64_e32 vcc, s[22:23], v[8:9]
	v_readlane_b32 s23, v9, 17
	s_movk_i32 s22, 46
	v_addc_co_u32_e32 v6, vcc, 0, v6, vcc
	v_cmp_gt_i64_e32 vcc, s[24:25], v[8:9]
	v_readlane_b32 s25, v9, 18
	s_movk_i32 s24, 45
; __device__ __forceinline__ void phase_nrr(const Frame& F, const Args& a, int l, const bf16_t* XA, const float* g, const float* modl, unsigned char* XN8) {
;     ...
;             int rank = 0;
; #pragma unroll 8
;             for (int e2 = 0; e2 < 64; ++e2) { const float v = __int_as_float(__builtin_amdgcn_readlane(__float_as_int(val), e2)); rank += (v > val || (v == val && e2 < lane)) ? 1 : 0; }
;             const bool sel = rank < TOPK;
;             const float ssum = wave_sum(sel ? sc : 0.f);
	v_addc_co_u32_e32 v6, vcc, 0, v6, vcc
	v_cmp_gt_i64_e32 vcc, s[22:23], v[8:9]
	v_readlane_b32 s23, v9, 19
	s_movk_i32 s22, 44
	v_addc_co_u32_e32 v6, vcc, 0, v6, vcc
	v_cmp_gt_i64_e32 vcc, s[24:25], v[8:9]
	v_readlane_b32 s25, v9, 20
	s_movk_i32 s24, 43
	v_addc_co_u32_e32 v6, vcc, 0, v6, vcc
	v_cmp_gt_i64_e32 vcc, s[22:23], v[8:9]
	v_readlane_b32 s23, v9, 21
	s_movk_i32 s22, 42
	v_addc_co_u32_e32 v6, vcc, 0, v6, vcc
	v_cmp_gt_i64_e32 vcc, s[24:25], v[8:9]
	v_readlane_b32 s25, v9, 22
	s_movk_i32 s24, 41
	v_addc_co_u32_e32 v6, vcc, 0, v6, vcc
	v_cmp_gt_i64_e32 vcc, s[22:23], v[8:9]
	v_readlane_b32 s23, v9, 23
	s_movk_i32 s22, 40
	v_addc_co_u32_e32 v6, vcc, 0, v6, vcc
	v_cmp_gt_i64_e32 vcc, s[24:25], v[8:9]
	v_readlane_b32 s25, v9, 24
	s_movk_i32 s24, 39
	v_addc_co_u32_e32 v6, vcc, 0, v6, vcc
	v_cmp_gt_i64_e32 vcc, s[22:23], v[8:9]
	v_readlane_b32 s23, v9, 25
	s_movk_i32 s22, 38
	v_addc_co_u32_e32 v6, vcc, 0, v6, vcc
	v_cmp_gt_i64_e32 vcc, s[24:25], v[8:9]
	v_readlane_b32 s25, v9, 26
	s_movk_i32 s24, 37
	v_addc_co_u32_e32 v6, vcc, 0, v6, vcc
	v_cmp_gt_i64_e32 vcc, s[22:23], v[8:9]
	v_readlane_b32 s23, v9, 27
	s_movk_i32 s22, 36
	v_addc_co_u32_e32 v6, vcc, 0, v6, vcc
	v_cmp_gt_i64_e32 vcc, s[24:25], v[8:9]
	v_readlane_b32 s25, v9, 28
	s_movk_i32 s24, 35
	v_addc_co_u32_e32 v6, vcc, 0, v6, vcc
	v_cmp_gt_i64_e32 vcc, s[22:23], v[8:9]
	v_readlane_b32 s23, v9, 29
	s_movk_i32 s22, 34
	v_addc_co_u32_e32 v6, vcc, 0, v6, vcc
	v_cmp_gt_i64_e32 vcc, s[24:25], v[8:9]
	v_readlane_b32 s25, v9, 30
	s_movk_i32 s24, 33
	v_addc_co_u32_e32 v6, vcc, 0, v6, vcc
	v_cmp_gt_i64_e32 vcc, s[22:23], v[8:9]
	v_readlane_b32 s23, v9, 31
	s_movk_i32 s22, 32
	v_addc_co_u32_e32 v6, vcc, 0, v6, vcc
	v_cmp_gt_i64_e32 vcc, s[24:25], v[8:9]
	v_readlane_b32 s25, v9, 32
	s_movk_i32 s24, 31
	v_addc_co_u32_e32 v6, vcc, 0, v6, vcc
	v_cmp_gt_i64_e32 vcc, s[22:23], v[8:9]
	v_readlane_b32 s23, v9, 33
	s_movk_i32 s22, 30
	v_addc_co_u32_e32 v6, vcc, 0, v6, vcc
	v_cmp_gt_i64_e32 vcc, s[24:25], v[8:9]
	v_readlane_b32 s25, v9, 34
	s_movk_i32 s24, 29
	v_addc_co_u32_e32 v6, vcc, 0, v6, vcc
	v_cmp_gt_i64_e32 vcc, s[22:23], v[8:9]
	v_readlane_b32 s23, v9, 35
	s_movk_i32 s22, 28
	v_addc_co_u32_e32 v6, vcc, 0, v6, vcc
	v_cmp_gt_i64_e32 vcc, s[24:25], v[8:9]
	v_readlane_b32 s25, v9, 36
	s_movk_i32 s24, 27
	v_addc_co_u32_e32 v6, vcc, 0, v6, vcc
	v_cmp_gt_i64_e32 vcc, s[22:23], v[8:9]
	v_readlane_b32 s23, v9, 37
	s_movk_i32 s22, 26
	v_addc_co_u32_e32 v6, vcc, 0, v6, vcc
	v_cmp_gt_i64_e32 vcc, s[24:25], v[8:9]
	v_readlane_b32 s25, v9, 38
	s_movk_i32 s24, 25
	v_addc_co_u32_e32 v6, vcc, 0, v6, vcc
	v_cmp_gt_i64_e32 vcc, s[22:23], v[8:9]
	v_readlane_b32 s23, v9, 39
	s_movk_i32 s22, 24
	v_addc_co_u32_e32 v6, vcc, 0, v6, vcc
	v_cmp_gt_i64_e32 vcc, s[24:25], v[8:9]
	v_readlane_b32 s25, v9, 40
	s_movk_i32 s24, 23
	v_addc_co_u32_e32 v6, vcc, 0, v6, vcc
	v_cmp_gt_i64_e32 vcc, s[22:23], v[8:9]
	v_readlane_b32 s23, v9, 41
	s_movk_i32 s22, 22
	v_addc_co_u32_e32 v6, vcc, 0, v6, vcc
	v_cmp_gt_i64_e32 vcc, s[24:25], v[8:9]
	v_readlane_b32 s25, v9, 42
	s_movk_i32 s24, 21
	v_addc_co_u32_e32 v6, vcc, 0, v6, vcc
	v_cmp_gt_i64_e32 vcc, s[22:23], v[8:9]
	v_readlane_b32 s23, v9, 43
	s_movk_i32 s22, 20
	v_addc_co_u32_e32 v6, vcc, 0, v6, vcc
	v_cmp_gt_i64_e32 vcc, s[24:25], v[8:9]
	v_readlane_b32 s25, v9, 44
	s_movk_i32 s24, 19
	v_addc_co_u32_e32 v6, vcc, 0, v6, vcc
	v_cmp_gt_i64_e32 vcc, s[22:23], v[8:9]
	v_readlane_b32 s23, v9, 45
	s_movk_i32 s22, 18
	v_addc_co_u32_e32 v6, vcc, 0, v6, vcc
	v_cmp_gt_i64_e32 vcc, s[24:25], v[8:9]
	v_readlane_b32 s25, v9, 46
	s_movk_i32 s24, 17
	v_addc_co_u32_e32 v6, vcc, 0, v6, vcc
	v_cmp_gt_i64_e32 vcc, s[22:23], v[8:9]
	v_readlane_b32 s23, v9, 47
	s_movk_i32 s22, 16
	v_addc_co_u32_e32 v6, vcc, 0, v6, vcc
	v_cmp_gt_i64_e32 vcc, s[24:25], v[8:9]
	v_readlane_b32 s25, v9, 48
	s_movk_i32 s24, 15
	v_addc_co_u32_e32 v6, vcc, 0, v6, vcc
	v_cmp_gt_i64_e32 vcc, s[22:23], v[8:9]
	v_readlane_b32 s23, v9, 49
	s_movk_i32 s22, 14
	v_addc_co_u32_e32 v6, vcc, 0, v6, vcc
	v_cmp_gt_i64_e32 vcc, s[24:25], v[8:9]
	v_readlane_b32 s25, v9, 50
	s_movk_i32 s24, 13
	v_addc_co_u32_e32 v6, vcc, 0, v6, vcc
	v_cmp_gt_i64_e32 vcc, s[22:23], v[8:9]
	v_readlane_b32 s23, v9, 51
	s_movk_i32 s22, 12
	v_addc_co_u32_e32 v6, vcc, 0, v6, vcc
	v_cmp_gt_i64_e32 vcc, s[24:25], v[8:9]
	v_readlane_b32 s25, v9, 52
	s_movk_i32 s24, 11
	v_addc_co_u32_e32 v6, vcc, 0, v6, vcc
	v_cmp_gt_i64_e32 vcc, s[22:23], v[8:9]
	v_readlane_b32 s23, v9, 53
	s_movk_i32 s22, 10
	v_addc_co_u32_e32 v6, vcc, 0, v6, vcc
	v_cmp_gt_i64_e32 vcc, s[24:25], v[8:9]
	v_readlane_b32 s25, v9, 54
	s_movk_i32 s24, 9
	v_addc_co_u32_e32 v6, vcc, 0, v6, vcc
	v_cmp_gt_i64_e32 vcc, s[22:23], v[8:9]
	v_readlane_b32 s23, v9, 55
	s_movk_i32 s22, 8
	v_addc_co_u32_e32 v6, vcc, 0, v6, vcc
	v_cmp_gt_i64_e32 vcc, s[24:25], v[8:9]
	v_readlane_b32 s25, v9, 56
	s_movk_i32 s24, 7
	v_addc_co_u32_e32 v6, vcc, 0, v6, vcc
	v_cmp_gt_i64_e32 vcc, s[22:23], v[8:9]
	v_readlane_b32 s23, v9, 57
	s_movk_i32 s22, 6
	v_addc_co_u32_e32 v6, vcc, 0, v6, vcc
	v_cmp_gt_i64_e32 vcc, s[24:25], v[8:9]
	v_readlane_b32 s25, v9, 58
	s_movk_i32 s24, 5
	v_addc_co_u32_e32 v6, vcc, 0, v6, vcc
	v_cmp_gt_i64_e32 vcc, s[22:23], v[8:9]
	v_readlane_b32 s23, v9, 59
	s_movk_i32 s22, 4
	v_addc_co_u32_e32 v6, vcc, 0, v6, vcc
	v_cmp_gt_i64_e32 vcc, s[24:25], v[8:9]
	v_readlane_b32 s25, v9, 60
	s_movk_i32 s24, 3
	v_addc_co_u32_e32 v6, vcc, 0, v6, vcc
	v_cmp_gt_i64_e32 vcc, s[22:23], v[8:9]
	v_readlane_b32 s23, v9, 61
	s_movk_i32 s22, 2
	v_addc_co_u32_e32 v6, vcc, 0, v6, vcc
	v_cmp_gt_i64_e32 vcc, s[24:25], v[8:9]
	v_readlane_b32 s25, v9, 62
	s_movk_i32 s24, 1
	v_addc_co_u32_e32 v6, vcc, 0, v6, vcc
	v_cmp_gt_i64_e32 vcc, s[22:23], v[8:9]
	v_readlane_b32 s23, v9, 63
	s_movk_i32 s22, 0
	v_addc_co_u32_e32 v6, vcc, 0, v6, vcc
	v_cmp_gt_i64_e32 vcc, s[24:25], v[8:9]
	s_nop 1
	v_addc_co_u32_e32 v6, vcc, 0, v6, vcc
	v_cmp_gt_i64_e32 vcc, s[22:23], v[8:9]
	s_nop 1
	v_addc_co_u32_e32 v6, vcc, 0, v6, vcc
	v_cmp_gt_u32_e32 vcc, 6, v6
	s_nop 1
	v_cndmask_b32_e32 v5, 0, v2, vcc
	ds_bpermute_b32 v7, v1, v5
	s_waitcnt lgkmcnt(0)
	v_add_f32_e32 v5, v5, v7
	ds_bpermute_b32 v7, v201, v5
	s_waitcnt lgkmcnt(0)
	v_add_f32_e32 v5, v5, v7
	ds_bpermute_b32 v7, v220, v5
	s_waitcnt lgkmcnt(0)
	v_add_f32_e32 v5, v5, v7
	ds_bpermute_b32 v7, v221, v5
	s_waitcnt lgkmcnt(0)
	v_add_f32_e32 v5, v5, v7
	ds_bpermute_b32 v7, v222, v5
	s_waitcnt lgkmcnt(0)
	v_add_f32_e32 v5, v5, v7
	ds_bpermute_b32 v7, v223, v5
	s_and_saveexec_b64 s[4:5], vcc
	s_cbranch_execz .LBB0_555
; __device__ __forceinline__ void phase_nrr(const Frame& F, const Args& a, int l, const bf16_t* XA, const float* g, const float* modl, unsigned char* XN8) {
;     ...
;         for (int i = 0; i < 8; ++i) { const int t = tb + i;
;             const float lg = Pl[(w * 8 + i) * NE + lane] + Pl[(64 + w * 8 + i) * NE + lane]; const float sc = 1.f / (1.f + __expf(-lg)); const float bb = sc + bias;
;             float m1 = bb; m1 = fmaxf(m1, __shfl_xor(m1, 1)); m1 = fmaxf(m1, __shfl_xor(m1, 2)); m1 = fmaxf(m1, __shfl_xor(m1, 4));
;             const unsigned long long eq = __ballot(bb == m1); const int gbase = lane & ~7; const unsigned grpmask = (unsigned)((eq >> gbase) & 0xffull);
;             const int first = gbase + __builtin_ctz(grpmask);
;             float m2 = (lane == first) ? -INFINITY : bb; m2 = fmaxf(m2, __shfl_xor(m2, 1)); m2 = fmaxf(m2, __shfl_xor(m2, 2)); m2 = fmaxf(m2, __shfl_xor(m2, 4));
;             const float gsum = m1 + m2; const int gq = lane >> 3;
;             int grank = 0;
; #pragma unroll
;             for (int g2 = 0; g2 < 8; ++g2) { const float v = __int_as_float(__builtin_amdgcn_readlane(__float_as_int(gsum), g2 * 8)); grank += (v > gsum || (v == gsum && g2 < gq)) ? 1 : 0; }
;             const bool keep = grank < 4; const float val = keep ? bb : -INFINITY;
;             int rank = 0;
; #pragma unroll 8
;             for (int e2 = 0; e2 < 64; ++e2) { const float v = __int_as_float(__builtin_amdgcn_readlane(__float_as_int(val), e2)); rank += (v > val || (v == val && e2 < lane)) ? 1 : 0; }
;             const bool sel = rank < TOPK;
;             const float ssum = wave_sum(sel ? sc : 0.f);
;             if (sel) { const int p = atomicAdd((int*)(hist + lane), 1); top_e[t * TOPK + rank] = lane; gate[t * TOPK + rank] = sc / ssum * 2.5f; lpos[t * TOPK + rank] = p; }
	s_waitcnt lgkmcnt(0)
	v_add_f32_e32 v5, v5, v7
	s_mul_i32 s2, s2, 6
	v_or_b32_e32 v6, s2, v6
	v_div_scale_f32 v11, s[2:3], v5, v5, v2
	v_rcp_f32_e32 v12, v11
	v_ashrrev_i32_e32 v7, 31, v6
	v_lshlrev_b64 v[6:7], 2, v[6:7]
	v_lshl_add_u64 v[8:9], s[26:27], 0, v[6:7]
	ds_add_rtn_u32 v10, v227, v243
	global_store_dword v[8:9], v230, off
	v_fma_f32 v8, -v11, v12, 1.0
	v_fmac_f32_e32 v12, v8, v12
	v_div_scale_f32 v8, vcc, v2, v5, v2
	v_mul_f32_e32 v9, v8, v12
	v_fma_f32 v13, -v11, v9, v8
	v_fmac_f32_e32 v9, v13, v12
	v_fma_f32 v8, -v11, v9, v8
	v_div_fmas_f32 v8, v8, v12, v9
	v_div_fixup_f32 v2, v8, v5, v2
	v_mul_f32_e32 v2, 0x40200000, v2
	v_lshl_add_u64 v[8:9], s[28:29], 0, v[6:7]
	v_lshl_add_u64 v[6:7], s[30:31], 0, v[6:7]
	global_store_dword v[8:9], v2, off
	s_waitcnt lgkmcnt(0)
	global_store_dword v[6:7], v10, off
.LBB0_555:
	s_or_b64 exec, exec, s[4:5]
	v_add_u32_e32 v2, s85, v226
	ds_read_b32 v2, v2
	ds_read_b32 v5, v4 offset:17664
	s_waitcnt lgkmcnt(0)
	v_add_f32_e32 v2, v2, v5
	v_mul_f32_e32 v2, 0xbfb8aa3b, v2
	v_exp_f32_e32 v2, v2
	s_nop 0
	v_add_f32_e32 v2, 1.0, v2
	v_div_scale_f32 v5, s[2:3], v2, v2, 1.0
	v_rcp_f32_e32 v6, v5
	s_mov_b32 s2, 0
	v_fma_f32 v7, -v5, v6, 1.0
	v_fmac_f32_e32 v6, v7, v6
	v_div_scale_f32 v7, vcc, 1.0, v2, 1.0
	v_mul_f32_e32 v8, v7, v6
	v_fma_f32 v9, -v5, v8, v7
	v_fmac_f32_e32 v8, v9, v6
	v_fma_f32 v5, -v5, v8, v7
	v_div_fmas_f32 v5, v5, v6, v8
	v_div_fixup_f32 v2, v5, v2, 1.0
	v_add_f32_e32 v5, v3, v2
	s_nop 1
	s_waitcnt lgkmcnt(0)
	v_max_f32_dpp v6, v5, v5 quad_perm:[1,0,3,2] row_mask:0xf bank_mask:0xf
	s_nop 1
	s_waitcnt lgkmcnt(0)
	v_max_f32_dpp v6, v6, v6 quad_perm:[2,3,0,1] row_mask:0xf bank_mask:0xf
	s_nop 1
	s_waitcnt lgkmcnt(0)
	v_max_f32_dpp v8, v6, v6 row_half_mirror row_mask:0xf bank_mask:0xf
	v_cmp_eq_f32_e32 vcc, v5, v8
	s_nop 1
	v_lshrrev_b64 v[6:7], v200, vcc
	v_ffbl_b32_sdwa v6, v6 dst_sel:DWORD dst_unused:UNUSED_PAD src0_sel:BYTE_0
	v_add_u32_e32 v6, v6, v200
	v_cmp_ne_u32_e32 vcc, v230, v6
	s_nop 1
	v_cndmask_b32_e32 v6, v245, v5, vcc
	s_nop 1
	s_waitcnt lgkmcnt(0)
	v_max_f32_dpp v6, v6, v6 quad_perm:[1,0,3,2] row_mask:0xf bank_mask:0xf
	s_nop 1
	s_waitcnt lgkmcnt(0)
	v_max_f32_dpp v6, v6, v6 quad_perm:[2,3,0,1] row_mask:0xf bank_mask:0xf
	s_nop 1
	s_waitcnt lgkmcnt(0)
	v_max_f32_dpp v6, v6, v6 row_half_mirror row_mask:0xf bank_mask:0xf
	v_add_f32_e32 v6, v8, v6
	s_nop 0
	v_readlane_b32 s3, v6, 0
	s_nop 1
	v_cmp_eq_f32_e64 s[22:23], s3, v6
	v_cmp_gt_f32_e32 vcc, s3, v6
	s_and_b64 s[4:5], s[6:7], s[22:23]
	v_readlane_b32 s3, v6, 8
	s_or_b64 s[4:5], vcc, s[4:5]
	v_cndmask_b32_e64 v7, 0, 1, s[4:5]
	v_cmp_eq_f32_e64 s[22:23], s3, v6
	v_cmp_gt_f32_e32 vcc, s3, v6
	s_and_b64 s[4:5], s[8:9], s[22:23]
	v_readlane_b32 s3, v6, 16
	s_or_b64 s[4:5], vcc, s[4:5]
	v_cndmask_b32_e64 v8, 0, 1, s[4:5]
	v_cmp_eq_f32_e64 s[22:23], s3, v6
	v_cmp_gt_f32_e32 vcc, s3, v6
	s_and_b64 s[4:5], s[10:11], s[22:23]
	v_readlane_b32 s3, v6, 24
	s_or_b64 s[4:5], vcc, s[4:5]
	v_cndmask_b32_e64 v9, 0, 1, s[4:5]
	v_cmp_eq_f32_e64 s[22:23], s3, v6
	v_cmp_gt_f32_e32 vcc, s3, v6
	s_and_b64 s[4:5], s[12:13], s[22:23]
	v_readlane_b32 s3, v6, 32
	s_or_b64 s[4:5], vcc, s[4:5]
	v_cndmask_b32_e64 v10, 0, 1, s[4:5]
	v_cmp_eq_f32_e64 s[22:23], s3, v6
	v_cmp_gt_f32_e32 vcc, s3, v6
	s_and_b64 s[4:5], s[14:15], s[22:23]
	v_readlane_b32 s3, v6, 40
	s_or_b64 s[4:5], vcc, s[4:5]
	v_cndmask_b32_e64 v11, 0, 1, s[4:5]
	v_cmp_eq_f32_e64 s[22:23], s3, v6
	v_cmp_gt_f32_e32 vcc, s3, v6
	s_and_b64 s[4:5], s[16:17], s[22:23]
	v_readlane_b32 s3, v6, 48
	s_or_b64 s[4:5], vcc, s[4:5]
	v_cndmask_b32_e64 v12, 0, 1, s[4:5]
	v_cmp_eq_f32_e64 s[22:23], s3, v6
	v_cmp_gt_f32_e32 vcc, s3, v6
	s_and_b64 s[4:5], s[18:19], s[22:23]
	v_readlane_b32 s3, v6, 56
	s_or_b64 s[4:5], vcc, s[4:5]
	v_cndmask_b32_e64 v13, 0, 1, s[4:5]
	v_cmp_gt_f32_e32 vcc, s3, v6
	s_nop 1
	v_cndmask_b32_e64 v6, 0, 1, vcc
	v_add_u32_e32 v6, v8, v6
	v_add3_u32 v6, v6, v7, v9
	v_add3_u32 v6, v6, v10, v11
	v_add3_u32 v6, v6, v12, v13
	v_cmp_gt_u32_e32 vcc, 4, v6
	v_mov_b32_e32 v6, 0
	s_nop 0
	v_cndmask_b32_e32 v5, v245, v5, vcc
	v_ashrrev_i32_e32 v9, 31, v5
	v_sub_u32_e32 v8, 63, v230
	v_and_b32_e32 v9, 0x7fffffff, v9
	v_xor_b32_e32 v9, v5, v9
	s_nop 0
	v_readlane_b32 s25, v9, 0
	s_movk_i32 s24, 63
	v_readlane_b32 s23, v9, 1
	s_movk_i32 s22, 62
	v_cmp_gt_i64_e32 vcc, s[24:25], v[8:9]
	v_readlane_b32 s25, v9, 2
	s_movk_i32 s24, 61
	v_addc_co_u32_e32 v6, vcc, 0, v6, vcc
	v_cmp_gt_i64_e32 vcc, s[22:23], v[8:9]
	v_readlane_b32 s23, v9, 3
	s_movk_i32 s22, 60
	v_addc_co_u32_e32 v6, vcc, 0, v6, vcc
	v_cmp_gt_i64_e32 vcc, s[24:25], v[8:9]
	v_readlane_b32 s25, v9, 4
	s_movk_i32 s24, 59
	v_addc_co_u32_e32 v6, vcc, 0, v6, vcc
	v_cmp_gt_i64_e32 vcc, s[22:23], v[8:9]
	v_readlane_b32 s23, v9, 5
	s_movk_i32 s22, 58
	v_addc_co_u32_e32 v6, vcc, 0, v6, vcc
	v_cmp_gt_i64_e32 vcc, s[24:25], v[8:9]
	v_readlane_b32 s25, v9, 6
	s_movk_i32 s24, 57
	v_addc_co_u32_e32 v6, vcc, 0, v6, vcc
	v_cmp_gt_i64_e32 vcc, s[22:23], v[8:9]
	v_readlane_b32 s23, v9, 7
	s_movk_i32 s22, 56
	v_addc_co_u32_e32 v6, vcc, 0, v6, vcc
	v_cmp_gt_i64_e32 vcc, s[24:25], v[8:9]
	v_readlane_b32 s25, v9, 8
	s_movk_i32 s24, 55
	v_addc_co_u32_e32 v6, vcc, 0, v6, vcc
	v_cmp_gt_i64_e32 vcc, s[22:23], v[8:9]
	v_readlane_b32 s23, v9, 9
	s_movk_i32 s22, 54
	v_addc_co_u32_e32 v6, vcc, 0, v6, vcc
	v_cmp_gt_i64_e32 vcc, s[24:25], v[8:9]
	v_readlane_b32 s25, v9, 10
	s_movk_i32 s24, 53
	v_addc_co_u32_e32 v6, vcc, 0, v6, vcc
	v_cmp_gt_i64_e32 vcc, s[22:23], v[8:9]
	v_readlane_b32 s23, v9, 11
	s_movk_i32 s22, 52
	v_addc_co_u32_e32 v6, vcc, 0, v6, vcc
	v_cmp_gt_i64_e32 vcc, s[24:25], v[8:9]
	v_readlane_b32 s25, v9, 12
	s_movk_i32 s24, 51
	v_addc_co_u32_e32 v6, vcc, 0, v6, vcc
; __device__ __forceinline__ void phase_nrr(const Frame& F, const Args& a, int l, const bf16_t* XA, const float* g, const float* modl, unsigned char* XN8) {
;     ...
;             int rank = 0;
; #pragma unroll 8
;             for (int e2 = 0; e2 < 64; ++e2) { const float v = __int_as_float(__builtin_amdgcn_readlane(__float_as_int(val), e2)); rank += (v > val || (v == val && e2 < lane)) ? 1 : 0; }
	v_cmp_gt_i64_e32 vcc, s[22:23], v[8:9]
	v_readlane_b32 s23, v9, 13
	s_movk_i32 s22, 50
	v_addc_co_u32_e32 v6, vcc, 0, v6, vcc
	v_cmp_gt_i64_e32 vcc, s[24:25], v[8:9]
	v_readlane_b32 s25, v9, 14
	s_movk_i32 s24, 49
	v_addc_co_u32_e32 v6, vcc, 0, v6, vcc
	v_cmp_gt_i64_e32 vcc, s[22:23], v[8:9]
	v_readlane_b32 s23, v9, 15
	s_movk_i32 s22, 48
	v_addc_co_u32_e32 v6, vcc, 0, v6, vcc
	v_cmp_gt_i64_e32 vcc, s[24:25], v[8:9]
	v_readlane_b32 s25, v9, 16
	s_movk_i32 s24, 47
	v_addc_co_u32_e32 v6, vcc, 0, v6, vcc
	v_cmp_gt_i64_e32 vcc, s[22:23], v[8:9]
	v_readlane_b32 s23, v9, 17
	s_movk_i32 s22, 46
	v_addc_co_u32_e32 v6, vcc, 0, v6, vcc
	v_cmp_gt_i64_e32 vcc, s[24:25], v[8:9]
	v_readlane_b32 s25, v9, 18
	s_movk_i32 s24, 45
	v_addc_co_u32_e32 v6, vcc, 0, v6, vcc
	v_cmp_gt_i64_e32 vcc, s[22:23], v[8:9]
	v_readlane_b32 s23, v9, 19
	s_movk_i32 s22, 44
	v_addc_co_u32_e32 v6, vcc, 0, v6, vcc
	v_cmp_gt_i64_e32 vcc, s[24:25], v[8:9]
	v_readlane_b32 s25, v9, 20
	s_movk_i32 s24, 43
	v_addc_co_u32_e32 v6, vcc, 0, v6, vcc
	v_cmp_gt_i64_e32 vcc, s[22:23], v[8:9]
	v_readlane_b32 s23, v9, 21
	s_movk_i32 s22, 42
	v_addc_co_u32_e32 v6, vcc, 0, v6, vcc
	v_cmp_gt_i64_e32 vcc, s[24:25], v[8:9]
	v_readlane_b32 s25, v9, 22
	s_movk_i32 s24, 41
	v_addc_co_u32_e32 v6, vcc, 0, v6, vcc
	v_cmp_gt_i64_e32 vcc, s[22:23], v[8:9]
	v_readlane_b32 s23, v9, 23
	s_movk_i32 s22, 40
	v_addc_co_u32_e32 v6, vcc, 0, v6, vcc
	v_cmp_gt_i64_e32 vcc, s[24:25], v[8:9]
	v_readlane_b32 s25, v9, 24
	s_movk_i32 s24, 39
	v_addc_co_u32_e32 v6, vcc, 0, v6, vcc
	v_cmp_gt_i64_e32 vcc, s[22:23], v[8:9]
	v_readlane_b32 s23, v9, 25
	s_movk_i32 s22, 38
	v_addc_co_u32_e32 v6, vcc, 0, v6, vcc
	v_cmp_gt_i64_e32 vcc, s[24:25], v[8:9]
	v_readlane_b32 s25, v9, 26
	s_movk_i32 s24, 37
	v_addc_co_u32_e32 v6, vcc, 0, v6, vcc
	v_cmp_gt_i64_e32 vcc, s[22:23], v[8:9]
	v_readlane_b32 s23, v9, 27
	s_movk_i32 s22, 36
	v_addc_co_u32_e32 v6, vcc, 0, v6, vcc
	v_cmp_gt_i64_e32 vcc, s[24:25], v[8:9]
	v_readlane_b32 s25, v9, 28
	s_movk_i32 s24, 35
	v_addc_co_u32_e32 v6, vcc, 0, v6, vcc
	v_cmp_gt_i64_e32 vcc, s[22:23], v[8:9]
	v_readlane_b32 s23, v9, 29
	s_movk_i32 s22, 34
	v_addc_co_u32_e32 v6, vcc, 0, v6, vcc
	v_cmp_gt_i64_e32 vcc, s[24:25], v[8:9]
	v_readlane_b32 s25, v9, 30
	s_movk_i32 s24, 33
	v_addc_co_u32_e32 v6, vcc, 0, v6, vcc
	v_cmp_gt_i64_e32 vcc, s[22:23], v[8:9]
	v_readlane_b32 s23, v9, 31
	s_movk_i32 s22, 32
	v_addc_co_u32_e32 v6, vcc, 0, v6, vcc
	v_cmp_gt_i64_e32 vcc, s[24:25], v[8:9]
	v_readlane_b32 s25, v9, 32
	s_movk_i32 s24, 31
	v_addc_co_u32_e32 v6, vcc, 0, v6, vcc
	v_cmp_gt_i64_e32 vcc, s[22:23], v[8:9]
	v_readlane_b32 s23, v9, 33
	s_movk_i32 s22, 30
	v_addc_co_u32_e32 v6, vcc, 0, v6, vcc
	v_cmp_gt_i64_e32 vcc, s[24:25], v[8:9]
	v_readlane_b32 s25, v9, 34
	s_movk_i32 s24, 29
	v_addc_co_u32_e32 v6, vcc, 0, v6, vcc
	v_cmp_gt_i64_e32 vcc, s[22:23], v[8:9]
	v_readlane_b32 s23, v9, 35
	s_movk_i32 s22, 28
	v_addc_co_u32_e32 v6, vcc, 0, v6, vcc
	v_cmp_gt_i64_e32 vcc, s[24:25], v[8:9]
	v_readlane_b32 s25, v9, 36
	s_movk_i32 s24, 27
	v_addc_co_u32_e32 v6, vcc, 0, v6, vcc
	v_cmp_gt_i64_e32 vcc, s[22:23], v[8:9]
	v_readlane_b32 s23, v9, 37
	s_movk_i32 s22, 26
	v_addc_co_u32_e32 v6, vcc, 0, v6, vcc
	v_cmp_gt_i64_e32 vcc, s[24:25], v[8:9]
	v_readlane_b32 s25, v9, 38
	s_movk_i32 s24, 25
	v_addc_co_u32_e32 v6, vcc, 0, v6, vcc
	v_cmp_gt_i64_e32 vcc, s[22:23], v[8:9]
	v_readlane_b32 s23, v9, 39
	s_movk_i32 s22, 24
	v_addc_co_u32_e32 v6, vcc, 0, v6, vcc
	v_cmp_gt_i64_e32 vcc, s[24:25], v[8:9]
	v_readlane_b32 s25, v9, 40
	s_movk_i32 s24, 23
	v_addc_co_u32_e32 v6, vcc, 0, v6, vcc
	v_cmp_gt_i64_e32 vcc, s[22:23], v[8:9]
	v_readlane_b32 s23, v9, 41
	s_movk_i32 s22, 22
	v_addc_co_u32_e32 v6, vcc, 0, v6, vcc
	v_cmp_gt_i64_e32 vcc, s[24:25], v[8:9]
	v_readlane_b32 s25, v9, 42
	s_movk_i32 s24, 21
	v_addc_co_u32_e32 v6, vcc, 0, v6, vcc
	v_cmp_gt_i64_e32 vcc, s[22:23], v[8:9]
	v_readlane_b32 s23, v9, 43
	s_movk_i32 s22, 20
	v_addc_co_u32_e32 v6, vcc, 0, v6, vcc
	v_cmp_gt_i64_e32 vcc, s[24:25], v[8:9]
	v_readlane_b32 s25, v9, 44
	s_movk_i32 s24, 19
	v_addc_co_u32_e32 v6, vcc, 0, v6, vcc
	v_cmp_gt_i64_e32 vcc, s[22:23], v[8:9]
	v_readlane_b32 s23, v9, 45
	s_movk_i32 s22, 18
	v_addc_co_u32_e32 v6, vcc, 0, v6, vcc
	v_cmp_gt_i64_e32 vcc, s[24:25], v[8:9]
	v_readlane_b32 s25, v9, 46
	s_movk_i32 s24, 17
	v_addc_co_u32_e32 v6, vcc, 0, v6, vcc
	v_cmp_gt_i64_e32 vcc, s[22:23], v[8:9]
	v_readlane_b32 s23, v9, 47
	s_movk_i32 s22, 16
	v_addc_co_u32_e32 v6, vcc, 0, v6, vcc
	v_cmp_gt_i64_e32 vcc, s[24:25], v[8:9]
	v_readlane_b32 s25, v9, 48
	s_movk_i32 s24, 15
	v_addc_co_u32_e32 v6, vcc, 0, v6, vcc
	v_cmp_gt_i64_e32 vcc, s[22:23], v[8:9]
	v_readlane_b32 s23, v9, 49
	s_movk_i32 s22, 14
	v_addc_co_u32_e32 v6, vcc, 0, v6, vcc
	v_cmp_gt_i64_e32 vcc, s[24:25], v[8:9]
	v_readlane_b32 s25, v9, 50
	s_movk_i32 s24, 13
	v_addc_co_u32_e32 v6, vcc, 0, v6, vcc
	v_cmp_gt_i64_e32 vcc, s[22:23], v[8:9]
	v_readlane_b32 s23, v9, 51
	s_movk_i32 s22, 12
	v_addc_co_u32_e32 v6, vcc, 0, v6, vcc
	v_cmp_gt_i64_e32 vcc, s[24:25], v[8:9]
	v_readlane_b32 s25, v9, 52
	s_movk_i32 s24, 11
	v_addc_co_u32_e32 v6, vcc, 0, v6, vcc
	v_cmp_gt_i64_e32 vcc, s[22:23], v[8:9]
	v_readlane_b32 s23, v9, 53
	s_movk_i32 s22, 10
	v_addc_co_u32_e32 v6, vcc, 0, v6, vcc
	v_cmp_gt_i64_e32 vcc, s[24:25], v[8:9]
	v_readlane_b32 s25, v9, 54
	s_movk_i32 s24, 9
	v_addc_co_u32_e32 v6, vcc, 0, v6, vcc
	v_cmp_gt_i64_e32 vcc, s[22:23], v[8:9]
	v_readlane_b32 s23, v9, 55
	s_movk_i32 s22, 8
	v_addc_co_u32_e32 v6, vcc, 0, v6, vcc
	v_cmp_gt_i64_e32 vcc, s[24:25], v[8:9]
	v_readlane_b32 s25, v9, 56
	s_movk_i32 s24, 7
	v_addc_co_u32_e32 v6, vcc, 0, v6, vcc
	v_cmp_gt_i64_e32 vcc, s[22:23], v[8:9]
	v_readlane_b32 s23, v9, 57
	s_movk_i32 s22, 6
	v_addc_co_u32_e32 v6, vcc, 0, v6, vcc
	v_cmp_gt_i64_e32 vcc, s[24:25], v[8:9]
	v_readlane_b32 s25, v9, 58
	s_movk_i32 s24, 5
	v_addc_co_u32_e32 v6, vcc, 0, v6, vcc
	v_cmp_gt_i64_e32 vcc, s[22:23], v[8:9]
	v_readlane_b32 s23, v9, 59
	s_movk_i32 s22, 4
	v_addc_co_u32_e32 v6, vcc, 0, v6, vcc
	v_cmp_gt_i64_e32 vcc, s[24:25], v[8:9]
	v_readlane_b32 s25, v9, 60
	s_movk_i32 s24, 3
	v_addc_co_u32_e32 v6, vcc, 0, v6, vcc
	v_cmp_gt_i64_e32 vcc, s[22:23], v[8:9]
	v_readlane_b32 s23, v9, 61
	s_movk_i32 s22, 2
	v_addc_co_u32_e32 v6, vcc, 0, v6, vcc
	v_cmp_gt_i64_e32 vcc, s[24:25], v[8:9]
	v_readlane_b32 s25, v9, 62
	s_movk_i32 s24, 1
	v_addc_co_u32_e32 v6, vcc, 0, v6, vcc
	v_cmp_gt_i64_e32 vcc, s[22:23], v[8:9]
	v_readlane_b32 s23, v9, 63
	s_movk_i32 s22, 0
	v_addc_co_u32_e32 v6, vcc, 0, v6, vcc
	v_cmp_gt_i64_e32 vcc, s[24:25], v[8:9]
	s_nop 1
	v_addc_co_u32_e32 v6, vcc, 0, v6, vcc
	v_cmp_gt_i64_e32 vcc, s[22:23], v[8:9]
	s_nop 1
	v_addc_co_u32_e32 v6, vcc, 0, v6, vcc
	v_cmp_gt_u32_e32 vcc, 6, v6
	s_nop 1
	v_cndmask_b32_e32 v5, 0, v2, vcc
	ds_bpermute_b32 v7, v1, v5
	s_waitcnt lgkmcnt(0)
; __device__ __forceinline__ void phase_nrr(const Frame& F, const Args& a, int l, const bf16_t* XA, const float* g, const float* modl, unsigned char* XN8) {
;     ...
;         for (int i = 0; i < 8; ++i) { const int t = tb + i;
;             const float lg = Pl[(w * 8 + i) * NE + lane] + Pl[(64 + w * 8 + i) * NE + lane]; const float sc = 1.f / (1.f + __expf(-lg)); const float bb = sc + bias;
;             float m1 = bb; m1 = fmaxf(m1, __shfl_xor(m1, 1)); m1 = fmaxf(m1, __shfl_xor(m1, 2)); m1 = fmaxf(m1, __shfl_xor(m1, 4));
;             const unsigned long long eq = __ballot(bb == m1); const int gbase = lane & ~7; const unsigned grpmask = (unsigned)((eq >> gbase) & 0xffull);
;             const int first = gbase + __builtin_ctz(grpmask);
;             float m2 = (lane == first) ? -INFINITY : bb; m2 = fmaxf(m2, __shfl_xor(m2, 1)); m2 = fmaxf(m2, __shfl_xor(m2, 2)); m2 = fmaxf(m2, __shfl_xor(m2, 4));
;             const float gsum = m1 + m2; const int gq = lane >> 3;
;             int grank = 0;
; #pragma unroll
;             for (int g2 = 0; g2 < 8; ++g2) { const float v = __int_as_float(__builtin_amdgcn_readlane(__float_as_int(gsum), g2 * 8)); grank += (v > gsum || (v == gsum && g2 < gq)) ? 1 : 0; }
;             const bool keep = grank < 4; const float val = keep ? bb : -INFINITY;
;             int rank = 0;
; #pragma unroll 8
;             for (int e2 = 0; e2 < 64; ++e2) { const float v = __int_as_float(__builtin_amdgcn_readlane(__float_as_int(val), e2)); rank += (v > val || (v == val && e2 < lane)) ? 1 : 0; }
;             const bool sel = rank < TOPK;
;             const float ssum = wave_sum(sel ? sc : 0.f);
;             if (sel) { const int p = atomicAdd((int*)(hist + lane), 1); top_e[t * TOPK + rank] = lane; gate[t * TOPK + rank] = sc / ssum * 2.5f; lpos[t * TOPK + rank] = p; }
	v_add_f32_e32 v5, v5, v7
	ds_bpermute_b32 v7, v201, v5
	s_waitcnt lgkmcnt(0)
	v_add_f32_e32 v5, v5, v7
	ds_bpermute_b32 v7, v220, v5
	s_waitcnt lgkmcnt(0)
	v_add_f32_e32 v5, v5, v7
	ds_bpermute_b32 v7, v221, v5
	s_waitcnt lgkmcnt(0)
	v_add_f32_e32 v5, v5, v7
	ds_bpermute_b32 v7, v222, v5
	s_waitcnt lgkmcnt(0)
	v_add_f32_e32 v5, v5, v7
	ds_bpermute_b32 v7, v223, v5
	s_and_saveexec_b64 s[2:3], vcc
	s_cbranch_execz .LBB0_559
	s_waitcnt lgkmcnt(0)
	v_add_f32_e32 v5, v5, v7
	v_div_scale_f32 v11, s[4:5], v5, v5, v2
	v_add3_u32 v6, s36, 30, v6
	v_rcp_f32_e32 v12, v11
	v_ashrrev_i32_e32 v7, 31, v6
	v_lshlrev_b64 v[6:7], 2, v[6:7]
	v_lshl_add_u64 v[8:9], s[26:27], 0, v[6:7]
	ds_add_rtn_u32 v10, v227, v243
	global_store_dword v[8:9], v230, off
	v_fma_f32 v8, -v11, v12, 1.0
	v_fmac_f32_e32 v12, v8, v12
	v_div_scale_f32 v8, vcc, v2, v5, v2
	v_mul_f32_e32 v9, v8, v12
	v_fma_f32 v13, -v11, v9, v8
	v_fmac_f32_e32 v9, v13, v12
	v_fma_f32 v8, -v11, v9, v8
	v_div_fmas_f32 v8, v8, v12, v9
	v_div_fixup_f32 v2, v8, v5, v2
	v_mul_f32_e32 v2, 0x40200000, v2
	v_lshl_add_u64 v[8:9], s[28:29], 0, v[6:7]
	v_lshl_add_u64 v[6:7], s[30:31], 0, v[6:7]
	global_store_dword v[8:9], v2, off
	s_waitcnt lgkmcnt(0)
	global_store_dword v[6:7], v10, off
.LBB0_559:
	s_or_b64 exec, exec, s[2:3]
	v_add_u32_e32 v2, s86, v226
	ds_read_b32 v2, v2
	ds_read_b32 v5, v4 offset:17920
	s_waitcnt lgkmcnt(0)
	v_add_f32_e32 v2, v2, v5
	v_mul_f32_e32 v2, 0xbfb8aa3b, v2
	v_exp_f32_e32 v2, v2
	s_nop 0
	v_add_f32_e32 v2, 1.0, v2
	v_div_scale_f32 v5, s[2:3], v2, v2, 1.0
	v_rcp_f32_e32 v6, v5
	s_mov_b32 s2, 0
	v_fma_f32 v7, -v5, v6, 1.0
	v_fmac_f32_e32 v6, v7, v6
	v_div_scale_f32 v7, vcc, 1.0, v2, 1.0
	v_mul_f32_e32 v8, v7, v6
	v_fma_f32 v9, -v5, v8, v7
	v_fmac_f32_e32 v8, v9, v6
	v_fma_f32 v5, -v5, v8, v7
	v_div_fmas_f32 v5, v5, v6, v8
	v_div_fixup_f32 v2, v5, v2, 1.0
	v_add_f32_e32 v5, v3, v2
	s_nop 1
	s_waitcnt lgkmcnt(0)
	v_max_f32_dpp v6, v5, v5 quad_perm:[1,0,3,2] row_mask:0xf bank_mask:0xf
	s_nop 1
	s_waitcnt lgkmcnt(0)
	v_max_f32_dpp v6, v6, v6 quad_perm:[2,3,0,1] row_mask:0xf bank_mask:0xf
	s_nop 1
	s_waitcnt lgkmcnt(0)
	v_max_f32_dpp v8, v6, v6 row_half_mirror row_mask:0xf bank_mask:0xf
	v_cmp_eq_f32_e32 vcc, v5, v8
	s_nop 1
	v_lshrrev_b64 v[6:7], v200, vcc
	v_ffbl_b32_sdwa v6, v6 dst_sel:DWORD dst_unused:UNUSED_PAD src0_sel:BYTE_0
	v_add_u32_e32 v6, v6, v200
	v_cmp_ne_u32_e32 vcc, v230, v6
	s_nop 1
	v_cndmask_b32_e32 v6, v245, v5, vcc
	s_nop 1
	s_waitcnt lgkmcnt(0)
	v_max_f32_dpp v6, v6, v6 quad_perm:[1,0,3,2] row_mask:0xf bank_mask:0xf
	s_nop 1
	s_waitcnt lgkmcnt(0)
	v_max_f32_dpp v6, v6, v6 quad_perm:[2,3,0,1] row_mask:0xf bank_mask:0xf
	s_nop 1
	s_waitcnt lgkmcnt(0)
	v_max_f32_dpp v6, v6, v6 row_half_mirror row_mask:0xf bank_mask:0xf
	v_add_f32_e32 v6, v8, v6
	s_nop 0
	v_readlane_b32 s3, v6, 0
	s_nop 1
	v_cmp_eq_f32_e64 s[22:23], s3, v6
	v_cmp_gt_f32_e32 vcc, s3, v6
	s_and_b64 s[4:5], s[6:7], s[22:23]
	v_readlane_b32 s3, v6, 8
	s_or_b64 s[4:5], vcc, s[4:5]
	v_cndmask_b32_e64 v7, 0, 1, s[4:5]
	v_cmp_eq_f32_e64 s[22:23], s3, v6
	v_cmp_gt_f32_e32 vcc, s3, v6
	s_and_b64 s[4:5], s[8:9], s[22:23]
	v_readlane_b32 s3, v6, 16
	s_or_b64 s[4:5], vcc, s[4:5]
	v_cndmask_b32_e64 v8, 0, 1, s[4:5]
	v_cmp_eq_f32_e64 s[22:23], s3, v6
	v_cmp_gt_f32_e32 vcc, s3, v6
	s_and_b64 s[4:5], s[10:11], s[22:23]
	v_readlane_b32 s3, v6, 24
	s_or_b64 s[4:5], vcc, s[4:5]
	v_cndmask_b32_e64 v9, 0, 1, s[4:5]
	v_cmp_eq_f32_e64 s[22:23], s3, v6
	v_cmp_gt_f32_e32 vcc, s3, v6
	s_and_b64 s[4:5], s[12:13], s[22:23]
	v_readlane_b32 s3, v6, 32
	s_or_b64 s[4:5], vcc, s[4:5]
	v_cndmask_b32_e64 v10, 0, 1, s[4:5]
	v_cmp_eq_f32_e64 s[22:23], s3, v6
	v_cmp_gt_f32_e32 vcc, s3, v6
	s_and_b64 s[4:5], s[14:15], s[22:23]
	v_readlane_b32 s3, v6, 40
	s_or_b64 s[4:5], vcc, s[4:5]
	v_cndmask_b32_e64 v11, 0, 1, s[4:5]
	v_cmp_eq_f32_e64 s[22:23], s3, v6
	v_cmp_gt_f32_e32 vcc, s3, v6
	s_and_b64 s[4:5], s[16:17], s[22:23]
	v_readlane_b32 s3, v6, 48
	s_or_b64 s[4:5], vcc, s[4:5]
	v_cndmask_b32_e64 v12, 0, 1, s[4:5]
	v_cmp_eq_f32_e64 s[22:23], s3, v6
	v_cmp_gt_f32_e32 vcc, s3, v6
	s_and_b64 s[4:5], s[18:19], s[22:23]
	v_readlane_b32 s3, v6, 56
	s_or_b64 s[4:5], vcc, s[4:5]
	v_cndmask_b32_e64 v13, 0, 1, s[4:5]
	v_cmp_gt_f32_e32 vcc, s3, v6
	s_nop 1
	v_cndmask_b32_e64 v6, 0, 1, vcc
	v_add_u32_e32 v6, v8, v6
	v_add3_u32 v6, v6, v7, v9
	v_add3_u32 v6, v6, v10, v11
	v_add3_u32 v6, v6, v12, v13
	v_cmp_gt_u32_e32 vcc, 4, v6
	v_mov_b32_e32 v6, 0
	s_nop 0
	v_cndmask_b32_e32 v5, v245, v5, vcc
	v_ashrrev_i32_e32 v9, 31, v5
	v_sub_u32_e32 v8, 63, v230
	v_and_b32_e32 v9, 0x7fffffff, v9
	v_xor_b32_e32 v9, v5, v9
	s_nop 0
	v_readlane_b32 s25, v9, 0
	s_movk_i32 s24, 63
	v_readlane_b32 s23, v9, 1
	s_movk_i32 s22, 62
	v_cmp_gt_i64_e32 vcc, s[24:25], v[8:9]
	v_readlane_b32 s25, v9, 2
	s_movk_i32 s24, 61
	v_addc_co_u32_e32 v6, vcc, 0, v6, vcc
	v_cmp_gt_i64_e32 vcc, s[22:23], v[8:9]
	v_readlane_b32 s23, v9, 3
	s_movk_i32 s22, 60
	v_addc_co_u32_e32 v6, vcc, 0, v6, vcc
	v_cmp_gt_i64_e32 vcc, s[24:25], v[8:9]
	v_readlane_b32 s25, v9, 4
	s_movk_i32 s24, 59
	v_addc_co_u32_e32 v6, vcc, 0, v6, vcc
	v_cmp_gt_i64_e32 vcc, s[22:23], v[8:9]
	v_readlane_b32 s23, v9, 5
	s_movk_i32 s22, 58
	v_addc_co_u32_e32 v6, vcc, 0, v6, vcc
	v_cmp_gt_i64_e32 vcc, s[24:25], v[8:9]
	v_readlane_b32 s25, v9, 6
	s_movk_i32 s24, 57
	v_addc_co_u32_e32 v6, vcc, 0, v6, vcc
	v_cmp_gt_i64_e32 vcc, s[22:23], v[8:9]
	v_readlane_b32 s23, v9, 7
	s_movk_i32 s22, 56
	v_addc_co_u32_e32 v6, vcc, 0, v6, vcc
	v_cmp_gt_i64_e32 vcc, s[24:25], v[8:9]
	v_readlane_b32 s25, v9, 8
	s_movk_i32 s24, 55
	v_addc_co_u32_e32 v6, vcc, 0, v6, vcc
	v_cmp_gt_i64_e32 vcc, s[22:23], v[8:9]
	v_readlane_b32 s23, v9, 9
	s_movk_i32 s22, 54
; __device__ __forceinline__ void phase_nrr(const Frame& F, const Args& a, int l, const bf16_t* XA, const float* g, const float* modl, unsigned char* XN8) {
;     ...
;             int rank = 0;
; #pragma unroll 8
;             for (int e2 = 0; e2 < 64; ++e2) { const float v = __int_as_float(__builtin_amdgcn_readlane(__float_as_int(val), e2)); rank += (v > val || (v == val && e2 < lane)) ? 1 : 0; }
	v_addc_co_u32_e32 v6, vcc, 0, v6, vcc
	v_cmp_gt_i64_e32 vcc, s[24:25], v[8:9]
	v_readlane_b32 s25, v9, 10
	s_movk_i32 s24, 53
	v_addc_co_u32_e32 v6, vcc, 0, v6, vcc
	v_cmp_gt_i64_e32 vcc, s[22:23], v[8:9]
	v_readlane_b32 s23, v9, 11
	s_movk_i32 s22, 52
	v_addc_co_u32_e32 v6, vcc, 0, v6, vcc
	v_cmp_gt_i64_e32 vcc, s[24:25], v[8:9]
	v_readlane_b32 s25, v9, 12
	s_movk_i32 s24, 51
	v_addc_co_u32_e32 v6, vcc, 0, v6, vcc
	v_cmp_gt_i64_e32 vcc, s[22:23], v[8:9]
	v_readlane_b32 s23, v9, 13
	s_movk_i32 s22, 50
	v_addc_co_u32_e32 v6, vcc, 0, v6, vcc
	v_cmp_gt_i64_e32 vcc, s[24:25], v[8:9]
	v_readlane_b32 s25, v9, 14
	s_movk_i32 s24, 49
	v_addc_co_u32_e32 v6, vcc, 0, v6, vcc
	v_cmp_gt_i64_e32 vcc, s[22:23], v[8:9]
	v_readlane_b32 s23, v9, 15
	s_movk_i32 s22, 48
	v_addc_co_u32_e32 v6, vcc, 0, v6, vcc
	v_cmp_gt_i64_e32 vcc, s[24:25], v[8:9]
	v_readlane_b32 s25, v9, 16
	s_movk_i32 s24, 47
	v_addc_co_u32_e32 v6, vcc, 0, v6, vcc
	v_cmp_gt_i64_e32 vcc, s[22:23], v[8:9]
	v_readlane_b32 s23, v9, 17
	s_movk_i32 s22, 46
	v_addc_co_u32_e32 v6, vcc, 0, v6, vcc
	v_cmp_gt_i64_e32 vcc, s[24:25], v[8:9]
	v_readlane_b32 s25, v9, 18
	s_movk_i32 s24, 45
	v_addc_co_u32_e32 v6, vcc, 0, v6, vcc
	v_cmp_gt_i64_e32 vcc, s[22:23], v[8:9]
	v_readlane_b32 s23, v9, 19
	s_movk_i32 s22, 44
	v_addc_co_u32_e32 v6, vcc, 0, v6, vcc
	v_cmp_gt_i64_e32 vcc, s[24:25], v[8:9]
	v_readlane_b32 s25, v9, 20
	s_movk_i32 s24, 43
	v_addc_co_u32_e32 v6, vcc, 0, v6, vcc
	v_cmp_gt_i64_e32 vcc, s[22:23], v[8:9]
	v_readlane_b32 s23, v9, 21
	s_movk_i32 s22, 42
	v_addc_co_u32_e32 v6, vcc, 0, v6, vcc
	v_cmp_gt_i64_e32 vcc, s[24:25], v[8:9]
	v_readlane_b32 s25, v9, 22
	s_movk_i32 s24, 41
	v_addc_co_u32_e32 v6, vcc, 0, v6, vcc
	v_cmp_gt_i64_e32 vcc, s[22:23], v[8:9]
	v_readlane_b32 s23, v9, 23
	s_movk_i32 s22, 40
	v_addc_co_u32_e32 v6, vcc, 0, v6, vcc
	v_cmp_gt_i64_e32 vcc, s[24:25], v[8:9]
	v_readlane_b32 s25, v9, 24
	s_movk_i32 s24, 39
	v_addc_co_u32_e32 v6, vcc, 0, v6, vcc
	v_cmp_gt_i64_e32 vcc, s[22:23], v[8:9]
	v_readlane_b32 s23, v9, 25
	s_movk_i32 s22, 38
	v_addc_co_u32_e32 v6, vcc, 0, v6, vcc
	v_cmp_gt_i64_e32 vcc, s[24:25], v[8:9]
	v_readlane_b32 s25, v9, 26
	s_movk_i32 s24, 37
	v_addc_co_u32_e32 v6, vcc, 0, v6, vcc
	v_cmp_gt_i64_e32 vcc, s[22:23], v[8:9]
	v_readlane_b32 s23, v9, 27
	s_movk_i32 s22, 36
	v_addc_co_u32_e32 v6, vcc, 0, v6, vcc
	v_cmp_gt_i64_e32 vcc, s[24:25], v[8:9]
	v_readlane_b32 s25, v9, 28
	s_movk_i32 s24, 35
	v_addc_co_u32_e32 v6, vcc, 0, v6, vcc
	v_cmp_gt_i64_e32 vcc, s[22:23], v[8:9]
	v_readlane_b32 s23, v9, 29
	s_movk_i32 s22, 34
	v_addc_co_u32_e32 v6, vcc, 0, v6, vcc
	v_cmp_gt_i64_e32 vcc, s[24:25], v[8:9]
	v_readlane_b32 s25, v9, 30
	s_movk_i32 s24, 33
	v_addc_co_u32_e32 v6, vcc, 0, v6, vcc
	v_cmp_gt_i64_e32 vcc, s[22:23], v[8:9]
	v_readlane_b32 s23, v9, 31
	s_movk_i32 s22, 32
	v_addc_co_u32_e32 v6, vcc, 0, v6, vcc
	v_cmp_gt_i64_e32 vcc, s[24:25], v[8:9]
	v_readlane_b32 s25, v9, 32
	s_movk_i32 s24, 31
	v_addc_co_u32_e32 v6, vcc, 0, v6, vcc
	v_cmp_gt_i64_e32 vcc, s[22:23], v[8:9]
	v_readlane_b32 s23, v9, 33
	s_movk_i32 s22, 30
	v_addc_co_u32_e32 v6, vcc, 0, v6, vcc
	v_cmp_gt_i64_e32 vcc, s[24:25], v[8:9]
	v_readlane_b32 s25, v9, 34
	s_movk_i32 s24, 29
	v_addc_co_u32_e32 v6, vcc, 0, v6, vcc
	v_cmp_gt_i64_e32 vcc, s[22:23], v[8:9]
	v_readlane_b32 s23, v9, 35
	s_movk_i32 s22, 28
	v_addc_co_u32_e32 v6, vcc, 0, v6, vcc
	v_cmp_gt_i64_e32 vcc, s[24:25], v[8:9]
	v_readlane_b32 s25, v9, 36
	s_movk_i32 s24, 27
	v_addc_co_u32_e32 v6, vcc, 0, v6, vcc
	v_cmp_gt_i64_e32 vcc, s[22:23], v[8:9]
	v_readlane_b32 s23, v9, 37
	s_movk_i32 s22, 26
	v_addc_co_u32_e32 v6, vcc, 0, v6, vcc
	v_cmp_gt_i64_e32 vcc, s[24:25], v[8:9]
	v_readlane_b32 s25, v9, 38
	s_movk_i32 s24, 25
	v_addc_co_u32_e32 v6, vcc, 0, v6, vcc
	v_cmp_gt_i64_e32 vcc, s[22:23], v[8:9]
	v_readlane_b32 s23, v9, 39
	s_movk_i32 s22, 24
	v_addc_co_u32_e32 v6, vcc, 0, v6, vcc
	v_cmp_gt_i64_e32 vcc, s[24:25], v[8:9]
	v_readlane_b32 s25, v9, 40
	s_movk_i32 s24, 23
	v_addc_co_u32_e32 v6, vcc, 0, v6, vcc
	v_cmp_gt_i64_e32 vcc, s[22:23], v[8:9]
	v_readlane_b32 s23, v9, 41
	s_movk_i32 s22, 22
	v_addc_co_u32_e32 v6, vcc, 0, v6, vcc
	v_cmp_gt_i64_e32 vcc, s[24:25], v[8:9]
	v_readlane_b32 s25, v9, 42
	s_movk_i32 s24, 21
	v_addc_co_u32_e32 v6, vcc, 0, v6, vcc
	v_cmp_gt_i64_e32 vcc, s[22:23], v[8:9]
	v_readlane_b32 s23, v9, 43
	s_movk_i32 s22, 20
	v_addc_co_u32_e32 v6, vcc, 0, v6, vcc
	v_cmp_gt_i64_e32 vcc, s[24:25], v[8:9]
	v_readlane_b32 s25, v9, 44
	s_movk_i32 s24, 19
	v_addc_co_u32_e32 v6, vcc, 0, v6, vcc
	v_cmp_gt_i64_e32 vcc, s[22:23], v[8:9]
	v_readlane_b32 s23, v9, 45
	s_movk_i32 s22, 18
	v_addc_co_u32_e32 v6, vcc, 0, v6, vcc
	v_cmp_gt_i64_e32 vcc, s[24:25], v[8:9]
	v_readlane_b32 s25, v9, 46
	s_movk_i32 s24, 17
	v_addc_co_u32_e32 v6, vcc, 0, v6, vcc
	v_cmp_gt_i64_e32 vcc, s[22:23], v[8:9]
	v_readlane_b32 s23, v9, 47
	s_movk_i32 s22, 16
	v_addc_co_u32_e32 v6, vcc, 0, v6, vcc
	v_cmp_gt_i64_e32 vcc, s[24:25], v[8:9]
	v_readlane_b32 s25, v9, 48
	s_movk_i32 s24, 15
	v_addc_co_u32_e32 v6, vcc, 0, v6, vcc
	v_cmp_gt_i64_e32 vcc, s[22:23], v[8:9]
	v_readlane_b32 s23, v9, 49
	s_movk_i32 s22, 14
	v_addc_co_u32_e32 v6, vcc, 0, v6, vcc
	v_cmp_gt_i64_e32 vcc, s[24:25], v[8:9]
	v_readlane_b32 s25, v9, 50
	s_movk_i32 s24, 13
	v_addc_co_u32_e32 v6, vcc, 0, v6, vcc
	v_cmp_gt_i64_e32 vcc, s[22:23], v[8:9]
	v_readlane_b32 s23, v9, 51
	s_movk_i32 s22, 12
	v_addc_co_u32_e32 v6, vcc, 0, v6, vcc
	v_cmp_gt_i64_e32 vcc, s[24:25], v[8:9]
	v_readlane_b32 s25, v9, 52
	s_movk_i32 s24, 11
	v_addc_co_u32_e32 v6, vcc, 0, v6, vcc
	v_cmp_gt_i64_e32 vcc, s[22:23], v[8:9]
	v_readlane_b32 s23, v9, 53
	s_movk_i32 s22, 10
	v_addc_co_u32_e32 v6, vcc, 0, v6, vcc
; __device__ __forceinline__ void phase_nrr(const Frame& F, const Args& a, int l, const bf16_t* XA, const float* g, const float* modl, unsigned char* XN8) {
;     ...
;         for (int i = 0; i < 8; ++i) { const int t = tb + i;
;             const float lg = Pl[(w * 8 + i) * NE + lane] + Pl[(64 + w * 8 + i) * NE + lane]; const float sc = 1.f / (1.f + __expf(-lg)); const float bb = sc + bias;
;             float m1 = bb; m1 = fmaxf(m1, __shfl_xor(m1, 1)); m1 = fmaxf(m1, __shfl_xor(m1, 2)); m1 = fmaxf(m1, __shfl_xor(m1, 4));
;             const unsigned long long eq = __ballot(bb == m1); const int gbase = lane & ~7; const unsigned grpmask = (unsigned)((eq >> gbase) & 0xffull);
;             const int first = gbase + __builtin_ctz(grpmask);
;             float m2 = (lane == first) ? -INFINITY : bb; m2 = fmaxf(m2, __shfl_xor(m2, 1)); m2 = fmaxf(m2, __shfl_xor(m2, 2)); m2 = fmaxf(m2, __shfl_xor(m2, 4));
;             const float gsum = m1 + m2; const int gq = lane >> 3;
;             int grank = 0;
; #pragma unroll
;             for (int g2 = 0; g2 < 8; ++g2) { const float v = __int_as_float(__builtin_amdgcn_readlane(__float_as_int(gsum), g2 * 8)); grank += (v > gsum || (v == gsum && g2 < gq)) ? 1 : 0; }
;             const bool keep = grank < 4; const float val = keep ? bb : -INFINITY;
;             int rank = 0;
; #pragma unroll 8
;             for (int e2 = 0; e2 < 64; ++e2) { const float v = __int_as_float(__builtin_amdgcn_readlane(__float_as_int(val), e2)); rank += (v > val || (v == val && e2 < lane)) ? 1 : 0; }
;             const bool sel = rank < TOPK;
;             const float ssum = wave_sum(sel ? sc : 0.f);
;             if (sel) { const int p = atomicAdd((int*)(hist + lane), 1); top_e[t * TOPK + rank] = lane; gate[t * TOPK + rank] = sc / ssum * 2.5f; lpos[t * TOPK + rank] = p; }
	v_cmp_gt_i64_e32 vcc, s[24:25], v[8:9]
	v_readlane_b32 s25, v9, 54
	s_movk_i32 s24, 9
	v_addc_co_u32_e32 v6, vcc, 0, v6, vcc
	v_cmp_gt_i64_e32 vcc, s[22:23], v[8:9]
	v_readlane_b32 s23, v9, 55
	s_movk_i32 s22, 8
	v_addc_co_u32_e32 v6, vcc, 0, v6, vcc
	v_cmp_gt_i64_e32 vcc, s[24:25], v[8:9]
	v_readlane_b32 s25, v9, 56
	s_movk_i32 s24, 7
	v_addc_co_u32_e32 v6, vcc, 0, v6, vcc
	v_cmp_gt_i64_e32 vcc, s[22:23], v[8:9]
	v_readlane_b32 s23, v9, 57
	s_movk_i32 s22, 6
	v_addc_co_u32_e32 v6, vcc, 0, v6, vcc
	v_cmp_gt_i64_e32 vcc, s[24:25], v[8:9]
	v_readlane_b32 s25, v9, 58
	s_movk_i32 s24, 5
	v_addc_co_u32_e32 v6, vcc, 0, v6, vcc
	v_cmp_gt_i64_e32 vcc, s[22:23], v[8:9]
	v_readlane_b32 s23, v9, 59
	s_movk_i32 s22, 4
	v_addc_co_u32_e32 v6, vcc, 0, v6, vcc
	v_cmp_gt_i64_e32 vcc, s[24:25], v[8:9]
	v_readlane_b32 s25, v9, 60
	s_movk_i32 s24, 3
	v_addc_co_u32_e32 v6, vcc, 0, v6, vcc
	v_cmp_gt_i64_e32 vcc, s[22:23], v[8:9]
	v_readlane_b32 s23, v9, 61
	s_movk_i32 s22, 2
	v_addc_co_u32_e32 v6, vcc, 0, v6, vcc
	v_cmp_gt_i64_e32 vcc, s[24:25], v[8:9]
	v_readlane_b32 s25, v9, 62
	s_movk_i32 s24, 1
	v_addc_co_u32_e32 v6, vcc, 0, v6, vcc
	v_cmp_gt_i64_e32 vcc, s[22:23], v[8:9]
	v_readlane_b32 s23, v9, 63
	s_movk_i32 s22, 0
	v_addc_co_u32_e32 v6, vcc, 0, v6, vcc
	v_cmp_gt_i64_e32 vcc, s[24:25], v[8:9]
	s_nop 1
	v_addc_co_u32_e32 v6, vcc, 0, v6, vcc
	v_cmp_gt_i64_e32 vcc, s[22:23], v[8:9]
	s_nop 1
	v_addc_co_u32_e32 v6, vcc, 0, v6, vcc
	v_cmp_gt_u32_e32 vcc, 6, v6
	s_nop 1
	v_cndmask_b32_e32 v5, 0, v2, vcc
	ds_bpermute_b32 v7, v1, v5
	s_waitcnt lgkmcnt(0)
	v_add_f32_e32 v5, v5, v7
	ds_bpermute_b32 v7, v201, v5
	s_waitcnt lgkmcnt(0)
	v_add_f32_e32 v5, v5, v7
	ds_bpermute_b32 v7, v220, v5
	s_waitcnt lgkmcnt(0)
	v_add_f32_e32 v5, v5, v7
	ds_bpermute_b32 v7, v221, v5
	s_waitcnt lgkmcnt(0)
	v_add_f32_e32 v5, v5, v7
	ds_bpermute_b32 v7, v222, v5
	s_waitcnt lgkmcnt(0)
	v_add_f32_e32 v5, v5, v7
	ds_bpermute_b32 v7, v223, v5
	s_and_saveexec_b64 s[2:3], vcc
	s_cbranch_execz .LBB0_563
	s_waitcnt lgkmcnt(0)
	v_add_f32_e32 v5, v5, v7
	v_div_scale_f32 v11, s[4:5], v5, v5, v2
	v_add3_u32 v6, s36, 36, v6
	v_rcp_f32_e32 v12, v11
	v_ashrrev_i32_e32 v7, 31, v6
	v_lshlrev_b64 v[6:7], 2, v[6:7]
	v_lshl_add_u64 v[8:9], s[26:27], 0, v[6:7]
	ds_add_rtn_u32 v10, v227, v243
	global_store_dword v[8:9], v230, off
	v_fma_f32 v8, -v11, v12, 1.0
	v_fmac_f32_e32 v12, v8, v12
	v_div_scale_f32 v8, vcc, v2, v5, v2
	v_mul_f32_e32 v9, v8, v12
	v_fma_f32 v13, -v11, v9, v8
	v_fmac_f32_e32 v9, v13, v12
	v_fma_f32 v8, -v11, v9, v8
	v_div_fmas_f32 v8, v8, v12, v9
	v_div_fixup_f32 v2, v8, v5, v2
	v_mul_f32_e32 v2, 0x40200000, v2
	v_lshl_add_u64 v[8:9], s[28:29], 0, v[6:7]
	v_lshl_add_u64 v[6:7], s[30:31], 0, v[6:7]
	global_store_dword v[8:9], v2, off
	s_waitcnt lgkmcnt(0)
	global_store_dword v[6:7], v10, off
.LBB0_563:
	s_or_b64 exec, exec, s[2:3]
	v_add_u32_e32 v2, s87, v226
	ds_read_b32 v2, v2
	ds_read_b32 v4, v4 offset:18176
	s_waitcnt lgkmcnt(0)
	v_add_f32_e32 v2, v2, v4
	v_mul_f32_e32 v2, 0xbfb8aa3b, v2
	v_exp_f32_e32 v2, v2
	s_nop 0
	v_add_f32_e32 v2, 1.0, v2
	v_div_scale_f32 v4, s[2:3], v2, v2, 1.0
	v_rcp_f32_e32 v5, v4
	s_mov_b32 s2, 0
	v_fma_f32 v6, -v4, v5, 1.0
	v_fmac_f32_e32 v5, v6, v5
	v_div_scale_f32 v6, vcc, 1.0, v2, 1.0
	v_mul_f32_e32 v7, v6, v5
	v_fma_f32 v8, -v4, v7, v6
	v_fmac_f32_e32 v7, v8, v5
	v_fma_f32 v4, -v4, v7, v6
	v_div_fmas_f32 v4, v4, v5, v7
	v_div_fixup_f32 v2, v4, v2, 1.0
	v_add_f32_e32 v3, v3, v2
	s_nop 1
	s_waitcnt lgkmcnt(0)
	v_max_f32_dpp v4, v3, v3 quad_perm:[1,0,3,2] row_mask:0xf bank_mask:0xf
	s_nop 1
	s_waitcnt lgkmcnt(0)
	v_max_f32_dpp v4, v4, v4 quad_perm:[2,3,0,1] row_mask:0xf bank_mask:0xf
	s_nop 1
	s_waitcnt lgkmcnt(0)
	v_max_f32_dpp v6, v4, v4 row_half_mirror row_mask:0xf bank_mask:0xf
	v_cmp_eq_f32_e32 vcc, v3, v6
	s_nop 1
	v_lshrrev_b64 v[4:5], v200, vcc
	v_ffbl_b32_sdwa v4, v4 dst_sel:DWORD dst_unused:UNUSED_PAD src0_sel:BYTE_0
	v_add_u32_e32 v4, v4, v200
	v_cmp_ne_u32_e32 vcc, v230, v4
	s_nop 1
	v_cndmask_b32_e32 v4, v245, v3, vcc
	s_nop 1
	s_waitcnt lgkmcnt(0)
	v_max_f32_dpp v4, v4, v4 quad_perm:[1,0,3,2] row_mask:0xf bank_mask:0xf
	s_nop 1
	s_waitcnt lgkmcnt(0)
	v_max_f32_dpp v4, v4, v4 quad_perm:[2,3,0,1] row_mask:0xf bank_mask:0xf
	s_nop 1
	s_waitcnt lgkmcnt(0)
	v_max_f32_dpp v4, v4, v4 row_half_mirror row_mask:0xf bank_mask:0xf
	v_add_f32_e32 v4, v6, v4
	s_nop 0
	v_readlane_b32 s3, v4, 0
	s_nop 1
	v_cmp_eq_f32_e64 s[22:23], s3, v4
	v_cmp_gt_f32_e32 vcc, s3, v4
	s_and_b64 s[4:5], s[6:7], s[22:23]
	v_readlane_b32 s3, v4, 8
	s_or_b64 s[4:5], vcc, s[4:5]
	v_cndmask_b32_e64 v5, 0, 1, s[4:5]
	v_cmp_eq_f32_e64 s[22:23], s3, v4
	v_cmp_gt_f32_e32 vcc, s3, v4
	s_and_b64 s[4:5], s[8:9], s[22:23]
	v_readlane_b32 s3, v4, 16
	s_or_b64 s[4:5], vcc, s[4:5]
	v_cndmask_b32_e64 v6, 0, 1, s[4:5]
	v_cmp_eq_f32_e64 s[22:23], s3, v4
	v_cmp_gt_f32_e32 vcc, s3, v4
	s_and_b64 s[4:5], s[10:11], s[22:23]
	v_readlane_b32 s3, v4, 24
	s_or_b64 s[4:5], vcc, s[4:5]
	v_cndmask_b32_e64 v7, 0, 1, s[4:5]
	v_cmp_eq_f32_e64 s[22:23], s3, v4
	v_cmp_gt_f32_e32 vcc, s3, v4
	s_and_b64 s[4:5], s[12:13], s[22:23]
	v_readlane_b32 s3, v4, 32
	s_or_b64 s[4:5], vcc, s[4:5]
	v_cndmask_b32_e64 v8, 0, 1, s[4:5]
	v_cmp_eq_f32_e64 s[22:23], s3, v4
	v_cmp_gt_f32_e32 vcc, s3, v4
	s_and_b64 s[4:5], s[14:15], s[22:23]
	v_readlane_b32 s3, v4, 40
	s_or_b64 s[4:5], vcc, s[4:5]
	v_cndmask_b32_e64 v9, 0, 1, s[4:5]
	v_cmp_eq_f32_e64 s[22:23], s3, v4
	v_cmp_gt_f32_e32 vcc, s3, v4
	s_and_b64 s[4:5], s[16:17], s[22:23]
	v_readlane_b32 s3, v4, 48
	s_or_b64 s[4:5], vcc, s[4:5]
	v_cndmask_b32_e64 v10, 0, 1, s[4:5]
	v_cmp_eq_f32_e64 s[22:23], s3, v4
	v_cmp_gt_f32_e32 vcc, s3, v4
	s_and_b64 s[4:5], s[18:19], s[22:23]
; __device__ __forceinline__ void phase_nrr(const Frame& F, const Args& a, int l, const bf16_t* XA, const float* g, const float* modl, unsigned char* XN8) {
;     ...
; #pragma unroll
;             for (int g2 = 0; g2 < 8; ++g2) { const float v = __int_as_float(__builtin_amdgcn_readlane(__float_as_int(gsum), g2 * 8)); grank += (v > gsum || (v == gsum && g2 < gq)) ? 1 : 0; }
;             const bool keep = grank < 4; const float val = keep ? bb : -INFINITY;
;             int rank = 0;
; #pragma unroll 8
;             for (int e2 = 0; e2 < 64; ++e2) { const float v = __int_as_float(__builtin_amdgcn_readlane(__float_as_int(val), e2)); rank += (v > val || (v == val && e2 < lane)) ? 1 : 0; }
	v_readlane_b32 s3, v4, 56
	s_or_b64 s[4:5], vcc, s[4:5]
	v_cndmask_b32_e64 v11, 0, 1, s[4:5]
	v_cmp_gt_f32_e32 vcc, s3, v4
	s_nop 1
	v_cndmask_b32_e64 v4, 0, 1, vcc
	v_add_u32_e32 v4, v6, v4
	v_add3_u32 v4, v4, v5, v7
	v_add3_u32 v4, v4, v8, v9
	v_add3_u32 v4, v4, v10, v11
	v_cmp_gt_u32_e32 vcc, 4, v4
	v_mov_b32_e32 v4, 0
	s_nop 0
	v_cndmask_b32_e32 v3, v245, v3, vcc
	v_ashrrev_i32_e32 v9, 31, v3
	v_sub_u32_e32 v8, 63, v230
	v_and_b32_e32 v9, 0x7fffffff, v9
	v_xor_b32_e32 v9, v3, v9
	s_nop 0
	v_readlane_b32 s25, v9, 0
	s_movk_i32 s24, 63
	v_readlane_b32 s23, v9, 1
	s_movk_i32 s22, 62
	v_cmp_gt_i64_e32 vcc, s[24:25], v[8:9]
	v_readlane_b32 s25, v9, 2
	s_movk_i32 s24, 61
	v_addc_co_u32_e32 v4, vcc, 0, v4, vcc
	v_cmp_gt_i64_e32 vcc, s[22:23], v[8:9]
	v_readlane_b32 s23, v9, 3
	s_movk_i32 s22, 60
	v_addc_co_u32_e32 v4, vcc, 0, v4, vcc
	v_cmp_gt_i64_e32 vcc, s[24:25], v[8:9]
	v_readlane_b32 s25, v9, 4
	s_movk_i32 s24, 59
	v_addc_co_u32_e32 v4, vcc, 0, v4, vcc
	v_cmp_gt_i64_e32 vcc, s[22:23], v[8:9]
	v_readlane_b32 s23, v9, 5
	s_movk_i32 s22, 58
	v_addc_co_u32_e32 v4, vcc, 0, v4, vcc
	v_cmp_gt_i64_e32 vcc, s[24:25], v[8:9]
	v_readlane_b32 s25, v9, 6
	s_movk_i32 s24, 57
	v_addc_co_u32_e32 v4, vcc, 0, v4, vcc
	v_cmp_gt_i64_e32 vcc, s[22:23], v[8:9]
	v_readlane_b32 s23, v9, 7
	s_movk_i32 s22, 56
	v_addc_co_u32_e32 v4, vcc, 0, v4, vcc
	v_cmp_gt_i64_e32 vcc, s[24:25], v[8:9]
	v_readlane_b32 s25, v9, 8
	s_movk_i32 s24, 55
	v_addc_co_u32_e32 v4, vcc, 0, v4, vcc
	v_cmp_gt_i64_e32 vcc, s[22:23], v[8:9]
	v_readlane_b32 s23, v9, 9
	s_movk_i32 s22, 54
	v_addc_co_u32_e32 v4, vcc, 0, v4, vcc
	v_cmp_gt_i64_e32 vcc, s[24:25], v[8:9]
	v_readlane_b32 s25, v9, 10
	s_movk_i32 s24, 53
	v_addc_co_u32_e32 v4, vcc, 0, v4, vcc
	v_cmp_gt_i64_e32 vcc, s[22:23], v[8:9]
	v_readlane_b32 s23, v9, 11
	s_movk_i32 s22, 52
	v_addc_co_u32_e32 v4, vcc, 0, v4, vcc
	v_cmp_gt_i64_e32 vcc, s[24:25], v[8:9]
	v_readlane_b32 s25, v9, 12
	s_movk_i32 s24, 51
	v_addc_co_u32_e32 v4, vcc, 0, v4, vcc
	v_cmp_gt_i64_e32 vcc, s[22:23], v[8:9]
	v_readlane_b32 s23, v9, 13
	s_movk_i32 s22, 50
	v_addc_co_u32_e32 v4, vcc, 0, v4, vcc
	v_cmp_gt_i64_e32 vcc, s[24:25], v[8:9]
	v_readlane_b32 s25, v9, 14
	s_movk_i32 s24, 49
	v_addc_co_u32_e32 v4, vcc, 0, v4, vcc
	v_cmp_gt_i64_e32 vcc, s[22:23], v[8:9]
	v_readlane_b32 s23, v9, 15
	s_movk_i32 s22, 48
	v_addc_co_u32_e32 v4, vcc, 0, v4, vcc
	v_cmp_gt_i64_e32 vcc, s[24:25], v[8:9]
	v_readlane_b32 s25, v9, 16
	s_movk_i32 s24, 47
	v_addc_co_u32_e32 v4, vcc, 0, v4, vcc
	v_cmp_gt_i64_e32 vcc, s[22:23], v[8:9]
	v_readlane_b32 s23, v9, 17
	s_movk_i32 s22, 46
	v_addc_co_u32_e32 v4, vcc, 0, v4, vcc
	v_cmp_gt_i64_e32 vcc, s[24:25], v[8:9]
	v_readlane_b32 s25, v9, 18
	s_movk_i32 s24, 45
	v_addc_co_u32_e32 v4, vcc, 0, v4, vcc
	v_cmp_gt_i64_e32 vcc, s[22:23], v[8:9]
	v_readlane_b32 s23, v9, 19
	s_movk_i32 s22, 44
	v_addc_co_u32_e32 v4, vcc, 0, v4, vcc
	v_cmp_gt_i64_e32 vcc, s[24:25], v[8:9]
	v_readlane_b32 s25, v9, 20
	s_movk_i32 s24, 43
	v_addc_co_u32_e32 v4, vcc, 0, v4, vcc
	v_cmp_gt_i64_e32 vcc, s[22:23], v[8:9]
	v_readlane_b32 s23, v9, 21
	s_movk_i32 s22, 42
	v_addc_co_u32_e32 v4, vcc, 0, v4, vcc
	v_cmp_gt_i64_e32 vcc, s[24:25], v[8:9]
	v_readlane_b32 s25, v9, 22
	s_movk_i32 s24, 41
	v_addc_co_u32_e32 v4, vcc, 0, v4, vcc
	v_cmp_gt_i64_e32 vcc, s[22:23], v[8:9]
	v_readlane_b32 s23, v9, 23
	s_movk_i32 s22, 40
	v_addc_co_u32_e32 v4, vcc, 0, v4, vcc
	v_cmp_gt_i64_e32 vcc, s[24:25], v[8:9]
	v_readlane_b32 s25, v9, 24
	s_movk_i32 s24, 39
	v_addc_co_u32_e32 v4, vcc, 0, v4, vcc
	v_cmp_gt_i64_e32 vcc, s[22:23], v[8:9]
	v_readlane_b32 s23, v9, 25
	s_movk_i32 s22, 38
	v_addc_co_u32_e32 v4, vcc, 0, v4, vcc
	v_cmp_gt_i64_e32 vcc, s[24:25], v[8:9]
	v_readlane_b32 s25, v9, 26
	s_movk_i32 s24, 37
	v_addc_co_u32_e32 v4, vcc, 0, v4, vcc
	v_cmp_gt_i64_e32 vcc, s[22:23], v[8:9]
	v_readlane_b32 s23, v9, 27
	s_movk_i32 s22, 36
	v_addc_co_u32_e32 v4, vcc, 0, v4, vcc
	v_cmp_gt_i64_e32 vcc, s[24:25], v[8:9]
	v_readlane_b32 s25, v9, 28
	s_movk_i32 s24, 35
	v_addc_co_u32_e32 v4, vcc, 0, v4, vcc
	v_cmp_gt_i64_e32 vcc, s[22:23], v[8:9]
	v_readlane_b32 s23, v9, 29
	s_movk_i32 s22, 34
	v_addc_co_u32_e32 v4, vcc, 0, v4, vcc
	v_cmp_gt_i64_e32 vcc, s[24:25], v[8:9]
	v_readlane_b32 s25, v9, 30
	s_movk_i32 s24, 33
	v_addc_co_u32_e32 v4, vcc, 0, v4, vcc
	v_cmp_gt_i64_e32 vcc, s[22:23], v[8:9]
	v_readlane_b32 s23, v9, 31
	s_movk_i32 s22, 32
	v_addc_co_u32_e32 v4, vcc, 0, v4, vcc
	v_cmp_gt_i64_e32 vcc, s[24:25], v[8:9]
	v_readlane_b32 s25, v9, 32
	s_movk_i32 s24, 31
	v_addc_co_u32_e32 v4, vcc, 0, v4, vcc
	v_cmp_gt_i64_e32 vcc, s[22:23], v[8:9]
	v_readlane_b32 s23, v9, 33
	s_movk_i32 s22, 30
	v_addc_co_u32_e32 v4, vcc, 0, v4, vcc
	v_cmp_gt_i64_e32 vcc, s[24:25], v[8:9]
	v_readlane_b32 s25, v9, 34
	s_movk_i32 s24, 29
	v_addc_co_u32_e32 v4, vcc, 0, v4, vcc
	v_cmp_gt_i64_e32 vcc, s[22:23], v[8:9]
	v_readlane_b32 s23, v9, 35
	s_movk_i32 s22, 28
	v_addc_co_u32_e32 v4, vcc, 0, v4, vcc
	v_cmp_gt_i64_e32 vcc, s[24:25], v[8:9]
	v_readlane_b32 s25, v9, 36
	s_movk_i32 s24, 27
; __device__ __forceinline__ void phase_nrr(const Frame& F, const Args& a, int l, const bf16_t* XA, const float* g, const float* modl, unsigned char* XN8) {
;     ...
;             int rank = 0;
; #pragma unroll 8
;             for (int e2 = 0; e2 < 64; ++e2) { const float v = __int_as_float(__builtin_amdgcn_readlane(__float_as_int(val), e2)); rank += (v > val || (v == val && e2 < lane)) ? 1 : 0; }
;             const bool sel = rank < TOPK;
;             const float ssum = wave_sum(sel ? sc : 0.f);
;             if (sel) { const int p = atomicAdd((int*)(hist + lane), 1); top_e[t * TOPK + rank] = lane; gate[t * TOPK + rank] = sc / ssum * 2.5f; lpos[t * TOPK + rank] = p; }
	v_addc_co_u32_e32 v4, vcc, 0, v4, vcc
	v_cmp_gt_i64_e32 vcc, s[22:23], v[8:9]
	v_readlane_b32 s23, v9, 37
	s_movk_i32 s22, 26
	v_addc_co_u32_e32 v4, vcc, 0, v4, vcc
	v_cmp_gt_i64_e32 vcc, s[24:25], v[8:9]
	v_readlane_b32 s25, v9, 38
	s_movk_i32 s24, 25
	v_addc_co_u32_e32 v4, vcc, 0, v4, vcc
	v_cmp_gt_i64_e32 vcc, s[22:23], v[8:9]
	v_readlane_b32 s23, v9, 39
	s_movk_i32 s22, 24
	v_addc_co_u32_e32 v4, vcc, 0, v4, vcc
	v_cmp_gt_i64_e32 vcc, s[24:25], v[8:9]
	v_readlane_b32 s25, v9, 40
	s_movk_i32 s24, 23
	v_addc_co_u32_e32 v4, vcc, 0, v4, vcc
	v_cmp_gt_i64_e32 vcc, s[22:23], v[8:9]
	v_readlane_b32 s23, v9, 41
	s_movk_i32 s22, 22
	v_addc_co_u32_e32 v4, vcc, 0, v4, vcc
	v_cmp_gt_i64_e32 vcc, s[24:25], v[8:9]
	v_readlane_b32 s25, v9, 42
	s_movk_i32 s24, 21
	v_addc_co_u32_e32 v4, vcc, 0, v4, vcc
	v_cmp_gt_i64_e32 vcc, s[22:23], v[8:9]
	v_readlane_b32 s23, v9, 43
	s_movk_i32 s22, 20
	v_addc_co_u32_e32 v4, vcc, 0, v4, vcc
	v_cmp_gt_i64_e32 vcc, s[24:25], v[8:9]
	v_readlane_b32 s25, v9, 44
	s_movk_i32 s24, 19
	v_addc_co_u32_e32 v4, vcc, 0, v4, vcc
	v_cmp_gt_i64_e32 vcc, s[22:23], v[8:9]
	v_readlane_b32 s23, v9, 45
	s_movk_i32 s22, 18
	v_addc_co_u32_e32 v4, vcc, 0, v4, vcc
	v_cmp_gt_i64_e32 vcc, s[24:25], v[8:9]
	v_readlane_b32 s25, v9, 46
	s_movk_i32 s24, 17
	v_addc_co_u32_e32 v4, vcc, 0, v4, vcc
	v_cmp_gt_i64_e32 vcc, s[22:23], v[8:9]
	v_readlane_b32 s23, v9, 47
	s_movk_i32 s22, 16
	v_addc_co_u32_e32 v4, vcc, 0, v4, vcc
	v_cmp_gt_i64_e32 vcc, s[24:25], v[8:9]
	v_readlane_b32 s25, v9, 48
	s_movk_i32 s24, 15
	v_addc_co_u32_e32 v4, vcc, 0, v4, vcc
	v_cmp_gt_i64_e32 vcc, s[22:23], v[8:9]
	v_readlane_b32 s23, v9, 49
	s_movk_i32 s22, 14
	v_addc_co_u32_e32 v4, vcc, 0, v4, vcc
	v_cmp_gt_i64_e32 vcc, s[24:25], v[8:9]
	v_readlane_b32 s25, v9, 50
	s_movk_i32 s24, 13
	v_addc_co_u32_e32 v4, vcc, 0, v4, vcc
	v_cmp_gt_i64_e32 vcc, s[22:23], v[8:9]
	v_readlane_b32 s23, v9, 51
	s_movk_i32 s22, 12
	v_addc_co_u32_e32 v4, vcc, 0, v4, vcc
	v_cmp_gt_i64_e32 vcc, s[24:25], v[8:9]
	v_readlane_b32 s25, v9, 52
	s_movk_i32 s24, 11
	v_addc_co_u32_e32 v4, vcc, 0, v4, vcc
	v_cmp_gt_i64_e32 vcc, s[22:23], v[8:9]
	v_readlane_b32 s23, v9, 53
	s_movk_i32 s22, 10
	v_addc_co_u32_e32 v4, vcc, 0, v4, vcc
	v_cmp_gt_i64_e32 vcc, s[24:25], v[8:9]
	v_readlane_b32 s25, v9, 54
	s_movk_i32 s24, 9
	v_addc_co_u32_e32 v4, vcc, 0, v4, vcc
	v_cmp_gt_i64_e32 vcc, s[22:23], v[8:9]
	v_readlane_b32 s23, v9, 55
	s_movk_i32 s22, 8
	v_addc_co_u32_e32 v4, vcc, 0, v4, vcc
	v_cmp_gt_i64_e32 vcc, s[24:25], v[8:9]
	v_readlane_b32 s25, v9, 56
	s_movk_i32 s24, 7
	v_addc_co_u32_e32 v4, vcc, 0, v4, vcc
	v_cmp_gt_i64_e32 vcc, s[22:23], v[8:9]
	v_readlane_b32 s23, v9, 57
	s_movk_i32 s22, 6
	v_addc_co_u32_e32 v4, vcc, 0, v4, vcc
	v_cmp_gt_i64_e32 vcc, s[24:25], v[8:9]
	v_readlane_b32 s25, v9, 58
	s_movk_i32 s24, 5
	v_addc_co_u32_e32 v4, vcc, 0, v4, vcc
	v_cmp_gt_i64_e32 vcc, s[22:23], v[8:9]
	v_readlane_b32 s23, v9, 59
	s_movk_i32 s22, 4
	v_addc_co_u32_e32 v4, vcc, 0, v4, vcc
	v_cmp_gt_i64_e32 vcc, s[24:25], v[8:9]
	v_readlane_b32 s25, v9, 60
	s_movk_i32 s24, 3
	v_addc_co_u32_e32 v4, vcc, 0, v4, vcc
	v_cmp_gt_i64_e32 vcc, s[22:23], v[8:9]
	v_readlane_b32 s23, v9, 61
	s_movk_i32 s22, 2
	v_addc_co_u32_e32 v4, vcc, 0, v4, vcc
	v_cmp_gt_i64_e32 vcc, s[24:25], v[8:9]
	v_readlane_b32 s25, v9, 62
	s_movk_i32 s24, 1
	v_addc_co_u32_e32 v4, vcc, 0, v4, vcc
	v_cmp_gt_i64_e32 vcc, s[22:23], v[8:9]
	v_readlane_b32 s23, v9, 63
	s_movk_i32 s22, 0
	v_addc_co_u32_e32 v4, vcc, 0, v4, vcc
	v_cmp_gt_i64_e32 vcc, s[24:25], v[8:9]
	s_nop 1
	v_addc_co_u32_e32 v4, vcc, 0, v4, vcc
	v_cmp_gt_i64_e32 vcc, s[22:23], v[8:9]
	s_nop 1
	v_addc_co_u32_e32 v4, vcc, 0, v4, vcc
	v_cmp_gt_u32_e32 vcc, 6, v4
	s_nop 1
	v_cndmask_b32_e32 v3, 0, v2, vcc
	ds_bpermute_b32 v5, v1, v3
	s_waitcnt lgkmcnt(0)
	v_add_f32_e32 v3, v3, v5
	ds_bpermute_b32 v5, v201, v3
	s_waitcnt lgkmcnt(0)
	v_add_f32_e32 v3, v3, v5
	ds_bpermute_b32 v5, v220, v3
	s_waitcnt lgkmcnt(0)
	v_add_f32_e32 v3, v3, v5
	ds_bpermute_b32 v5, v221, v3
	s_waitcnt lgkmcnt(0)
	v_add_f32_e32 v3, v3, v5
	ds_bpermute_b32 v5, v222, v3
	s_waitcnt lgkmcnt(0)
	v_add_f32_e32 v3, v3, v5
	ds_bpermute_b32 v5, v223, v3
	s_and_saveexec_b64 s[2:3], vcc
	s_cbranch_execz .LBB0_567
	s_waitcnt lgkmcnt(0)
	v_add_f32_e32 v3, v3, v5
	v_div_scale_f32 v9, s[4:5], v3, v3, v2
	v_add3_u32 v4, s36, 42, v4
	v_rcp_f32_e32 v10, v9
	v_ashrrev_i32_e32 v5, 31, v4
	v_lshlrev_b64 v[4:5], 2, v[4:5]
	v_lshl_add_u64 v[6:7], s[26:27], 0, v[4:5]
	ds_add_rtn_u32 v8, v227, v243
	global_store_dword v[6:7], v230, off
	v_fma_f32 v6, -v9, v10, 1.0
	v_fmac_f32_e32 v10, v6, v10
	v_div_scale_f32 v6, vcc, v2, v3, v2
	v_mul_f32_e32 v7, v6, v10
	v_fma_f32 v11, -v9, v7, v6
	v_fmac_f32_e32 v7, v11, v10
	v_fma_f32 v6, -v9, v7, v6
	v_div_fmas_f32 v6, v6, v10, v7
	v_div_fixup_f32 v2, v6, v3, v2
	v_mul_f32_e32 v6, 0x40200000, v2
	v_lshl_add_u64 v[2:3], s[28:29], 0, v[4:5]
	global_store_dword v[2:3], v6, off
	v_lshl_add_u64 v[2:3], s[30:31], 0, v[4:5]
	s_waitcnt lgkmcnt(0)
	global_store_dword v[2:3], v8, off

; #define LAS __attribute__((address_space(3)))
; __device__ __forceinline__ void phase_nrr(const Frame& F, const Args& a, int l, const bf16_t* XA, const float* g, const float* modl, unsigned char* XN8) {
;     ...
; #pragma unroll
;         for (int rb = 0; rb < 4; ++rb) *(LAS f32x4*)(Pl + (size_t)((kq * 64 + 16 * rb + fr) * NE + 16 * eb + 4 * fq)) = acc[rb];
;         __syncthreads();
;         const float bias = rbias[lane];
; #pragma unroll
;         for (int i = 0; i < 8; ++i) { const int t = tb + i;
;             const float lg = Pl[(w * 8 + i) * NE + lane] + Pl[(64 + w * 8 + i) * NE + lane]; const float sc = 1.f / (1.f + __expf(-lg)); const float bb = sc + bias;
;             float m1 = bb; m1 = fmaxf(m1, __shfl_xor(m1, 1)); m1 = fmaxf(m1, __shfl_xor(m1, 2)); m1 = fmaxf(m1, __shfl_xor(m1, 4));
;             const unsigned long long eq = __ballot(bb == m1); const int gbase = lane & ~7; const unsigned grpmask = (unsigned)((eq >> gbase) & 0xffull);
;             const int first = gbase + __builtin_ctz(grpmask);
;             float m2 = (lane == first) ? -INFINITY : bb; m2 = fmaxf(m2, __shfl_xor(m2, 1)); m2 = fmaxf(m2, __shfl_xor(m2, 2)); m2 = fmaxf(m2, __shfl_xor(m2, 4));
;             const float gsum = m1 + m2; const int gq = lane >> 3;
;             int grank = 0;
; #pragma unroll
;             for (int g2 = 0; g2 < 8; ++g2) { const float v = __int_as_float(__builtin_amdgcn_readlane(__float_as_int(gsum), g2 * 8)); grank += (v > gsum || (v == gsum && g2 < gq)) ? 1 : 0; }
;             const bool keep = grank < 4; const float val = keep ? bb : -INFINITY;
;             int rank = 0;
; #pragma unroll 8
;             for (int e2 = 0; e2 < 64; ++e2) { const float v = __int_as_float(__builtin_amdgcn_readlane(__float_as_int(val), e2)); rank += (v > val || (v == val && e2 < lane)) ? 1 : 0; }
.LBB0_1308:
	s_barrier
	ds_write_b128 v242, v[110:113]
	ds_write_b128 v242, v[118:121] offset:4096
	s_nop 0
	ds_write_b128 v242, v[126:129] offset:8192
	s_nop 1
	ds_write_b128 v242, v[130:133] offset:12288
	s_waitcnt lgkmcnt(0)
	s_barrier
	global_load_dword v3, v[198:199], off offset:256
	s_waitcnt vmcnt(15)
	v_add_u32_e32 v4, s33, v226
	ds_read2st64_b32 v[6:7], v4 offset1:64
	s_mov_b32 s3, 0
	s_waitcnt lgkmcnt(0)
	v_add_f32_e32 v2, v6, v7
	v_mul_f32_e32 v2, 0xbfb8aa3b, v2
	v_exp_f32_e32 v2, v2
	s_nop 0
	v_add_f32_e32 v2, 1.0, v2
	v_div_scale_f32 v5, s[20:21], v2, v2, 1.0
	v_rcp_f32_e32 v6, v5
	s_nop 0
	v_fma_f32 v7, -v5, v6, 1.0
	v_fmac_f32_e32 v6, v7, v6
	v_div_scale_f32 v7, vcc, 1.0, v2, 1.0
	v_mul_f32_e32 v8, v7, v6
	v_fma_f32 v9, -v5, v8, v7
	v_fmac_f32_e32 v8, v9, v6
	v_fma_f32 v5, -v5, v8, v7
	v_div_fmas_f32 v5, v5, v6, v8
	v_div_fixup_f32 v2, v5, v2, 1.0
	s_waitcnt vmcnt(0)
	v_add_f32_e32 v5, v3, v2
	s_nop 1
	s_waitcnt lgkmcnt(0)
	v_max_f32_dpp v6, v5, v5 quad_perm:[1,0,3,2] row_mask:0xf bank_mask:0xf
	s_nop 1
	s_waitcnt lgkmcnt(0)
	v_max_f32_dpp v6, v6, v6 quad_perm:[2,3,0,1] row_mask:0xf bank_mask:0xf
	s_nop 1
	s_waitcnt lgkmcnt(0)
	v_max_f32_dpp v8, v6, v6 row_half_mirror row_mask:0xf bank_mask:0xf
	v_cmp_eq_f32_e32 vcc, v5, v8
	s_nop 1
	v_lshrrev_b64 v[6:7], v200, vcc
	v_ffbl_b32_sdwa v6, v6 dst_sel:DWORD dst_unused:UNUSED_PAD src0_sel:BYTE_0
	v_add_u32_e32 v6, v6, v200
	v_cmp_ne_u32_e32 vcc, v230, v6
	s_nop 1
	v_cndmask_b32_e32 v6, v245, v5, vcc
	s_nop 1
	s_waitcnt lgkmcnt(0)
	v_max_f32_dpp v6, v6, v6 quad_perm:[1,0,3,2] row_mask:0xf bank_mask:0xf
	s_nop 1
	s_waitcnt lgkmcnt(0)
	v_max_f32_dpp v6, v6, v6 quad_perm:[2,3,0,1] row_mask:0xf bank_mask:0xf
	s_nop 1
	s_waitcnt lgkmcnt(0)
	v_max_f32_dpp v6, v6, v6 row_half_mirror row_mask:0xf bank_mask:0xf
	v_add_f32_e32 v6, v8, v6
	s_nop 0
	v_readlane_b32 s5, v6, 0
	s_nop 1
	v_cmp_eq_f32_e64 s[20:21], s5, v6
	v_cmp_gt_f32_e32 vcc, s5, v6
	s_and_b64 s[20:21], s[0:1], s[20:21]
	s_or_b64 s[20:21], vcc, s[20:21]
	v_readlane_b32 s5, v6, 8
	v_cndmask_b32_e64 v7, 0, 1, s[20:21]
	s_nop 0
	v_cmp_eq_f32_e64 s[20:21], s5, v6
	v_cmp_gt_f32_e32 vcc, s5, v6
	s_and_b64 s[20:21], s[6:7], s[20:21]
	s_or_b64 s[20:21], vcc, s[20:21]
	v_readlane_b32 s5, v6, 16
	v_cndmask_b32_e64 v8, 0, 1, s[20:21]
	s_nop 0
	v_cmp_eq_f32_e64 s[20:21], s5, v6
	v_cmp_gt_f32_e32 vcc, s5, v6
	s_and_b64 s[20:21], s[8:9], s[20:21]
	s_or_b64 s[20:21], vcc, s[20:21]
	v_readlane_b32 s5, v6, 24
	v_cndmask_b32_e64 v9, 0, 1, s[20:21]
	s_nop 0
	v_cmp_eq_f32_e64 s[20:21], s5, v6
	v_cmp_gt_f32_e32 vcc, s5, v6
	s_and_b64 s[20:21], s[10:11], s[20:21]
	s_or_b64 s[20:21], vcc, s[20:21]
	v_readlane_b32 s5, v6, 32
	v_cndmask_b32_e64 v10, 0, 1, s[20:21]
	s_nop 0
	v_cmp_eq_f32_e64 s[20:21], s5, v6
	v_cmp_gt_f32_e32 vcc, s5, v6
	s_and_b64 s[20:21], s[12:13], s[20:21]
	s_or_b64 s[20:21], vcc, s[20:21]
	v_readlane_b32 s5, v6, 40
	v_cndmask_b32_e64 v11, 0, 1, s[20:21]
	s_nop 0
	v_cmp_eq_f32_e64 s[20:21], s5, v6
	v_cmp_gt_f32_e32 vcc, s5, v6
	s_and_b64 s[20:21], s[14:15], s[20:21]
	s_or_b64 s[20:21], vcc, s[20:21]
	v_readlane_b32 s5, v6, 48
	v_cndmask_b32_e64 v12, 0, 1, s[20:21]
	s_nop 0
	v_cmp_eq_f32_e64 s[20:21], s5, v6
	v_cmp_gt_f32_e32 vcc, s5, v6
	s_and_b64 s[20:21], s[16:17], s[20:21]
	v_readlane_b32 s5, v6, 56
	s_or_b64 s[20:21], vcc, s[20:21]
	v_cndmask_b32_e64 v13, 0, 1, s[20:21]
	v_cmp_gt_f32_e32 vcc, s5, v6
	s_nop 1
	v_cndmask_b32_e64 v6, 0, 1, vcc
	v_add_u32_e32 v6, v8, v6
	v_add3_u32 v6, v6, v7, v9
	v_add3_u32 v6, v6, v10, v11
	v_add3_u32 v6, v6, v12, v13
	v_cmp_gt_u32_e32 vcc, 4, v6
	v_mov_b32_e32 v6, 0
	s_nop 0
	v_cndmask_b32_e32 v5, v245, v5, vcc
	v_ashrrev_i32_e32 v9, 31, v5
	v_sub_u32_e32 v8, 63, v230
	v_and_b32_e32 v9, 0x7fffffff, v9
	v_xor_b32_e32 v9, v5, v9
	s_nop 0
	v_readlane_b32 s23, v9, 0
	s_movk_i32 s22, 63
	v_readlane_b32 s21, v9, 1
	s_movk_i32 s20, 62
	v_cmp_gt_i64_e32 vcc, s[22:23], v[8:9]
	v_readlane_b32 s23, v9, 2
	s_movk_i32 s22, 61
	v_addc_co_u32_e32 v6, vcc, 0, v6, vcc
	v_cmp_gt_i64_e32 vcc, s[20:21], v[8:9]
	v_readlane_b32 s21, v9, 3
	s_movk_i32 s20, 60
	v_addc_co_u32_e32 v6, vcc, 0, v6, vcc
	v_cmp_gt_i64_e32 vcc, s[22:23], v[8:9]
	v_readlane_b32 s23, v9, 4
	s_movk_i32 s22, 59
	v_addc_co_u32_e32 v6, vcc, 0, v6, vcc
	v_cmp_gt_i64_e32 vcc, s[20:21], v[8:9]
	v_readlane_b32 s21, v9, 5
	s_movk_i32 s20, 58
	v_addc_co_u32_e32 v6, vcc, 0, v6, vcc
	v_cmp_gt_i64_e32 vcc, s[22:23], v[8:9]
	v_readlane_b32 s23, v9, 6
	s_movk_i32 s22, 57
	v_addc_co_u32_e32 v6, vcc, 0, v6, vcc
	v_cmp_gt_i64_e32 vcc, s[20:21], v[8:9]
	v_readlane_b32 s21, v9, 7
	s_movk_i32 s20, 56
	v_addc_co_u32_e32 v6, vcc, 0, v6, vcc
	v_cmp_gt_i64_e32 vcc, s[22:23], v[8:9]
	v_readlane_b32 s23, v9, 8
	s_movk_i32 s22, 55
	v_addc_co_u32_e32 v6, vcc, 0, v6, vcc
	v_cmp_gt_i64_e32 vcc, s[20:21], v[8:9]
	v_readlane_b32 s21, v9, 9
	s_movk_i32 s20, 54
	v_addc_co_u32_e32 v6, vcc, 0, v6, vcc
	v_cmp_gt_i64_e32 vcc, s[22:23], v[8:9]
	v_readlane_b32 s23, v9, 10
	s_movk_i32 s22, 53
	v_addc_co_u32_e32 v6, vcc, 0, v6, vcc
	v_cmp_gt_i64_e32 vcc, s[20:21], v[8:9]
	v_readlane_b32 s21, v9, 11
	s_movk_i32 s20, 52
	v_addc_co_u32_e32 v6, vcc, 0, v6, vcc
	v_cmp_gt_i64_e32 vcc, s[22:23], v[8:9]
	v_readlane_b32 s23, v9, 12
	s_movk_i32 s22, 51
	v_addc_co_u32_e32 v6, vcc, 0, v6, vcc
	v_cmp_gt_i64_e32 vcc, s[20:21], v[8:9]
	v_readlane_b32 s21, v9, 13
	s_movk_i32 s20, 50
	v_addc_co_u32_e32 v6, vcc, 0, v6, vcc
	v_cmp_gt_i64_e32 vcc, s[22:23], v[8:9]
	v_readlane_b32 s23, v9, 14
	s_movk_i32 s22, 49
	v_addc_co_u32_e32 v6, vcc, 0, v6, vcc
	v_cmp_gt_i64_e32 vcc, s[20:21], v[8:9]
	v_readlane_b32 s21, v9, 15
	s_movk_i32 s20, 48
	v_addc_co_u32_e32 v6, vcc, 0, v6, vcc
	v_cmp_gt_i64_e32 vcc, s[22:23], v[8:9]
; __device__ __forceinline__ void phase_nrr(const Frame& F, const Args& a, int l, const bf16_t* XA, const float* g, const float* modl, unsigned char* XN8) {
;     ...
;             int rank = 0;
; #pragma unroll 8
;             for (int e2 = 0; e2 < 64; ++e2) { const float v = __int_as_float(__builtin_amdgcn_readlane(__float_as_int(val), e2)); rank += (v > val || (v == val && e2 < lane)) ? 1 : 0; }
;             const bool sel = rank < TOPK;
;             const float ssum = wave_sum(sel ? sc : 0.f);
;             if (sel) { const int p = atomicAdd((int*)(hist + lane), 1); top_e[t * TOPK + rank] = lane; gate[t * TOPK + rank] = sc / ssum * 2.5f; lpos[t * TOPK + rank] = p; }
	v_readlane_b32 s23, v9, 16
	s_movk_i32 s22, 47
	v_addc_co_u32_e32 v6, vcc, 0, v6, vcc
	v_cmp_gt_i64_e32 vcc, s[20:21], v[8:9]
	v_readlane_b32 s21, v9, 17
	s_movk_i32 s20, 46
	v_addc_co_u32_e32 v6, vcc, 0, v6, vcc
	v_cmp_gt_i64_e32 vcc, s[22:23], v[8:9]
	v_readlane_b32 s23, v9, 18
	s_movk_i32 s22, 45
	v_addc_co_u32_e32 v6, vcc, 0, v6, vcc
	v_cmp_gt_i64_e32 vcc, s[20:21], v[8:9]
	v_readlane_b32 s21, v9, 19
	s_movk_i32 s20, 44
	v_addc_co_u32_e32 v6, vcc, 0, v6, vcc
	v_cmp_gt_i64_e32 vcc, s[22:23], v[8:9]
	v_readlane_b32 s23, v9, 20
	s_movk_i32 s22, 43
	v_addc_co_u32_e32 v6, vcc, 0, v6, vcc
	v_cmp_gt_i64_e32 vcc, s[20:21], v[8:9]
	v_readlane_b32 s21, v9, 21
	s_movk_i32 s20, 42
	v_addc_co_u32_e32 v6, vcc, 0, v6, vcc
	v_cmp_gt_i64_e32 vcc, s[22:23], v[8:9]
	v_readlane_b32 s23, v9, 22
	s_movk_i32 s22, 41
	v_addc_co_u32_e32 v6, vcc, 0, v6, vcc
	v_cmp_gt_i64_e32 vcc, s[20:21], v[8:9]
	v_readlane_b32 s21, v9, 23
	s_movk_i32 s20, 40
	v_addc_co_u32_e32 v6, vcc, 0, v6, vcc
	v_cmp_gt_i64_e32 vcc, s[22:23], v[8:9]
	v_readlane_b32 s23, v9, 24
	s_movk_i32 s22, 39
	v_addc_co_u32_e32 v6, vcc, 0, v6, vcc
	v_cmp_gt_i64_e32 vcc, s[20:21], v[8:9]
	v_readlane_b32 s21, v9, 25
	s_movk_i32 s20, 38
	v_addc_co_u32_e32 v6, vcc, 0, v6, vcc
	v_cmp_gt_i64_e32 vcc, s[22:23], v[8:9]
	v_readlane_b32 s23, v9, 26
	s_movk_i32 s22, 37
	v_addc_co_u32_e32 v6, vcc, 0, v6, vcc
	v_cmp_gt_i64_e32 vcc, s[20:21], v[8:9]
	v_readlane_b32 s21, v9, 27
	s_movk_i32 s20, 36
	v_addc_co_u32_e32 v6, vcc, 0, v6, vcc
	v_cmp_gt_i64_e32 vcc, s[22:23], v[8:9]
	v_readlane_b32 s23, v9, 28
	s_movk_i32 s22, 35
	v_addc_co_u32_e32 v6, vcc, 0, v6, vcc
	v_cmp_gt_i64_e32 vcc, s[20:21], v[8:9]
	v_readlane_b32 s21, v9, 29
	s_movk_i32 s20, 34
	v_addc_co_u32_e32 v6, vcc, 0, v6, vcc
	v_cmp_gt_i64_e32 vcc, s[22:23], v[8:9]
	v_readlane_b32 s23, v9, 30
	s_movk_i32 s22, 33
	v_addc_co_u32_e32 v6, vcc, 0, v6, vcc
	v_cmp_gt_i64_e32 vcc, s[20:21], v[8:9]
	v_readlane_b32 s21, v9, 31
	s_movk_i32 s20, 32
	v_addc_co_u32_e32 v6, vcc, 0, v6, vcc
	v_cmp_gt_i64_e32 vcc, s[22:23], v[8:9]
	v_readlane_b32 s23, v9, 32
	s_movk_i32 s22, 31
	v_addc_co_u32_e32 v6, vcc, 0, v6, vcc
	v_cmp_gt_i64_e32 vcc, s[20:21], v[8:9]
	v_readlane_b32 s21, v9, 33
	s_movk_i32 s20, 30
	v_addc_co_u32_e32 v6, vcc, 0, v6, vcc
	v_cmp_gt_i64_e32 vcc, s[22:23], v[8:9]
	v_readlane_b32 s23, v9, 34
	s_movk_i32 s22, 29
	v_addc_co_u32_e32 v6, vcc, 0, v6, vcc
	v_cmp_gt_i64_e32 vcc, s[20:21], v[8:9]
	v_readlane_b32 s21, v9, 35
	s_movk_i32 s20, 28
	v_addc_co_u32_e32 v6, vcc, 0, v6, vcc
	v_cmp_gt_i64_e32 vcc, s[22:23], v[8:9]
	v_readlane_b32 s23, v9, 36
	s_movk_i32 s22, 27
	v_addc_co_u32_e32 v6, vcc, 0, v6, vcc
	v_cmp_gt_i64_e32 vcc, s[20:21], v[8:9]
	v_readlane_b32 s21, v9, 37
	s_movk_i32 s20, 26
	v_addc_co_u32_e32 v6, vcc, 0, v6, vcc
	v_cmp_gt_i64_e32 vcc, s[22:23], v[8:9]
	v_readlane_b32 s23, v9, 38
	s_movk_i32 s22, 25
	v_addc_co_u32_e32 v6, vcc, 0, v6, vcc
	v_cmp_gt_i64_e32 vcc, s[20:21], v[8:9]
	v_readlane_b32 s21, v9, 39
	s_movk_i32 s20, 24
	v_addc_co_u32_e32 v6, vcc, 0, v6, vcc
	v_cmp_gt_i64_e32 vcc, s[22:23], v[8:9]
	v_readlane_b32 s23, v9, 40
	s_movk_i32 s22, 23
	v_addc_co_u32_e32 v6, vcc, 0, v6, vcc
	v_cmp_gt_i64_e32 vcc, s[20:21], v[8:9]
	v_readlane_b32 s21, v9, 41
	s_movk_i32 s20, 22
	v_addc_co_u32_e32 v6, vcc, 0, v6, vcc
	v_cmp_gt_i64_e32 vcc, s[22:23], v[8:9]
	v_readlane_b32 s23, v9, 42
	s_movk_i32 s22, 21
	v_addc_co_u32_e32 v6, vcc, 0, v6, vcc
	v_cmp_gt_i64_e32 vcc, s[20:21], v[8:9]
	v_readlane_b32 s21, v9, 43
	s_movk_i32 s20, 20
	v_addc_co_u32_e32 v6, vcc, 0, v6, vcc
	v_cmp_gt_i64_e32 vcc, s[22:23], v[8:9]
	v_readlane_b32 s23, v9, 44
	s_movk_i32 s22, 19
	v_addc_co_u32_e32 v6, vcc, 0, v6, vcc
	v_cmp_gt_i64_e32 vcc, s[20:21], v[8:9]
	v_readlane_b32 s21, v9, 45
	s_movk_i32 s20, 18
	v_addc_co_u32_e32 v6, vcc, 0, v6, vcc
	v_cmp_gt_i64_e32 vcc, s[22:23], v[8:9]
	v_readlane_b32 s23, v9, 46
	s_movk_i32 s22, 17
	v_addc_co_u32_e32 v6, vcc, 0, v6, vcc
	v_cmp_gt_i64_e32 vcc, s[20:21], v[8:9]
	v_readlane_b32 s21, v9, 47
	s_movk_i32 s20, 16
	v_addc_co_u32_e32 v6, vcc, 0, v6, vcc
	v_cmp_gt_i64_e32 vcc, s[22:23], v[8:9]
	v_readlane_b32 s23, v9, 48
	s_movk_i32 s22, 15
	v_addc_co_u32_e32 v6, vcc, 0, v6, vcc
	v_cmp_gt_i64_e32 vcc, s[20:21], v[8:9]
	v_readlane_b32 s21, v9, 49
	s_movk_i32 s20, 14
	v_addc_co_u32_e32 v6, vcc, 0, v6, vcc
	v_cmp_gt_i64_e32 vcc, s[22:23], v[8:9]
	v_readlane_b32 s23, v9, 50
	s_movk_i32 s22, 13
	v_addc_co_u32_e32 v6, vcc, 0, v6, vcc
	v_cmp_gt_i64_e32 vcc, s[20:21], v[8:9]
	v_readlane_b32 s21, v9, 51
	s_movk_i32 s20, 12
	v_addc_co_u32_e32 v6, vcc, 0, v6, vcc
	v_cmp_gt_i64_e32 vcc, s[22:23], v[8:9]
	v_readlane_b32 s23, v9, 52
	s_movk_i32 s22, 11
	v_addc_co_u32_e32 v6, vcc, 0, v6, vcc
	v_cmp_gt_i64_e32 vcc, s[20:21], v[8:9]
	v_readlane_b32 s21, v9, 53
	s_movk_i32 s20, 10
	v_addc_co_u32_e32 v6, vcc, 0, v6, vcc
	v_cmp_gt_i64_e32 vcc, s[22:23], v[8:9]
	v_readlane_b32 s23, v9, 54
	s_movk_i32 s22, 9
	v_addc_co_u32_e32 v6, vcc, 0, v6, vcc
	v_cmp_gt_i64_e32 vcc, s[20:21], v[8:9]
	v_readlane_b32 s21, v9, 55
	s_movk_i32 s20, 8
	v_addc_co_u32_e32 v6, vcc, 0, v6, vcc
	v_cmp_gt_i64_e32 vcc, s[22:23], v[8:9]
	v_readlane_b32 s23, v9, 56
	s_movk_i32 s22, 7
	v_addc_co_u32_e32 v6, vcc, 0, v6, vcc
	v_cmp_gt_i64_e32 vcc, s[20:21], v[8:9]
	v_readlane_b32 s21, v9, 57
	s_movk_i32 s20, 6
	v_addc_co_u32_e32 v6, vcc, 0, v6, vcc
	v_cmp_gt_i64_e32 vcc, s[22:23], v[8:9]
	v_readlane_b32 s23, v9, 58
	s_movk_i32 s22, 5
	v_addc_co_u32_e32 v6, vcc, 0, v6, vcc
	v_cmp_gt_i64_e32 vcc, s[20:21], v[8:9]
	v_readlane_b32 s21, v9, 59
	s_movk_i32 s20, 4
	v_addc_co_u32_e32 v6, vcc, 0, v6, vcc
	v_cmp_gt_i64_e32 vcc, s[22:23], v[8:9]
	v_readlane_b32 s23, v9, 60
	s_movk_i32 s22, 3
	v_addc_co_u32_e32 v6, vcc, 0, v6, vcc
	v_cmp_gt_i64_e32 vcc, s[20:21], v[8:9]
	v_readlane_b32 s21, v9, 61
	s_movk_i32 s20, 2
	v_addc_co_u32_e32 v6, vcc, 0, v6, vcc
	v_cmp_gt_i64_e32 vcc, s[22:23], v[8:9]
	v_readlane_b32 s23, v9, 62
	s_movk_i32 s22, 1
	v_addc_co_u32_e32 v6, vcc, 0, v6, vcc
	v_cmp_gt_i64_e32 vcc, s[20:21], v[8:9]
	v_readlane_b32 s21, v9, 63
	s_movk_i32 s20, 0
	v_addc_co_u32_e32 v6, vcc, 0, v6, vcc
	v_cmp_gt_i64_e32 vcc, s[22:23], v[8:9]
	s_nop 1
	v_addc_co_u32_e32 v6, vcc, 0, v6, vcc
	v_cmp_gt_i64_e32 vcc, s[20:21], v[8:9]
	s_nop 1
	v_addc_co_u32_e32 v6, vcc, 0, v6, vcc
	v_cmp_gt_u32_e32 vcc, 6, v6
	s_mul_i32 s50, s24, 6
	s_nop 0
	v_cndmask_b32_e32 v5, 0, v2, vcc
	ds_bpermute_b32 v7, v1, v5
	s_waitcnt lgkmcnt(0)
	v_add_f32_e32 v5, v5, v7
	ds_bpermute_b32 v7, v201, v5
	s_waitcnt lgkmcnt(0)
	v_add_f32_e32 v5, v5, v7
	ds_bpermute_b32 v7, v220, v5
	s_waitcnt lgkmcnt(0)
	v_add_f32_e32 v5, v5, v7
	ds_bpermute_b32 v7, v221, v5
	s_waitcnt lgkmcnt(0)
	v_add_f32_e32 v5, v5, v7
	ds_bpermute_b32 v7, v222, v5
	s_waitcnt lgkmcnt(0)
	v_add_f32_e32 v5, v5, v7
	ds_bpermute_b32 v7, v223, v5
	s_and_saveexec_b64 s[20:21], vcc
	s_cbranch_execz .LBB0_1312
; __device__ __forceinline__ void phase_nrr(const Frame& F, const Args& a, int l, const bf16_t* XA, const float* g, const float* modl, unsigned char* XN8) {
;     ...
;         for (int i = 0; i < 8; ++i) { const int t = tb + i;
;             const float lg = Pl[(w * 8 + i) * NE + lane] + Pl[(64 + w * 8 + i) * NE + lane]; const float sc = 1.f / (1.f + __expf(-lg)); const float bb = sc + bias;
;             float m1 = bb; m1 = fmaxf(m1, __shfl_xor(m1, 1)); m1 = fmaxf(m1, __shfl_xor(m1, 2)); m1 = fmaxf(m1, __shfl_xor(m1, 4));
;             const unsigned long long eq = __ballot(bb == m1); const int gbase = lane & ~7; const unsigned grpmask = (unsigned)((eq >> gbase) & 0xffull);
;             const int first = gbase + __builtin_ctz(grpmask);
;             float m2 = (lane == first) ? -INFINITY : bb; m2 = fmaxf(m2, __shfl_xor(m2, 1)); m2 = fmaxf(m2, __shfl_xor(m2, 2)); m2 = fmaxf(m2, __shfl_xor(m2, 4));
;             const float gsum = m1 + m2; const int gq = lane >> 3;
;             int grank = 0;
; #pragma unroll
;             for (int g2 = 0; g2 < 8; ++g2) { const float v = __int_as_float(__builtin_amdgcn_readlane(__float_as_int(gsum), g2 * 8)); grank += (v > gsum || (v == gsum && g2 < gq)) ? 1 : 0; }
;             const bool keep = grank < 4; const float val = keep ? bb : -INFINITY;
;             int rank = 0;
; #pragma unroll 8
;             for (int e2 = 0; e2 < 64; ++e2) { const float v = __int_as_float(__builtin_amdgcn_readlane(__float_as_int(val), e2)); rank += (v > val || (v == val && e2 < lane)) ? 1 : 0; }
;             const bool sel = rank < TOPK;
;             const float ssum = wave_sum(sel ? sc : 0.f);
;             if (sel) { const int p = atomicAdd((int*)(hist + lane), 1); top_e[t * TOPK + rank] = lane; gate[t * TOPK + rank] = sc / ssum * 2.5f; lpos[t * TOPK + rank] = p; }
	s_waitcnt lgkmcnt(0)
	v_add_f32_e32 v5, v5, v7
	v_div_scale_f32 v11, s[22:23], v5, v5, v2
	v_or_b32_e32 v6, s50, v6
	v_rcp_f32_e32 v12, v11
	v_ashrrev_i32_e32 v7, 31, v6
	v_lshlrev_b64 v[6:7], 2, v[6:7]
	v_lshl_add_u64 v[8:9], s[42:43], 0, v[6:7]
	ds_add_rtn_u32 v10, v227, v243
	global_store_dword v[8:9], v230, off
	v_fma_f32 v8, -v11, v12, 1.0
	v_fmac_f32_e32 v12, v8, v12
	v_div_scale_f32 v8, vcc, v2, v5, v2
	v_mul_f32_e32 v9, v8, v12
	v_fma_f32 v13, -v11, v9, v8
	v_fmac_f32_e32 v9, v13, v12
	v_fma_f32 v8, -v11, v9, v8
	v_div_fmas_f32 v8, v8, v12, v9
	v_div_fixup_f32 v2, v8, v5, v2
	v_mul_f32_e32 v2, 0x40200000, v2
	v_lshl_add_u64 v[8:9], s[44:45], 0, v[6:7]
	v_lshl_add_u64 v[6:7], s[46:47], 0, v[6:7]
	global_store_dword v[8:9], v2, off
	s_waitcnt lgkmcnt(0)
	global_store_dword v[6:7], v10, off
.LBB0_1312:
	s_or_b64 exec, exec, s[20:21]
	v_add_u32_e32 v2, s76, v226
	ds_read_b32 v2, v2
	ds_read_b32 v5, v4 offset:16640
	s_mov_b32 s3, 0
	s_waitcnt lgkmcnt(0)
	v_add_f32_e32 v2, v2, v5
	v_mul_f32_e32 v2, 0xbfb8aa3b, v2
	v_exp_f32_e32 v2, v2
	s_nop 0
	v_add_f32_e32 v2, 1.0, v2
	v_div_scale_f32 v5, s[20:21], v2, v2, 1.0
	v_rcp_f32_e32 v6, v5
	v_div_scale_f32 v7, vcc, 1.0, v2, 1.0
	v_fma_f32 v8, -v5, v6, 1.0
	v_fmac_f32_e32 v6, v8, v6
	v_mul_f32_e32 v8, v7, v6
	v_fma_f32 v9, -v5, v8, v7
	v_fmac_f32_e32 v8, v9, v6
	v_fma_f32 v5, -v5, v8, v7
	v_div_fmas_f32 v5, v5, v6, v8
	v_div_fixup_f32 v5, v5, v2, 1.0
	v_add_f32_e32 v2, v3, v5
	s_nop 1
	s_waitcnt lgkmcnt(0)
	v_max_f32_dpp v6, v2, v2 quad_perm:[1,0,3,2] row_mask:0xf bank_mask:0xf
	s_nop 1
	s_waitcnt lgkmcnt(0)
	v_max_f32_dpp v6, v6, v6 quad_perm:[2,3,0,1] row_mask:0xf bank_mask:0xf
	s_nop 1
	s_waitcnt lgkmcnt(0)
	v_max_f32_dpp v8, v6, v6 row_half_mirror row_mask:0xf bank_mask:0xf
	v_cmp_eq_f32_e32 vcc, v2, v8
	s_nop 1
	v_lshrrev_b64 v[6:7], v200, vcc
	v_ffbl_b32_sdwa v6, v6 dst_sel:DWORD dst_unused:UNUSED_PAD src0_sel:BYTE_0
	v_add_u32_e32 v6, v6, v200
	v_cmp_ne_u32_e32 vcc, v230, v6
	s_nop 1
	v_cndmask_b32_e32 v6, v245, v2, vcc
	s_nop 1
	s_waitcnt lgkmcnt(0)
	v_max_f32_dpp v6, v6, v6 quad_perm:[1,0,3,2] row_mask:0xf bank_mask:0xf
	s_nop 1
	s_waitcnt lgkmcnt(0)
	v_max_f32_dpp v6, v6, v6 quad_perm:[2,3,0,1] row_mask:0xf bank_mask:0xf
	s_nop 1
	s_waitcnt lgkmcnt(0)
	v_max_f32_dpp v6, v6, v6 row_half_mirror row_mask:0xf bank_mask:0xf
	v_add_f32_e32 v6, v8, v6
	s_nop 0
	v_readlane_b32 s5, v6, 0
	v_readlane_b32 s24, v6, 8
	v_readlane_b32 s28, v6, 16
	v_cmp_eq_f32_e64 s[20:21], s5, v6
	v_cmp_gt_f32_e32 vcc, s5, v6
	v_cmp_gt_f32_e64 s[22:23], s24, v6
	v_cmp_eq_f32_e64 s[24:25], s24, v6
	s_and_b64 s[20:21], s[0:1], s[20:21]
	v_readlane_b32 s34, v6, 24
	v_cmp_gt_f32_e64 s[26:27], s28, v6
	v_cmp_eq_f32_e64 s[28:29], s28, v6
	s_and_b64 s[24:25], s[6:7], s[24:25]
	s_or_b64 s[20:21], vcc, s[20:21]
	v_readlane_b32 s40, v6, 32
	v_cmp_gt_f32_e64 s[30:31], s34, v6
	v_cmp_eq_f32_e64 s[34:35], s34, v6
	s_and_b64 s[28:29], s[8:9], s[28:29]
	v_cndmask_b32_e64 v7, 0, 1, s[20:21]
	s_or_b64 s[20:21], s[22:23], s[24:25]
	v_cmp_gt_f32_e64 s[36:37], s40, v6
	v_cmp_eq_f32_e64 s[40:41], s40, v6
	s_and_b64 s[34:35], s[10:11], s[34:35]
	v_cndmask_b32_e64 v8, 0, 1, s[20:21]
	s_or_b64 s[20:21], s[26:27], s[28:29]
	s_and_b64 s[40:41], s[12:13], s[40:41]
	v_cndmask_b32_e64 v9, 0, 1, s[20:21]
	s_or_b64 s[20:21], s[30:31], s[34:35]
	v_readlane_b32 s55, v6, 40
	v_cndmask_b32_e64 v10, 0, 1, s[20:21]
	s_or_b64 s[20:21], s[36:37], s[40:41]
	v_cndmask_b32_e64 v11, 0, 1, s[20:21]
	v_cmp_eq_f32_e64 s[20:21], s55, v6
	v_cmp_gt_f32_e32 vcc, s55, v6
	s_and_b64 s[20:21], s[14:15], s[20:21]
	s_or_b64 s[20:21], vcc, s[20:21]
	v_readlane_b32 s5, v6, 48
	v_cndmask_b32_e64 v12, 0, 1, s[20:21]
	s_nop 0
	v_cmp_eq_f32_e64 s[20:21], s5, v6
	v_cmp_gt_f32_e32 vcc, s5, v6
	s_and_b64 s[20:21], s[16:17], s[20:21]
	v_readlane_b32 s5, v6, 56
	s_or_b64 s[20:21], vcc, s[20:21]
	v_cndmask_b32_e64 v13, 0, 1, s[20:21]
	v_cmp_gt_f32_e32 vcc, s5, v6
	s_nop 1
	v_cndmask_b32_e64 v6, 0, 1, vcc
	v_add_u32_e32 v6, v8, v6
	v_add3_u32 v6, v6, v7, v9
	v_add3_u32 v6, v6, v10, v11
	v_add3_u32 v6, v6, v12, v13
	v_cmp_gt_u32_e32 vcc, 4, v6
	s_nop 1
	v_cndmask_b32_e32 v6, v245, v2, vcc
	v_mov_b32_e32 v2, 0
	v_ashrrev_i32_e32 v9, 31, v6
	v_sub_u32_e32 v8, 63, v230
	v_and_b32_e32 v9, 0x7fffffff, v9
	v_xor_b32_e32 v9, v6, v9
	s_nop 0
	v_readlane_b32 s23, v9, 0
	s_movk_i32 s22, 63
	v_readlane_b32 s21, v9, 1
	s_movk_i32 s20, 62
	v_cmp_gt_i64_e32 vcc, s[22:23], v[8:9]
	v_readlane_b32 s23, v9, 2
	s_movk_i32 s22, 61
	v_addc_co_u32_e32 v2, vcc, 0, v2, vcc
	v_cmp_gt_i64_e32 vcc, s[20:21], v[8:9]
	v_readlane_b32 s21, v9, 3
	s_movk_i32 s20, 60
	v_addc_co_u32_e32 v2, vcc, 0, v2, vcc
	v_cmp_gt_i64_e32 vcc, s[22:23], v[8:9]
	v_readlane_b32 s23, v9, 4
	s_movk_i32 s22, 59
	v_addc_co_u32_e32 v2, vcc, 0, v2, vcc
	v_cmp_gt_i64_e32 vcc, s[20:21], v[8:9]
	v_readlane_b32 s21, v9, 5
	s_movk_i32 s20, 58
	v_addc_co_u32_e32 v2, vcc, 0, v2, vcc
	v_cmp_gt_i64_e32 vcc, s[22:23], v[8:9]
	v_readlane_b32 s23, v9, 6
	s_movk_i32 s22, 57
	v_addc_co_u32_e32 v2, vcc, 0, v2, vcc
	v_cmp_gt_i64_e32 vcc, s[20:21], v[8:9]
	v_readlane_b32 s21, v9, 7
	s_movk_i32 s20, 56
	v_addc_co_u32_e32 v2, vcc, 0, v2, vcc
	v_cmp_gt_i64_e32 vcc, s[22:23], v[8:9]
	v_readlane_b32 s23, v9, 8
	s_movk_i32 s22, 55
	v_addc_co_u32_e32 v2, vcc, 0, v2, vcc
	v_cmp_gt_i64_e32 vcc, s[20:21], v[8:9]
	v_readlane_b32 s21, v9, 9
	s_movk_i32 s20, 54
	v_addc_co_u32_e32 v2, vcc, 0, v2, vcc
	v_cmp_gt_i64_e32 vcc, s[22:23], v[8:9]
	v_readlane_b32 s23, v9, 10
	s_movk_i32 s22, 53
	v_addc_co_u32_e32 v2, vcc, 0, v2, vcc
	v_cmp_gt_i64_e32 vcc, s[20:21], v[8:9]
	v_readlane_b32 s21, v9, 11
	s_movk_i32 s20, 52
	v_addc_co_u32_e32 v2, vcc, 0, v2, vcc
; __device__ __forceinline__ void phase_nrr(const Frame& F, const Args& a, int l, const bf16_t* XA, const float* g, const float* modl, unsigned char* XN8) {
;     ...
;             int rank = 0;
; #pragma unroll 8
;             for (int e2 = 0; e2 < 64; ++e2) { const float v = __int_as_float(__builtin_amdgcn_readlane(__float_as_int(val), e2)); rank += (v > val || (v == val && e2 < lane)) ? 1 : 0; }
	v_cmp_gt_i64_e32 vcc, s[22:23], v[8:9]
	v_readlane_b32 s23, v9, 12
	s_movk_i32 s22, 51
	v_addc_co_u32_e32 v2, vcc, 0, v2, vcc
	v_cmp_gt_i64_e32 vcc, s[20:21], v[8:9]
	v_readlane_b32 s21, v9, 13
	s_movk_i32 s20, 50
	v_addc_co_u32_e32 v2, vcc, 0, v2, vcc
	v_cmp_gt_i64_e32 vcc, s[22:23], v[8:9]
	v_readlane_b32 s23, v9, 14
	s_movk_i32 s22, 49
	v_addc_co_u32_e32 v2, vcc, 0, v2, vcc
	v_cmp_gt_i64_e32 vcc, s[20:21], v[8:9]
	v_readlane_b32 s21, v9, 15
	s_movk_i32 s20, 48
	v_addc_co_u32_e32 v2, vcc, 0, v2, vcc
	v_cmp_gt_i64_e32 vcc, s[22:23], v[8:9]
	v_readlane_b32 s23, v9, 16
	s_movk_i32 s22, 47
	v_addc_co_u32_e32 v2, vcc, 0, v2, vcc
	v_cmp_gt_i64_e32 vcc, s[20:21], v[8:9]
	v_readlane_b32 s21, v9, 17
	s_movk_i32 s20, 46
	v_addc_co_u32_e32 v2, vcc, 0, v2, vcc
	v_cmp_gt_i64_e32 vcc, s[22:23], v[8:9]
	v_readlane_b32 s23, v9, 18
	s_movk_i32 s22, 45
	v_addc_co_u32_e32 v2, vcc, 0, v2, vcc
	v_cmp_gt_i64_e32 vcc, s[20:21], v[8:9]
	v_readlane_b32 s21, v9, 19
	s_movk_i32 s20, 44
	v_addc_co_u32_e32 v2, vcc, 0, v2, vcc
	v_cmp_gt_i64_e32 vcc, s[22:23], v[8:9]
	v_readlane_b32 s23, v9, 20
	s_movk_i32 s22, 43
	v_addc_co_u32_e32 v2, vcc, 0, v2, vcc
	v_cmp_gt_i64_e32 vcc, s[20:21], v[8:9]
	v_readlane_b32 s21, v9, 21
	s_movk_i32 s20, 42
	v_addc_co_u32_e32 v2, vcc, 0, v2, vcc
	v_cmp_gt_i64_e32 vcc, s[22:23], v[8:9]
	v_readlane_b32 s23, v9, 22
	s_movk_i32 s22, 41
	v_addc_co_u32_e32 v2, vcc, 0, v2, vcc
	v_cmp_gt_i64_e32 vcc, s[20:21], v[8:9]
	v_readlane_b32 s21, v9, 23
	s_movk_i32 s20, 40
	v_addc_co_u32_e32 v2, vcc, 0, v2, vcc
	v_cmp_gt_i64_e32 vcc, s[22:23], v[8:9]
	v_readlane_b32 s23, v9, 24
	s_movk_i32 s22, 39
	v_addc_co_u32_e32 v2, vcc, 0, v2, vcc
	v_cmp_gt_i64_e32 vcc, s[20:21], v[8:9]
	v_readlane_b32 s21, v9, 25
	s_movk_i32 s20, 38
	v_addc_co_u32_e32 v2, vcc, 0, v2, vcc
	v_cmp_gt_i64_e32 vcc, s[22:23], v[8:9]
	v_readlane_b32 s23, v9, 26
	s_movk_i32 s22, 37
	v_addc_co_u32_e32 v2, vcc, 0, v2, vcc
	v_cmp_gt_i64_e32 vcc, s[20:21], v[8:9]
	v_readlane_b32 s21, v9, 27
	s_movk_i32 s20, 36
	v_addc_co_u32_e32 v2, vcc, 0, v2, vcc
	v_cmp_gt_i64_e32 vcc, s[22:23], v[8:9]
	v_readlane_b32 s23, v9, 28
	s_movk_i32 s22, 35
	v_addc_co_u32_e32 v2, vcc, 0, v2, vcc
	v_cmp_gt_i64_e32 vcc, s[20:21], v[8:9]
	v_readlane_b32 s21, v9, 29
	s_movk_i32 s20, 34
	v_addc_co_u32_e32 v2, vcc, 0, v2, vcc
	v_cmp_gt_i64_e32 vcc, s[22:23], v[8:9]
	v_readlane_b32 s23, v9, 30
	s_movk_i32 s22, 33
	v_addc_co_u32_e32 v2, vcc, 0, v2, vcc
	v_cmp_gt_i64_e32 vcc, s[20:21], v[8:9]
	v_readlane_b32 s21, v9, 31
	s_movk_i32 s20, 32
	v_addc_co_u32_e32 v2, vcc, 0, v2, vcc
	v_cmp_gt_i64_e32 vcc, s[22:23], v[8:9]
	v_readlane_b32 s23, v9, 32
	s_movk_i32 s22, 31
	v_addc_co_u32_e32 v2, vcc, 0, v2, vcc
	v_cmp_gt_i64_e32 vcc, s[20:21], v[8:9]
	v_readlane_b32 s21, v9, 33
	s_movk_i32 s20, 30
	v_addc_co_u32_e32 v2, vcc, 0, v2, vcc
	v_cmp_gt_i64_e32 vcc, s[22:23], v[8:9]
	v_readlane_b32 s23, v9, 34
	s_movk_i32 s22, 29
	v_addc_co_u32_e32 v2, vcc, 0, v2, vcc
	v_cmp_gt_i64_e32 vcc, s[20:21], v[8:9]
	v_readlane_b32 s21, v9, 35
	s_movk_i32 s20, 28
	v_addc_co_u32_e32 v2, vcc, 0, v2, vcc
	v_cmp_gt_i64_e32 vcc, s[22:23], v[8:9]
	v_readlane_b32 s23, v9, 36
	s_movk_i32 s22, 27
	v_addc_co_u32_e32 v2, vcc, 0, v2, vcc
	v_cmp_gt_i64_e32 vcc, s[20:21], v[8:9]
	v_readlane_b32 s21, v9, 37
	s_movk_i32 s20, 26
	v_addc_co_u32_e32 v2, vcc, 0, v2, vcc
	v_cmp_gt_i64_e32 vcc, s[22:23], v[8:9]
	v_readlane_b32 s23, v9, 38
	s_movk_i32 s22, 25
	v_addc_co_u32_e32 v2, vcc, 0, v2, vcc
	v_cmp_gt_i64_e32 vcc, s[20:21], v[8:9]
	v_readlane_b32 s21, v9, 39
	s_movk_i32 s20, 24
	v_addc_co_u32_e32 v2, vcc, 0, v2, vcc
	v_cmp_gt_i64_e32 vcc, s[22:23], v[8:9]
	v_readlane_b32 s23, v9, 40
	s_movk_i32 s22, 23
	v_addc_co_u32_e32 v2, vcc, 0, v2, vcc
	v_cmp_gt_i64_e32 vcc, s[20:21], v[8:9]
	v_readlane_b32 s21, v9, 41
	s_movk_i32 s20, 22
	v_addc_co_u32_e32 v2, vcc, 0, v2, vcc
	v_cmp_gt_i64_e32 vcc, s[22:23], v[8:9]
	v_readlane_b32 s23, v9, 42
	s_movk_i32 s22, 21
	v_addc_co_u32_e32 v2, vcc, 0, v2, vcc
	v_cmp_gt_i64_e32 vcc, s[20:21], v[8:9]
	v_readlane_b32 s21, v9, 43
	s_movk_i32 s20, 20
	v_addc_co_u32_e32 v2, vcc, 0, v2, vcc
	v_cmp_gt_i64_e32 vcc, s[22:23], v[8:9]
	v_readlane_b32 s23, v9, 44
	s_movk_i32 s22, 19
	v_addc_co_u32_e32 v2, vcc, 0, v2, vcc
	v_cmp_gt_i64_e32 vcc, s[20:21], v[8:9]
	v_readlane_b32 s21, v9, 45
	s_movk_i32 s20, 18
	v_addc_co_u32_e32 v2, vcc, 0, v2, vcc
	v_cmp_gt_i64_e32 vcc, s[22:23], v[8:9]
	v_readlane_b32 s23, v9, 46
	s_movk_i32 s22, 17
	v_addc_co_u32_e32 v2, vcc, 0, v2, vcc
	v_cmp_gt_i64_e32 vcc, s[20:21], v[8:9]
	v_readlane_b32 s21, v9, 47
	s_movk_i32 s20, 16
	v_addc_co_u32_e32 v2, vcc, 0, v2, vcc
	v_cmp_gt_i64_e32 vcc, s[22:23], v[8:9]
	v_readlane_b32 s23, v9, 48
	s_movk_i32 s22, 15
	v_addc_co_u32_e32 v2, vcc, 0, v2, vcc
	v_cmp_gt_i64_e32 vcc, s[20:21], v[8:9]
	v_readlane_b32 s21, v9, 49
	s_movk_i32 s20, 14
	v_addc_co_u32_e32 v2, vcc, 0, v2, vcc
	v_cmp_gt_i64_e32 vcc, s[22:23], v[8:9]
	v_readlane_b32 s23, v9, 50
	s_movk_i32 s22, 13
	v_addc_co_u32_e32 v2, vcc, 0, v2, vcc
	v_cmp_gt_i64_e32 vcc, s[20:21], v[8:9]
	v_readlane_b32 s21, v9, 51
	s_movk_i32 s20, 12
	v_addc_co_u32_e32 v2, vcc, 0, v2, vcc
	v_cmp_gt_i64_e32 vcc, s[22:23], v[8:9]
	v_readlane_b32 s23, v9, 52
	s_movk_i32 s22, 11
	v_addc_co_u32_e32 v2, vcc, 0, v2, vcc
	v_cmp_gt_i64_e32 vcc, s[20:21], v[8:9]
	v_readlane_b32 s21, v9, 53
	s_movk_i32 s20, 10
	v_addc_co_u32_e32 v2, vcc, 0, v2, vcc
	v_cmp_gt_i64_e32 vcc, s[22:23], v[8:9]
	v_readlane_b32 s23, v9, 54
	s_movk_i32 s22, 9
	v_addc_co_u32_e32 v2, vcc, 0, v2, vcc
	v_cmp_gt_i64_e32 vcc, s[20:21], v[8:9]
	v_readlane_b32 s21, v9, 55
	s_movk_i32 s20, 8
	v_addc_co_u32_e32 v2, vcc, 0, v2, vcc
	v_cmp_gt_i64_e32 vcc, s[22:23], v[8:9]
	v_readlane_b32 s23, v9, 56
	s_movk_i32 s22, 7
	v_addc_co_u32_e32 v2, vcc, 0, v2, vcc
	v_cmp_gt_i64_e32 vcc, s[20:21], v[8:9]
	v_readlane_b32 s21, v9, 57
	s_movk_i32 s20, 6
	v_addc_co_u32_e32 v2, vcc, 0, v2, vcc
	v_cmp_gt_i64_e32 vcc, s[22:23], v[8:9]
	v_readlane_b32 s23, v9, 58
	s_movk_i32 s22, 5
	v_addc_co_u32_e32 v2, vcc, 0, v2, vcc
	v_cmp_gt_i64_e32 vcc, s[20:21], v[8:9]
	v_readlane_b32 s21, v9, 59
	s_movk_i32 s20, 4
	v_addc_co_u32_e32 v2, vcc, 0, v2, vcc
	v_cmp_gt_i64_e32 vcc, s[22:23], v[8:9]
	v_readlane_b32 s23, v9, 60
	s_movk_i32 s22, 3
	v_addc_co_u32_e32 v2, vcc, 0, v2, vcc
	v_cmp_gt_i64_e32 vcc, s[20:21], v[8:9]
	v_readlane_b32 s21, v9, 61
	s_movk_i32 s20, 2
	v_addc_co_u32_e32 v2, vcc, 0, v2, vcc
	v_cmp_gt_i64_e32 vcc, s[22:23], v[8:9]
	v_readlane_b32 s23, v9, 62
	s_movk_i32 s22, 1
	v_addc_co_u32_e32 v2, vcc, 0, v2, vcc
	v_cmp_gt_i64_e32 vcc, s[20:21], v[8:9]
	v_readlane_b32 s21, v9, 63
	s_movk_i32 s20, 0
	v_addc_co_u32_e32 v2, vcc, 0, v2, vcc
	v_cmp_gt_i64_e32 vcc, s[22:23], v[8:9]
	s_nop 1
	v_addc_co_u32_e32 v2, vcc, 0, v2, vcc
	v_cmp_gt_i64_e32 vcc, s[20:21], v[8:9]
	s_nop 1
	v_addc_co_u32_e32 v2, vcc, 0, v2, vcc
	v_cmp_gt_u32_e32 vcc, 6, v2
	s_nop 1
	v_cndmask_b32_e32 v6, 0, v5, vcc
	ds_bpermute_b32 v7, v1, v6
	s_waitcnt lgkmcnt(0)
; __device__ __forceinline__ void phase_nrr(const Frame& F, const Args& a, int l, const bf16_t* XA, const float* g, const float* modl, unsigned char* XN8) {
;     ...
;         for (int i = 0; i < 8; ++i) { const int t = tb + i;
;             const float lg = Pl[(w * 8 + i) * NE + lane] + Pl[(64 + w * 8 + i) * NE + lane]; const float sc = 1.f / (1.f + __expf(-lg)); const float bb = sc + bias;
;             float m1 = bb; m1 = fmaxf(m1, __shfl_xor(m1, 1)); m1 = fmaxf(m1, __shfl_xor(m1, 2)); m1 = fmaxf(m1, __shfl_xor(m1, 4));
;             const unsigned long long eq = __ballot(bb == m1); const int gbase = lane & ~7; const unsigned grpmask = (unsigned)((eq >> gbase) & 0xffull);
;             const int first = gbase + __builtin_ctz(grpmask);
;             float m2 = (lane == first) ? -INFINITY : bb; m2 = fmaxf(m2, __shfl_xor(m2, 1)); m2 = fmaxf(m2, __shfl_xor(m2, 2)); m2 = fmaxf(m2, __shfl_xor(m2, 4));
;             const float gsum = m1 + m2; const int gq = lane >> 3;
;             int grank = 0;
; #pragma unroll
;             for (int g2 = 0; g2 < 8; ++g2) { const float v = __int_as_float(__builtin_amdgcn_readlane(__float_as_int(gsum), g2 * 8)); grank += (v > gsum || (v == gsum && g2 < gq)) ? 1 : 0; }
;             const bool keep = grank < 4; const float val = keep ? bb : -INFINITY;
;             int rank = 0;
; #pragma unroll 8
;             for (int e2 = 0; e2 < 64; ++e2) { const float v = __int_as_float(__builtin_amdgcn_readlane(__float_as_int(val), e2)); rank += (v > val || (v == val && e2 < lane)) ? 1 : 0; }
;             const bool sel = rank < TOPK;
;             const float ssum = wave_sum(sel ? sc : 0.f);
;             if (sel) { const int p = atomicAdd((int*)(hist + lane), 1); top_e[t * TOPK + rank] = lane; gate[t * TOPK + rank] = sc / ssum * 2.5f; lpos[t * TOPK + rank] = p; }
	v_add_f32_e32 v6, v6, v7
	ds_bpermute_b32 v7, v201, v6
	s_waitcnt lgkmcnt(0)
	v_add_f32_e32 v6, v6, v7
	ds_bpermute_b32 v7, v220, v6
	s_waitcnt lgkmcnt(0)
	v_add_f32_e32 v6, v6, v7
	ds_bpermute_b32 v7, v221, v6
	s_waitcnt lgkmcnt(0)
	v_add_f32_e32 v6, v6, v7
	ds_bpermute_b32 v7, v222, v6
	s_waitcnt lgkmcnt(0)
	v_add_f32_e32 v6, v6, v7
	ds_bpermute_b32 v7, v223, v6
	s_and_saveexec_b64 s[20:21], vcc
	s_cbranch_execz .LBB0_1316
	s_waitcnt lgkmcnt(0)
	v_add_f32_e32 v10, v6, v7
	v_mad_u64_u32 v[6:7], s[22:23], s56, 6, v[2:3]
	v_div_scale_f32 v2, s[22:23], v10, v10, v5
	v_rcp_f32_e32 v12, v2
	v_ashrrev_i32_e32 v7, 31, v6
	v_lshlrev_b64 v[6:7], 2, v[6:7]
	v_lshl_add_u64 v[8:9], s[42:43], 0, v[6:7]
	ds_add_rtn_u32 v11, v227, v243
	global_store_dword v[8:9], v230, off
	v_fma_f32 v8, -v2, v12, 1.0
	v_fmac_f32_e32 v12, v8, v12
	v_div_scale_f32 v8, vcc, v5, v10, v5
	v_mul_f32_e32 v9, v8, v12
	v_fma_f32 v13, -v2, v9, v8
	v_fmac_f32_e32 v9, v13, v12
	v_fma_f32 v2, -v2, v9, v8
	v_div_fmas_f32 v2, v2, v12, v9
	v_div_fixup_f32 v2, v2, v10, v5
	v_mul_f32_e32 v2, 0x40200000, v2
	v_lshl_add_u64 v[8:9], s[44:45], 0, v[6:7]
	v_lshl_add_u64 v[6:7], s[46:47], 0, v[6:7]
	global_store_dword v[8:9], v2, off
	s_waitcnt lgkmcnt(0)
	global_store_dword v[6:7], v11, off
.LBB0_1316:
	s_or_b64 exec, exec, s[20:21]
	v_add_u32_e32 v2, s77, v226
	ds_read_b32 v2, v2
	ds_read_b32 v5, v4 offset:16896
	s_mov_b32 s3, 0
	s_waitcnt lgkmcnt(0)
	v_add_f32_e32 v2, v2, v5
	v_mul_f32_e32 v2, 0xbfb8aa3b, v2
	v_exp_f32_e32 v2, v2
	s_nop 0
	v_add_f32_e32 v2, 1.0, v2
	v_div_scale_f32 v5, s[20:21], v2, v2, 1.0
	v_rcp_f32_e32 v6, v5
	v_div_scale_f32 v7, vcc, 1.0, v2, 1.0
	v_fma_f32 v8, -v5, v6, 1.0
	v_fmac_f32_e32 v6, v8, v6
	v_mul_f32_e32 v8, v7, v6
	v_fma_f32 v9, -v5, v8, v7
	v_fmac_f32_e32 v8, v9, v6
	v_fma_f32 v5, -v5, v8, v7
	v_div_fmas_f32 v5, v5, v6, v8
	v_div_fixup_f32 v5, v5, v2, 1.0
	v_add_f32_e32 v2, v3, v5
	s_nop 1
	s_waitcnt lgkmcnt(0)
	v_max_f32_dpp v6, v2, v2 quad_perm:[1,0,3,2] row_mask:0xf bank_mask:0xf
	s_nop 1
	s_waitcnt lgkmcnt(0)
	v_max_f32_dpp v6, v6, v6 quad_perm:[2,3,0,1] row_mask:0xf bank_mask:0xf
	s_nop 1
	s_waitcnt lgkmcnt(0)
	v_max_f32_dpp v8, v6, v6 row_half_mirror row_mask:0xf bank_mask:0xf
	v_cmp_eq_f32_e32 vcc, v2, v8
	s_nop 1
	v_lshrrev_b64 v[6:7], v200, vcc
	v_ffbl_b32_sdwa v6, v6 dst_sel:DWORD dst_unused:UNUSED_PAD src0_sel:BYTE_0
	v_add_u32_e32 v6, v6, v200
	v_cmp_ne_u32_e32 vcc, v230, v6
	s_nop 1
	v_cndmask_b32_e32 v6, v245, v2, vcc
	s_nop 1
	s_waitcnt lgkmcnt(0)
	v_max_f32_dpp v6, v6, v6 quad_perm:[1,0,3,2] row_mask:0xf bank_mask:0xf
	s_nop 1
	s_waitcnt lgkmcnt(0)
	v_max_f32_dpp v6, v6, v6 quad_perm:[2,3,0,1] row_mask:0xf bank_mask:0xf
	s_nop 1
	s_waitcnt lgkmcnt(0)
	v_max_f32_dpp v6, v6, v6 row_half_mirror row_mask:0xf bank_mask:0xf
	v_add_f32_e32 v6, v8, v6
	s_nop 0
	v_readlane_b32 s5, v6, 0
	v_readlane_b32 s24, v6, 8
	v_readlane_b32 s28, v6, 16
	v_cmp_eq_f32_e64 s[20:21], s5, v6
	v_cmp_gt_f32_e32 vcc, s5, v6
	v_cmp_gt_f32_e64 s[22:23], s24, v6
	v_cmp_eq_f32_e64 s[24:25], s24, v6
	s_and_b64 s[20:21], s[0:1], s[20:21]
	v_readlane_b32 s34, v6, 24
	v_cmp_gt_f32_e64 s[26:27], s28, v6
	v_cmp_eq_f32_e64 s[28:29], s28, v6
	s_and_b64 s[24:25], s[6:7], s[24:25]
	s_or_b64 s[20:21], vcc, s[20:21]
	v_readlane_b32 s40, v6, 32
	v_cmp_gt_f32_e64 s[30:31], s34, v6
	v_cmp_eq_f32_e64 s[34:35], s34, v6
	s_and_b64 s[28:29], s[8:9], s[28:29]
	v_cndmask_b32_e64 v7, 0, 1, s[20:21]
	s_or_b64 s[20:21], s[22:23], s[24:25]
	v_cmp_gt_f32_e64 s[36:37], s40, v6
	v_cmp_eq_f32_e64 s[40:41], s40, v6
	s_and_b64 s[34:35], s[10:11], s[34:35]
	v_cndmask_b32_e64 v8, 0, 1, s[20:21]
	s_or_b64 s[20:21], s[26:27], s[28:29]
	s_and_b64 s[40:41], s[12:13], s[40:41]
	v_cndmask_b32_e64 v9, 0, 1, s[20:21]
	s_or_b64 s[20:21], s[30:31], s[34:35]
	v_readlane_b32 s55, v6, 40
	v_cndmask_b32_e64 v10, 0, 1, s[20:21]
	s_or_b64 s[20:21], s[36:37], s[40:41]
	v_cndmask_b32_e64 v11, 0, 1, s[20:21]
	v_cmp_eq_f32_e64 s[20:21], s55, v6
	v_cmp_gt_f32_e32 vcc, s55, v6
	s_and_b64 s[20:21], s[14:15], s[20:21]
	s_or_b64 s[20:21], vcc, s[20:21]
	v_readlane_b32 s5, v6, 48
	v_cndmask_b32_e64 v12, 0, 1, s[20:21]
	s_nop 0
	v_cmp_eq_f32_e64 s[20:21], s5, v6
	v_cmp_gt_f32_e32 vcc, s5, v6
	s_and_b64 s[20:21], s[16:17], s[20:21]
	v_readlane_b32 s5, v6, 56
	s_or_b64 s[20:21], vcc, s[20:21]
	v_cndmask_b32_e64 v13, 0, 1, s[20:21]
	v_cmp_gt_f32_e32 vcc, s5, v6
	s_nop 1
	v_cndmask_b32_e64 v6, 0, 1, vcc
	v_add_u32_e32 v6, v8, v6
	v_add3_u32 v6, v6, v7, v9
	v_add3_u32 v6, v6, v10, v11
	v_add3_u32 v6, v6, v12, v13
	v_cmp_gt_u32_e32 vcc, 4, v6
	s_nop 1
	v_cndmask_b32_e32 v6, v245, v2, vcc
	v_mov_b32_e32 v2, 0
	v_ashrrev_i32_e32 v9, 31, v6
	v_sub_u32_e32 v8, 63, v230
	v_and_b32_e32 v9, 0x7fffffff, v9
	v_xor_b32_e32 v9, v6, v9
	s_nop 0
	v_readlane_b32 s23, v9, 0
	s_movk_i32 s22, 63
	v_readlane_b32 s21, v9, 1
	s_movk_i32 s20, 62
	v_cmp_gt_i64_e32 vcc, s[22:23], v[8:9]
	v_readlane_b32 s23, v9, 2
	s_movk_i32 s22, 61
	v_addc_co_u32_e32 v2, vcc, 0, v2, vcc
	v_cmp_gt_i64_e32 vcc, s[20:21], v[8:9]
	v_readlane_b32 s21, v9, 3
	s_movk_i32 s20, 60
	v_addc_co_u32_e32 v2, vcc, 0, v2, vcc
	v_cmp_gt_i64_e32 vcc, s[22:23], v[8:9]
	v_readlane_b32 s23, v9, 4
	s_movk_i32 s22, 59
	v_addc_co_u32_e32 v2, vcc, 0, v2, vcc
	v_cmp_gt_i64_e32 vcc, s[20:21], v[8:9]
	v_readlane_b32 s21, v9, 5
	s_movk_i32 s20, 58
	v_addc_co_u32_e32 v2, vcc, 0, v2, vcc
	v_cmp_gt_i64_e32 vcc, s[22:23], v[8:9]
	v_readlane_b32 s23, v9, 6
	s_movk_i32 s22, 57
	v_addc_co_u32_e32 v2, vcc, 0, v2, vcc
	v_cmp_gt_i64_e32 vcc, s[20:21], v[8:9]
	v_readlane_b32 s21, v9, 7
	s_movk_i32 s20, 56
	v_addc_co_u32_e32 v2, vcc, 0, v2, vcc
	v_cmp_gt_i64_e32 vcc, s[22:23], v[8:9]
	v_readlane_b32 s23, v9, 8
; __device__ __forceinline__ void phase_nrr(const Frame& F, const Args& a, int l, const bf16_t* XA, const float* g, const float* modl, unsigned char* XN8) {
;     ...
;             int rank = 0;
; #pragma unroll 8
;             for (int e2 = 0; e2 < 64; ++e2) { const float v = __int_as_float(__builtin_amdgcn_readlane(__float_as_int(val), e2)); rank += (v > val || (v == val && e2 < lane)) ? 1 : 0; }
	s_movk_i32 s22, 55
	v_addc_co_u32_e32 v2, vcc, 0, v2, vcc
	v_cmp_gt_i64_e32 vcc, s[20:21], v[8:9]
	v_readlane_b32 s21, v9, 9
	s_movk_i32 s20, 54
	v_addc_co_u32_e32 v2, vcc, 0, v2, vcc
	v_cmp_gt_i64_e32 vcc, s[22:23], v[8:9]
	v_readlane_b32 s23, v9, 10
	s_movk_i32 s22, 53
	v_addc_co_u32_e32 v2, vcc, 0, v2, vcc
	v_cmp_gt_i64_e32 vcc, s[20:21], v[8:9]
	v_readlane_b32 s21, v9, 11
	s_movk_i32 s20, 52
	v_addc_co_u32_e32 v2, vcc, 0, v2, vcc
	v_cmp_gt_i64_e32 vcc, s[22:23], v[8:9]
	v_readlane_b32 s23, v9, 12
	s_movk_i32 s22, 51
	v_addc_co_u32_e32 v2, vcc, 0, v2, vcc
	v_cmp_gt_i64_e32 vcc, s[20:21], v[8:9]
	v_readlane_b32 s21, v9, 13
	s_movk_i32 s20, 50
	v_addc_co_u32_e32 v2, vcc, 0, v2, vcc
	v_cmp_gt_i64_e32 vcc, s[22:23], v[8:9]
	v_readlane_b32 s23, v9, 14
	s_movk_i32 s22, 49
	v_addc_co_u32_e32 v2, vcc, 0, v2, vcc
	v_cmp_gt_i64_e32 vcc, s[20:21], v[8:9]
	v_readlane_b32 s21, v9, 15
	s_movk_i32 s20, 48
	v_addc_co_u32_e32 v2, vcc, 0, v2, vcc
	v_cmp_gt_i64_e32 vcc, s[22:23], v[8:9]
	v_readlane_b32 s23, v9, 16
	s_movk_i32 s22, 47
	v_addc_co_u32_e32 v2, vcc, 0, v2, vcc
	v_cmp_gt_i64_e32 vcc, s[20:21], v[8:9]
	v_readlane_b32 s21, v9, 17
	s_movk_i32 s20, 46
	v_addc_co_u32_e32 v2, vcc, 0, v2, vcc
	v_cmp_gt_i64_e32 vcc, s[22:23], v[8:9]
	v_readlane_b32 s23, v9, 18
	s_movk_i32 s22, 45
	v_addc_co_u32_e32 v2, vcc, 0, v2, vcc
	v_cmp_gt_i64_e32 vcc, s[20:21], v[8:9]
	v_readlane_b32 s21, v9, 19
	s_movk_i32 s20, 44
	v_addc_co_u32_e32 v2, vcc, 0, v2, vcc
	v_cmp_gt_i64_e32 vcc, s[22:23], v[8:9]
	v_readlane_b32 s23, v9, 20
	s_movk_i32 s22, 43
	v_addc_co_u32_e32 v2, vcc, 0, v2, vcc
	v_cmp_gt_i64_e32 vcc, s[20:21], v[8:9]
	v_readlane_b32 s21, v9, 21
	s_movk_i32 s20, 42
	v_addc_co_u32_e32 v2, vcc, 0, v2, vcc
	v_cmp_gt_i64_e32 vcc, s[22:23], v[8:9]
	v_readlane_b32 s23, v9, 22
	s_movk_i32 s22, 41
	v_addc_co_u32_e32 v2, vcc, 0, v2, vcc
	v_cmp_gt_i64_e32 vcc, s[20:21], v[8:9]
	v_readlane_b32 s21, v9, 23
	s_movk_i32 s20, 40
	v_addc_co_u32_e32 v2, vcc, 0, v2, vcc
	v_cmp_gt_i64_e32 vcc, s[22:23], v[8:9]
	v_readlane_b32 s23, v9, 24
	s_movk_i32 s22, 39
	v_addc_co_u32_e32 v2, vcc, 0, v2, vcc
	v_cmp_gt_i64_e32 vcc, s[20:21], v[8:9]
	v_readlane_b32 s21, v9, 25
	s_movk_i32 s20, 38
	v_addc_co_u32_e32 v2, vcc, 0, v2, vcc
	v_cmp_gt_i64_e32 vcc, s[22:23], v[8:9]
	v_readlane_b32 s23, v9, 26
	s_movk_i32 s22, 37
	v_addc_co_u32_e32 v2, vcc, 0, v2, vcc
	v_cmp_gt_i64_e32 vcc, s[20:21], v[8:9]
	v_readlane_b32 s21, v9, 27
	s_movk_i32 s20, 36
	v_addc_co_u32_e32 v2, vcc, 0, v2, vcc
	v_cmp_gt_i64_e32 vcc, s[22:23], v[8:9]
	v_readlane_b32 s23, v9, 28
	s_movk_i32 s22, 35
	v_addc_co_u32_e32 v2, vcc, 0, v2, vcc
	v_cmp_gt_i64_e32 vcc, s[20:21], v[8:9]
	v_readlane_b32 s21, v9, 29
	s_movk_i32 s20, 34
	v_addc_co_u32_e32 v2, vcc, 0, v2, vcc
	v_cmp_gt_i64_e32 vcc, s[22:23], v[8:9]
	v_readlane_b32 s23, v9, 30
	s_movk_i32 s22, 33
	v_addc_co_u32_e32 v2, vcc, 0, v2, vcc
	v_cmp_gt_i64_e32 vcc, s[20:21], v[8:9]
	v_readlane_b32 s21, v9, 31
	s_movk_i32 s20, 32
	v_addc_co_u32_e32 v2, vcc, 0, v2, vcc
	v_cmp_gt_i64_e32 vcc, s[22:23], v[8:9]
	v_readlane_b32 s23, v9, 32
	s_movk_i32 s22, 31
	v_addc_co_u32_e32 v2, vcc, 0, v2, vcc
	v_cmp_gt_i64_e32 vcc, s[20:21], v[8:9]
	v_readlane_b32 s21, v9, 33
	s_movk_i32 s20, 30
	v_addc_co_u32_e32 v2, vcc, 0, v2, vcc
	v_cmp_gt_i64_e32 vcc, s[22:23], v[8:9]
	v_readlane_b32 s23, v9, 34
	s_movk_i32 s22, 29
	v_addc_co_u32_e32 v2, vcc, 0, v2, vcc
	v_cmp_gt_i64_e32 vcc, s[20:21], v[8:9]
	v_readlane_b32 s21, v9, 35
	s_movk_i32 s20, 28
	v_addc_co_u32_e32 v2, vcc, 0, v2, vcc
	v_cmp_gt_i64_e32 vcc, s[22:23], v[8:9]
	v_readlane_b32 s23, v9, 36
	s_movk_i32 s22, 27
	v_addc_co_u32_e32 v2, vcc, 0, v2, vcc
	v_cmp_gt_i64_e32 vcc, s[20:21], v[8:9]
	v_readlane_b32 s21, v9, 37
	s_movk_i32 s20, 26
	v_addc_co_u32_e32 v2, vcc, 0, v2, vcc
	v_cmp_gt_i64_e32 vcc, s[22:23], v[8:9]
	v_readlane_b32 s23, v9, 38
	s_movk_i32 s22, 25
	v_addc_co_u32_e32 v2, vcc, 0, v2, vcc
	v_cmp_gt_i64_e32 vcc, s[20:21], v[8:9]
	v_readlane_b32 s21, v9, 39
	s_movk_i32 s20, 24
	v_addc_co_u32_e32 v2, vcc, 0, v2, vcc
	v_cmp_gt_i64_e32 vcc, s[22:23], v[8:9]
	v_readlane_b32 s23, v9, 40
	s_movk_i32 s22, 23
	v_addc_co_u32_e32 v2, vcc, 0, v2, vcc
	v_cmp_gt_i64_e32 vcc, s[20:21], v[8:9]
	v_readlane_b32 s21, v9, 41
	s_movk_i32 s20, 22
	v_addc_co_u32_e32 v2, vcc, 0, v2, vcc
	v_cmp_gt_i64_e32 vcc, s[22:23], v[8:9]
	v_readlane_b32 s23, v9, 42
	s_movk_i32 s22, 21
	v_addc_co_u32_e32 v2, vcc, 0, v2, vcc
	v_cmp_gt_i64_e32 vcc, s[20:21], v[8:9]
	v_readlane_b32 s21, v9, 43
	s_movk_i32 s20, 20
	v_addc_co_u32_e32 v2, vcc, 0, v2, vcc
	v_cmp_gt_i64_e32 vcc, s[22:23], v[8:9]
	v_readlane_b32 s23, v9, 44
	s_movk_i32 s22, 19
	v_addc_co_u32_e32 v2, vcc, 0, v2, vcc
	v_cmp_gt_i64_e32 vcc, s[20:21], v[8:9]
	v_readlane_b32 s21, v9, 45
	s_movk_i32 s20, 18
	v_addc_co_u32_e32 v2, vcc, 0, v2, vcc
	v_cmp_gt_i64_e32 vcc, s[22:23], v[8:9]
	v_readlane_b32 s23, v9, 46
	s_movk_i32 s22, 17
	v_addc_co_u32_e32 v2, vcc, 0, v2, vcc
	v_cmp_gt_i64_e32 vcc, s[20:21], v[8:9]
	v_readlane_b32 s21, v9, 47
	s_movk_i32 s20, 16
	v_addc_co_u32_e32 v2, vcc, 0, v2, vcc
	v_cmp_gt_i64_e32 vcc, s[22:23], v[8:9]
	v_readlane_b32 s23, v9, 48
	s_movk_i32 s22, 15
	v_addc_co_u32_e32 v2, vcc, 0, v2, vcc
	v_cmp_gt_i64_e32 vcc, s[20:21], v[8:9]
	v_readlane_b32 s21, v9, 49
	s_movk_i32 s20, 14
	v_addc_co_u32_e32 v2, vcc, 0, v2, vcc
	v_cmp_gt_i64_e32 vcc, s[22:23], v[8:9]
	v_readlane_b32 s23, v9, 50
	s_movk_i32 s22, 13
	v_addc_co_u32_e32 v2, vcc, 0, v2, vcc
	v_cmp_gt_i64_e32 vcc, s[20:21], v[8:9]
	v_readlane_b32 s21, v9, 51
	s_movk_i32 s20, 12
	v_addc_co_u32_e32 v2, vcc, 0, v2, vcc
	v_cmp_gt_i64_e32 vcc, s[22:23], v[8:9]
	v_readlane_b32 s23, v9, 52
	s_movk_i32 s22, 11
	v_addc_co_u32_e32 v2, vcc, 0, v2, vcc
; __device__ __forceinline__ void phase_nrr(const Frame& F, const Args& a, int l, const bf16_t* XA, const float* g, const float* modl, unsigned char* XN8) {
;     ...
;         for (int i = 0; i < 8; ++i) { const int t = tb + i;
;             const float lg = Pl[(w * 8 + i) * NE + lane] + Pl[(64 + w * 8 + i) * NE + lane]; const float sc = 1.f / (1.f + __expf(-lg)); const float bb = sc + bias;
;             float m1 = bb; m1 = fmaxf(m1, __shfl_xor(m1, 1)); m1 = fmaxf(m1, __shfl_xor(m1, 2)); m1 = fmaxf(m1, __shfl_xor(m1, 4));
;             const unsigned long long eq = __ballot(bb == m1); const int gbase = lane & ~7; const unsigned grpmask = (unsigned)((eq >> gbase) & 0xffull);
;             const int first = gbase + __builtin_ctz(grpmask);
;             float m2 = (lane == first) ? -INFINITY : bb; m2 = fmaxf(m2, __shfl_xor(m2, 1)); m2 = fmaxf(m2, __shfl_xor(m2, 2)); m2 = fmaxf(m2, __shfl_xor(m2, 4));
;             const float gsum = m1 + m2; const int gq = lane >> 3;
;             int grank = 0;
; #pragma unroll
;             for (int g2 = 0; g2 < 8; ++g2) { const float v = __int_as_float(__builtin_amdgcn_readlane(__float_as_int(gsum), g2 * 8)); grank += (v > gsum || (v == gsum && g2 < gq)) ? 1 : 0; }
;             const bool keep = grank < 4; const float val = keep ? bb : -INFINITY;
;             int rank = 0;
; #pragma unroll 8
;             for (int e2 = 0; e2 < 64; ++e2) { const float v = __int_as_float(__builtin_amdgcn_readlane(__float_as_int(val), e2)); rank += (v > val || (v == val && e2 < lane)) ? 1 : 0; }
;             const bool sel = rank < TOPK;
;             const float ssum = wave_sum(sel ? sc : 0.f);
;             if (sel) { const int p = atomicAdd((int*)(hist + lane), 1); top_e[t * TOPK + rank] = lane; gate[t * TOPK + rank] = sc / ssum * 2.5f; lpos[t * TOPK + rank] = p; }
	v_cmp_gt_i64_e32 vcc, s[20:21], v[8:9]
	v_readlane_b32 s21, v9, 53
	s_movk_i32 s20, 10
	v_addc_co_u32_e32 v2, vcc, 0, v2, vcc
	v_cmp_gt_i64_e32 vcc, s[22:23], v[8:9]
	v_readlane_b32 s23, v9, 54
	s_movk_i32 s22, 9
	v_addc_co_u32_e32 v2, vcc, 0, v2, vcc
	v_cmp_gt_i64_e32 vcc, s[20:21], v[8:9]
	v_readlane_b32 s21, v9, 55
	s_movk_i32 s20, 8
	v_addc_co_u32_e32 v2, vcc, 0, v2, vcc
	v_cmp_gt_i64_e32 vcc, s[22:23], v[8:9]
	v_readlane_b32 s23, v9, 56
	s_movk_i32 s22, 7
	v_addc_co_u32_e32 v2, vcc, 0, v2, vcc
	v_cmp_gt_i64_e32 vcc, s[20:21], v[8:9]
	v_readlane_b32 s21, v9, 57
	s_movk_i32 s20, 6
	v_addc_co_u32_e32 v2, vcc, 0, v2, vcc
	v_cmp_gt_i64_e32 vcc, s[22:23], v[8:9]
	v_readlane_b32 s23, v9, 58
	s_movk_i32 s22, 5
	v_addc_co_u32_e32 v2, vcc, 0, v2, vcc
	v_cmp_gt_i64_e32 vcc, s[20:21], v[8:9]
	v_readlane_b32 s21, v9, 59
	s_movk_i32 s20, 4
	v_addc_co_u32_e32 v2, vcc, 0, v2, vcc
	v_cmp_gt_i64_e32 vcc, s[22:23], v[8:9]
	v_readlane_b32 s23, v9, 60
	s_movk_i32 s22, 3
	v_addc_co_u32_e32 v2, vcc, 0, v2, vcc
	v_cmp_gt_i64_e32 vcc, s[20:21], v[8:9]
	v_readlane_b32 s21, v9, 61
	s_movk_i32 s20, 2
	v_addc_co_u32_e32 v2, vcc, 0, v2, vcc
	v_cmp_gt_i64_e32 vcc, s[22:23], v[8:9]
	v_readlane_b32 s23, v9, 62
	s_movk_i32 s22, 1
	v_addc_co_u32_e32 v2, vcc, 0, v2, vcc
	v_cmp_gt_i64_e32 vcc, s[20:21], v[8:9]
	v_readlane_b32 s21, v9, 63
	s_movk_i32 s20, 0
	v_addc_co_u32_e32 v2, vcc, 0, v2, vcc
	v_cmp_gt_i64_e32 vcc, s[22:23], v[8:9]
	s_nop 1
	v_addc_co_u32_e32 v2, vcc, 0, v2, vcc
	v_cmp_gt_i64_e32 vcc, s[20:21], v[8:9]
	s_nop 1
	v_addc_co_u32_e32 v2, vcc, 0, v2, vcc
	v_cmp_gt_u32_e32 vcc, 6, v2
	s_nop 1
	v_cndmask_b32_e32 v6, 0, v5, vcc
	ds_bpermute_b32 v7, v1, v6
	s_waitcnt lgkmcnt(0)
	v_add_f32_e32 v6, v6, v7
	ds_bpermute_b32 v7, v201, v6
	s_waitcnt lgkmcnt(0)
	v_add_f32_e32 v6, v6, v7
	ds_bpermute_b32 v7, v220, v6
	s_waitcnt lgkmcnt(0)
	v_add_f32_e32 v6, v6, v7
	ds_bpermute_b32 v7, v221, v6
	s_waitcnt lgkmcnt(0)
	v_add_f32_e32 v6, v6, v7
	ds_bpermute_b32 v7, v222, v6
	s_waitcnt lgkmcnt(0)
	v_add_f32_e32 v6, v6, v7
	ds_bpermute_b32 v7, v223, v6
	s_and_saveexec_b64 s[20:21], vcc
	s_cbranch_execz .LBB0_1320
	s_waitcnt lgkmcnt(0)
	v_add_f32_e32 v10, v6, v7
	v_mad_u64_u32 v[6:7], s[22:23], s54, 6, v[2:3]
	v_div_scale_f32 v2, s[22:23], v10, v10, v5
	v_rcp_f32_e32 v12, v2
	v_ashrrev_i32_e32 v7, 31, v6
	v_lshlrev_b64 v[6:7], 2, v[6:7]
	v_lshl_add_u64 v[8:9], s[42:43], 0, v[6:7]
	ds_add_rtn_u32 v11, v227, v243
	global_store_dword v[8:9], v230, off
	v_fma_f32 v8, -v2, v12, 1.0
	v_fmac_f32_e32 v12, v8, v12
	v_div_scale_f32 v8, vcc, v5, v10, v5
	v_mul_f32_e32 v9, v8, v12
	v_fma_f32 v13, -v2, v9, v8
	v_fmac_f32_e32 v9, v13, v12
	v_fma_f32 v2, -v2, v9, v8
	v_div_fmas_f32 v2, v2, v12, v9
	v_div_fixup_f32 v2, v2, v10, v5
	v_mul_f32_e32 v2, 0x40200000, v2
	v_lshl_add_u64 v[8:9], s[44:45], 0, v[6:7]
	v_lshl_add_u64 v[6:7], s[46:47], 0, v[6:7]
	global_store_dword v[8:9], v2, off
	s_waitcnt lgkmcnt(0)
	global_store_dword v[6:7], v11, off
.LBB0_1320:
	s_or_b64 exec, exec, s[20:21]
	v_add_u32_e32 v2, s78, v226
	ds_read_b32 v2, v2
	ds_read_b32 v5, v4 offset:17152
	s_mov_b32 s3, 0
	s_waitcnt lgkmcnt(0)
	v_add_f32_e32 v2, v2, v5
	v_mul_f32_e32 v2, 0xbfb8aa3b, v2
	v_exp_f32_e32 v2, v2
	s_nop 0
	v_add_f32_e32 v2, 1.0, v2
	v_div_scale_f32 v5, s[20:21], v2, v2, 1.0
	v_rcp_f32_e32 v6, v5
	v_div_scale_f32 v7, vcc, 1.0, v2, 1.0
	v_fma_f32 v8, -v5, v6, 1.0
	v_fmac_f32_e32 v6, v8, v6
	v_mul_f32_e32 v8, v7, v6
	v_fma_f32 v9, -v5, v8, v7
	v_fmac_f32_e32 v8, v9, v6
	v_fma_f32 v5, -v5, v8, v7
	v_div_fmas_f32 v5, v5, v6, v8
	v_div_fixup_f32 v5, v5, v2, 1.0
	v_add_f32_e32 v2, v3, v5
	s_nop 1
	s_waitcnt lgkmcnt(0)
	v_max_f32_dpp v6, v2, v2 quad_perm:[1,0,3,2] row_mask:0xf bank_mask:0xf
	s_nop 1
	s_waitcnt lgkmcnt(0)
	v_max_f32_dpp v6, v6, v6 quad_perm:[2,3,0,1] row_mask:0xf bank_mask:0xf
	s_nop 1
	s_waitcnt lgkmcnt(0)
	v_max_f32_dpp v8, v6, v6 row_half_mirror row_mask:0xf bank_mask:0xf
	v_cmp_eq_f32_e32 vcc, v2, v8
	s_nop 1
	v_lshrrev_b64 v[6:7], v200, vcc
	v_ffbl_b32_sdwa v6, v6 dst_sel:DWORD dst_unused:UNUSED_PAD src0_sel:BYTE_0
	v_add_u32_e32 v6, v6, v200
	v_cmp_ne_u32_e32 vcc, v230, v6
	s_nop 1
	v_cndmask_b32_e32 v6, v245, v2, vcc
	s_nop 1
	s_waitcnt lgkmcnt(0)
	v_max_f32_dpp v6, v6, v6 quad_perm:[1,0,3,2] row_mask:0xf bank_mask:0xf
	s_nop 1
	s_waitcnt lgkmcnt(0)
	v_max_f32_dpp v6, v6, v6 quad_perm:[2,3,0,1] row_mask:0xf bank_mask:0xf
	s_nop 1
	s_waitcnt lgkmcnt(0)
; __device__ __forceinline__ void phase_nrr(const Frame& F, const Args& a, int l, const bf16_t* XA, const float* g, const float* modl, unsigned char* XN8) {
;     ...
;             float m2 = (lane == first) ? -INFINITY : bb; m2 = fmaxf(m2, __shfl_xor(m2, 1)); m2 = fmaxf(m2, __shfl_xor(m2, 2)); m2 = fmaxf(m2, __shfl_xor(m2, 4));
;             const float gsum = m1 + m2; const int gq = lane >> 3;
;             int grank = 0;
; #pragma unroll
;             for (int g2 = 0; g2 < 8; ++g2) { const float v = __int_as_float(__builtin_amdgcn_readlane(__float_as_int(gsum), g2 * 8)); grank += (v > gsum || (v == gsum && g2 < gq)) ? 1 : 0; }
;             const bool keep = grank < 4; const float val = keep ? bb : -INFINITY;
;             int rank = 0;
; #pragma unroll 8
;             for (int e2 = 0; e2 < 64; ++e2) { const float v = __int_as_float(__builtin_amdgcn_readlane(__float_as_int(val), e2)); rank += (v > val || (v == val && e2 < lane)) ? 1 : 0; }
	v_max_f32_dpp v6, v6, v6 row_half_mirror row_mask:0xf bank_mask:0xf
	v_add_f32_e32 v6, v8, v6
	s_nop 0
	v_readlane_b32 s5, v6, 0
	v_readlane_b32 s24, v6, 8
	v_readlane_b32 s28, v6, 16
	v_cmp_eq_f32_e64 s[20:21], s5, v6
	v_cmp_gt_f32_e32 vcc, s5, v6
	v_cmp_gt_f32_e64 s[22:23], s24, v6
	v_cmp_eq_f32_e64 s[24:25], s24, v6
	s_and_b64 s[20:21], s[0:1], s[20:21]
	v_readlane_b32 s34, v6, 24
	v_cmp_gt_f32_e64 s[26:27], s28, v6
	v_cmp_eq_f32_e64 s[28:29], s28, v6
	s_and_b64 s[24:25], s[6:7], s[24:25]
	s_or_b64 s[20:21], vcc, s[20:21]
	v_readlane_b32 s40, v6, 32
	v_cmp_gt_f32_e64 s[30:31], s34, v6
	v_cmp_eq_f32_e64 s[34:35], s34, v6
	s_and_b64 s[28:29], s[8:9], s[28:29]
	v_cndmask_b32_e64 v7, 0, 1, s[20:21]
	s_or_b64 s[20:21], s[22:23], s[24:25]
	v_cmp_gt_f32_e64 s[36:37], s40, v6
	v_cmp_eq_f32_e64 s[40:41], s40, v6
	s_and_b64 s[34:35], s[10:11], s[34:35]
	v_cndmask_b32_e64 v8, 0, 1, s[20:21]
	s_or_b64 s[20:21], s[26:27], s[28:29]
	s_and_b64 s[40:41], s[12:13], s[40:41]
	v_cndmask_b32_e64 v9, 0, 1, s[20:21]
	s_or_b64 s[20:21], s[30:31], s[34:35]
	v_readlane_b32 s54, v6, 40
	v_cndmask_b32_e64 v10, 0, 1, s[20:21]
	s_or_b64 s[20:21], s[36:37], s[40:41]
	v_cndmask_b32_e64 v11, 0, 1, s[20:21]
	v_cmp_eq_f32_e64 s[20:21], s54, v6
	v_cmp_gt_f32_e32 vcc, s54, v6
	s_and_b64 s[20:21], s[14:15], s[20:21]
	s_or_b64 s[20:21], vcc, s[20:21]
	v_readlane_b32 s5, v6, 48
	v_cndmask_b32_e64 v12, 0, 1, s[20:21]
	s_nop 0
	v_cmp_eq_f32_e64 s[20:21], s5, v6
	v_cmp_gt_f32_e32 vcc, s5, v6
	s_and_b64 s[20:21], s[16:17], s[20:21]
	v_readlane_b32 s5, v6, 56
	s_or_b64 s[20:21], vcc, s[20:21]
	v_cndmask_b32_e64 v13, 0, 1, s[20:21]
	v_cmp_gt_f32_e32 vcc, s5, v6
	s_nop 1
	v_cndmask_b32_e64 v6, 0, 1, vcc
	v_add_u32_e32 v6, v8, v6
	v_add3_u32 v6, v6, v7, v9
	v_add3_u32 v6, v6, v10, v11
	v_add3_u32 v6, v6, v12, v13
	v_cmp_gt_u32_e32 vcc, 4, v6
	s_nop 1
	v_cndmask_b32_e32 v6, v245, v2, vcc
	v_mov_b32_e32 v2, 0
	v_ashrrev_i32_e32 v9, 31, v6
	v_sub_u32_e32 v8, 63, v230
	v_and_b32_e32 v9, 0x7fffffff, v9
	v_xor_b32_e32 v9, v6, v9
	s_nop 0
	v_readlane_b32 s23, v9, 0
	s_movk_i32 s22, 63
	v_readlane_b32 s21, v9, 1
	s_movk_i32 s20, 62
	v_cmp_gt_i64_e32 vcc, s[22:23], v[8:9]
	v_readlane_b32 s23, v9, 2
	s_movk_i32 s22, 61
	v_addc_co_u32_e32 v2, vcc, 0, v2, vcc
	v_cmp_gt_i64_e32 vcc, s[20:21], v[8:9]
	v_readlane_b32 s21, v9, 3
	s_movk_i32 s20, 60
	v_addc_co_u32_e32 v2, vcc, 0, v2, vcc
	v_cmp_gt_i64_e32 vcc, s[22:23], v[8:9]
	v_readlane_b32 s23, v9, 4
	s_movk_i32 s22, 59
	v_addc_co_u32_e32 v2, vcc, 0, v2, vcc
	v_cmp_gt_i64_e32 vcc, s[20:21], v[8:9]
	v_readlane_b32 s21, v9, 5
	s_movk_i32 s20, 58
	v_addc_co_u32_e32 v2, vcc, 0, v2, vcc
	v_cmp_gt_i64_e32 vcc, s[22:23], v[8:9]
	v_readlane_b32 s23, v9, 6
	s_movk_i32 s22, 57
	v_addc_co_u32_e32 v2, vcc, 0, v2, vcc
	v_cmp_gt_i64_e32 vcc, s[20:21], v[8:9]
	v_readlane_b32 s21, v9, 7
	s_movk_i32 s20, 56
	v_addc_co_u32_e32 v2, vcc, 0, v2, vcc
	v_cmp_gt_i64_e32 vcc, s[22:23], v[8:9]
	v_readlane_b32 s23, v9, 8
	s_movk_i32 s22, 55
	v_addc_co_u32_e32 v2, vcc, 0, v2, vcc
	v_cmp_gt_i64_e32 vcc, s[20:21], v[8:9]
	v_readlane_b32 s21, v9, 9
	s_movk_i32 s20, 54
	v_addc_co_u32_e32 v2, vcc, 0, v2, vcc
	v_cmp_gt_i64_e32 vcc, s[22:23], v[8:9]
	v_readlane_b32 s23, v9, 10
	s_movk_i32 s22, 53
	v_addc_co_u32_e32 v2, vcc, 0, v2, vcc
	v_cmp_gt_i64_e32 vcc, s[20:21], v[8:9]
	v_readlane_b32 s21, v9, 11
	s_movk_i32 s20, 52
	v_addc_co_u32_e32 v2, vcc, 0, v2, vcc
	v_cmp_gt_i64_e32 vcc, s[22:23], v[8:9]
	v_readlane_b32 s23, v9, 12
	s_movk_i32 s22, 51
	v_addc_co_u32_e32 v2, vcc, 0, v2, vcc
	v_cmp_gt_i64_e32 vcc, s[20:21], v[8:9]
	v_readlane_b32 s21, v9, 13
	s_movk_i32 s20, 50
	v_addc_co_u32_e32 v2, vcc, 0, v2, vcc
	v_cmp_gt_i64_e32 vcc, s[22:23], v[8:9]
	v_readlane_b32 s23, v9, 14
	s_movk_i32 s22, 49
	v_addc_co_u32_e32 v2, vcc, 0, v2, vcc
	v_cmp_gt_i64_e32 vcc, s[20:21], v[8:9]
	v_readlane_b32 s21, v9, 15
	s_movk_i32 s20, 48
	v_addc_co_u32_e32 v2, vcc, 0, v2, vcc
	v_cmp_gt_i64_e32 vcc, s[22:23], v[8:9]
	v_readlane_b32 s23, v9, 16
	s_movk_i32 s22, 47
	v_addc_co_u32_e32 v2, vcc, 0, v2, vcc
	v_cmp_gt_i64_e32 vcc, s[20:21], v[8:9]
	v_readlane_b32 s21, v9, 17
	s_movk_i32 s20, 46
	v_addc_co_u32_e32 v2, vcc, 0, v2, vcc
	v_cmp_gt_i64_e32 vcc, s[22:23], v[8:9]
	v_readlane_b32 s23, v9, 18
	s_movk_i32 s22, 45
	v_addc_co_u32_e32 v2, vcc, 0, v2, vcc
	v_cmp_gt_i64_e32 vcc, s[20:21], v[8:9]
	v_readlane_b32 s21, v9, 19
	s_movk_i32 s20, 44
	v_addc_co_u32_e32 v2, vcc, 0, v2, vcc
	v_cmp_gt_i64_e32 vcc, s[22:23], v[8:9]
	v_readlane_b32 s23, v9, 20
	s_movk_i32 s22, 43
	v_addc_co_u32_e32 v2, vcc, 0, v2, vcc
	v_cmp_gt_i64_e32 vcc, s[20:21], v[8:9]
	v_readlane_b32 s21, v9, 21
	s_movk_i32 s20, 42
	v_addc_co_u32_e32 v2, vcc, 0, v2, vcc
	v_cmp_gt_i64_e32 vcc, s[22:23], v[8:9]
	v_readlane_b32 s23, v9, 22
	s_movk_i32 s22, 41
	v_addc_co_u32_e32 v2, vcc, 0, v2, vcc
	v_cmp_gt_i64_e32 vcc, s[20:21], v[8:9]
	v_readlane_b32 s21, v9, 23
	s_movk_i32 s20, 40
	v_addc_co_u32_e32 v2, vcc, 0, v2, vcc
	v_cmp_gt_i64_e32 vcc, s[22:23], v[8:9]
	v_readlane_b32 s23, v9, 24
	s_movk_i32 s22, 39
	v_addc_co_u32_e32 v2, vcc, 0, v2, vcc
	v_cmp_gt_i64_e32 vcc, s[20:21], v[8:9]
	v_readlane_b32 s21, v9, 25
	s_movk_i32 s20, 38
	v_addc_co_u32_e32 v2, vcc, 0, v2, vcc
	v_cmp_gt_i64_e32 vcc, s[22:23], v[8:9]
	v_readlane_b32 s23, v9, 26
	s_movk_i32 s22, 37
	v_addc_co_u32_e32 v2, vcc, 0, v2, vcc
	v_cmp_gt_i64_e32 vcc, s[20:21], v[8:9]
	v_readlane_b32 s21, v9, 27
	s_movk_i32 s20, 36
	v_addc_co_u32_e32 v2, vcc, 0, v2, vcc
	v_cmp_gt_i64_e32 vcc, s[22:23], v[8:9]
	v_readlane_b32 s23, v9, 28
	s_movk_i32 s22, 35
	v_addc_co_u32_e32 v2, vcc, 0, v2, vcc
	v_cmp_gt_i64_e32 vcc, s[20:21], v[8:9]
	v_readlane_b32 s21, v9, 29
	s_movk_i32 s20, 34
; __device__ __forceinline__ void phase_nrr(const Frame& F, const Args& a, int l, const bf16_t* XA, const float* g, const float* modl, unsigned char* XN8) {
;     ...
;             int rank = 0;
; #pragma unroll 8
;             for (int e2 = 0; e2 < 64; ++e2) { const float v = __int_as_float(__builtin_amdgcn_readlane(__float_as_int(val), e2)); rank += (v > val || (v == val && e2 < lane)) ? 1 : 0; }
;             const bool sel = rank < TOPK;
;             const float ssum = wave_sum(sel ? sc : 0.f);
;             if (sel) { const int p = atomicAdd((int*)(hist + lane), 1); top_e[t * TOPK + rank] = lane; gate[t * TOPK + rank] = sc / ssum * 2.5f; lpos[t * TOPK + rank] = p; }
	v_addc_co_u32_e32 v2, vcc, 0, v2, vcc
	v_cmp_gt_i64_e32 vcc, s[22:23], v[8:9]
	v_readlane_b32 s23, v9, 30
	s_movk_i32 s22, 33
	v_addc_co_u32_e32 v2, vcc, 0, v2, vcc
	v_cmp_gt_i64_e32 vcc, s[20:21], v[8:9]
	v_readlane_b32 s21, v9, 31
	s_movk_i32 s20, 32
	v_addc_co_u32_e32 v2, vcc, 0, v2, vcc
	v_cmp_gt_i64_e32 vcc, s[22:23], v[8:9]
	v_readlane_b32 s23, v9, 32
	s_movk_i32 s22, 31
	v_addc_co_u32_e32 v2, vcc, 0, v2, vcc
	v_cmp_gt_i64_e32 vcc, s[20:21], v[8:9]
	v_readlane_b32 s21, v9, 33
	s_movk_i32 s20, 30
	v_addc_co_u32_e32 v2, vcc, 0, v2, vcc
	v_cmp_gt_i64_e32 vcc, s[22:23], v[8:9]
	v_readlane_b32 s23, v9, 34
	s_movk_i32 s22, 29
	v_addc_co_u32_e32 v2, vcc, 0, v2, vcc
	v_cmp_gt_i64_e32 vcc, s[20:21], v[8:9]
	v_readlane_b32 s21, v9, 35
	s_movk_i32 s20, 28
	v_addc_co_u32_e32 v2, vcc, 0, v2, vcc
	v_cmp_gt_i64_e32 vcc, s[22:23], v[8:9]
	v_readlane_b32 s23, v9, 36
	s_movk_i32 s22, 27
	v_addc_co_u32_e32 v2, vcc, 0, v2, vcc
	v_cmp_gt_i64_e32 vcc, s[20:21], v[8:9]
	v_readlane_b32 s21, v9, 37
	s_movk_i32 s20, 26
	v_addc_co_u32_e32 v2, vcc, 0, v2, vcc
	v_cmp_gt_i64_e32 vcc, s[22:23], v[8:9]
	v_readlane_b32 s23, v9, 38
	s_movk_i32 s22, 25
	v_addc_co_u32_e32 v2, vcc, 0, v2, vcc
	v_cmp_gt_i64_e32 vcc, s[20:21], v[8:9]
	v_readlane_b32 s21, v9, 39
	s_movk_i32 s20, 24
	v_addc_co_u32_e32 v2, vcc, 0, v2, vcc
	v_cmp_gt_i64_e32 vcc, s[22:23], v[8:9]
	v_readlane_b32 s23, v9, 40
	s_movk_i32 s22, 23
	v_addc_co_u32_e32 v2, vcc, 0, v2, vcc
	v_cmp_gt_i64_e32 vcc, s[20:21], v[8:9]
	v_readlane_b32 s21, v9, 41
	s_movk_i32 s20, 22
	v_addc_co_u32_e32 v2, vcc, 0, v2, vcc
	v_cmp_gt_i64_e32 vcc, s[22:23], v[8:9]
	v_readlane_b32 s23, v9, 42
	s_movk_i32 s22, 21
	v_addc_co_u32_e32 v2, vcc, 0, v2, vcc
	v_cmp_gt_i64_e32 vcc, s[20:21], v[8:9]
	v_readlane_b32 s21, v9, 43
	s_movk_i32 s20, 20
	v_addc_co_u32_e32 v2, vcc, 0, v2, vcc
	v_cmp_gt_i64_e32 vcc, s[22:23], v[8:9]
	v_readlane_b32 s23, v9, 44
	s_movk_i32 s22, 19
	v_addc_co_u32_e32 v2, vcc, 0, v2, vcc
	v_cmp_gt_i64_e32 vcc, s[20:21], v[8:9]
	v_readlane_b32 s21, v9, 45
	s_movk_i32 s20, 18
	v_addc_co_u32_e32 v2, vcc, 0, v2, vcc
	v_cmp_gt_i64_e32 vcc, s[22:23], v[8:9]
	v_readlane_b32 s23, v9, 46
	s_movk_i32 s22, 17
	v_addc_co_u32_e32 v2, vcc, 0, v2, vcc
	v_cmp_gt_i64_e32 vcc, s[20:21], v[8:9]
	v_readlane_b32 s21, v9, 47
	s_movk_i32 s20, 16
	v_addc_co_u32_e32 v2, vcc, 0, v2, vcc
	v_cmp_gt_i64_e32 vcc, s[22:23], v[8:9]
	v_readlane_b32 s23, v9, 48
	s_movk_i32 s22, 15
	v_addc_co_u32_e32 v2, vcc, 0, v2, vcc
	v_cmp_gt_i64_e32 vcc, s[20:21], v[8:9]
	v_readlane_b32 s21, v9, 49
	s_movk_i32 s20, 14
	v_addc_co_u32_e32 v2, vcc, 0, v2, vcc
	v_cmp_gt_i64_e32 vcc, s[22:23], v[8:9]
	v_readlane_b32 s23, v9, 50
	s_movk_i32 s22, 13
	v_addc_co_u32_e32 v2, vcc, 0, v2, vcc
	v_cmp_gt_i64_e32 vcc, s[20:21], v[8:9]
	v_readlane_b32 s21, v9, 51
	s_movk_i32 s20, 12
	v_addc_co_u32_e32 v2, vcc, 0, v2, vcc
	v_cmp_gt_i64_e32 vcc, s[22:23], v[8:9]
	v_readlane_b32 s23, v9, 52
	s_movk_i32 s22, 11
	v_addc_co_u32_e32 v2, vcc, 0, v2, vcc
	v_cmp_gt_i64_e32 vcc, s[20:21], v[8:9]
	v_readlane_b32 s21, v9, 53
	s_movk_i32 s20, 10
	v_addc_co_u32_e32 v2, vcc, 0, v2, vcc
	v_cmp_gt_i64_e32 vcc, s[22:23], v[8:9]
	v_readlane_b32 s23, v9, 54
	s_movk_i32 s22, 9
	v_addc_co_u32_e32 v2, vcc, 0, v2, vcc
	v_cmp_gt_i64_e32 vcc, s[20:21], v[8:9]
	v_readlane_b32 s21, v9, 55
	s_movk_i32 s20, 8
	v_addc_co_u32_e32 v2, vcc, 0, v2, vcc
	v_cmp_gt_i64_e32 vcc, s[22:23], v[8:9]
	v_readlane_b32 s23, v9, 56
	s_movk_i32 s22, 7
	v_addc_co_u32_e32 v2, vcc, 0, v2, vcc
	v_cmp_gt_i64_e32 vcc, s[20:21], v[8:9]
	v_readlane_b32 s21, v9, 57
	s_movk_i32 s20, 6
	v_addc_co_u32_e32 v2, vcc, 0, v2, vcc
	v_cmp_gt_i64_e32 vcc, s[22:23], v[8:9]
	v_readlane_b32 s23, v9, 58
	s_movk_i32 s22, 5
	v_addc_co_u32_e32 v2, vcc, 0, v2, vcc
	v_cmp_gt_i64_e32 vcc, s[20:21], v[8:9]
	v_readlane_b32 s21, v9, 59
	s_movk_i32 s20, 4
	v_addc_co_u32_e32 v2, vcc, 0, v2, vcc
	v_cmp_gt_i64_e32 vcc, s[22:23], v[8:9]
	v_readlane_b32 s23, v9, 60
	s_movk_i32 s22, 3
	v_addc_co_u32_e32 v2, vcc, 0, v2, vcc
	v_cmp_gt_i64_e32 vcc, s[20:21], v[8:9]
	v_readlane_b32 s21, v9, 61
	s_movk_i32 s20, 2
	v_addc_co_u32_e32 v2, vcc, 0, v2, vcc
	v_cmp_gt_i64_e32 vcc, s[22:23], v[8:9]
	v_readlane_b32 s23, v9, 62
	s_movk_i32 s22, 1
	v_addc_co_u32_e32 v2, vcc, 0, v2, vcc
	v_cmp_gt_i64_e32 vcc, s[20:21], v[8:9]
	v_readlane_b32 s21, v9, 63
	s_movk_i32 s20, 0
	v_addc_co_u32_e32 v2, vcc, 0, v2, vcc
	v_cmp_gt_i64_e32 vcc, s[22:23], v[8:9]
	s_nop 1
	v_addc_co_u32_e32 v2, vcc, 0, v2, vcc
	v_cmp_gt_i64_e32 vcc, s[20:21], v[8:9]
	s_nop 1
	v_addc_co_u32_e32 v2, vcc, 0, v2, vcc
	v_cmp_gt_u32_e32 vcc, 6, v2
	s_nop 1
	v_cndmask_b32_e32 v6, 0, v5, vcc
	ds_bpermute_b32 v7, v1, v6
	s_waitcnt lgkmcnt(0)
	v_add_f32_e32 v6, v6, v7
	ds_bpermute_b32 v7, v201, v6
	s_waitcnt lgkmcnt(0)
	v_add_f32_e32 v6, v6, v7
	ds_bpermute_b32 v7, v220, v6
	s_waitcnt lgkmcnt(0)
	v_add_f32_e32 v6, v6, v7
	ds_bpermute_b32 v7, v221, v6
	s_waitcnt lgkmcnt(0)
	v_add_f32_e32 v6, v6, v7
	ds_bpermute_b32 v7, v222, v6
	s_waitcnt lgkmcnt(0)
	v_add_f32_e32 v6, v6, v7
	ds_bpermute_b32 v7, v223, v6
	s_and_saveexec_b64 s[20:21], vcc
	s_cbranch_execz .LBB0_1324
	s_waitcnt lgkmcnt(0)
	v_add_f32_e32 v10, v6, v7
	v_mad_u64_u32 v[6:7], s[4:5], s4, 6, v[2:3]
	v_div_scale_f32 v2, s[4:5], v10, v10, v5
	v_rcp_f32_e32 v12, v2
	v_ashrrev_i32_e32 v7, 31, v6
	v_lshlrev_b64 v[6:7], 2, v[6:7]
	v_lshl_add_u64 v[8:9], s[42:43], 0, v[6:7]
	ds_add_rtn_u32 v11, v227, v243
	global_store_dword v[8:9], v230, off
	v_fma_f32 v8, -v2, v12, 1.0
	v_fmac_f32_e32 v12, v8, v12
	v_div_scale_f32 v8, vcc, v5, v10, v5
	v_mul_f32_e32 v9, v8, v12
	v_fma_f32 v13, -v2, v9, v8
	v_fmac_f32_e32 v9, v13, v12
	v_fma_f32 v2, -v2, v9, v8
	v_div_fmas_f32 v2, v2, v12, v9
	v_div_fixup_f32 v2, v2, v10, v5
	v_mul_f32_e32 v2, 0x40200000, v2
	v_lshl_add_u64 v[8:9], s[44:45], 0, v[6:7]
	v_lshl_add_u64 v[6:7], s[46:47], 0, v[6:7]
	global_store_dword v[8:9], v2, off
	s_waitcnt lgkmcnt(0)
	global_store_dword v[6:7], v11, off
; __device__ __forceinline__ void phase_nrr(const Frame& F, const Args& a, int l, const bf16_t* XA, const float* g, const float* modl, unsigned char* XN8) {
;     ...
;         for (int i = 0; i < 8; ++i) { const int t = tb + i;
;             const float lg = Pl[(w * 8 + i) * NE + lane] + Pl[(64 + w * 8 + i) * NE + lane]; const float sc = 1.f / (1.f + __expf(-lg)); const float bb = sc + bias;
;             float m1 = bb; m1 = fmaxf(m1, __shfl_xor(m1, 1)); m1 = fmaxf(m1, __shfl_xor(m1, 2)); m1 = fmaxf(m1, __shfl_xor(m1, 4));
;             const unsigned long long eq = __ballot(bb == m1); const int gbase = lane & ~7; const unsigned grpmask = (unsigned)((eq >> gbase) & 0xffull);
;             const int first = gbase + __builtin_ctz(grpmask);
;             float m2 = (lane == first) ? -INFINITY : bb; m2 = fmaxf(m2, __shfl_xor(m2, 1)); m2 = fmaxf(m2, __shfl_xor(m2, 2)); m2 = fmaxf(m2, __shfl_xor(m2, 4));
;             const float gsum = m1 + m2; const int gq = lane >> 3;
;             int grank = 0;
; #pragma unroll
;             for (int g2 = 0; g2 < 8; ++g2) { const float v = __int_as_float(__builtin_amdgcn_readlane(__float_as_int(gsum), g2 * 8)); grank += (v > gsum || (v == gsum && g2 < gq)) ? 1 : 0; }
;             const bool keep = grank < 4; const float val = keep ? bb : -INFINITY;
;             int rank = 0;
; #pragma unroll 8
;             for (int e2 = 0; e2 < 64; ++e2) { const float v = __int_as_float(__builtin_amdgcn_readlane(__float_as_int(val), e2)); rank += (v > val || (v == val && e2 < lane)) ? 1 : 0; }
.LBB0_1324:
	s_or_b64 exec, exec, s[20:21]
	v_add_u32_e32 v2, s79, v226
	ds_read_b32 v2, v2
	ds_read_b32 v5, v4 offset:17408
	s_mov_b32 s3, 0
	s_waitcnt lgkmcnt(0)
	v_add_f32_e32 v2, v2, v5
	v_mul_f32_e32 v2, 0xbfb8aa3b, v2
	v_exp_f32_e32 v2, v2
	s_nop 0
	v_add_f32_e32 v2, 1.0, v2
	v_div_scale_f32 v5, s[4:5], v2, v2, 1.0
	v_rcp_f32_e32 v6, v5
	v_div_scale_f32 v7, vcc, 1.0, v2, 1.0
	v_fma_f32 v8, -v5, v6, 1.0
	v_fmac_f32_e32 v6, v8, v6
	v_mul_f32_e32 v8, v7, v6
	v_fma_f32 v9, -v5, v8, v7
	v_fmac_f32_e32 v8, v9, v6
	v_fma_f32 v5, -v5, v8, v7
	v_div_fmas_f32 v5, v5, v6, v8
	v_div_fixup_f32 v2, v5, v2, 1.0
	v_add_f32_e32 v5, v3, v2
	s_nop 1
	s_waitcnt lgkmcnt(0)
	v_max_f32_dpp v6, v5, v5 quad_perm:[1,0,3,2] row_mask:0xf bank_mask:0xf
	s_nop 1
	s_waitcnt lgkmcnt(0)
	v_max_f32_dpp v6, v6, v6 quad_perm:[2,3,0,1] row_mask:0xf bank_mask:0xf
	s_nop 1
	s_waitcnt lgkmcnt(0)
	v_max_f32_dpp v8, v6, v6 row_half_mirror row_mask:0xf bank_mask:0xf
	v_cmp_eq_f32_e32 vcc, v5, v8
	s_nop 1
	v_lshrrev_b64 v[6:7], v200, vcc
	v_ffbl_b32_sdwa v6, v6 dst_sel:DWORD dst_unused:UNUSED_PAD src0_sel:BYTE_0
	v_add_u32_e32 v6, v6, v200
	v_cmp_ne_u32_e32 vcc, v230, v6
	s_nop 1
	v_cndmask_b32_e32 v6, v245, v5, vcc
	s_nop 1
	s_waitcnt lgkmcnt(0)
	v_max_f32_dpp v6, v6, v6 quad_perm:[1,0,3,2] row_mask:0xf bank_mask:0xf
	s_nop 1
	s_waitcnt lgkmcnt(0)
	v_max_f32_dpp v6, v6, v6 quad_perm:[2,3,0,1] row_mask:0xf bank_mask:0xf
	s_nop 1
	s_waitcnt lgkmcnt(0)
	v_max_f32_dpp v6, v6, v6 row_half_mirror row_mask:0xf bank_mask:0xf
	v_add_f32_e32 v6, v8, v6
	s_nop 0
	v_readlane_b32 s4, v6, 0
	v_readlane_b32 s5, v6, 8
	v_readlane_b32 s28, v6, 16
	v_cmp_eq_f32_e64 s[20:21], s4, v6
	v_cmp_gt_f32_e32 vcc, s4, v6
	v_cmp_gt_f32_e64 s[22:23], s5, v6
	v_cmp_eq_f32_e64 s[24:25], s5, v6
	s_and_b64 s[4:5], s[0:1], s[20:21]
	v_readlane_b32 s34, v6, 24
	v_cmp_gt_f32_e64 s[26:27], s28, v6
	v_cmp_eq_f32_e64 s[28:29], s28, v6
	s_and_b64 s[20:21], s[6:7], s[24:25]
	s_or_b64 s[4:5], vcc, s[4:5]
	v_readlane_b32 s40, v6, 32
	v_cmp_gt_f32_e64 s[30:31], s34, v6
	v_cmp_eq_f32_e64 s[34:35], s34, v6
	s_and_b64 s[24:25], s[8:9], s[28:29]
	v_cndmask_b32_e64 v7, 0, 1, s[4:5]
	s_or_b64 s[4:5], s[22:23], s[20:21]
	v_cmp_gt_f32_e64 s[36:37], s40, v6
	v_cmp_eq_f32_e64 s[40:41], s40, v6
	s_and_b64 s[28:29], s[10:11], s[34:35]
	v_cndmask_b32_e64 v8, 0, 1, s[4:5]
	s_or_b64 s[4:5], s[26:27], s[24:25]
	v_readlane_b32 s54, v6, 40
	s_and_b64 s[34:35], s[12:13], s[40:41]
	v_cndmask_b32_e64 v9, 0, 1, s[4:5]
	s_or_b64 s[4:5], s[30:31], s[28:29]
	v_cndmask_b32_e64 v10, 0, 1, s[4:5]
	s_or_b64 s[4:5], s[36:37], s[34:35]
	v_cmp_eq_f32_e64 s[20:21], s54, v6
	v_cndmask_b32_e64 v11, 0, 1, s[4:5]
	v_cmp_gt_f32_e32 vcc, s54, v6
	s_and_b64 s[4:5], s[14:15], s[20:21]
	s_or_b64 s[4:5], vcc, s[4:5]
	v_cndmask_b32_e64 v12, 0, 1, s[4:5]
	v_readlane_b32 s4, v6, 48
	s_nop 1
	v_cmp_eq_f32_e64 s[20:21], s4, v6
	v_cmp_gt_f32_e32 vcc, s4, v6
	s_and_b64 s[4:5], s[16:17], s[20:21]
	s_or_b64 s[4:5], vcc, s[4:5]
	v_cndmask_b32_e64 v13, 0, 1, s[4:5]
	v_readlane_b32 s4, v6, 56
	s_nop 1
	v_cmp_gt_f32_e32 vcc, s4, v6
	s_nop 1
	v_cndmask_b32_e64 v6, 0, 1, vcc
	v_add_u32_e32 v6, v8, v6
	v_add3_u32 v6, v6, v7, v9
	v_add3_u32 v6, v6, v10, v11
	v_add3_u32 v6, v6, v12, v13
	v_cmp_gt_u32_e32 vcc, 4, v6
	v_mov_b32_e32 v6, 0
	s_nop 0
	v_cndmask_b32_e32 v5, v245, v5, vcc
	v_ashrrev_i32_e32 v9, 31, v5
	v_sub_u32_e32 v8, 63, v230
	v_and_b32_e32 v9, 0x7fffffff, v9
	v_xor_b32_e32 v9, v5, v9
	s_nop 0
	v_readlane_b32 s23, v9, 0
	s_movk_i32 s22, 63
	v_readlane_b32 s21, v9, 1
	s_movk_i32 s20, 62
	v_cmp_gt_i64_e32 vcc, s[22:23], v[8:9]
	v_readlane_b32 s23, v9, 2
	s_movk_i32 s22, 61
	v_addc_co_u32_e32 v6, vcc, 0, v6, vcc
	v_cmp_gt_i64_e32 vcc, s[20:21], v[8:9]
	v_readlane_b32 s21, v9, 3
	s_movk_i32 s20, 60
	v_addc_co_u32_e32 v6, vcc, 0, v6, vcc
	v_cmp_gt_i64_e32 vcc, s[22:23], v[8:9]
	v_readlane_b32 s23, v9, 4
	s_movk_i32 s22, 59
	v_addc_co_u32_e32 v6, vcc, 0, v6, vcc
	v_cmp_gt_i64_e32 vcc, s[20:21], v[8:9]
	v_readlane_b32 s21, v9, 5
	s_movk_i32 s20, 58
	v_addc_co_u32_e32 v6, vcc, 0, v6, vcc
	v_cmp_gt_i64_e32 vcc, s[22:23], v[8:9]
	v_readlane_b32 s23, v9, 6
	s_movk_i32 s22, 57
	v_addc_co_u32_e32 v6, vcc, 0, v6, vcc
	v_cmp_gt_i64_e32 vcc, s[20:21], v[8:9]
	v_readlane_b32 s21, v9, 7
	s_movk_i32 s20, 56
	v_addc_co_u32_e32 v6, vcc, 0, v6, vcc
	v_cmp_gt_i64_e32 vcc, s[22:23], v[8:9]
	v_readlane_b32 s23, v9, 8
	s_movk_i32 s22, 55
	v_addc_co_u32_e32 v6, vcc, 0, v6, vcc
	v_cmp_gt_i64_e32 vcc, s[20:21], v[8:9]
	v_readlane_b32 s21, v9, 9
	s_movk_i32 s20, 54
	v_addc_co_u32_e32 v6, vcc, 0, v6, vcc
	v_cmp_gt_i64_e32 vcc, s[22:23], v[8:9]
	v_readlane_b32 s23, v9, 10
	s_movk_i32 s22, 53
	v_addc_co_u32_e32 v6, vcc, 0, v6, vcc
	v_cmp_gt_i64_e32 vcc, s[20:21], v[8:9]
	v_readlane_b32 s21, v9, 11
	s_movk_i32 s20, 52
	v_addc_co_u32_e32 v6, vcc, 0, v6, vcc
	v_cmp_gt_i64_e32 vcc, s[22:23], v[8:9]
	v_readlane_b32 s23, v9, 12
	s_movk_i32 s22, 51
	v_addc_co_u32_e32 v6, vcc, 0, v6, vcc
	v_cmp_gt_i64_e32 vcc, s[20:21], v[8:9]
	v_readlane_b32 s21, v9, 13
	s_movk_i32 s20, 50
	v_addc_co_u32_e32 v6, vcc, 0, v6, vcc
	v_cmp_gt_i64_e32 vcc, s[22:23], v[8:9]
	v_readlane_b32 s23, v9, 14
	s_movk_i32 s22, 49
	v_addc_co_u32_e32 v6, vcc, 0, v6, vcc
	v_cmp_gt_i64_e32 vcc, s[20:21], v[8:9]
	v_readlane_b32 s21, v9, 15
	s_movk_i32 s20, 48
	v_addc_co_u32_e32 v6, vcc, 0, v6, vcc
	v_cmp_gt_i64_e32 vcc, s[22:23], v[8:9]
	v_readlane_b32 s23, v9, 16
	s_movk_i32 s22, 47
	v_addc_co_u32_e32 v6, vcc, 0, v6, vcc
	v_cmp_gt_i64_e32 vcc, s[20:21], v[8:9]
	v_readlane_b32 s21, v9, 17
	s_movk_i32 s20, 46
	v_addc_co_u32_e32 v6, vcc, 0, v6, vcc
	v_cmp_gt_i64_e32 vcc, s[22:23], v[8:9]
	v_readlane_b32 s23, v9, 18
	s_movk_i32 s22, 45
; __device__ __forceinline__ void phase_nrr(const Frame& F, const Args& a, int l, const bf16_t* XA, const float* g, const float* modl, unsigned char* XN8) {
;     ...
;             int rank = 0;
; #pragma unroll 8
;             for (int e2 = 0; e2 < 64; ++e2) { const float v = __int_as_float(__builtin_amdgcn_readlane(__float_as_int(val), e2)); rank += (v > val || (v == val && e2 < lane)) ? 1 : 0; }
;             const bool sel = rank < TOPK;
;             const float ssum = wave_sum(sel ? sc : 0.f);
;             if (sel) { const int p = atomicAdd((int*)(hist + lane), 1); top_e[t * TOPK + rank] = lane; gate[t * TOPK + rank] = sc / ssum * 2.5f; lpos[t * TOPK + rank] = p; }
	v_addc_co_u32_e32 v6, vcc, 0, v6, vcc
	v_cmp_gt_i64_e32 vcc, s[20:21], v[8:9]
	v_readlane_b32 s21, v9, 19
	s_movk_i32 s20, 44
	v_addc_co_u32_e32 v6, vcc, 0, v6, vcc
	v_cmp_gt_i64_e32 vcc, s[22:23], v[8:9]
	v_readlane_b32 s23, v9, 20
	s_movk_i32 s22, 43
	v_addc_co_u32_e32 v6, vcc, 0, v6, vcc
	v_cmp_gt_i64_e32 vcc, s[20:21], v[8:9]
	v_readlane_b32 s21, v9, 21
	s_movk_i32 s20, 42
	v_addc_co_u32_e32 v6, vcc, 0, v6, vcc
	v_cmp_gt_i64_e32 vcc, s[22:23], v[8:9]
	v_readlane_b32 s23, v9, 22
	s_movk_i32 s22, 41
	v_addc_co_u32_e32 v6, vcc, 0, v6, vcc
	v_cmp_gt_i64_e32 vcc, s[20:21], v[8:9]
	v_readlane_b32 s21, v9, 23
	s_movk_i32 s20, 40
	v_addc_co_u32_e32 v6, vcc, 0, v6, vcc
	v_cmp_gt_i64_e32 vcc, s[22:23], v[8:9]
	v_readlane_b32 s23, v9, 24
	s_movk_i32 s22, 39
	v_addc_co_u32_e32 v6, vcc, 0, v6, vcc
	v_cmp_gt_i64_e32 vcc, s[20:21], v[8:9]
	v_readlane_b32 s21, v9, 25
	s_movk_i32 s20, 38
	v_addc_co_u32_e32 v6, vcc, 0, v6, vcc
	v_cmp_gt_i64_e32 vcc, s[22:23], v[8:9]
	v_readlane_b32 s23, v9, 26
	s_movk_i32 s22, 37
	v_addc_co_u32_e32 v6, vcc, 0, v6, vcc
	v_cmp_gt_i64_e32 vcc, s[20:21], v[8:9]
	v_readlane_b32 s21, v9, 27
	s_movk_i32 s20, 36
	v_addc_co_u32_e32 v6, vcc, 0, v6, vcc
	v_cmp_gt_i64_e32 vcc, s[22:23], v[8:9]
	v_readlane_b32 s23, v9, 28
	s_movk_i32 s22, 35
	v_addc_co_u32_e32 v6, vcc, 0, v6, vcc
	v_cmp_gt_i64_e32 vcc, s[20:21], v[8:9]
	v_readlane_b32 s21, v9, 29
	s_movk_i32 s20, 34
	v_addc_co_u32_e32 v6, vcc, 0, v6, vcc
	v_cmp_gt_i64_e32 vcc, s[22:23], v[8:9]
	v_readlane_b32 s23, v9, 30
	s_movk_i32 s22, 33
	v_addc_co_u32_e32 v6, vcc, 0, v6, vcc
	v_cmp_gt_i64_e32 vcc, s[20:21], v[8:9]
	v_readlane_b32 s21, v9, 31
	s_movk_i32 s20, 32
	v_addc_co_u32_e32 v6, vcc, 0, v6, vcc
	v_cmp_gt_i64_e32 vcc, s[22:23], v[8:9]
	v_readlane_b32 s23, v9, 32
	s_movk_i32 s22, 31
	v_addc_co_u32_e32 v6, vcc, 0, v6, vcc
	v_cmp_gt_i64_e32 vcc, s[20:21], v[8:9]
	v_readlane_b32 s21, v9, 33
	s_movk_i32 s20, 30
	v_addc_co_u32_e32 v6, vcc, 0, v6, vcc
	v_cmp_gt_i64_e32 vcc, s[22:23], v[8:9]
	v_readlane_b32 s23, v9, 34
	s_movk_i32 s22, 29
	v_addc_co_u32_e32 v6, vcc, 0, v6, vcc
	v_cmp_gt_i64_e32 vcc, s[20:21], v[8:9]
	v_readlane_b32 s21, v9, 35
	s_movk_i32 s20, 28
	v_addc_co_u32_e32 v6, vcc, 0, v6, vcc
	v_cmp_gt_i64_e32 vcc, s[22:23], v[8:9]
	v_readlane_b32 s23, v9, 36
	s_movk_i32 s22, 27
	v_addc_co_u32_e32 v6, vcc, 0, v6, vcc
	v_cmp_gt_i64_e32 vcc, s[20:21], v[8:9]
	v_readlane_b32 s21, v9, 37
	s_movk_i32 s20, 26
	v_addc_co_u32_e32 v6, vcc, 0, v6, vcc
	v_cmp_gt_i64_e32 vcc, s[22:23], v[8:9]
	v_readlane_b32 s23, v9, 38
	s_movk_i32 s22, 25
	v_addc_co_u32_e32 v6, vcc, 0, v6, vcc
	v_cmp_gt_i64_e32 vcc, s[20:21], v[8:9]
	v_readlane_b32 s21, v9, 39
	s_movk_i32 s20, 24
	v_addc_co_u32_e32 v6, vcc, 0, v6, vcc
	v_cmp_gt_i64_e32 vcc, s[22:23], v[8:9]
	v_readlane_b32 s23, v9, 40
	s_movk_i32 s22, 23
	v_addc_co_u32_e32 v6, vcc, 0, v6, vcc
	v_cmp_gt_i64_e32 vcc, s[20:21], v[8:9]
	v_readlane_b32 s21, v9, 41
	s_movk_i32 s20, 22
	v_addc_co_u32_e32 v6, vcc, 0, v6, vcc
	v_cmp_gt_i64_e32 vcc, s[22:23], v[8:9]
	v_readlane_b32 s23, v9, 42
	s_movk_i32 s22, 21
	v_addc_co_u32_e32 v6, vcc, 0, v6, vcc
	v_cmp_gt_i64_e32 vcc, s[20:21], v[8:9]
	v_readlane_b32 s21, v9, 43
	s_movk_i32 s20, 20
	v_addc_co_u32_e32 v6, vcc, 0, v6, vcc
	v_cmp_gt_i64_e32 vcc, s[22:23], v[8:9]
	v_readlane_b32 s23, v9, 44
	s_movk_i32 s22, 19
	v_addc_co_u32_e32 v6, vcc, 0, v6, vcc
	v_cmp_gt_i64_e32 vcc, s[20:21], v[8:9]
	v_readlane_b32 s21, v9, 45
	s_movk_i32 s20, 18
	v_addc_co_u32_e32 v6, vcc, 0, v6, vcc
	v_cmp_gt_i64_e32 vcc, s[22:23], v[8:9]
	v_readlane_b32 s23, v9, 46
	s_movk_i32 s22, 17
	v_addc_co_u32_e32 v6, vcc, 0, v6, vcc
	v_cmp_gt_i64_e32 vcc, s[20:21], v[8:9]
	v_readlane_b32 s21, v9, 47
	s_movk_i32 s20, 16
	v_addc_co_u32_e32 v6, vcc, 0, v6, vcc
	v_cmp_gt_i64_e32 vcc, s[22:23], v[8:9]
	v_readlane_b32 s23, v9, 48
	s_movk_i32 s22, 15
	v_addc_co_u32_e32 v6, vcc, 0, v6, vcc
	v_cmp_gt_i64_e32 vcc, s[20:21], v[8:9]
	v_readlane_b32 s21, v9, 49
	s_movk_i32 s20, 14
	v_addc_co_u32_e32 v6, vcc, 0, v6, vcc
	v_cmp_gt_i64_e32 vcc, s[22:23], v[8:9]
	v_readlane_b32 s23, v9, 50
	s_movk_i32 s22, 13
	v_addc_co_u32_e32 v6, vcc, 0, v6, vcc
	v_cmp_gt_i64_e32 vcc, s[20:21], v[8:9]
	v_readlane_b32 s21, v9, 51
	s_movk_i32 s20, 12
	v_addc_co_u32_e32 v6, vcc, 0, v6, vcc
	v_cmp_gt_i64_e32 vcc, s[22:23], v[8:9]
	v_readlane_b32 s23, v9, 52
	s_movk_i32 s22, 11
	v_addc_co_u32_e32 v6, vcc, 0, v6, vcc
	v_cmp_gt_i64_e32 vcc, s[20:21], v[8:9]
	v_readlane_b32 s21, v9, 53
	s_movk_i32 s20, 10
	v_addc_co_u32_e32 v6, vcc, 0, v6, vcc
	v_cmp_gt_i64_e32 vcc, s[22:23], v[8:9]
	v_readlane_b32 s23, v9, 54
	s_movk_i32 s22, 9
	v_addc_co_u32_e32 v6, vcc, 0, v6, vcc
	v_cmp_gt_i64_e32 vcc, s[20:21], v[8:9]
	v_readlane_b32 s21, v9, 55
	s_movk_i32 s20, 8
	v_addc_co_u32_e32 v6, vcc, 0, v6, vcc
	v_cmp_gt_i64_e32 vcc, s[22:23], v[8:9]
	v_readlane_b32 s23, v9, 56
	s_movk_i32 s22, 7
	v_addc_co_u32_e32 v6, vcc, 0, v6, vcc
	v_cmp_gt_i64_e32 vcc, s[20:21], v[8:9]
	v_readlane_b32 s21, v9, 57
	s_movk_i32 s20, 6
	v_addc_co_u32_e32 v6, vcc, 0, v6, vcc
	v_cmp_gt_i64_e32 vcc, s[22:23], v[8:9]
	v_readlane_b32 s23, v9, 58
	s_movk_i32 s22, 5
	v_addc_co_u32_e32 v6, vcc, 0, v6, vcc
	v_cmp_gt_i64_e32 vcc, s[20:21], v[8:9]
	v_readlane_b32 s21, v9, 59
	s_movk_i32 s20, 4
	v_addc_co_u32_e32 v6, vcc, 0, v6, vcc
	v_cmp_gt_i64_e32 vcc, s[22:23], v[8:9]
	v_readlane_b32 s23, v9, 60
	s_movk_i32 s22, 3
	v_addc_co_u32_e32 v6, vcc, 0, v6, vcc
	v_cmp_gt_i64_e32 vcc, s[20:21], v[8:9]
	v_readlane_b32 s21, v9, 61
	s_movk_i32 s20, 2
	v_addc_co_u32_e32 v6, vcc, 0, v6, vcc
	v_cmp_gt_i64_e32 vcc, s[22:23], v[8:9]
	v_readlane_b32 s23, v9, 62
	s_movk_i32 s22, 1
	v_addc_co_u32_e32 v6, vcc, 0, v6, vcc
	v_cmp_gt_i64_e32 vcc, s[20:21], v[8:9]
	v_readlane_b32 s21, v9, 63
	s_movk_i32 s20, 0
	v_addc_co_u32_e32 v6, vcc, 0, v6, vcc
	v_cmp_gt_i64_e32 vcc, s[22:23], v[8:9]
	s_nop 1
	v_addc_co_u32_e32 v6, vcc, 0, v6, vcc
	v_cmp_gt_i64_e32 vcc, s[20:21], v[8:9]
	s_nop 1
	v_addc_co_u32_e32 v6, vcc, 0, v6, vcc
	v_cmp_gt_u32_e32 vcc, 6, v6
	s_nop 1
	v_cndmask_b32_e32 v5, 0, v2, vcc
	ds_bpermute_b32 v7, v1, v5
	s_waitcnt lgkmcnt(0)
	v_add_f32_e32 v5, v5, v7
	ds_bpermute_b32 v7, v201, v5
	s_waitcnt lgkmcnt(0)
	v_add_f32_e32 v5, v5, v7
	ds_bpermute_b32 v7, v220, v5
	s_waitcnt lgkmcnt(0)
	v_add_f32_e32 v5, v5, v7
	ds_bpermute_b32 v7, v221, v5
	s_waitcnt lgkmcnt(0)
	v_add_f32_e32 v5, v5, v7
	ds_bpermute_b32 v7, v222, v5
	s_waitcnt lgkmcnt(0)
	v_add_f32_e32 v5, v5, v7
	ds_bpermute_b32 v7, v223, v5
	s_and_saveexec_b64 s[4:5], vcc
	s_cbranch_execz .LBB0_1328
; __device__ __forceinline__ void phase_nrr(const Frame& F, const Args& a, int l, const bf16_t* XA, const float* g, const float* modl, unsigned char* XN8) {
;     ...
;         for (int i = 0; i < 8; ++i) { const int t = tb + i;
;             const float lg = Pl[(w * 8 + i) * NE + lane] + Pl[(64 + w * 8 + i) * NE + lane]; const float sc = 1.f / (1.f + __expf(-lg)); const float bb = sc + bias;
;             float m1 = bb; m1 = fmaxf(m1, __shfl_xor(m1, 1)); m1 = fmaxf(m1, __shfl_xor(m1, 2)); m1 = fmaxf(m1, __shfl_xor(m1, 4));
;             const unsigned long long eq = __ballot(bb == m1); const int gbase = lane & ~7; const unsigned grpmask = (unsigned)((eq >> gbase) & 0xffull);
;             const int first = gbase + __builtin_ctz(grpmask);
;             float m2 = (lane == first) ? -INFINITY : bb; m2 = fmaxf(m2, __shfl_xor(m2, 1)); m2 = fmaxf(m2, __shfl_xor(m2, 2)); m2 = fmaxf(m2, __shfl_xor(m2, 4));
;             const float gsum = m1 + m2; const int gq = lane >> 3;
;             int grank = 0;
; #pragma unroll
;             for (int g2 = 0; g2 < 8; ++g2) { const float v = __int_as_float(__builtin_amdgcn_readlane(__float_as_int(gsum), g2 * 8)); grank += (v > gsum || (v == gsum && g2 < gq)) ? 1 : 0; }
;             const bool keep = grank < 4; const float val = keep ? bb : -INFINITY;
;             int rank = 0;
; #pragma unroll 8
;             for (int e2 = 0; e2 < 64; ++e2) { const float v = __int_as_float(__builtin_amdgcn_readlane(__float_as_int(val), e2)); rank += (v > val || (v == val && e2 < lane)) ? 1 : 0; }
;     ...
;             if (sel) { const int p = atomicAdd((int*)(hist + lane), 1); top_e[t * TOPK + rank] = lane; gate[t * TOPK + rank] = sc / ssum * 2.5f; lpos[t * TOPK + rank] = p; }
	s_waitcnt lgkmcnt(0)
	v_add_f32_e32 v5, v5, v7
	s_mul_i32 s2, s2, 6
	v_or_b32_e32 v6, s2, v6
	v_div_scale_f32 v11, s[2:3], v5, v5, v2
	v_rcp_f32_e32 v12, v11
	v_ashrrev_i32_e32 v7, 31, v6
	v_lshlrev_b64 v[6:7], 2, v[6:7]
	v_lshl_add_u64 v[8:9], s[42:43], 0, v[6:7]
	ds_add_rtn_u32 v10, v227, v243
	global_store_dword v[8:9], v230, off
	v_fma_f32 v8, -v11, v12, 1.0
	v_fmac_f32_e32 v12, v8, v12
	v_div_scale_f32 v8, vcc, v2, v5, v2
	v_mul_f32_e32 v9, v8, v12
	v_fma_f32 v13, -v11, v9, v8
	v_fmac_f32_e32 v9, v13, v12
	v_fma_f32 v8, -v11, v9, v8
	v_div_fmas_f32 v8, v8, v12, v9
	v_div_fixup_f32 v2, v8, v5, v2
	v_mul_f32_e32 v2, 0x40200000, v2
	v_lshl_add_u64 v[8:9], s[44:45], 0, v[6:7]
	v_lshl_add_u64 v[6:7], s[46:47], 0, v[6:7]
	global_store_dword v[8:9], v2, off
	s_waitcnt lgkmcnt(0)
	global_store_dword v[6:7], v10, off
.LBB0_1328:
	s_or_b64 exec, exec, s[4:5]
	v_add_u32_e32 v2, s80, v226
	ds_read_b32 v2, v2
	ds_read_b32 v5, v4 offset:17664
	s_waitcnt lgkmcnt(0)
	v_add_f32_e32 v2, v2, v5
	v_mul_f32_e32 v2, 0xbfb8aa3b, v2
	v_exp_f32_e32 v2, v2
	s_nop 0
	v_add_f32_e32 v2, 1.0, v2
	v_div_scale_f32 v5, s[2:3], v2, v2, 1.0
	v_rcp_f32_e32 v6, v5
	v_div_scale_f32 v7, vcc, 1.0, v2, 1.0
	s_mov_b32 s2, 0
	v_fma_f32 v8, -v5, v6, 1.0
	v_fmac_f32_e32 v6, v8, v6
	v_mul_f32_e32 v8, v7, v6
	v_fma_f32 v9, -v5, v8, v7
	v_fmac_f32_e32 v8, v9, v6
	v_fma_f32 v5, -v5, v8, v7
	v_div_fmas_f32 v5, v5, v6, v8
	v_div_fixup_f32 v2, v5, v2, 1.0
	v_add_f32_e32 v5, v3, v2
	s_nop 1
	s_waitcnt lgkmcnt(0)
	v_max_f32_dpp v6, v5, v5 quad_perm:[1,0,3,2] row_mask:0xf bank_mask:0xf
	s_nop 1
	s_waitcnt lgkmcnt(0)
	v_max_f32_dpp v6, v6, v6 quad_perm:[2,3,0,1] row_mask:0xf bank_mask:0xf
	s_nop 1
	s_waitcnt lgkmcnt(0)
	v_max_f32_dpp v8, v6, v6 row_half_mirror row_mask:0xf bank_mask:0xf
	v_cmp_eq_f32_e32 vcc, v5, v8
	s_nop 1
	v_lshrrev_b64 v[6:7], v200, vcc
	v_ffbl_b32_sdwa v6, v6 dst_sel:DWORD dst_unused:UNUSED_PAD src0_sel:BYTE_0
	v_add_u32_e32 v6, v6, v200
	v_cmp_ne_u32_e32 vcc, v230, v6
	s_nop 1
	v_cndmask_b32_e32 v6, v245, v5, vcc
	s_nop 1
	s_waitcnt lgkmcnt(0)
	v_max_f32_dpp v6, v6, v6 quad_perm:[1,0,3,2] row_mask:0xf bank_mask:0xf
	s_nop 1
	s_waitcnt lgkmcnt(0)
	v_max_f32_dpp v6, v6, v6 quad_perm:[2,3,0,1] row_mask:0xf bank_mask:0xf
	s_nop 1
	s_waitcnt lgkmcnt(0)
	v_max_f32_dpp v6, v6, v6 row_half_mirror row_mask:0xf bank_mask:0xf
	v_add_f32_e32 v6, v8, v6
	s_nop 0
	v_readlane_b32 s3, v6, 0
	v_readlane_b32 s4, v6, 8
	v_readlane_b32 s5, v6, 16
	v_cmp_eq_f32_e64 s[20:21], s3, v6
	v_cmp_gt_f32_e32 vcc, s3, v6
	v_cmp_gt_f32_e64 s[22:23], s4, v6
	v_cmp_eq_f32_e64 s[24:25], s4, v6
	v_cmp_gt_f32_e64 s[26:27], s5, v6
	v_cmp_eq_f32_e64 s[28:29], s5, v6
	s_and_b64 s[4:5], s[0:1], s[20:21]
	v_readlane_b32 s34, v6, 24
	s_and_b64 s[20:21], s[6:7], s[24:25]
	s_or_b64 s[4:5], vcc, s[4:5]
	v_readlane_b32 s40, v6, 32
	v_cmp_gt_f32_e64 s[30:31], s34, v6
	v_cmp_eq_f32_e64 s[34:35], s34, v6
	s_and_b64 s[24:25], s[8:9], s[28:29]
	v_cndmask_b32_e64 v7, 0, 1, s[4:5]
	s_or_b64 s[4:5], s[22:23], s[20:21]
	v_cmp_gt_f32_e64 s[36:37], s40, v6
	v_cmp_eq_f32_e64 s[40:41], s40, v6
	s_and_b64 s[28:29], s[10:11], s[34:35]
	v_cndmask_b32_e64 v8, 0, 1, s[4:5]
	s_or_b64 s[4:5], s[26:27], s[24:25]
	v_readlane_b32 s54, v6, 40
	s_and_b64 s[34:35], s[12:13], s[40:41]
	v_cndmask_b32_e64 v9, 0, 1, s[4:5]
	s_or_b64 s[4:5], s[30:31], s[28:29]
	v_cndmask_b32_e64 v10, 0, 1, s[4:5]
	s_or_b64 s[4:5], s[36:37], s[34:35]
	v_cmp_eq_f32_e64 s[20:21], s54, v6
	v_cndmask_b32_e64 v11, 0, 1, s[4:5]
	v_cmp_gt_f32_e32 vcc, s54, v6
	s_and_b64 s[4:5], s[14:15], s[20:21]
	v_readlane_b32 s3, v6, 48
	s_or_b64 s[4:5], vcc, s[4:5]
	v_cndmask_b32_e64 v12, 0, 1, s[4:5]
	v_cmp_eq_f32_e64 s[20:21], s3, v6
	v_cmp_gt_f32_e32 vcc, s3, v6
	s_and_b64 s[4:5], s[16:17], s[20:21]
	v_readlane_b32 s3, v6, 56
	s_or_b64 s[4:5], vcc, s[4:5]
	v_cndmask_b32_e64 v13, 0, 1, s[4:5]
	v_cmp_gt_f32_e32 vcc, s3, v6
	s_nop 1
	v_cndmask_b32_e64 v6, 0, 1, vcc
	v_add_u32_e32 v6, v8, v6
	v_add3_u32 v6, v6, v7, v9
	v_add3_u32 v6, v6, v10, v11
	v_add3_u32 v6, v6, v12, v13
	v_cmp_gt_u32_e32 vcc, 4, v6
	v_mov_b32_e32 v6, 0
	s_nop 0
	v_cndmask_b32_e32 v5, v245, v5, vcc
	v_ashrrev_i32_e32 v9, 31, v5
	v_sub_u32_e32 v8, 63, v230
	v_and_b32_e32 v9, 0x7fffffff, v9
	v_xor_b32_e32 v9, v5, v9
	s_nop 0
	v_readlane_b32 s23, v9, 0
	s_movk_i32 s22, 63
	v_readlane_b32 s21, v9, 1
	s_movk_i32 s20, 62
	v_cmp_gt_i64_e32 vcc, s[22:23], v[8:9]
	v_readlane_b32 s23, v9, 2
	s_movk_i32 s22, 61
	v_addc_co_u32_e32 v6, vcc, 0, v6, vcc
	v_cmp_gt_i64_e32 vcc, s[20:21], v[8:9]
	v_readlane_b32 s21, v9, 3
	s_movk_i32 s20, 60
	v_addc_co_u32_e32 v6, vcc, 0, v6, vcc
	v_cmp_gt_i64_e32 vcc, s[22:23], v[8:9]
	v_readlane_b32 s23, v9, 4
	s_movk_i32 s22, 59
	v_addc_co_u32_e32 v6, vcc, 0, v6, vcc
	v_cmp_gt_i64_e32 vcc, s[20:21], v[8:9]
	v_readlane_b32 s21, v9, 5
	s_movk_i32 s20, 58
	v_addc_co_u32_e32 v6, vcc, 0, v6, vcc
	v_cmp_gt_i64_e32 vcc, s[22:23], v[8:9]
	v_readlane_b32 s23, v9, 6
	s_movk_i32 s22, 57
	v_addc_co_u32_e32 v6, vcc, 0, v6, vcc
	v_cmp_gt_i64_e32 vcc, s[20:21], v[8:9]
	v_readlane_b32 s21, v9, 7
	s_movk_i32 s20, 56
	v_addc_co_u32_e32 v6, vcc, 0, v6, vcc
	v_cmp_gt_i64_e32 vcc, s[22:23], v[8:9]
	v_readlane_b32 s23, v9, 8
	s_movk_i32 s22, 55
	v_addc_co_u32_e32 v6, vcc, 0, v6, vcc
	v_cmp_gt_i64_e32 vcc, s[20:21], v[8:9]
	v_readlane_b32 s21, v9, 9
	s_movk_i32 s20, 54
	v_addc_co_u32_e32 v6, vcc, 0, v6, vcc
	v_cmp_gt_i64_e32 vcc, s[22:23], v[8:9]
	v_readlane_b32 s23, v9, 10
	s_movk_i32 s22, 53
	v_addc_co_u32_e32 v6, vcc, 0, v6, vcc
	v_cmp_gt_i64_e32 vcc, s[20:21], v[8:9]
	v_readlane_b32 s21, v9, 11
	s_movk_i32 s20, 52
	v_addc_co_u32_e32 v6, vcc, 0, v6, vcc
	v_cmp_gt_i64_e32 vcc, s[22:23], v[8:9]
; __device__ __forceinline__ void phase_nrr(const Frame& F, const Args& a, int l, const bf16_t* XA, const float* g, const float* modl, unsigned char* XN8) {
;     ...
;             int rank = 0;
; #pragma unroll 8
;             for (int e2 = 0; e2 < 64; ++e2) { const float v = __int_as_float(__builtin_amdgcn_readlane(__float_as_int(val), e2)); rank += (v > val || (v == val && e2 < lane)) ? 1 : 0; }
;             const bool sel = rank < TOPK;
	v_readlane_b32 s23, v9, 12
	s_movk_i32 s22, 51
	v_addc_co_u32_e32 v6, vcc, 0, v6, vcc
	v_cmp_gt_i64_e32 vcc, s[20:21], v[8:9]
	v_readlane_b32 s21, v9, 13
	s_movk_i32 s20, 50
	v_addc_co_u32_e32 v6, vcc, 0, v6, vcc
	v_cmp_gt_i64_e32 vcc, s[22:23], v[8:9]
	v_readlane_b32 s23, v9, 14
	s_movk_i32 s22, 49
	v_addc_co_u32_e32 v6, vcc, 0, v6, vcc
	v_cmp_gt_i64_e32 vcc, s[20:21], v[8:9]
	v_readlane_b32 s21, v9, 15
	s_movk_i32 s20, 48
	v_addc_co_u32_e32 v6, vcc, 0, v6, vcc
	v_cmp_gt_i64_e32 vcc, s[22:23], v[8:9]
	v_readlane_b32 s23, v9, 16
	s_movk_i32 s22, 47
	v_addc_co_u32_e32 v6, vcc, 0, v6, vcc
	v_cmp_gt_i64_e32 vcc, s[20:21], v[8:9]
	v_readlane_b32 s21, v9, 17
	s_movk_i32 s20, 46
	v_addc_co_u32_e32 v6, vcc, 0, v6, vcc
	v_cmp_gt_i64_e32 vcc, s[22:23], v[8:9]
	v_readlane_b32 s23, v9, 18
	s_movk_i32 s22, 45
	v_addc_co_u32_e32 v6, vcc, 0, v6, vcc
	v_cmp_gt_i64_e32 vcc, s[20:21], v[8:9]
	v_readlane_b32 s21, v9, 19
	s_movk_i32 s20, 44
	v_addc_co_u32_e32 v6, vcc, 0, v6, vcc
	v_cmp_gt_i64_e32 vcc, s[22:23], v[8:9]
	v_readlane_b32 s23, v9, 20
	s_movk_i32 s22, 43
	v_addc_co_u32_e32 v6, vcc, 0, v6, vcc
	v_cmp_gt_i64_e32 vcc, s[20:21], v[8:9]
	v_readlane_b32 s21, v9, 21
	s_movk_i32 s20, 42
	v_addc_co_u32_e32 v6, vcc, 0, v6, vcc
	v_cmp_gt_i64_e32 vcc, s[22:23], v[8:9]
	v_readlane_b32 s23, v9, 22
	s_movk_i32 s22, 41
	v_addc_co_u32_e32 v6, vcc, 0, v6, vcc
	v_cmp_gt_i64_e32 vcc, s[20:21], v[8:9]
	v_readlane_b32 s21, v9, 23
	s_movk_i32 s20, 40
	v_addc_co_u32_e32 v6, vcc, 0, v6, vcc
	v_cmp_gt_i64_e32 vcc, s[22:23], v[8:9]
	v_readlane_b32 s23, v9, 24
	s_movk_i32 s22, 39
	v_addc_co_u32_e32 v6, vcc, 0, v6, vcc
	v_cmp_gt_i64_e32 vcc, s[20:21], v[8:9]
	v_readlane_b32 s21, v9, 25
	s_movk_i32 s20, 38
	v_addc_co_u32_e32 v6, vcc, 0, v6, vcc
	v_cmp_gt_i64_e32 vcc, s[22:23], v[8:9]
	v_readlane_b32 s23, v9, 26
	s_movk_i32 s22, 37
	v_addc_co_u32_e32 v6, vcc, 0, v6, vcc
	v_cmp_gt_i64_e32 vcc, s[20:21], v[8:9]
	v_readlane_b32 s21, v9, 27
	s_movk_i32 s20, 36
	v_addc_co_u32_e32 v6, vcc, 0, v6, vcc
	v_cmp_gt_i64_e32 vcc, s[22:23], v[8:9]
	v_readlane_b32 s23, v9, 28
	s_movk_i32 s22, 35
	v_addc_co_u32_e32 v6, vcc, 0, v6, vcc
	v_cmp_gt_i64_e32 vcc, s[20:21], v[8:9]
	v_readlane_b32 s21, v9, 29
	s_movk_i32 s20, 34
	v_addc_co_u32_e32 v6, vcc, 0, v6, vcc
	v_cmp_gt_i64_e32 vcc, s[22:23], v[8:9]
	v_readlane_b32 s23, v9, 30
	s_movk_i32 s22, 33
	v_addc_co_u32_e32 v6, vcc, 0, v6, vcc
	v_cmp_gt_i64_e32 vcc, s[20:21], v[8:9]
	v_readlane_b32 s21, v9, 31
	s_movk_i32 s20, 32
	v_addc_co_u32_e32 v6, vcc, 0, v6, vcc
	v_cmp_gt_i64_e32 vcc, s[22:23], v[8:9]
	v_readlane_b32 s23, v9, 32
	s_movk_i32 s22, 31
	v_addc_co_u32_e32 v6, vcc, 0, v6, vcc
	v_cmp_gt_i64_e32 vcc, s[20:21], v[8:9]
	v_readlane_b32 s21, v9, 33
	s_movk_i32 s20, 30
	v_addc_co_u32_e32 v6, vcc, 0, v6, vcc
	v_cmp_gt_i64_e32 vcc, s[22:23], v[8:9]
	v_readlane_b32 s23, v9, 34
	s_movk_i32 s22, 29
	v_addc_co_u32_e32 v6, vcc, 0, v6, vcc
	v_cmp_gt_i64_e32 vcc, s[20:21], v[8:9]
	v_readlane_b32 s21, v9, 35
	s_movk_i32 s20, 28
	v_addc_co_u32_e32 v6, vcc, 0, v6, vcc
	v_cmp_gt_i64_e32 vcc, s[22:23], v[8:9]
	v_readlane_b32 s23, v9, 36
	s_movk_i32 s22, 27
	v_addc_co_u32_e32 v6, vcc, 0, v6, vcc
	v_cmp_gt_i64_e32 vcc, s[20:21], v[8:9]
	v_readlane_b32 s21, v9, 37
	s_movk_i32 s20, 26
	v_addc_co_u32_e32 v6, vcc, 0, v6, vcc
	v_cmp_gt_i64_e32 vcc, s[22:23], v[8:9]
	v_readlane_b32 s23, v9, 38
	s_movk_i32 s22, 25
	v_addc_co_u32_e32 v6, vcc, 0, v6, vcc
	v_cmp_gt_i64_e32 vcc, s[20:21], v[8:9]
	v_readlane_b32 s21, v9, 39
	s_movk_i32 s20, 24
	v_addc_co_u32_e32 v6, vcc, 0, v6, vcc
	v_cmp_gt_i64_e32 vcc, s[22:23], v[8:9]
	v_readlane_b32 s23, v9, 40
	s_movk_i32 s22, 23
	v_addc_co_u32_e32 v6, vcc, 0, v6, vcc
	v_cmp_gt_i64_e32 vcc, s[20:21], v[8:9]
	v_readlane_b32 s21, v9, 41
	s_movk_i32 s20, 22
	v_addc_co_u32_e32 v6, vcc, 0, v6, vcc
	v_cmp_gt_i64_e32 vcc, s[22:23], v[8:9]
	v_readlane_b32 s23, v9, 42
	s_movk_i32 s22, 21
	v_addc_co_u32_e32 v6, vcc, 0, v6, vcc
	v_cmp_gt_i64_e32 vcc, s[20:21], v[8:9]
	v_readlane_b32 s21, v9, 43
	s_movk_i32 s20, 20
	v_addc_co_u32_e32 v6, vcc, 0, v6, vcc
	v_cmp_gt_i64_e32 vcc, s[22:23], v[8:9]
	v_readlane_b32 s23, v9, 44
	s_movk_i32 s22, 19
	v_addc_co_u32_e32 v6, vcc, 0, v6, vcc
	v_cmp_gt_i64_e32 vcc, s[20:21], v[8:9]
	v_readlane_b32 s21, v9, 45
	s_movk_i32 s20, 18
	v_addc_co_u32_e32 v6, vcc, 0, v6, vcc
	v_cmp_gt_i64_e32 vcc, s[22:23], v[8:9]
	v_readlane_b32 s23, v9, 46
	s_movk_i32 s22, 17
	v_addc_co_u32_e32 v6, vcc, 0, v6, vcc
	v_cmp_gt_i64_e32 vcc, s[20:21], v[8:9]
	v_readlane_b32 s21, v9, 47
	s_movk_i32 s20, 16
	v_addc_co_u32_e32 v6, vcc, 0, v6, vcc
	v_cmp_gt_i64_e32 vcc, s[22:23], v[8:9]
	v_readlane_b32 s23, v9, 48
	s_movk_i32 s22, 15
	v_addc_co_u32_e32 v6, vcc, 0, v6, vcc
	v_cmp_gt_i64_e32 vcc, s[20:21], v[8:9]
	v_readlane_b32 s21, v9, 49
	s_movk_i32 s20, 14
	v_addc_co_u32_e32 v6, vcc, 0, v6, vcc
	v_cmp_gt_i64_e32 vcc, s[22:23], v[8:9]
	v_readlane_b32 s23, v9, 50
	s_movk_i32 s22, 13
	v_addc_co_u32_e32 v6, vcc, 0, v6, vcc
	v_cmp_gt_i64_e32 vcc, s[20:21], v[8:9]
	v_readlane_b32 s21, v9, 51
	s_movk_i32 s20, 12
	v_addc_co_u32_e32 v6, vcc, 0, v6, vcc
	v_cmp_gt_i64_e32 vcc, s[22:23], v[8:9]
	v_readlane_b32 s23, v9, 52
	s_movk_i32 s22, 11
	v_addc_co_u32_e32 v6, vcc, 0, v6, vcc
	v_cmp_gt_i64_e32 vcc, s[20:21], v[8:9]
	v_readlane_b32 s21, v9, 53
	s_movk_i32 s20, 10
	v_addc_co_u32_e32 v6, vcc, 0, v6, vcc
	v_cmp_gt_i64_e32 vcc, s[22:23], v[8:9]
	v_readlane_b32 s23, v9, 54
	s_movk_i32 s22, 9
	v_addc_co_u32_e32 v6, vcc, 0, v6, vcc
	v_cmp_gt_i64_e32 vcc, s[20:21], v[8:9]
	v_readlane_b32 s21, v9, 55
	s_movk_i32 s20, 8
	v_addc_co_u32_e32 v6, vcc, 0, v6, vcc
	v_cmp_gt_i64_e32 vcc, s[22:23], v[8:9]
	v_readlane_b32 s23, v9, 56
	s_movk_i32 s22, 7
	v_addc_co_u32_e32 v6, vcc, 0, v6, vcc
	v_cmp_gt_i64_e32 vcc, s[20:21], v[8:9]
	v_readlane_b32 s21, v9, 57
	s_movk_i32 s20, 6
	v_addc_co_u32_e32 v6, vcc, 0, v6, vcc
	v_cmp_gt_i64_e32 vcc, s[22:23], v[8:9]
	v_readlane_b32 s23, v9, 58
	s_movk_i32 s22, 5
	v_addc_co_u32_e32 v6, vcc, 0, v6, vcc
	v_cmp_gt_i64_e32 vcc, s[20:21], v[8:9]
	v_readlane_b32 s21, v9, 59
	s_movk_i32 s20, 4
	v_addc_co_u32_e32 v6, vcc, 0, v6, vcc
	v_cmp_gt_i64_e32 vcc, s[22:23], v[8:9]
	v_readlane_b32 s23, v9, 60
	s_movk_i32 s22, 3
	v_addc_co_u32_e32 v6, vcc, 0, v6, vcc
	v_cmp_gt_i64_e32 vcc, s[20:21], v[8:9]
	v_readlane_b32 s21, v9, 61
	s_movk_i32 s20, 2
	v_addc_co_u32_e32 v6, vcc, 0, v6, vcc
	v_cmp_gt_i64_e32 vcc, s[22:23], v[8:9]
	v_readlane_b32 s23, v9, 62
	s_movk_i32 s22, 1
	v_addc_co_u32_e32 v6, vcc, 0, v6, vcc
	v_cmp_gt_i64_e32 vcc, s[20:21], v[8:9]
	v_readlane_b32 s21, v9, 63
	s_movk_i32 s20, 0
	v_addc_co_u32_e32 v6, vcc, 0, v6, vcc
	v_cmp_gt_i64_e32 vcc, s[22:23], v[8:9]
	s_nop 1
	v_addc_co_u32_e32 v6, vcc, 0, v6, vcc
	v_cmp_gt_i64_e32 vcc, s[20:21], v[8:9]
	s_nop 1
	v_addc_co_u32_e32 v6, vcc, 0, v6, vcc
	v_cmp_gt_u32_e32 vcc, 6, v6
	s_nop 1
	v_cndmask_b32_e32 v5, 0, v2, vcc
	ds_bpermute_b32 v7, v1, v5
	s_waitcnt lgkmcnt(0)
; __device__ __forceinline__ void phase_nrr(const Frame& F, const Args& a, int l, const bf16_t* XA, const float* g, const float* modl, unsigned char* XN8) {
;     ...
;         for (int i = 0; i < 8; ++i) { const int t = tb + i;
;             const float lg = Pl[(w * 8 + i) * NE + lane] + Pl[(64 + w * 8 + i) * NE + lane]; const float sc = 1.f / (1.f + __expf(-lg)); const float bb = sc + bias;
;             float m1 = bb; m1 = fmaxf(m1, __shfl_xor(m1, 1)); m1 = fmaxf(m1, __shfl_xor(m1, 2)); m1 = fmaxf(m1, __shfl_xor(m1, 4));
;             const unsigned long long eq = __ballot(bb == m1); const int gbase = lane & ~7; const unsigned grpmask = (unsigned)((eq >> gbase) & 0xffull);
;             const int first = gbase + __builtin_ctz(grpmask);
;             float m2 = (lane == first) ? -INFINITY : bb; m2 = fmaxf(m2, __shfl_xor(m2, 1)); m2 = fmaxf(m2, __shfl_xor(m2, 2)); m2 = fmaxf(m2, __shfl_xor(m2, 4));
;             const float gsum = m1 + m2; const int gq = lane >> 3;
;             int grank = 0;
; #pragma unroll
;             for (int g2 = 0; g2 < 8; ++g2) { const float v = __int_as_float(__builtin_amdgcn_readlane(__float_as_int(gsum), g2 * 8)); grank += (v > gsum || (v == gsum && g2 < gq)) ? 1 : 0; }
;             const bool keep = grank < 4; const float val = keep ? bb : -INFINITY;
;             int rank = 0;
; #pragma unroll 8
;             for (int e2 = 0; e2 < 64; ++e2) { const float v = __int_as_float(__builtin_amdgcn_readlane(__float_as_int(val), e2)); rank += (v > val || (v == val && e2 < lane)) ? 1 : 0; }
;     ...
;             const float ssum = wave_sum(sel ? sc : 0.f);
;             if (sel) { const int p = atomicAdd((int*)(hist + lane), 1); top_e[t * TOPK + rank] = lane; gate[t * TOPK + rank] = sc / ssum * 2.5f; lpos[t * TOPK + rank] = p; }
	v_add_f32_e32 v5, v5, v7
	ds_bpermute_b32 v7, v201, v5
	s_waitcnt lgkmcnt(0)
	v_add_f32_e32 v5, v5, v7
	ds_bpermute_b32 v7, v220, v5
	s_waitcnt lgkmcnt(0)
	v_add_f32_e32 v5, v5, v7
	ds_bpermute_b32 v7, v221, v5
	s_waitcnt lgkmcnt(0)
	v_add_f32_e32 v5, v5, v7
	ds_bpermute_b32 v7, v222, v5
	s_waitcnt lgkmcnt(0)
	v_add_f32_e32 v5, v5, v7
	ds_bpermute_b32 v7, v223, v5
	s_and_saveexec_b64 s[2:3], vcc
	s_cbranch_execz .LBB0_1332
	s_waitcnt lgkmcnt(0)
	v_add_f32_e32 v5, v5, v7
	v_div_scale_f32 v11, s[4:5], v5, v5, v2
	v_add3_u32 v6, s50, 30, v6
	v_rcp_f32_e32 v12, v11
	v_ashrrev_i32_e32 v7, 31, v6
	v_lshlrev_b64 v[6:7], 2, v[6:7]
	v_lshl_add_u64 v[8:9], s[42:43], 0, v[6:7]
	ds_add_rtn_u32 v10, v227, v243
	global_store_dword v[8:9], v230, off
	v_fma_f32 v8, -v11, v12, 1.0
	v_fmac_f32_e32 v12, v8, v12
	v_div_scale_f32 v8, vcc, v2, v5, v2
	v_mul_f32_e32 v9, v8, v12
	v_fma_f32 v13, -v11, v9, v8
	v_fmac_f32_e32 v9, v13, v12
	v_fma_f32 v8, -v11, v9, v8
	v_div_fmas_f32 v8, v8, v12, v9
	v_div_fixup_f32 v2, v8, v5, v2
	v_mul_f32_e32 v2, 0x40200000, v2
	v_lshl_add_u64 v[8:9], s[44:45], 0, v[6:7]
	v_lshl_add_u64 v[6:7], s[46:47], 0, v[6:7]
	global_store_dword v[8:9], v2, off
	s_waitcnt lgkmcnt(0)
	global_store_dword v[6:7], v10, off
.LBB0_1332:
	s_or_b64 exec, exec, s[2:3]
	v_add_u32_e32 v2, s81, v226
	ds_read_b32 v2, v2
	ds_read_b32 v5, v4 offset:17920
	s_waitcnt lgkmcnt(0)
	v_add_f32_e32 v2, v2, v5
	v_mul_f32_e32 v2, 0xbfb8aa3b, v2
	v_exp_f32_e32 v2, v2
	s_nop 0
	v_add_f32_e32 v2, 1.0, v2
	v_div_scale_f32 v5, s[2:3], v2, v2, 1.0
	v_rcp_f32_e32 v6, v5
	v_div_scale_f32 v7, vcc, 1.0, v2, 1.0
	s_mov_b32 s2, 0
	v_fma_f32 v8, -v5, v6, 1.0
	v_fmac_f32_e32 v6, v8, v6
	v_mul_f32_e32 v8, v7, v6
	v_fma_f32 v9, -v5, v8, v7
	v_fmac_f32_e32 v8, v9, v6
	v_fma_f32 v5, -v5, v8, v7
	v_div_fmas_f32 v5, v5, v6, v8
	v_div_fixup_f32 v2, v5, v2, 1.0
	v_add_f32_e32 v5, v3, v2
	s_nop 1
	s_waitcnt lgkmcnt(0)
	v_max_f32_dpp v6, v5, v5 quad_perm:[1,0,3,2] row_mask:0xf bank_mask:0xf
	s_nop 1
	s_waitcnt lgkmcnt(0)
	v_max_f32_dpp v6, v6, v6 quad_perm:[2,3,0,1] row_mask:0xf bank_mask:0xf
	s_nop 1
	s_waitcnt lgkmcnt(0)
	v_max_f32_dpp v8, v6, v6 row_half_mirror row_mask:0xf bank_mask:0xf
	v_cmp_eq_f32_e32 vcc, v5, v8
	s_nop 1
	v_lshrrev_b64 v[6:7], v200, vcc
	v_ffbl_b32_sdwa v6, v6 dst_sel:DWORD dst_unused:UNUSED_PAD src0_sel:BYTE_0
	v_add_u32_e32 v6, v6, v200
	v_cmp_ne_u32_e32 vcc, v230, v6
	s_nop 1
	v_cndmask_b32_e32 v6, v245, v5, vcc
	s_nop 1
	s_waitcnt lgkmcnt(0)
	v_max_f32_dpp v6, v6, v6 quad_perm:[1,0,3,2] row_mask:0xf bank_mask:0xf
	s_nop 1
	s_waitcnt lgkmcnt(0)
	v_max_f32_dpp v6, v6, v6 quad_perm:[2,3,0,1] row_mask:0xf bank_mask:0xf
	s_nop 1
	s_waitcnt lgkmcnt(0)
	v_max_f32_dpp v6, v6, v6 row_half_mirror row_mask:0xf bank_mask:0xf
	v_add_f32_e32 v6, v8, v6
	s_nop 0
	v_readlane_b32 s3, v6, 0
	v_readlane_b32 s4, v6, 8
	v_readlane_b32 s5, v6, 16
	v_cmp_eq_f32_e64 s[20:21], s3, v6
	v_cmp_gt_f32_e32 vcc, s3, v6
	v_cmp_gt_f32_e64 s[22:23], s4, v6
	v_cmp_eq_f32_e64 s[24:25], s4, v6
	v_cmp_gt_f32_e64 s[26:27], s5, v6
	v_cmp_eq_f32_e64 s[28:29], s5, v6
	s_and_b64 s[4:5], s[0:1], s[20:21]
	v_readlane_b32 s34, v6, 24
	s_and_b64 s[20:21], s[6:7], s[24:25]
	s_or_b64 s[4:5], vcc, s[4:5]
	v_readlane_b32 s40, v6, 32
	v_cmp_gt_f32_e64 s[30:31], s34, v6
	v_cmp_eq_f32_e64 s[34:35], s34, v6
	s_and_b64 s[24:25], s[8:9], s[28:29]
	v_cndmask_b32_e64 v7, 0, 1, s[4:5]
	s_or_b64 s[4:5], s[22:23], s[20:21]
	v_cmp_gt_f32_e64 s[36:37], s40, v6
	v_cmp_eq_f32_e64 s[40:41], s40, v6
	s_and_b64 s[28:29], s[10:11], s[34:35]
	v_cndmask_b32_e64 v8, 0, 1, s[4:5]
	s_or_b64 s[4:5], s[26:27], s[24:25]
	v_readlane_b32 s54, v6, 40
	s_and_b64 s[34:35], s[12:13], s[40:41]
	v_cndmask_b32_e64 v9, 0, 1, s[4:5]
	s_or_b64 s[4:5], s[30:31], s[28:29]
	v_cndmask_b32_e64 v10, 0, 1, s[4:5]
	s_or_b64 s[4:5], s[36:37], s[34:35]
	v_cmp_eq_f32_e64 s[20:21], s54, v6
	v_cndmask_b32_e64 v11, 0, 1, s[4:5]
	v_cmp_gt_f32_e32 vcc, s54, v6
	s_and_b64 s[4:5], s[14:15], s[20:21]
	v_readlane_b32 s3, v6, 48
	s_or_b64 s[4:5], vcc, s[4:5]
	v_cndmask_b32_e64 v12, 0, 1, s[4:5]
	v_cmp_eq_f32_e64 s[20:21], s3, v6
	v_cmp_gt_f32_e32 vcc, s3, v6
	s_and_b64 s[4:5], s[16:17], s[20:21]
	v_readlane_b32 s3, v6, 56
	s_or_b64 s[4:5], vcc, s[4:5]
	v_cndmask_b32_e64 v13, 0, 1, s[4:5]
	v_cmp_gt_f32_e32 vcc, s3, v6
	s_nop 1
	v_cndmask_b32_e64 v6, 0, 1, vcc
	v_add_u32_e32 v6, v8, v6
	v_add3_u32 v6, v6, v7, v9
	v_add3_u32 v6, v6, v10, v11
	v_add3_u32 v6, v6, v12, v13
	v_cmp_gt_u32_e32 vcc, 4, v6
	v_mov_b32_e32 v6, 0
	s_nop 0
	v_cndmask_b32_e32 v5, v245, v5, vcc
	v_ashrrev_i32_e32 v9, 31, v5
	v_sub_u32_e32 v8, 63, v230
	v_and_b32_e32 v9, 0x7fffffff, v9
	v_xor_b32_e32 v9, v5, v9
	s_nop 0
	v_readlane_b32 s23, v9, 0
	s_movk_i32 s22, 63
	v_readlane_b32 s21, v9, 1
	s_movk_i32 s20, 62
	v_cmp_gt_i64_e32 vcc, s[22:23], v[8:9]
	v_readlane_b32 s23, v9, 2
	s_movk_i32 s22, 61
	v_addc_co_u32_e32 v6, vcc, 0, v6, vcc
	v_cmp_gt_i64_e32 vcc, s[20:21], v[8:9]
	v_readlane_b32 s21, v9, 3
	s_movk_i32 s20, 60
	v_addc_co_u32_e32 v6, vcc, 0, v6, vcc
	v_cmp_gt_i64_e32 vcc, s[22:23], v[8:9]
	v_readlane_b32 s23, v9, 4
	s_movk_i32 s22, 59
	v_addc_co_u32_e32 v6, vcc, 0, v6, vcc
	v_cmp_gt_i64_e32 vcc, s[20:21], v[8:9]
	v_readlane_b32 s21, v9, 5
	s_movk_i32 s20, 58
	v_addc_co_u32_e32 v6, vcc, 0, v6, vcc
	v_cmp_gt_i64_e32 vcc, s[22:23], v[8:9]
	v_readlane_b32 s23, v9, 6
	s_movk_i32 s22, 57
	v_addc_co_u32_e32 v6, vcc, 0, v6, vcc
	v_cmp_gt_i64_e32 vcc, s[20:21], v[8:9]
	v_readlane_b32 s21, v9, 7
	s_movk_i32 s20, 56
	v_addc_co_u32_e32 v6, vcc, 0, v6, vcc
	v_cmp_gt_i64_e32 vcc, s[22:23], v[8:9]
	v_readlane_b32 s23, v9, 8
	s_movk_i32 s22, 55
	v_addc_co_u32_e32 v6, vcc, 0, v6, vcc
	v_cmp_gt_i64_e32 vcc, s[20:21], v[8:9]
; __device__ __forceinline__ void phase_nrr(const Frame& F, const Args& a, int l, const bf16_t* XA, const float* g, const float* modl, unsigned char* XN8) {
;     ...
;             int rank = 0;
; #pragma unroll 8
;             for (int e2 = 0; e2 < 64; ++e2) { const float v = __int_as_float(__builtin_amdgcn_readlane(__float_as_int(val), e2)); rank += (v > val || (v == val && e2 < lane)) ? 1 : 0; }
	v_readlane_b32 s21, v9, 9
	s_movk_i32 s20, 54
	v_addc_co_u32_e32 v6, vcc, 0, v6, vcc
	v_cmp_gt_i64_e32 vcc, s[22:23], v[8:9]
	v_readlane_b32 s23, v9, 10
	s_movk_i32 s22, 53
	v_addc_co_u32_e32 v6, vcc, 0, v6, vcc
	v_cmp_gt_i64_e32 vcc, s[20:21], v[8:9]
	v_readlane_b32 s21, v9, 11
	s_movk_i32 s20, 52
	v_addc_co_u32_e32 v6, vcc, 0, v6, vcc
	v_cmp_gt_i64_e32 vcc, s[22:23], v[8:9]
	v_readlane_b32 s23, v9, 12
	s_movk_i32 s22, 51
	v_addc_co_u32_e32 v6, vcc, 0, v6, vcc
	v_cmp_gt_i64_e32 vcc, s[20:21], v[8:9]
	v_readlane_b32 s21, v9, 13
	s_movk_i32 s20, 50
	v_addc_co_u32_e32 v6, vcc, 0, v6, vcc
	v_cmp_gt_i64_e32 vcc, s[22:23], v[8:9]
	v_readlane_b32 s23, v9, 14
	s_movk_i32 s22, 49
	v_addc_co_u32_e32 v6, vcc, 0, v6, vcc
	v_cmp_gt_i64_e32 vcc, s[20:21], v[8:9]
	v_readlane_b32 s21, v9, 15
	s_movk_i32 s20, 48
	v_addc_co_u32_e32 v6, vcc, 0, v6, vcc
	v_cmp_gt_i64_e32 vcc, s[22:23], v[8:9]
	v_readlane_b32 s23, v9, 16
	s_movk_i32 s22, 47
	v_addc_co_u32_e32 v6, vcc, 0, v6, vcc
	v_cmp_gt_i64_e32 vcc, s[20:21], v[8:9]
	v_readlane_b32 s21, v9, 17
	s_movk_i32 s20, 46
	v_addc_co_u32_e32 v6, vcc, 0, v6, vcc
	v_cmp_gt_i64_e32 vcc, s[22:23], v[8:9]
	v_readlane_b32 s23, v9, 18
	s_movk_i32 s22, 45
	v_addc_co_u32_e32 v6, vcc, 0, v6, vcc
	v_cmp_gt_i64_e32 vcc, s[20:21], v[8:9]
	v_readlane_b32 s21, v9, 19
	s_movk_i32 s20, 44
	v_addc_co_u32_e32 v6, vcc, 0, v6, vcc
	v_cmp_gt_i64_e32 vcc, s[22:23], v[8:9]
	v_readlane_b32 s23, v9, 20
	s_movk_i32 s22, 43
	v_addc_co_u32_e32 v6, vcc, 0, v6, vcc
	v_cmp_gt_i64_e32 vcc, s[20:21], v[8:9]
	v_readlane_b32 s21, v9, 21
	s_movk_i32 s20, 42
	v_addc_co_u32_e32 v6, vcc, 0, v6, vcc
	v_cmp_gt_i64_e32 vcc, s[22:23], v[8:9]
	v_readlane_b32 s23, v9, 22
	s_movk_i32 s22, 41
	v_addc_co_u32_e32 v6, vcc, 0, v6, vcc
	v_cmp_gt_i64_e32 vcc, s[20:21], v[8:9]
	v_readlane_b32 s21, v9, 23
	s_movk_i32 s20, 40
	v_addc_co_u32_e32 v6, vcc, 0, v6, vcc
	v_cmp_gt_i64_e32 vcc, s[22:23], v[8:9]
	v_readlane_b32 s23, v9, 24
	s_movk_i32 s22, 39
	v_addc_co_u32_e32 v6, vcc, 0, v6, vcc
	v_cmp_gt_i64_e32 vcc, s[20:21], v[8:9]
	v_readlane_b32 s21, v9, 25
	s_movk_i32 s20, 38
	v_addc_co_u32_e32 v6, vcc, 0, v6, vcc
	v_cmp_gt_i64_e32 vcc, s[22:23], v[8:9]
	v_readlane_b32 s23, v9, 26
	s_movk_i32 s22, 37
	v_addc_co_u32_e32 v6, vcc, 0, v6, vcc
	v_cmp_gt_i64_e32 vcc, s[20:21], v[8:9]
	v_readlane_b32 s21, v9, 27
	s_movk_i32 s20, 36
	v_addc_co_u32_e32 v6, vcc, 0, v6, vcc
	v_cmp_gt_i64_e32 vcc, s[22:23], v[8:9]
	v_readlane_b32 s23, v9, 28
	s_movk_i32 s22, 35
	v_addc_co_u32_e32 v6, vcc, 0, v6, vcc
	v_cmp_gt_i64_e32 vcc, s[20:21], v[8:9]
	v_readlane_b32 s21, v9, 29
	s_movk_i32 s20, 34
	v_addc_co_u32_e32 v6, vcc, 0, v6, vcc
	v_cmp_gt_i64_e32 vcc, s[22:23], v[8:9]
	v_readlane_b32 s23, v9, 30
	s_movk_i32 s22, 33
	v_addc_co_u32_e32 v6, vcc, 0, v6, vcc
	v_cmp_gt_i64_e32 vcc, s[20:21], v[8:9]
	v_readlane_b32 s21, v9, 31
	s_movk_i32 s20, 32
	v_addc_co_u32_e32 v6, vcc, 0, v6, vcc
	v_cmp_gt_i64_e32 vcc, s[22:23], v[8:9]
	v_readlane_b32 s23, v9, 32
	s_movk_i32 s22, 31
	v_addc_co_u32_e32 v6, vcc, 0, v6, vcc
	v_cmp_gt_i64_e32 vcc, s[20:21], v[8:9]
	v_readlane_b32 s21, v9, 33
	s_movk_i32 s20, 30
	v_addc_co_u32_e32 v6, vcc, 0, v6, vcc
	v_cmp_gt_i64_e32 vcc, s[22:23], v[8:9]
	v_readlane_b32 s23, v9, 34
	s_movk_i32 s22, 29
	v_addc_co_u32_e32 v6, vcc, 0, v6, vcc
	v_cmp_gt_i64_e32 vcc, s[20:21], v[8:9]
	v_readlane_b32 s21, v9, 35
	s_movk_i32 s20, 28
	v_addc_co_u32_e32 v6, vcc, 0, v6, vcc
	v_cmp_gt_i64_e32 vcc, s[22:23], v[8:9]
	v_readlane_b32 s23, v9, 36
	s_movk_i32 s22, 27
	v_addc_co_u32_e32 v6, vcc, 0, v6, vcc
	v_cmp_gt_i64_e32 vcc, s[20:21], v[8:9]
	v_readlane_b32 s21, v9, 37
	s_movk_i32 s20, 26
	v_addc_co_u32_e32 v6, vcc, 0, v6, vcc
	v_cmp_gt_i64_e32 vcc, s[22:23], v[8:9]
	v_readlane_b32 s23, v9, 38
	s_movk_i32 s22, 25
	v_addc_co_u32_e32 v6, vcc, 0, v6, vcc
	v_cmp_gt_i64_e32 vcc, s[20:21], v[8:9]
	v_readlane_b32 s21, v9, 39
	s_movk_i32 s20, 24
	v_addc_co_u32_e32 v6, vcc, 0, v6, vcc
	v_cmp_gt_i64_e32 vcc, s[22:23], v[8:9]
	v_readlane_b32 s23, v9, 40
	s_movk_i32 s22, 23
	v_addc_co_u32_e32 v6, vcc, 0, v6, vcc
	v_cmp_gt_i64_e32 vcc, s[20:21], v[8:9]
	v_readlane_b32 s21, v9, 41
	s_movk_i32 s20, 22
	v_addc_co_u32_e32 v6, vcc, 0, v6, vcc
	v_cmp_gt_i64_e32 vcc, s[22:23], v[8:9]
	v_readlane_b32 s23, v9, 42
	s_movk_i32 s22, 21
	v_addc_co_u32_e32 v6, vcc, 0, v6, vcc
	v_cmp_gt_i64_e32 vcc, s[20:21], v[8:9]
	v_readlane_b32 s21, v9, 43
	s_movk_i32 s20, 20
	v_addc_co_u32_e32 v6, vcc, 0, v6, vcc
	v_cmp_gt_i64_e32 vcc, s[22:23], v[8:9]
	v_readlane_b32 s23, v9, 44
	s_movk_i32 s22, 19
	v_addc_co_u32_e32 v6, vcc, 0, v6, vcc
	v_cmp_gt_i64_e32 vcc, s[20:21], v[8:9]
	v_readlane_b32 s21, v9, 45
	s_movk_i32 s20, 18
	v_addc_co_u32_e32 v6, vcc, 0, v6, vcc
	v_cmp_gt_i64_e32 vcc, s[22:23], v[8:9]
	v_readlane_b32 s23, v9, 46
	s_movk_i32 s22, 17
	v_addc_co_u32_e32 v6, vcc, 0, v6, vcc
	v_cmp_gt_i64_e32 vcc, s[20:21], v[8:9]
	v_readlane_b32 s21, v9, 47
	s_movk_i32 s20, 16
	v_addc_co_u32_e32 v6, vcc, 0, v6, vcc
	v_cmp_gt_i64_e32 vcc, s[22:23], v[8:9]
	v_readlane_b32 s23, v9, 48
	s_movk_i32 s22, 15
	v_addc_co_u32_e32 v6, vcc, 0, v6, vcc
	v_cmp_gt_i64_e32 vcc, s[20:21], v[8:9]
	v_readlane_b32 s21, v9, 49
	s_movk_i32 s20, 14
	v_addc_co_u32_e32 v6, vcc, 0, v6, vcc
	v_cmp_gt_i64_e32 vcc, s[22:23], v[8:9]
	v_readlane_b32 s23, v9, 50
	s_movk_i32 s22, 13
	v_addc_co_u32_e32 v6, vcc, 0, v6, vcc
	v_cmp_gt_i64_e32 vcc, s[20:21], v[8:9]
	v_readlane_b32 s21, v9, 51
	s_movk_i32 s20, 12
	v_addc_co_u32_e32 v6, vcc, 0, v6, vcc
	v_cmp_gt_i64_e32 vcc, s[22:23], v[8:9]
	v_readlane_b32 s23, v9, 52
	s_movk_i32 s22, 11
	v_addc_co_u32_e32 v6, vcc, 0, v6, vcc
	v_cmp_gt_i64_e32 vcc, s[20:21], v[8:9]
	v_readlane_b32 s21, v9, 53
	s_movk_i32 s20, 10
; __device__ __forceinline__ void phase_nrr(const Frame& F, const Args& a, int l, const bf16_t* XA, const float* g, const float* modl, unsigned char* XN8) {
;     ...
;         for (int i = 0; i < 8; ++i) { const int t = tb + i;
;             const float lg = Pl[(w * 8 + i) * NE + lane] + Pl[(64 + w * 8 + i) * NE + lane]; const float sc = 1.f / (1.f + __expf(-lg)); const float bb = sc + bias;
;             float m1 = bb; m1 = fmaxf(m1, __shfl_xor(m1, 1)); m1 = fmaxf(m1, __shfl_xor(m1, 2)); m1 = fmaxf(m1, __shfl_xor(m1, 4));
;             const unsigned long long eq = __ballot(bb == m1); const int gbase = lane & ~7; const unsigned grpmask = (unsigned)((eq >> gbase) & 0xffull);
;             const int first = gbase + __builtin_ctz(grpmask);
;             float m2 = (lane == first) ? -INFINITY : bb; m2 = fmaxf(m2, __shfl_xor(m2, 1)); m2 = fmaxf(m2, __shfl_xor(m2, 2)); m2 = fmaxf(m2, __shfl_xor(m2, 4));
;             const float gsum = m1 + m2; const int gq = lane >> 3;
;             int grank = 0;
; #pragma unroll
;             for (int g2 = 0; g2 < 8; ++g2) { const float v = __int_as_float(__builtin_amdgcn_readlane(__float_as_int(gsum), g2 * 8)); grank += (v > gsum || (v == gsum && g2 < gq)) ? 1 : 0; }
;             const bool keep = grank < 4; const float val = keep ? bb : -INFINITY;
;             int rank = 0;
; #pragma unroll 8
;             for (int e2 = 0; e2 < 64; ++e2) { const float v = __int_as_float(__builtin_amdgcn_readlane(__float_as_int(val), e2)); rank += (v > val || (v == val && e2 < lane)) ? 1 : 0; }
;             const bool sel = rank < TOPK;
;             const float ssum = wave_sum(sel ? sc : 0.f);
;             if (sel) { const int p = atomicAdd((int*)(hist + lane), 1); top_e[t * TOPK + rank] = lane; gate[t * TOPK + rank] = sc / ssum * 2.5f; lpos[t * TOPK + rank] = p; }
	v_addc_co_u32_e32 v6, vcc, 0, v6, vcc
	v_cmp_gt_i64_e32 vcc, s[22:23], v[8:9]
	v_readlane_b32 s23, v9, 54
	s_movk_i32 s22, 9
	v_addc_co_u32_e32 v6, vcc, 0, v6, vcc
	v_cmp_gt_i64_e32 vcc, s[20:21], v[8:9]
	v_readlane_b32 s21, v9, 55
	s_movk_i32 s20, 8
	v_addc_co_u32_e32 v6, vcc, 0, v6, vcc
	v_cmp_gt_i64_e32 vcc, s[22:23], v[8:9]
	v_readlane_b32 s23, v9, 56
	s_movk_i32 s22, 7
	v_addc_co_u32_e32 v6, vcc, 0, v6, vcc
	v_cmp_gt_i64_e32 vcc, s[20:21], v[8:9]
	v_readlane_b32 s21, v9, 57
	s_movk_i32 s20, 6
	v_addc_co_u32_e32 v6, vcc, 0, v6, vcc
	v_cmp_gt_i64_e32 vcc, s[22:23], v[8:9]
	v_readlane_b32 s23, v9, 58
	s_movk_i32 s22, 5
	v_addc_co_u32_e32 v6, vcc, 0, v6, vcc
	v_cmp_gt_i64_e32 vcc, s[20:21], v[8:9]
	v_readlane_b32 s21, v9, 59
	s_movk_i32 s20, 4
	v_addc_co_u32_e32 v6, vcc, 0, v6, vcc
	v_cmp_gt_i64_e32 vcc, s[22:23], v[8:9]
	v_readlane_b32 s23, v9, 60
	s_movk_i32 s22, 3
	v_addc_co_u32_e32 v6, vcc, 0, v6, vcc
	v_cmp_gt_i64_e32 vcc, s[20:21], v[8:9]
	v_readlane_b32 s21, v9, 61
	s_movk_i32 s20, 2
	v_addc_co_u32_e32 v6, vcc, 0, v6, vcc
	v_cmp_gt_i64_e32 vcc, s[22:23], v[8:9]
	v_readlane_b32 s23, v9, 62
	s_movk_i32 s22, 1
	v_addc_co_u32_e32 v6, vcc, 0, v6, vcc
	v_cmp_gt_i64_e32 vcc, s[20:21], v[8:9]
	v_readlane_b32 s21, v9, 63
	s_movk_i32 s20, 0
	v_addc_co_u32_e32 v6, vcc, 0, v6, vcc
	v_cmp_gt_i64_e32 vcc, s[22:23], v[8:9]
	s_nop 1
	v_addc_co_u32_e32 v6, vcc, 0, v6, vcc
	v_cmp_gt_i64_e32 vcc, s[20:21], v[8:9]
	s_nop 1
	v_addc_co_u32_e32 v6, vcc, 0, v6, vcc
	v_cmp_gt_u32_e32 vcc, 6, v6
	s_nop 1
	v_cndmask_b32_e32 v5, 0, v2, vcc
	ds_bpermute_b32 v7, v1, v5
	s_waitcnt lgkmcnt(0)
	v_add_f32_e32 v5, v5, v7
	ds_bpermute_b32 v7, v201, v5
	s_waitcnt lgkmcnt(0)
	v_add_f32_e32 v5, v5, v7
	ds_bpermute_b32 v7, v220, v5
	s_waitcnt lgkmcnt(0)
	v_add_f32_e32 v5, v5, v7
	ds_bpermute_b32 v7, v221, v5
	s_waitcnt lgkmcnt(0)
	v_add_f32_e32 v5, v5, v7
	ds_bpermute_b32 v7, v222, v5
	s_waitcnt lgkmcnt(0)
	v_add_f32_e32 v5, v5, v7
	ds_bpermute_b32 v7, v223, v5
	s_and_saveexec_b64 s[2:3], vcc
	s_cbranch_execz .LBB0_1336
	s_waitcnt lgkmcnt(0)
	v_add_f32_e32 v5, v5, v7
	v_div_scale_f32 v11, s[4:5], v5, v5, v2
	v_add3_u32 v6, s50, 36, v6
	v_rcp_f32_e32 v12, v11
	v_ashrrev_i32_e32 v7, 31, v6
	v_lshlrev_b64 v[6:7], 2, v[6:7]
	v_lshl_add_u64 v[8:9], s[42:43], 0, v[6:7]
	ds_add_rtn_u32 v10, v227, v243
	global_store_dword v[8:9], v230, off
	v_fma_f32 v8, -v11, v12, 1.0
	v_fmac_f32_e32 v12, v8, v12
	v_div_scale_f32 v8, vcc, v2, v5, v2
	v_mul_f32_e32 v9, v8, v12
	v_fma_f32 v13, -v11, v9, v8
	v_fmac_f32_e32 v9, v13, v12
	v_fma_f32 v8, -v11, v9, v8
	v_div_fmas_f32 v8, v8, v12, v9
	v_div_fixup_f32 v2, v8, v5, v2
	v_mul_f32_e32 v2, 0x40200000, v2
	v_lshl_add_u64 v[8:9], s[44:45], 0, v[6:7]
	v_lshl_add_u64 v[6:7], s[46:47], 0, v[6:7]
	global_store_dword v[8:9], v2, off
	s_waitcnt lgkmcnt(0)
	global_store_dword v[6:7], v10, off
.LBB0_1336:
	s_or_b64 exec, exec, s[2:3]
	v_add_u32_e32 v2, s82, v226
	ds_read_b32 v2, v2
	ds_read_b32 v4, v4 offset:18176
	s_waitcnt lgkmcnt(0)
	v_add_f32_e32 v2, v2, v4
	v_mul_f32_e32 v2, 0xbfb8aa3b, v2
	v_exp_f32_e32 v2, v2
	s_nop 0
	v_add_f32_e32 v2, 1.0, v2
	v_div_scale_f32 v4, s[2:3], v2, v2, 1.0
	v_rcp_f32_e32 v5, v4
	v_div_scale_f32 v6, vcc, 1.0, v2, 1.0
	s_mov_b32 s2, 0
	v_fma_f32 v7, -v4, v5, 1.0
	v_fmac_f32_e32 v5, v7, v5
	v_mul_f32_e32 v7, v6, v5
	v_fma_f32 v8, -v4, v7, v6
	v_fmac_f32_e32 v7, v8, v5
	v_fma_f32 v4, -v4, v7, v6
	v_div_fmas_f32 v4, v4, v5, v7
	v_div_fixup_f32 v2, v4, v2, 1.0
	v_add_f32_e32 v3, v3, v2
	s_nop 1
	s_waitcnt lgkmcnt(0)
	v_max_f32_dpp v4, v3, v3 quad_perm:[1,0,3,2] row_mask:0xf bank_mask:0xf
	s_nop 1
	s_waitcnt lgkmcnt(0)
	v_max_f32_dpp v4, v4, v4 quad_perm:[2,3,0,1] row_mask:0xf bank_mask:0xf
	s_nop 1
	s_waitcnt lgkmcnt(0)
	v_max_f32_dpp v6, v4, v4 row_half_mirror row_mask:0xf bank_mask:0xf
	v_cmp_eq_f32_e32 vcc, v3, v6
	s_nop 1
	v_lshrrev_b64 v[4:5], v200, vcc
	v_ffbl_b32_sdwa v4, v4 dst_sel:DWORD dst_unused:UNUSED_PAD src0_sel:BYTE_0
	v_add_u32_e32 v4, v4, v200
	v_cmp_ne_u32_e32 vcc, v230, v4
	s_nop 1
	v_cndmask_b32_e32 v4, v245, v3, vcc
	s_nop 1
	s_waitcnt lgkmcnt(0)
	v_max_f32_dpp v4, v4, v4 quad_perm:[1,0,3,2] row_mask:0xf bank_mask:0xf
	s_nop 1
	s_waitcnt lgkmcnt(0)
	v_max_f32_dpp v4, v4, v4 quad_perm:[2,3,0,1] row_mask:0xf bank_mask:0xf
	s_nop 1
	s_waitcnt lgkmcnt(0)
; __device__ __forceinline__ void phase_nrr(const Frame& F, const Args& a, int l, const bf16_t* XA, const float* g, const float* modl, unsigned char* XN8) {
;     ...
;             float m2 = (lane == first) ? -INFINITY : bb; m2 = fmaxf(m2, __shfl_xor(m2, 1)); m2 = fmaxf(m2, __shfl_xor(m2, 2)); m2 = fmaxf(m2, __shfl_xor(m2, 4));
;             const float gsum = m1 + m2; const int gq = lane >> 3;
;             int grank = 0;
; #pragma unroll
;             for (int g2 = 0; g2 < 8; ++g2) { const float v = __int_as_float(__builtin_amdgcn_readlane(__float_as_int(gsum), g2 * 8)); grank += (v > gsum || (v == gsum && g2 < gq)) ? 1 : 0; }
;             const bool keep = grank < 4; const float val = keep ? bb : -INFINITY;
;             int rank = 0;
; #pragma unroll 8
;             for (int e2 = 0; e2 < 64; ++e2) { const float v = __int_as_float(__builtin_amdgcn_readlane(__float_as_int(val), e2)); rank += (v > val || (v == val && e2 < lane)) ? 1 : 0; }
	v_max_f32_dpp v4, v4, v4 row_half_mirror row_mask:0xf bank_mask:0xf
	v_add_f32_e32 v4, v6, v4
	s_nop 0
	v_readlane_b32 s3, v4, 0
	v_readlane_b32 s4, v4, 8
	v_readlane_b32 s5, v4, 16
	v_cmp_eq_f32_e64 s[20:21], s3, v4
	v_cmp_gt_f32_e32 vcc, s3, v4
	v_cmp_gt_f32_e64 s[22:23], s4, v4
	v_cmp_eq_f32_e64 s[24:25], s4, v4
	v_cmp_gt_f32_e64 s[26:27], s5, v4
	v_cmp_eq_f32_e64 s[28:29], s5, v4
	s_and_b64 s[4:5], s[0:1], s[20:21]
	v_readlane_b32 s34, v4, 24
	s_and_b64 s[20:21], s[6:7], s[24:25]
	s_or_b64 s[4:5], vcc, s[4:5]
	v_readlane_b32 s40, v4, 32
	v_cmp_gt_f32_e64 s[30:31], s34, v4
	v_cmp_eq_f32_e64 s[34:35], s34, v4
	s_and_b64 s[24:25], s[8:9], s[28:29]
	v_cndmask_b32_e64 v5, 0, 1, s[4:5]
	s_or_b64 s[4:5], s[22:23], s[20:21]
	v_cmp_gt_f32_e64 s[36:37], s40, v4
	v_cmp_eq_f32_e64 s[40:41], s40, v4
	s_and_b64 s[28:29], s[10:11], s[34:35]
	v_cndmask_b32_e64 v6, 0, 1, s[4:5]
	s_or_b64 s[4:5], s[26:27], s[24:25]
	v_readlane_b32 s54, v4, 40
	s_and_b64 s[34:35], s[12:13], s[40:41]
	v_cndmask_b32_e64 v7, 0, 1, s[4:5]
	s_or_b64 s[4:5], s[30:31], s[28:29]
	v_cndmask_b32_e64 v8, 0, 1, s[4:5]
	s_or_b64 s[4:5], s[36:37], s[34:35]
	v_cmp_eq_f32_e64 s[20:21], s54, v4
	v_cndmask_b32_e64 v9, 0, 1, s[4:5]
	v_cmp_gt_f32_e32 vcc, s54, v4
	s_and_b64 s[4:5], s[14:15], s[20:21]
	v_readlane_b32 s3, v4, 48
	s_or_b64 s[4:5], vcc, s[4:5]
	v_cndmask_b32_e64 v10, 0, 1, s[4:5]
	v_cmp_eq_f32_e64 s[20:21], s3, v4
	v_cmp_gt_f32_e32 vcc, s3, v4
	s_and_b64 s[4:5], s[16:17], s[20:21]
	v_readlane_b32 s3, v4, 56
	s_or_b64 s[4:5], vcc, s[4:5]
	v_cndmask_b32_e64 v11, 0, 1, s[4:5]
	v_cmp_gt_f32_e32 vcc, s3, v4
	s_nop 1
	v_cndmask_b32_e64 v4, 0, 1, vcc
	v_add_u32_e32 v4, v6, v4
	v_add3_u32 v4, v4, v5, v7
	v_add3_u32 v4, v4, v8, v9
	v_add3_u32 v4, v4, v10, v11
	v_cmp_gt_u32_e32 vcc, 4, v4
	v_mov_b32_e32 v4, 0
	s_nop 0
	v_cndmask_b32_e32 v3, v245, v3, vcc
	v_ashrrev_i32_e32 v9, 31, v3
	v_sub_u32_e32 v8, 63, v230
	v_and_b32_e32 v9, 0x7fffffff, v9
	v_xor_b32_e32 v9, v3, v9
	s_nop 0
	v_readlane_b32 s23, v9, 0
	s_movk_i32 s22, 63
	v_readlane_b32 s21, v9, 1
	s_movk_i32 s20, 62
	v_cmp_gt_i64_e32 vcc, s[22:23], v[8:9]
	v_readlane_b32 s23, v9, 2
	s_movk_i32 s22, 61
	v_addc_co_u32_e32 v4, vcc, 0, v4, vcc
	v_cmp_gt_i64_e32 vcc, s[20:21], v[8:9]
	v_readlane_b32 s21, v9, 3
	s_movk_i32 s20, 60
	v_addc_co_u32_e32 v4, vcc, 0, v4, vcc
	v_cmp_gt_i64_e32 vcc, s[22:23], v[8:9]
	v_readlane_b32 s23, v9, 4
	s_movk_i32 s22, 59
	v_addc_co_u32_e32 v4, vcc, 0, v4, vcc
	v_cmp_gt_i64_e32 vcc, s[20:21], v[8:9]
	v_readlane_b32 s21, v9, 5
	s_movk_i32 s20, 58
	v_addc_co_u32_e32 v4, vcc, 0, v4, vcc
	v_cmp_gt_i64_e32 vcc, s[22:23], v[8:9]
	v_readlane_b32 s23, v9, 6
	s_movk_i32 s22, 57
	v_addc_co_u32_e32 v4, vcc, 0, v4, vcc
	v_cmp_gt_i64_e32 vcc, s[20:21], v[8:9]
	v_readlane_b32 s21, v9, 7
	s_movk_i32 s20, 56
	v_addc_co_u32_e32 v4, vcc, 0, v4, vcc
	v_cmp_gt_i64_e32 vcc, s[22:23], v[8:9]
	v_readlane_b32 s23, v9, 8
	s_movk_i32 s22, 55
	v_addc_co_u32_e32 v4, vcc, 0, v4, vcc
	v_cmp_gt_i64_e32 vcc, s[20:21], v[8:9]
	v_readlane_b32 s21, v9, 9
	s_movk_i32 s20, 54
	v_addc_co_u32_e32 v4, vcc, 0, v4, vcc
	v_cmp_gt_i64_e32 vcc, s[22:23], v[8:9]
	v_readlane_b32 s23, v9, 10
	s_movk_i32 s22, 53
	v_addc_co_u32_e32 v4, vcc, 0, v4, vcc
	v_cmp_gt_i64_e32 vcc, s[20:21], v[8:9]
	v_readlane_b32 s21, v9, 11
	s_movk_i32 s20, 52
	v_addc_co_u32_e32 v4, vcc, 0, v4, vcc
	v_cmp_gt_i64_e32 vcc, s[22:23], v[8:9]
	v_readlane_b32 s23, v9, 12
	s_movk_i32 s22, 51
	v_addc_co_u32_e32 v4, vcc, 0, v4, vcc
	v_cmp_gt_i64_e32 vcc, s[20:21], v[8:9]
	v_readlane_b32 s21, v9, 13
	s_movk_i32 s20, 50
	v_addc_co_u32_e32 v4, vcc, 0, v4, vcc
	v_cmp_gt_i64_e32 vcc, s[22:23], v[8:9]
	v_readlane_b32 s23, v9, 14
	s_movk_i32 s22, 49
	v_addc_co_u32_e32 v4, vcc, 0, v4, vcc
	v_cmp_gt_i64_e32 vcc, s[20:21], v[8:9]
	v_readlane_b32 s21, v9, 15
	s_movk_i32 s20, 48
	v_addc_co_u32_e32 v4, vcc, 0, v4, vcc
	v_cmp_gt_i64_e32 vcc, s[22:23], v[8:9]
	v_readlane_b32 s23, v9, 16
	s_movk_i32 s22, 47
	v_addc_co_u32_e32 v4, vcc, 0, v4, vcc
	v_cmp_gt_i64_e32 vcc, s[20:21], v[8:9]
	v_readlane_b32 s21, v9, 17
	s_movk_i32 s20, 46
	v_addc_co_u32_e32 v4, vcc, 0, v4, vcc
	v_cmp_gt_i64_e32 vcc, s[22:23], v[8:9]
	v_readlane_b32 s23, v9, 18
	s_movk_i32 s22, 45
	v_addc_co_u32_e32 v4, vcc, 0, v4, vcc
	v_cmp_gt_i64_e32 vcc, s[20:21], v[8:9]
	v_readlane_b32 s21, v9, 19
	s_movk_i32 s20, 44
	v_addc_co_u32_e32 v4, vcc, 0, v4, vcc
	v_cmp_gt_i64_e32 vcc, s[22:23], v[8:9]
	v_readlane_b32 s23, v9, 20
	s_movk_i32 s22, 43
	v_addc_co_u32_e32 v4, vcc, 0, v4, vcc
	v_cmp_gt_i64_e32 vcc, s[20:21], v[8:9]
	v_readlane_b32 s21, v9, 21
	s_movk_i32 s20, 42
	v_addc_co_u32_e32 v4, vcc, 0, v4, vcc
	v_cmp_gt_i64_e32 vcc, s[22:23], v[8:9]
	v_readlane_b32 s23, v9, 22
	s_movk_i32 s22, 41
	v_addc_co_u32_e32 v4, vcc, 0, v4, vcc
	v_cmp_gt_i64_e32 vcc, s[20:21], v[8:9]
	v_readlane_b32 s21, v9, 23
	s_movk_i32 s20, 40
	v_addc_co_u32_e32 v4, vcc, 0, v4, vcc
	v_cmp_gt_i64_e32 vcc, s[22:23], v[8:9]
	v_readlane_b32 s23, v9, 24
	s_movk_i32 s22, 39
	v_addc_co_u32_e32 v4, vcc, 0, v4, vcc
	v_cmp_gt_i64_e32 vcc, s[20:21], v[8:9]
	v_readlane_b32 s21, v9, 25
	s_movk_i32 s20, 38
	v_addc_co_u32_e32 v4, vcc, 0, v4, vcc
	v_cmp_gt_i64_e32 vcc, s[22:23], v[8:9]
	v_readlane_b32 s23, v9, 26
	s_movk_i32 s22, 37
	v_addc_co_u32_e32 v4, vcc, 0, v4, vcc
	v_cmp_gt_i64_e32 vcc, s[20:21], v[8:9]
	v_readlane_b32 s21, v9, 27
	s_movk_i32 s20, 36
	v_addc_co_u32_e32 v4, vcc, 0, v4, vcc
	v_cmp_gt_i64_e32 vcc, s[22:23], v[8:9]
	v_readlane_b32 s23, v9, 28
	s_movk_i32 s22, 35
	v_addc_co_u32_e32 v4, vcc, 0, v4, vcc
	v_cmp_gt_i64_e32 vcc, s[20:21], v[8:9]
	v_readlane_b32 s21, v9, 29
	s_movk_i32 s20, 34
	v_addc_co_u32_e32 v4, vcc, 0, v4, vcc
	v_cmp_gt_i64_e32 vcc, s[22:23], v[8:9]
; __device__ __forceinline__ void phase_nrr(const Frame& F, const Args& a, int l, const bf16_t* XA, const float* g, const float* modl, unsigned char* XN8) {
;     ...
;             for (int e2 = 0; e2 < 64; ++e2) { const float v = __int_as_float(__builtin_amdgcn_readlane(__float_as_int(val), e2)); rank += (v > val || (v == val && e2 < lane)) ? 1 : 0; }
;             const bool sel = rank < TOPK;
;             const float ssum = wave_sum(sel ? sc : 0.f);
;             if (sel) { const int p = atomicAdd((int*)(hist + lane), 1); top_e[t * TOPK + rank] = lane; gate[t * TOPK + rank] = sc / ssum * 2.5f; lpos[t * TOPK + rank] = p; }
	v_readlane_b32 s23, v9, 30
	s_movk_i32 s22, 33
	v_addc_co_u32_e32 v4, vcc, 0, v4, vcc
	v_cmp_gt_i64_e32 vcc, s[20:21], v[8:9]
	v_readlane_b32 s21, v9, 31
	s_movk_i32 s20, 32
	v_addc_co_u32_e32 v4, vcc, 0, v4, vcc
	v_cmp_gt_i64_e32 vcc, s[22:23], v[8:9]
	v_readlane_b32 s23, v9, 32
	s_movk_i32 s22, 31
	v_addc_co_u32_e32 v4, vcc, 0, v4, vcc
	v_cmp_gt_i64_e32 vcc, s[20:21], v[8:9]
	v_readlane_b32 s21, v9, 33
	s_movk_i32 s20, 30
	v_addc_co_u32_e32 v4, vcc, 0, v4, vcc
	v_cmp_gt_i64_e32 vcc, s[22:23], v[8:9]
	v_readlane_b32 s23, v9, 34
	s_movk_i32 s22, 29
	v_addc_co_u32_e32 v4, vcc, 0, v4, vcc
	v_cmp_gt_i64_e32 vcc, s[20:21], v[8:9]
	v_readlane_b32 s21, v9, 35
	s_movk_i32 s20, 28
	v_addc_co_u32_e32 v4, vcc, 0, v4, vcc
	v_cmp_gt_i64_e32 vcc, s[22:23], v[8:9]
	v_readlane_b32 s23, v9, 36
	s_movk_i32 s22, 27
	v_addc_co_u32_e32 v4, vcc, 0, v4, vcc
	v_cmp_gt_i64_e32 vcc, s[20:21], v[8:9]
	v_readlane_b32 s21, v9, 37
	s_movk_i32 s20, 26
	v_addc_co_u32_e32 v4, vcc, 0, v4, vcc
	v_cmp_gt_i64_e32 vcc, s[22:23], v[8:9]
	v_readlane_b32 s23, v9, 38
	s_movk_i32 s22, 25
	v_addc_co_u32_e32 v4, vcc, 0, v4, vcc
	v_cmp_gt_i64_e32 vcc, s[20:21], v[8:9]
	v_readlane_b32 s21, v9, 39
	s_movk_i32 s20, 24
	v_addc_co_u32_e32 v4, vcc, 0, v4, vcc
	v_cmp_gt_i64_e32 vcc, s[22:23], v[8:9]
	v_readlane_b32 s23, v9, 40
	s_movk_i32 s22, 23
	v_addc_co_u32_e32 v4, vcc, 0, v4, vcc
	v_cmp_gt_i64_e32 vcc, s[20:21], v[8:9]
	v_readlane_b32 s21, v9, 41
	s_movk_i32 s20, 22
	v_addc_co_u32_e32 v4, vcc, 0, v4, vcc
	v_cmp_gt_i64_e32 vcc, s[22:23], v[8:9]
	v_readlane_b32 s23, v9, 42
	s_movk_i32 s22, 21
	v_addc_co_u32_e32 v4, vcc, 0, v4, vcc
	v_cmp_gt_i64_e32 vcc, s[20:21], v[8:9]
	v_readlane_b32 s21, v9, 43
	s_movk_i32 s20, 20
	v_addc_co_u32_e32 v4, vcc, 0, v4, vcc
	v_cmp_gt_i64_e32 vcc, s[22:23], v[8:9]
	v_readlane_b32 s23, v9, 44
	s_movk_i32 s22, 19
	v_addc_co_u32_e32 v4, vcc, 0, v4, vcc
	v_cmp_gt_i64_e32 vcc, s[20:21], v[8:9]
	v_readlane_b32 s21, v9, 45
	s_movk_i32 s20, 18
	v_addc_co_u32_e32 v4, vcc, 0, v4, vcc
	v_cmp_gt_i64_e32 vcc, s[22:23], v[8:9]
	v_readlane_b32 s23, v9, 46
	s_movk_i32 s22, 17
	v_addc_co_u32_e32 v4, vcc, 0, v4, vcc
	v_cmp_gt_i64_e32 vcc, s[20:21], v[8:9]
	v_readlane_b32 s21, v9, 47
	s_movk_i32 s20, 16
	v_addc_co_u32_e32 v4, vcc, 0, v4, vcc
	v_cmp_gt_i64_e32 vcc, s[22:23], v[8:9]
	v_readlane_b32 s23, v9, 48
	s_movk_i32 s22, 15
	v_addc_co_u32_e32 v4, vcc, 0, v4, vcc
	v_cmp_gt_i64_e32 vcc, s[20:21], v[8:9]
	v_readlane_b32 s21, v9, 49
	s_movk_i32 s20, 14
	v_addc_co_u32_e32 v4, vcc, 0, v4, vcc
	v_cmp_gt_i64_e32 vcc, s[22:23], v[8:9]
	v_readlane_b32 s23, v9, 50
	s_movk_i32 s22, 13
	v_addc_co_u32_e32 v4, vcc, 0, v4, vcc
	v_cmp_gt_i64_e32 vcc, s[20:21], v[8:9]
	v_readlane_b32 s21, v9, 51
	s_movk_i32 s20, 12
	v_addc_co_u32_e32 v4, vcc, 0, v4, vcc
	v_cmp_gt_i64_e32 vcc, s[22:23], v[8:9]
	v_readlane_b32 s23, v9, 52
	s_movk_i32 s22, 11
	v_addc_co_u32_e32 v4, vcc, 0, v4, vcc
	v_cmp_gt_i64_e32 vcc, s[20:21], v[8:9]
	v_readlane_b32 s21, v9, 53
	s_movk_i32 s20, 10
	v_addc_co_u32_e32 v4, vcc, 0, v4, vcc
	v_cmp_gt_i64_e32 vcc, s[22:23], v[8:9]
	v_readlane_b32 s23, v9, 54
	s_movk_i32 s22, 9
	v_addc_co_u32_e32 v4, vcc, 0, v4, vcc
	v_cmp_gt_i64_e32 vcc, s[20:21], v[8:9]
	v_readlane_b32 s21, v9, 55
	s_movk_i32 s20, 8
	v_addc_co_u32_e32 v4, vcc, 0, v4, vcc
	v_cmp_gt_i64_e32 vcc, s[22:23], v[8:9]
	v_readlane_b32 s23, v9, 56
	s_movk_i32 s22, 7
	v_addc_co_u32_e32 v4, vcc, 0, v4, vcc
	v_cmp_gt_i64_e32 vcc, s[20:21], v[8:9]
	v_readlane_b32 s21, v9, 57
	s_movk_i32 s20, 6
	v_addc_co_u32_e32 v4, vcc, 0, v4, vcc
	v_cmp_gt_i64_e32 vcc, s[22:23], v[8:9]
	v_readlane_b32 s23, v9, 58
	s_movk_i32 s22, 5
	v_addc_co_u32_e32 v4, vcc, 0, v4, vcc
	v_cmp_gt_i64_e32 vcc, s[20:21], v[8:9]
	v_readlane_b32 s21, v9, 59
	s_movk_i32 s20, 4
	v_addc_co_u32_e32 v4, vcc, 0, v4, vcc
	v_cmp_gt_i64_e32 vcc, s[22:23], v[8:9]
	v_readlane_b32 s23, v9, 60
	s_movk_i32 s22, 3
	v_addc_co_u32_e32 v4, vcc, 0, v4, vcc
	v_cmp_gt_i64_e32 vcc, s[20:21], v[8:9]
	v_readlane_b32 s21, v9, 61
	s_movk_i32 s20, 2
	v_addc_co_u32_e32 v4, vcc, 0, v4, vcc
	v_cmp_gt_i64_e32 vcc, s[22:23], v[8:9]
	v_readlane_b32 s23, v9, 62
	s_movk_i32 s22, 1
	v_addc_co_u32_e32 v4, vcc, 0, v4, vcc
	v_cmp_gt_i64_e32 vcc, s[20:21], v[8:9]
	v_readlane_b32 s21, v9, 63
	s_movk_i32 s20, 0
	v_addc_co_u32_e32 v4, vcc, 0, v4, vcc
	v_cmp_gt_i64_e32 vcc, s[22:23], v[8:9]
	s_nop 1
	v_addc_co_u32_e32 v4, vcc, 0, v4, vcc
	v_cmp_gt_i64_e32 vcc, s[20:21], v[8:9]
	s_nop 1
	v_addc_co_u32_e32 v4, vcc, 0, v4, vcc
	v_cmp_gt_u32_e32 vcc, 6, v4
	s_nop 1
	v_cndmask_b32_e32 v3, 0, v2, vcc
	ds_bpermute_b32 v5, v1, v3
	s_waitcnt lgkmcnt(0)
	v_add_f32_e32 v3, v3, v5
	ds_bpermute_b32 v5, v201, v3
	s_waitcnt lgkmcnt(0)
	v_add_f32_e32 v3, v3, v5
	ds_bpermute_b32 v5, v220, v3
	s_waitcnt lgkmcnt(0)
	v_add_f32_e32 v3, v3, v5
	ds_bpermute_b32 v5, v221, v3
	s_waitcnt lgkmcnt(0)
	v_add_f32_e32 v3, v3, v5
	ds_bpermute_b32 v5, v222, v3
	s_waitcnt lgkmcnt(0)
	v_add_f32_e32 v3, v3, v5
	ds_bpermute_b32 v5, v223, v3
	s_and_saveexec_b64 s[2:3], vcc
	s_cbranch_execz .LBB0_1340
	s_waitcnt lgkmcnt(0)
	v_add_f32_e32 v3, v3, v5
	v_div_scale_f32 v9, s[4:5], v3, v3, v2
	v_add3_u32 v4, s50, 42, v4
	v_rcp_f32_e32 v10, v9
	v_ashrrev_i32_e32 v5, 31, v4
	v_lshlrev_b64 v[4:5], 2, v[4:5]
	v_lshl_add_u64 v[6:7], s[42:43], 0, v[4:5]
	ds_add_rtn_u32 v8, v227, v243
	global_store_dword v[6:7], v230, off
	v_fma_f32 v6, -v9, v10, 1.0
	v_fmac_f32_e32 v10, v6, v10
	v_div_scale_f32 v6, vcc, v2, v3, v2
	v_mul_f32_e32 v7, v6, v10
	v_fma_f32 v11, -v9, v7, v6
	v_fmac_f32_e32 v7, v11, v10
	v_fma_f32 v6, -v9, v7, v6
	v_div_fmas_f32 v6, v6, v10, v7
	v_div_fixup_f32 v2, v6, v3, v2
	v_mul_f32_e32 v6, 0x40200000, v2
	v_lshl_add_u64 v[2:3], s[44:45], 0, v[4:5]
	global_store_dword v[2:3], v6, off
	v_lshl_add_u64 v[2:3], s[46:47], 0, v[4:5]
	s_waitcnt lgkmcnt(0)
	global_store_dword v[2:3], v8, off
